# removed the 112 s_nop 15 x2 pads around MFMA groups (every Table-38 distance is already supplied by the remaining nops; checked all rows incl. branch edges)
# speedup vs baseline: 1.0071x; 1.0024x over previous
.LBB0_253:
	s_ashr_i32 s6, s15, 7
	s_lshl_b32 s7, s15, 5
	s_and_b32 s22, s7, 0xfe0
	s_ashr_i32 s7, s6, 31
	s_lshl_b64 s[10:11], s[6:7], 12
	s_or_b32 s20, s10, s22
	v_or_b32_e32 v0, s20, v64
	v_mad_u64_u32 v[4:5], s[6:7], v0, s27, v[100:101]
	v_mad_i32_i24 v5, s11, v192, v5
	v_or_b32_e32 v110, s20, v66
	global_load_dwordx4 v[48:51], v[4:5], off offset:1024
	global_load_dwordx4 v[52:55], v[4:5], off offset:1056
	global_load_dwordx4 v[56:59], v[4:5], off offset:1088
	global_load_dwordx4 v[60:63], v[4:5], off offset:1120
	global_load_dwordx4 v[0:3], v[4:5], off offset:2048
	global_load_dwordx4 v[112:115], v[4:5], off offset:2080
	global_load_dwordx4 v[116:119], v[4:5], off offset:2112
	global_load_dwordx4 v[120:123], v[4:5], off offset:2144
	v_mad_u64_u32 v[4:5], s[6:7], v110, s27, v[102:103]
	v_mad_i32_i24 v5, s11, v192, v5
	v_add_co_u32_e32 v6, vcc, s26, v4
	s_movk_i32 s6, 0x3000
	s_nop 0
	v_addc_co_u32_e32 v7, vcc, 0, v5, vcc
	v_add_co_u32_e32 v8, vcc, s6, v4
	s_mov_b32 s6, 0x9000
	s_nop 0
	v_addc_co_u32_e32 v9, vcc, 0, v5, vcc
	v_add_co_u32_e32 v10, vcc, s87, v4
	s_mov_b32 s21, s11
	s_nop 0
	v_addc_co_u32_e32 v11, vcc, 0, v5, vcc
	v_add_co_u32_e32 v12, vcc, s6, v4
	s_mov_b32 s6, 0xa000
	s_nop 0
	v_addc_co_u32_e32 v13, vcc, 0, v5, vcc
	global_load_ushort v19, v[6:7], off offset:3584
	global_load_ushort v16, v[6:7], off offset:3648
	global_load_ushort v21, v[8:9], off
	global_load_ushort v17, v[8:9], off offset:64
	global_load_ushort v22, v[10:11], off offset:512
	global_load_ushort v18, v[10:11], off offset:576
	global_load_ushort v23, v[12:13], off offset:3072
	global_load_ushort v20, v[12:13], off offset:3136
	v_add_co_u32_e32 v6, vcc, s6, v4
	s_mov_b32 s6, 0xc000
	s_nop 0
	v_addc_co_u32_e32 v7, vcc, 0, v5, vcc
	v_add_co_u32_e32 v8, vcc, s6, v4
	s_mov_b32 s6, 0xd000
	s_nop 0
	v_addc_co_u32_e32 v9, vcc, 0, v5, vcc
	v_add_co_u32_e32 v10, vcc, s6, v4
	s_mov_b32 s6, 0x12000
	s_nop 0
	v_addc_co_u32_e32 v11, vcc, 0, v5, vcc
	v_add_co_u32_e32 v12, vcc, s6, v4
	s_mov_b32 s6, 0x13000
	s_nop 0
	v_addc_co_u32_e32 v13, vcc, 0, v5, vcc
	global_load_ushort v27, v[6:7], off offset:3584
	global_load_ushort v24, v[6:7], off offset:3648
	global_load_ushort v28, v[8:9], off
	global_load_ushort v25, v[8:9], off offset:64
	global_load_ushort v29, v[10:11], off offset:512
	global_load_ushort v26, v[10:11], off offset:576
	global_load_ushort v33, v[12:13], off offset:3072
	global_load_ushort v32, v[12:13], off offset:3136
	v_add_co_u32_e32 v6, vcc, s6, v4
	s_mov_b32 s6, 0x15000
	s_nop 0
	v_addc_co_u32_e32 v7, vcc, 0, v5, vcc
	v_add_co_u32_e32 v8, vcc, s6, v4
	s_mov_b32 s6, 0x16000
	s_nop 0
	v_addc_co_u32_e32 v9, vcc, 0, v5, vcc
	v_add_co_u32_e32 v10, vcc, s6, v4
	s_mov_b32 s6, 0x1b000
	s_nop 0
	v_addc_co_u32_e32 v11, vcc, 0, v5, vcc
	v_add_co_u32_e32 v12, vcc, s6, v4
	s_mov_b32 s6, 0x1c000
	s_nop 0
	v_addc_co_u32_e32 v13, vcc, 0, v5, vcc
	global_load_ushort v37, v[6:7], off offset:3584
	global_load_ushort v34, v[6:7], off offset:3648
	global_load_ushort v39, v[8:9], off
	global_load_ushort v35, v[8:9], off offset:64
	global_load_ushort v40, v[10:11], off offset:512
	global_load_ushort v36, v[10:11], off offset:576
	global_load_ushort v41, v[12:13], off offset:3072
	global_load_ushort v38, v[12:13], off offset:3136
	v_add_co_u32_e32 v6, vcc, s6, v4
	s_mov_b32 s6, 0x1e000
	s_nop 0
	v_addc_co_u32_e32 v7, vcc, 0, v5, vcc
	v_add_co_u32_e32 v8, vcc, s6, v4
	s_mov_b32 s6, 0x1f000
	s_nop 0
	v_addc_co_u32_e32 v9, vcc, 0, v5, vcc
	v_add_co_u32_e32 v10, vcc, s6, v4
	v_mov_b32_e32 v111, s11
	s_nop 0
	v_addc_co_u32_e32 v11, vcc, 0, v5, vcc
	global_load_ushort v31, v[4:5], off offset:3072
	global_load_ushort v30, v[4:5], off offset:3136
	global_load_ushort v45, v[6:7], off offset:3584
	global_load_ushort v42, v[6:7], off offset:3648
	global_load_ushort v46, v[8:9], off
	global_load_ushort v43, v[8:9], off offset:64
	global_load_ushort v47, v[10:11], off offset:512
	global_load_ushort v44, v[10:11], off offset:576
	s_waitcnt vmcnt(35)
	v_mfma_f32_32x32x16_bf16 v[0:15], v[0:3], v[48:51], 0
	s_waitcnt vmcnt(34)
	v_mfma_f32_32x32x16_bf16 v[0:15], v[112:115], v[52:55], v[0:15]
	s_waitcnt vmcnt(33)
	v_mfma_f32_32x32x16_bf16 v[0:15], v[116:119], v[56:59], v[0:15]
	s_waitcnt vmcnt(32)
	v_mfma_f32_32x32x16_bf16 v[0:15], v[120:123], v[60:63], v[0:15]
	s_nop 11
	v_mul_f32_e32 v0, 0x3e000000, v0
	v_mul_f32_e64 v79, |v0|, s28
	v_exp_f32_e32 v79, v79
	v_mul_f32_e32 v1, 0x3e000000, v1
	v_mul_f32_e64 v83, |v1|, s28
	v_exp_f32_e32 v83, v83
	v_add_f32_e32 v79, 1.0, v79
	v_mul_f32_e32 v2, 0x3e000000, v2
	v_mul_f32_e32 v3, 0x3e000000, v3
	v_log_f32_e32 v79, v79
	v_max_f32_e32 v81, 0, v0
	v_min_f32_e32 v0, 0, v0
	v_mul_f32_e32 v87, 0x3f317217, v79
	v_fma_f32 v87, v79, s30, -v87
	v_fmac_f32_e32 v87, 0x3377d1cf, v79
	s_nop 1
	v_fma_f32 v79, v79, s30, v87
	v_add_f32_e32 v81, v81, v79
	v_sub_f32_e32 v0, v0, v79
	v_add_f32_e32 v79, 1.0, v83
	v_cndmask_b32_e64 v81, 0, -v81, s[48:49]
	s_nop 0
	v_log_f32_e32 v79, v79
	v_cndmask_b32_e64 v83, v194, v0, s[48:49]
	v_max_f32_e32 v0, 0, v1
	v_min_f32_e32 v1, 0, v1
	v_mul_f32_e32 v85, 0x3f317217, v79
	v_fma_f32 v85, v79, s30, -v85
	v_fmac_f32_e32 v85, 0x3377d1cf, v79
	s_nop 1
	v_fma_f32 v79, v79, s30, v85
	v_mul_f32_e64 v85, |v2|, s28
	v_exp_f32_e32 v85, v85
	v_add_f32_e32 v0, v0, v79
	v_sub_f32_e32 v1, v1, v79
	v_cndmask_b32_e64 v87, 0, -v0, s[50:51]
	v_add_f32_e32 v79, 1.0, v85
	v_max_f32_e32 v0, 0, v2
	v_min_f32_e32 v2, 0, v2
	v_log_f32_e32 v79, v79
	v_cndmask_b32_e64 v85, v194, v1, s[50:51]
	v_mul_f32_e32 v1, 0x3f317217, v79
	v_fma_f32 v1, v79, s30, -v1
	v_fmac_f32_e32 v1, 0x3377d1cf, v79
	s_nop 1
	v_fma_f32 v1, v79, s30, v1
	v_mul_f32_e64 v79, |v3|, s28
	v_exp_f32_e32 v79, v79
	v_add_f32_e32 v0, v0, v1
	v_sub_f32_e32 v1, v2, v1
	v_cndmask_b32_e64 v89, 0, -v0, s[52:53]
	v_add_f32_e32 v2, 1.0, v79
	v_max_f32_e32 v0, 0, v3
	v_min_f32_e32 v3, 0, v3
	v_log_f32_e32 v2, v2
	v_cndmask_b32_e64 v79, v194, v1, s[52:53]
	v_mul_f32_e32 v1, 0x3f317217, v2
	v_fma_f32 v1, v2, s30, -v1
	v_fmac_f32_e32 v1, 0x3377d1cf, v2
	s_nop 1
	v_fma_f32 v1, v2, s30, v1
	v_mul_f32_e32 v2, 0x3e000000, v4
	v_mul_f32_e64 v4, |v2|, s28
	v_exp_f32_e32 v4, v4
	v_add_f32_e32 v0, v0, v1
	v_sub_f32_e32 v1, v3, v1
	v_cndmask_b32_e64 v91, v194, v1, s[54:55]
	v_add_f32_e32 v3, 1.0, v4
	v_cndmask_b32_e64 v93, 0, -v0, s[54:55]
	v_max_f32_e32 v0, 0, v2
	v_log_f32_e32 v3, v3
	v_min_f32_e32 v2, 0, v2
	v_mul_f32_e32 v1, 0x3f317217, v3
	v_fma_f32 v1, v3, s30, -v1
	v_fmac_f32_e32 v1, 0x3377d1cf, v3
	s_nop 1
	v_fma_f32 v1, v3, s30, v1
	v_mul_f32_e32 v3, 0x3e000000, v5
	v_mul_f32_e64 v4, |v3|, s28
	v_exp_f32_e32 v4, v4
	v_add_f32_e32 v0, v0, v1
	v_sub_f32_e32 v1, v2, v1
	v_cndmask_b32_e64 v95, v194, v1, s[56:57]
	v_add_f32_e32 v2, 1.0, v4
	v_cndmask_b32_e64 v5, 0, -v0, s[56:57]
	v_max_f32_e32 v0, 0, v3
	v_log_f32_e32 v2, v2
	v_min_f32_e32 v3, 0, v3
	v_mul_f32_e32 v1, 0x3f317217, v2
	v_fma_f32 v1, v2, s30, -v1
	v_fmac_f32_e32 v1, 0x3377d1cf, v2
	s_nop 1
	v_fma_f32 v1, v2, s30, v1
	v_mul_f32_e32 v2, 0x3e000000, v6
	v_mul_f32_e64 v4, |v2|, s28
	v_exp_f32_e32 v4, v4
	v_add_f32_e32 v0, v0, v1
	v_sub_f32_e32 v1, v3, v1
	v_cndmask_b32_e64 v97, v194, v1, s[58:59]
	v_add_f32_e32 v3, 1.0, v4
	v_cndmask_b32_e64 v112, 0, -v0, s[58:59]
	v_max_f32_e32 v0, 0, v2
	v_log_f32_e32 v3, v3
	v_min_f32_e32 v2, 0, v2
	v_mul_f32_e32 v1, 0x3f317217, v3
	v_fma_f32 v1, v3, s30, -v1
	v_fmac_f32_e32 v1, 0x3377d1cf, v3
	s_nop 1
	v_fma_f32 v1, v3, s30, v1
	v_mul_f32_e32 v3, 0x3e000000, v7
	v_mul_f32_e64 v4, |v3|, s28
	v_exp_f32_e32 v4, v4
	v_add_f32_e32 v0, v0, v1
	v_sub_f32_e32 v1, v2, v1
	v_cndmask_b32_e64 v113, v194, v1, s[60:61]
	v_add_f32_e32 v2, 1.0, v4
	v_cndmask_b32_e64 v114, 0, -v0, s[60:61]
	v_max_f32_e32 v0, 0, v3
	v_log_f32_e32 v2, v2
	v_min_f32_e32 v3, 0, v3
	v_mul_f32_e32 v1, 0x3f317217, v2
	v_fma_f32 v1, v2, s30, -v1
	v_fmac_f32_e32 v1, 0x3377d1cf, v2
	s_nop 1
	v_fma_f32 v1, v2, s30, v1
	v_mul_f32_e32 v2, 0x3e000000, v8
	v_mul_f32_e64 v4, |v2|, s28
	v_exp_f32_e32 v4, v4
	v_add_f32_e32 v0, v0, v1
	v_sub_f32_e32 v1, v3, v1
	v_cndmask_b32_e64 v115, v194, v1, s[62:63]
	v_add_f32_e32 v3, 1.0, v4
	v_cndmask_b32_e64 v116, 0, -v0, s[62:63]
	v_max_f32_e32 v0, 0, v2
	v_log_f32_e32 v3, v3
	v_min_f32_e32 v2, 0, v2
	v_mul_f32_e32 v1, 0x3f317217, v3
	v_fma_f32 v1, v3, s30, -v1
	v_fmac_f32_e32 v1, 0x3377d1cf, v3
	s_nop 1
	v_fma_f32 v1, v3, s30, v1
	v_mul_f32_e32 v3, 0x3e000000, v9
	v_mul_f32_e64 v4, |v3|, s28
	v_exp_f32_e32 v4, v4
	v_add_f32_e32 v0, v0, v1
	v_sub_f32_e32 v1, v2, v1
	v_cndmask_b32_e64 v117, v194, v1, s[64:65]
	v_add_f32_e32 v2, 1.0, v4
	v_cmp_gt_f32_e32 vcc, s29, v2
	s_nop 1
	v_cndmask_b32_e64 v4, 0, 32, vcc
	v_ldexp_f32 v2, v2, v4
	v_log_f32_e32 v4, v2
	v_cndmask_b32_e64 v2, 0, -v0, s[64:65]
	v_max_f32_e32 v0, 0, v3
	v_min_f32_e32 v3, 0, v3
	v_mul_f32_e32 v1, 0x3f317217, v4
	v_fma_f32 v1, v4, s30, -v1
	v_fmac_f32_e32 v1, 0x3377d1cf, v4
	v_fmac_f32_e32 v1, 0x3f317217, v4
	v_cmp_lt_f32_e64 s[6:7], |v4|, s31
	s_nop 1
	v_cndmask_b32_e64 v1, v4, v1, s[6:7]
	v_cndmask_b32_e32 v4, 0, v193, vcc
	v_sub_f32_e32 v1, v1, v4
	v_mul_f32_e32 v4, 0x3e000000, v10
	v_mul_f32_e64 v6, |v4|, s28
	v_exp_f32_e32 v6, v6
	v_add_f32_e32 v0, v0, v1
	v_sub_f32_e32 v1, v3, v1
	v_cndmask_b32_e64 v118, v194, v1, s[66:67]
	v_add_f32_e32 v3, 1.0, v6
	v_max_f32_e32 v1, 0, v4
	v_min_f32_e32 v4, 0, v4
	v_log_f32_e32 v3, v3
	v_cndmask_b32_e64 v0, 0, -v0, s[66:67]
	v_mul_f32_e32 v6, 0x3f317217, v3
	v_fma_f32 v6, v3, s30, -v6
	v_fmac_f32_e32 v6, 0x3377d1cf, v3
	s_nop 1
	v_fma_f32 v3, v3, s30, v6
	v_mul_f32_e32 v6, 0x3e000000, v11
	v_mul_f32_e64 v7, |v6|, s28
	v_exp_f32_e32 v7, v7
	v_add_f32_e32 v1, v1, v3
	v_sub_f32_e32 v3, v4, v3
	v_cndmask_b32_e64 v119, v194, v3, s[68:69]
	v_add_f32_e32 v4, 1.0, v7
	v_cndmask_b32_e64 v122, 0, -v1, s[68:69]
	v_max_f32_e32 v1, 0, v6
	v_log_f32_e32 v4, v4
	v_min_f32_e32 v6, 0, v6
	v_mul_f32_e32 v3, 0x3f317217, v4
	v_fma_f32 v3, v4, s30, -v3
	v_fmac_f32_e32 v3, 0x3377d1cf, v4
	s_nop 1
	v_fma_f32 v3, v4, s30, v3
	v_mul_f32_e32 v4, 0x3e000000, v12
	v_mul_f32_e64 v7, |v4|, s28
	v_exp_f32_e32 v7, v7
	v_add_f32_e32 v1, v1, v3
	v_sub_f32_e32 v3, v6, v3
	v_cndmask_b32_e64 v12, v194, v3, s[70:71]
	v_add_f32_e32 v6, 1.0, v7
	v_cndmask_b32_e64 v123, 0, -v1, s[70:71]
	v_max_f32_e32 v1, 0, v4
	v_log_f32_e32 v6, v6
	v_min_f32_e32 v4, 0, v4
	v_mul_f32_e32 v3, 0x3f317217, v6
	v_fma_f32 v3, v6, s30, -v3
	v_fmac_f32_e32 v3, 0x3377d1cf, v6
	s_nop 1
	v_fma_f32 v3, v6, s30, v3
	v_mul_f32_e32 v6, 0x3e000000, v13
	v_mul_f32_e64 v7, |v6|, s28
	v_exp_f32_e32 v7, v7
	v_add_f32_e32 v1, v1, v3
	v_sub_f32_e32 v3, v4, v3
	v_cndmask_b32_e64 v13, v194, v3, s[72:73]
	v_add_f32_e32 v4, 1.0, v7
	v_max_f32_e32 v3, 0, v6
	v_min_f32_e32 v6, 0, v6
	v_log_f32_e32 v4, v4
	v_cndmask_b32_e64 v1, 0, -v1, s[72:73]
	v_mul_f32_e32 v7, 0x3f317217, v4
	v_fma_f32 v7, v4, s30, -v7
	v_fmac_f32_e32 v7, 0x3377d1cf, v4
	s_nop 1
	v_fma_f32 v4, v4, s30, v7
	v_mul_f32_e32 v7, 0x3e000000, v14
	v_mul_f32_e64 v8, |v7|, s28
	v_exp_f32_e32 v8, v8
	v_add_f32_e32 v3, v3, v4
	v_sub_f32_e32 v4, v6, v4
	v_cndmask_b32_e64 v14, v194, v4, s[74:75]
	v_add_f32_e32 v6, 1.0, v8
	v_cndmask_b32_e64 v124, 0, -v3, s[74:75]
	v_max_f32_e32 v3, 0, v7
	v_log_f32_e32 v6, v6
	v_min_f32_e32 v7, 0, v7
	v_mul_f32_e32 v4, 0x3f317217, v6
	v_fma_f32 v4, v6, s30, -v4
	v_fmac_f32_e32 v4, 0x3377d1cf, v6
	s_nop 1
	v_fma_f32 v4, v6, s30, v4
	v_mul_f32_e32 v6, 0x3e000000, v15
	v_mul_f32_e64 v8, |v6|, s28
	v_exp_f32_e32 v8, v8
	v_add_f32_e32 v3, v3, v4
	v_sub_f32_e32 v4, v7, v4
	v_cndmask_b32_e64 v15, v194, v4, s[76:77]
	v_add_f32_e32 v7, 1.0, v8
	v_cndmask_b32_e64 v125, 0, -v3, s[76:77]
	v_max_f32_e32 v3, 0, v6
	v_log_f32_e32 v7, v7
	v_min_f32_e32 v6, 0, v6
	v_mul_f32_e32 v4, 0x3f317217, v7
	v_fma_f32 v4, v7, s30, -v4
	v_fmac_f32_e32 v4, 0x3377d1cf, v7
	s_nop 1
	v_fma_f32 v4, v7, s30, v4
	v_add_f32_e32 v3, v3, v4
	v_sub_f32_e32 v4, v6, v4
	v_cndmask_b32_e64 v126, v194, v4, s[78:79]
	v_cndmask_b32_e64 v127, 0, -v3, s[78:79]
	v_add_f32_e32 v3, v81, v87
	v_add_f32_e32 v4, v89, v93
	v_add_f32_e32 v4, v3, v4
	v_add_f32_e32 v3, v1, v124
	v_add_f32_e32 v1, v125, v127
	v_pk_add_f32 v[2:3], v[2:3], v[0:1]
	ds_bpermute_b32 v7, v184, v3
	v_add_f32_e32 v6, v122, v123
	v_add_f32_e32 v1, v5, v112
	v_add_f32_e32 v5, v114, v116
	ds_bpermute_b32 v8, v184, v4
	s_waitcnt lgkmcnt(0)
	v_pk_add_f32 v[2:3], v[2:3], v[6:7]
	ds_bpermute_b32 v144, v184, v2
	v_add_f32_e32 v6, v1, v5
	ds_bpermute_b32 v10, v184, v6
	v_add_f32_e32 v1, 0, v7
	v_cndmask_b32_e64 v1, 0, v1, s[42:43]
	s_waitcnt lgkmcnt(0)
	v_pk_add_f32 v[2:3], v[2:3], v[144:145]
	v_cndmask_b32_e64 v5, 0, v144, s[42:43]
	v_mov_b32_e32 v7, v2
	v_mov_b32_e32 v11, v3
	v_add_f32_e32 v81, v5, v3
	s_waitcnt lgkmcnt(0)
	v_cndmask_b32_e64 v5, 0, v10, s[42:43]
	v_pk_add_f32 v[2:3], v[6:7], v[10:11]
	v_cndmask_b32_e64 v7, 0, v8, s[42:43]
	v_add_f32_e32 v6, v5, v3
	v_mov_b32_e32 v5, v2
	v_mov_b32_e32 v9, v3
	v_pk_add_f32 v[120:121], v[4:5], v[8:9]
	v_add_f32_e32 v10, v12, v81
	v_add_f32_e32 v2, v7, v121
	v_add_f32_e32 v3, v91, v2
	v_add_f32_e32 v2, v93, v2
	v_mul_f32_e32 v10, 0x3fb8aa3b, v10
	v_add_f32_e32 v4, v79, v2
	v_exp_f32_e32 v79, v10
	v_add_f32_e32 v10, v123, v81
	v_add_f32_e32 v11, v119, v10
	v_add_f32_e32 v10, v122, v10
	v_add_f32_e32 v0, v0, v10
	v_add_f32_e32 v0, v117, v0
	v_add_f32_e32 v2, v89, v2
	v_add_f32_e32 v7, v115, v6
	v_add_f32_e32 v6, v116, v6
	v_mul_f32_e32 v0, 0x3fb8aa3b, v0
	v_add_f32_e32 v5, v85, v2
	v_add_f32_e32 v8, v113, v6
	v_add_f32_e32 v6, v114, v6
	v_exp_f32_e32 v85, v0
	v_add_f32_e32 v0, v126, v1
	v_add_f32_e32 v2, v87, v2
	v_add_f32_e32 v9, v97, v6
	v_add_f32_e32 v6, v112, v6
	v_mul_f32_e32 v0, 0x3fb8aa3b, v0
	v_add_f32_e32 v2, v83, v2
	v_add_f32_e32 v6, v95, v6
	v_exp_f32_e32 v87, v0
	v_add_f32_e32 v0, v127, v1
	v_mul_f32_e32 v3, 0x3fb8aa3b, v3
	v_mul_f32_e32 v4, 0x3fb8aa3b, v4
	v_mul_f32_e32 v5, 0x3fb8aa3b, v5
	v_mul_f32_e32 v2, 0x3fb8aa3b, v2
	v_mul_f32_e32 v7, 0x3fb8aa3b, v7
	v_mul_f32_e32 v8, 0x3fb8aa3b, v8
	v_mul_f32_e32 v9, 0x3fb8aa3b, v9
	v_mul_f32_e32 v6, 0x3fb8aa3b, v6
	v_add_f32_e32 v1, v15, v0
	v_exp_f32_e32 v3, v3
	v_exp_f32_e32 v4, v4
	v_exp_f32_e32 v5, v5
	v_exp_f32_e32 v2, v2
	v_exp_f32_e32 v7, v7
	v_exp_f32_e32 v8, v8
	v_exp_f32_e32 v9, v9
	v_exp_f32_e32 v6, v6
	v_mul_f32_e32 v1, 0x3fb8aa3b, v1
	v_add_f32_e32 v0, v125, v0
	v_mul_f32_e32 v11, 0x3fb8aa3b, v11
	v_exp_f32_e32 v89, v1
	v_add_f32_e32 v1, v14, v0
	v_add_f32_e32 v0, v124, v0
	v_exp_f32_e32 v81, v11
	v_add_f32_e32 v11, v118, v10
	v_add_f32_e32 v0, v13, v0
	v_mul_f32_e32 v11, 0x3fb8aa3b, v11
	v_mul_f32_e32 v1, 0x3fb8aa3b, v1
	v_mul_f32_e32 v0, 0x3fb8aa3b, v0
	v_exp_f32_e32 v83, v11
	v_exp_f32_e32 v91, v1
	v_exp_f32_e32 v93, v0
	v_cvt_pk_bf16_f32 v113, v4, v3
	v_cvt_pk_bf16_f32 v112, v2, v5
	v_cvt_pk_bf16_f32 v115, v8, v7
	v_cvt_pk_bf16_f32 v114, v6, v9
	s_waitcnt vmcnt(19)
	v_perm_b32 v3, v29, v28, s38
	v_perm_b32 v2, v27, v23, s38
	v_perm_b32 v1, v22, v21, s38
	s_waitcnt vmcnt(7)
	v_perm_b32 v0, v19, v31, s38
	v_perm_b32 v21, v26, v25, s38
	v_perm_b32 v20, v24, v20, s38
	v_perm_b32 v19, v18, v17, s38
	s_waitcnt vmcnt(6)
	v_perm_b32 v18, v16, v30, s38
	v_mfma_f32_32x32x16_bf16 v[0:15], v[112:115], v[0:3], 0
	s_waitcnt vmcnt(1)
	v_perm_b32 v119, v47, v46, s38
	v_perm_b32 v118, v45, v41, s38
	v_perm_b32 v117, v40, v39, s38
	v_perm_b32 v116, v37, v33, s38
	s_waitcnt vmcnt(0)
	v_perm_b32 v39, v44, v43, s38
	v_perm_b32 v38, v42, v38, s38
	v_perm_b32 v37, v36, v35, s38
	v_mfma_f32_32x32x16_bf16 v[16:31], v[112:115], v[18:21], 0
	v_cvt_pk_bf16_f32 v113, v81, v79
	v_cvt_pk_bf16_f32 v112, v85, v83
	v_cvt_pk_bf16_f32 v115, v89, v87
	v_cvt_pk_bf16_f32 v114, v93, v91
	v_perm_b32 v36, v34, v32, s38
	v_add_f32_e32 v95, v120, v121
	v_mfma_f32_32x32x16_bf16 v[0:15], v[112:115], v[116:119], v[0:15]
	v_mfma_f32_32x32x16_bf16 v[16:31], v[112:115], v[36:39], v[16:31]
	v_cmp_gt_f32_e32 vcc, s34, v95
	s_cmp_eq_u64 vcc, exec
	s_cselect_b64 s[6:7], -1, 0
	s_cmp_eq_u32 s22, 0
	s_cselect_b64 s[24:25], -1, 0
	s_or_b64 s[6:7], s[24:25], s[6:7]
	s_and_b64 vcc, exec, s[6:7]
	s_cbranch_vccnz .LBB0_256
	s_and_b32 s6, s14, 0xfe0
	s_sub_i32 s6, s6, 32
	s_add_u32 s6, s6, s10
	s_addc_u32 s7, 0, s11
	v_lshl_add_u64 v[32:33], s[6:7], 0, v[66:67]
	v_mad_u64_u32 v[112:113], s[10:11], v32, s27, v[106:107]
	v_mad_i32_i24 v113, v33, s27, v113
	v_lshl_add_u64 v[32:33], s[6:7], 0, v[64:65]
	v_mad_u64_u32 v[114:115], s[6:7], v32, s27, v[108:109]
	s_mov_b32 s24, 0xfffdc000
	v_mad_i32_i24 v115, v33, s27, v115
	s_mov_b32 s25, -1
.LBB0_255:
	v_lshl_add_u64 v[36:37], v[114:115], 0, v[98:99]
	global_load_dwordx4 v[32:35], v[36:37], off offset:-64
	global_load_dwordx4 v[116:119], v[36:37], off offset:-32
	global_load_dwordx4 v[120:123], v[36:37], off
	global_load_dwordx4 v[124:127], v[36:37], off offset:32
	v_lshl_add_u64 v[36:37], v[112:113], 0, v[98:99]
	v_add_co_u32_e32 v38, vcc, 0x8640000, v36
	s_sub_i32 s10, s22, 32
	s_nop 0
	v_addc_co_u32_e32 v39, vcc, 0, v37, vcc
	v_add_co_u32_e32 v40, vcc, 0x8641000, v36
	s_nop 1
	v_addc_co_u32_e32 v41, vcc, 0, v37, vcc
	v_add_co_u32_e32 v42, vcc, 0x8643000, v36
	s_nop 1
	v_addc_co_u32_e32 v43, vcc, 0, v37, vcc
	v_add_co_u32_e32 v44, vcc, 0x8644000, v36
	s_nop 1
	v_addc_co_u32_e32 v45, vcc, 0, v37, vcc
	global_load_ushort v85, v[38:39], off offset:3072
	global_load_ushort v79, v[38:39], off offset:3136
	global_load_ushort v89, v[40:41], off offset:3584
	global_load_ushort v81, v[40:41], off offset:3648
	global_load_ushort v91, v[42:43], off
	global_load_ushort v83, v[42:43], off offset:64
	global_load_ushort v93, v[44:45], off offset:512
	global_load_ushort v87, v[44:45], off offset:576
	v_add_co_u32_e32 v38, vcc, 0x8649000, v36
	s_nop 1
	v_addc_co_u32_e32 v39, vcc, 0, v37, vcc
	v_add_co_u32_e32 v40, vcc, 0x864a000, v36
	s_nop 1
	v_addc_co_u32_e32 v41, vcc, 0, v37, vcc
	v_add_co_u32_e32 v42, vcc, 0x864c000, v36
	s_nop 1
	v_addc_co_u32_e32 v43, vcc, 0, v37, vcc
	v_add_co_u32_e32 v44, vcc, 0x864d000, v36
	s_nop 1
	v_addc_co_u32_e32 v45, vcc, 0, v37, vcc
	global_load_ushort v139, v[38:39], off offset:3072
	global_load_ushort v97, v[38:39], off offset:3136
	global_load_ushort v142, v[40:41], off offset:3584
	global_load_ushort v136, v[40:41], off offset:3648
	global_load_ushort v144, v[42:43], off
	global_load_ushort v137, v[42:43], off offset:64
	global_load_ushort v154, v[44:45], off offset:512
	global_load_ushort v140, v[44:45], off offset:576
	v_add_co_u32_e32 v38, vcc, 0x8652000, v36
	s_nop 1
	v_addc_co_u32_e32 v39, vcc, 0, v37, vcc
	v_add_co_u32_e32 v40, vcc, 0x8653000, v36
	s_nop 1
	v_addc_co_u32_e32 v41, vcc, 0, v37, vcc
	v_add_co_u32_e32 v42, vcc, 0x8655000, v36
	s_nop 1
	v_addc_co_u32_e32 v43, vcc, 0, v37, vcc
	v_add_co_u32_e32 v44, vcc, 0x8656000, v36
	s_nop 1
	v_addc_co_u32_e32 v45, vcc, 0, v37, vcc
	global_load_ushort v152, v[38:39], off offset:3072
	global_load_ushort v138, v[38:39], off offset:3136
	global_load_ushort v155, v[40:41], off offset:3584
	global_load_ushort v141, v[40:41], off offset:3648
	global_load_ushort v156, v[42:43], off
	global_load_ushort v143, v[42:43], off offset:64
	global_load_ushort v157, v[44:45], off offset:512
	global_load_ushort v153, v[44:45], off offset:576
	v_add_co_u32_e32 v38, vcc, 0x865b000, v36
	s_nop 1
	v_addc_co_u32_e32 v39, vcc, 0, v37, vcc
	v_add_co_u32_e32 v40, vcc, 0x865c000, v36
	s_nop 1
	v_addc_co_u32_e32 v41, vcc, 0, v37, vcc
	v_add_co_u32_e32 v42, vcc, 0x865e000, v36
	s_nop 1
	v_addc_co_u32_e32 v43, vcc, 0, v37, vcc
	v_add_co_u32_e32 v36, vcc, 0x865f000, v36
	s_nop 1
	v_addc_co_u32_e32 v37, vcc, 0, v37, vcc
	global_load_ushort v161, v[38:39], off offset:3072
	global_load_ushort v158, v[38:39], off offset:3136
	global_load_ushort v163, v[40:41], off offset:3584
	global_load_ushort v159, v[40:41], off offset:3648
	global_load_ushort v164, v[42:43], off
	global_load_ushort v160, v[42:43], off offset:64
	global_load_ushort v165, v[36:37], off offset:512
	global_load_ushort v162, v[36:37], off offset:576
	s_waitcnt vmcnt(35)
	v_mfma_f32_32x32x16_bf16 v[32:47], v[32:35], v[48:51], 0
	s_waitcnt vmcnt(34)
	v_mfma_f32_32x32x16_bf16 v[32:47], v[116:119], v[52:55], v[32:47]
	s_waitcnt vmcnt(33)
	v_mfma_f32_32x32x16_bf16 v[32:47], v[120:123], v[56:59], v[32:47]
	s_waitcnt vmcnt(32)
	v_mfma_f32_32x32x16_bf16 v[32:47], v[124:127], v[60:63], v[32:47]
	s_nop 11
	v_mul_f32_e32 v117, 0x3e000000, v32
	v_mul_f32_e64 v32, |v117|, s28
	v_exp_f32_e32 v32, v32
	v_mul_f32_e32 v33, 0x3e000000, v33
	v_mul_f32_e32 v121, 0x3e000000, v34
	v_mul_f32_e64 v34, |v121|, s28
	v_add_f32_e32 v32, 1.0, v32
	v_exp_f32_e32 v34, v34
	v_max_f32_e32 v122, 0, v117
	v_log_f32_e32 v32, v32
	v_mul_f32_e64 v116, |v33|, s28
	v_exp_f32_e32 v116, v116
	v_mul_f32_e32 v119, 0x3f317217, v32
	v_fma_f32 v119, v32, s30, -v119
	v_fmac_f32_e32 v119, 0x3377d1cf, v32
	v_add_f32_e32 v116, 1.0, v116
	v_add_f32_e32 v34, 1.0, v34
	v_fma_f32 v32, v32, s30, v119
	v_cmp_gt_f32_e32 vcc, s29, v116
	v_max_f32_e32 v124, 0, v33
	s_nop 0
	v_cndmask_b32_e64 v119, 0, 32, vcc
	v_ldexp_f32 v116, v116, v119
	v_log_f32_e32 v119, v116
	v_min_f32_e32 v116, 0, v117
	v_cndmask_b32_e32 v118, 0, v193, vcc
	v_cmp_gt_f32_e32 vcc, s29, v34
	v_mul_f32_e32 v117, 0x3f317217, v119
	v_fma_f32 v117, v119, s30, -v117
	v_fmac_f32_e32 v117, 0x3377d1cf, v119
	v_fmac_f32_e32 v117, 0x3f317217, v119
	v_cmp_lt_f32_e64 s[6:7], |v119|, s31
	v_mul_f32_e32 v36, 0x3e000000, v36
	v_max_f32_e32 v123, 0, v121
	v_cndmask_b32_e64 v117, v119, v117, s[6:7]
	v_cndmask_b32_e64 v119, 0, 32, vcc
	v_ldexp_f32 v34, v34, v119
	v_log_f32_e32 v119, v34
	v_sub_f32_e32 v34, v117, v118
	v_mul_f32_e32 v117, 0x3e000000, v35
	v_mul_f32_e64 v35, |v117|, s28
	v_exp_f32_e32 v35, v35
	v_min_f32_e32 v118, 0, v33
	v_mul_f32_e32 v33, 0x3f317217, v119
	v_fma_f32 v33, v119, s30, -v33
	v_fmac_f32_e32 v33, 0x3377d1cf, v119
	v_fmac_f32_e32 v33, 0x3f317217, v119
	v_cmp_lt_f32_e64 s[6:7], |v119|, s31
	v_add_f32_e32 v35, 1.0, v35
	v_max_f32_e32 v125, 0, v117
	v_cndmask_b32_e64 v33, v119, v33, s[6:7]
	v_cndmask_b32_e32 v119, 0, v193, vcc
	v_sub_f32_e32 v33, v33, v119
	v_mul_f32_e32 v37, 0x3e000000, v37
	v_log_f32_e32 v35, v35
	v_min_f32_e32 v120, 0, v121
	v_mul_f32_e64 v121, |v36|, s28
	v_exp_f32_e32 v121, v121
	v_mul_f32_e32 v119, 0x3f317217, v35
	v_fma_f32 v119, v35, s30, -v119
	v_fmac_f32_e32 v119, 0x3377d1cf, v35
	v_mul_f32_e32 v39, 0x3e000000, v39
	v_mul_f32_e32 v41, 0x3e000000, v41
	v_fma_f32 v35, v35, s30, v119
	v_add_f32_e32 v119, 1.0, v121
	v_min_f32_e32 v132, 0, v41
	v_max_f32_e32 v168, 0, v41
	v_log_f32_e32 v119, v119
	v_min_f32_e32 v121, 0, v117
	v_sub_f32_e32 v131, v121, v35
	v_mul_f32_e32 v117, 0x3f317217, v119
	v_fma_f32 v117, v119, s30, -v117
	v_fmac_f32_e32 v117, 0x3377d1cf, v119
	v_mul_f32_e32 v45, 0x3e000000, v45
	v_min_f32_e32 v176, 0, v45
	v_fma_f32 v117, v119, s30, v117
	v_mul_f32_e64 v119, |v37|, s28
	v_exp_f32_e32 v119, v119
	v_min_f32_e32 v121, 0, v36
	v_sub_f32_e32 v133, v121, v117
	v_add_f32_e32 v119, 1.0, v119
	v_mul_f32_e32 v121, 0x3e000000, v38
	v_mul_f32_e64 v38, |v121|, s28
	v_log_f32_e32 v119, v119
	v_max_f32_e32 v36, 0, v36
	v_exp_f32_e32 v38, v38
	v_add_f32_e32 v117, v36, v117
	v_mul_f32_e32 v36, 0x3f317217, v119
	v_fma_f32 v36, v119, s30, -v36
	v_fmac_f32_e32 v36, 0x3377d1cf, v119
	v_add_f32_e32 v38, 1.0, v38
	v_mul_f32_e64 v126, |v39|, s28
	v_fma_f32 v36, v119, s30, v36
	v_cmp_gt_f32_e32 vcc, s29, v38
	v_exp_f32_e32 v127, v126
	s_nop 0
	v_cndmask_b32_e64 v119, 0, 32, vcc
	v_ldexp_f32 v38, v38, v119
	v_log_f32_e32 v119, v38
	v_min_f32_e32 v38, 0, v37
	v_max_f32_e32 v37, 0, v37
	v_add_f32_e32 v171, v37, v36
	v_mul_f32_e32 v37, 0x3f317217, v119
	v_fma_f32 v37, v119, s30, -v37
	v_fmac_f32_e32 v37, 0x3377d1cf, v119
	v_fmac_f32_e32 v37, 0x3f317217, v119
	v_cmp_lt_f32_e64 s[6:7], |v119|, s31
	v_min_f32_e32 v128, 0, v121
	v_max_f32_e32 v178, 0, v45
	v_cndmask_b32_e64 v37, v119, v37, s[6:7]
	v_cndmask_b32_e32 v119, 0, v193, vcc
	v_sub_f32_e32 v126, v37, v119
	v_add_f32_e32 v37, 1.0, v127
	v_cmp_gt_f32_e32 vcc, s29, v37
	v_pk_add_f32 v[124:125], v[124:125], v[34:35]
	v_sub_f32_e64 v206, -v171, v117
	v_cndmask_b32_e64 v119, 0, 32, vcc
	v_ldexp_f32 v37, v37, v119
	v_log_f32_e32 v119, v37
	v_max_f32_e32 v37, 0, v121
	v_cndmask_b32_e32 v127, 0, v193, vcc
	v_add_f32_e32 v37, v37, v126
	v_mul_f32_e32 v121, 0x3f317217, v119
	v_fma_f32 v121, v119, s30, -v121
	v_fmac_f32_e32 v121, 0x3377d1cf, v119
	v_fmac_f32_e32 v121, 0x3f317217, v119
	v_cmp_lt_f32_e64 s[6:7], |v119|, s31
	v_pk_add_f32 v[122:123], v[122:123], v[32:33]
	s_nop 0
	v_cndmask_b32_e64 v119, v119, v121, s[6:7]
	v_mul_f32_e32 v121, 0x3e000000, v40
	v_mul_f32_e64 v40, |v121|, s28
	v_exp_f32_e32 v40, v40
	v_sub_f32_e32 v119, v119, v127
	v_min_f32_e32 v127, 0, v39
	v_max_f32_e32 v39, 0, v39
	v_add_f32_e32 v40, 1.0, v40
	v_sub_f32_e32 v174, v127, v119
	v_add_f32_e32 v127, v39, v119
	v_log_f32_e32 v40, v40
	v_mul_f32_e64 v119, |v41|, s28
	v_exp_f32_e32 v119, v119
	v_min_f32_e32 v130, 0, v121
	v_mul_f32_e32 v39, 0x3f317217, v40
	v_fma_f32 v39, v40, s30, -v39
	v_fmac_f32_e32 v39, 0x3377d1cf, v40
	v_add_f32_e32 v119, 1.0, v119
	v_max_f32_e32 v166, 0, v121
	v_fma_f32 v39, v40, s30, v39
	v_mul_f32_e32 v121, 0x3e000000, v42
	v_mul_f32_e64 v42, |v121|, s28
	v_log_f32_e32 v119, v119
	v_exp_f32_e32 v42, v42
	v_mov_b32_e32 v40, v39
	v_min_f32_e32 v134, 0, v121
	v_mul_f32_e32 v39, 0x3f317217, v119
	v_fma_f32 v39, v119, s30, -v39
	v_fmac_f32_e32 v39, 0x3377d1cf, v119
	v_add_f32_e32 v42, 1.0, v42
	v_max_f32_e32 v167, 0, v121
	v_fma_f32 v39, v119, s30, v39
	v_cmp_gt_f32_e32 vcc, s29, v42
	v_mul_f32_e32 v121, 0x3e000000, v44
	v_min_f32_e32 v170, 0, v121
	v_cndmask_b32_e64 v129, 0, 32, vcc
	v_ldexp_f32 v42, v42, v129
	v_log_f32_e32 v129, v42
	v_mov_b32_e32 v42, v39
	v_mul_f32_e32 v119, 0x3e000000, v43
	v_mul_f32_e64 v41, |v119|, s28
	v_exp_f32_e32 v41, v41
	v_mul_f32_e32 v39, 0x3f317217, v129
	v_fma_f32 v39, v129, s30, -v39
	v_fmac_f32_e32 v39, 0x3377d1cf, v129
	v_add_f32_e32 v41, 1.0, v41
	v_fmac_f32_e32 v39, 0x3f317217, v129
	v_cmp_lt_f32_e64 s[6:7], |v129|, s31
	v_cndmask_b32_e32 v43, 0, v193, vcc
	v_cmp_gt_f32_e32 vcc, s29, v41
	v_cndmask_b32_e64 v39, v129, v39, s[6:7]
	v_max_f32_e32 v169, 0, v119
	v_cndmask_b32_e64 v129, 0, 32, vcc
	v_ldexp_f32 v41, v41, v129
	v_log_f32_e32 v129, v41
	v_sub_f32_e32 v41, v39, v43
	v_mul_f32_e64 v43, |v121|, s28
	v_exp_f32_e32 v44, v43
	v_mul_f32_e32 v39, 0x3f317217, v129
	v_fma_f32 v39, v129, s30, -v39
	v_fmac_f32_e32 v39, 0x3377d1cf, v129
	v_fmac_f32_e32 v39, 0x3f317217, v129
	v_cmp_lt_f32_e64 s[6:7], |v129|, s31
	v_cndmask_b32_e32 v43, 0, v193, vcc
	v_max_f32_e32 v172, 0, v121
	v_cndmask_b32_e64 v39, v129, v39, s[6:7]
	v_sub_f32_e32 v43, v39, v43
	v_add_f32_e32 v39, 1.0, v44
	v_mul_f32_e32 v121, 0x3e000000, v46
	v_mul_f32_e64 v46, |v121|, s28
	v_log_f32_e32 v39, v39
	v_min_f32_e32 v44, 0, v119
	v_mul_f32_e64 v119, |v45|, s28
	v_exp_f32_e32 v119, v119
	v_sub_f32_e32 v177, v44, v43
	v_mul_f32_e32 v44, 0x3f317217, v39
	v_fma_f32 v44, v39, s30, -v44
	v_fmac_f32_e32 v44, 0x3377d1cf, v39
	v_add_f32_e32 v119, 1.0, v119
	v_exp_f32_e32 v46, v46
	v_fma_f32 v39, v39, s30, v44
	v_mov_b32_e32 v44, v39
	v_add_f32_e32 v46, 1.0, v46
	v_log_f32_e32 v119, v119
	v_pk_add_f32 v[166:167], v[166:167], v[40:41]
	v_pk_add_f32 v[168:169], v[168:169], v[42:43]
	v_max_f32_e32 v173, 0, v121
	v_mul_f32_e32 v39, 0x3f317217, v119
	v_fma_f32 v39, v119, s30, -v39
	v_fmac_f32_e32 v39, 0x3377d1cf, v119
	v_pk_add_f32 v[208:209], v[168:169], v[166:167] neg_lo:[1,1] neg_hi:[1,1]
	v_sub_f32_e64 v210, -v127, v37
	v_fma_f32 v39, v119, s30, v39
	v_cmp_gt_f32_e32 vcc, s29, v46
	v_pk_add_f32 v[208:209], v[208:209], v[208:209] op_sel:[0,1] op_sel_hi:[1,0]
	ds_bpermute_b32 v211, v184, v208
	v_cndmask_b32_e64 v129, 0, 32, vcc
	v_ldexp_f32 v46, v46, v129
	v_log_f32_e32 v129, v46
	v_mov_b32_e32 v46, v39
	v_mul_f32_e32 v119, 0x3e000000, v47
	v_mul_f32_e64 v45, |v119|, s28
	v_exp_f32_e32 v45, v45
	v_mul_f32_e32 v39, 0x3f317217, v129
	v_fma_f32 v39, v129, s30, -v39
	v_fmac_f32_e32 v39, 0x3377d1cf, v129
	v_add_f32_e32 v45, 1.0, v45
	v_fmac_f32_e32 v39, 0x3f317217, v129
	v_cmp_lt_f32_e64 s[6:7], |v129|, s31
	v_cndmask_b32_e32 v47, 0, v193, vcc
	v_cmp_gt_f32_e32 vcc, s29, v45
	v_cndmask_b32_e64 v39, v129, v39, s[6:7]
	v_max_f32_e32 v179, 0, v119
	v_cndmask_b32_e64 v129, 0, 32, vcc
	v_ldexp_f32 v45, v45, v129
	v_log_f32_e32 v129, v45
	v_sub_f32_e32 v45, v39, v47
	v_cndmask_b32_e32 v47, 0, v193, vcc
	v_pk_add_f32 v[172:173], v[172:173], v[44:45]
	v_mul_f32_e32 v39, 0x3f317217, v129
	v_fma_f32 v39, v129, s30, -v39
	v_fmac_f32_e32 v39, 0x3377d1cf, v129
	v_fmac_f32_e32 v39, 0x3f317217, v129
	v_cmp_lt_f32_e64 s[6:7], |v129|, s31
	v_mov_b32_e32 v207, v208
	s_waitcnt lgkmcnt(0)
	v_pk_add_f32 v[206:207], v[206:207], v[210:211]
	v_cndmask_b32_e64 v39, v129, v39, s[6:7]
	v_sub_f32_e32 v47, v39, v47
	v_pk_add_f32 v[178:179], v[178:179], v[46:47]
	v_min_f32_e32 v39, 0, v119
	v_pk_add_f32 v[212:213], v[178:179], v[172:173] neg_lo:[1,1] neg_hi:[1,1]
	v_sub_f32_e32 v190, v39, v47
	v_add_f32_e32 v35, v212, v213
	ds_bpermute_b32 v39, v184, v35
	ds_bpermute_b32 v208, v184, v206
	v_pk_add_f32 v[182:183], v[124:125], v[122:123] neg_lo:[1,1] neg_hi:[1,1]
	v_min_f32_e32 v180, 0, v121
	v_mov_b32_e32 v212, v182
	s_waitcnt lgkmcnt(0)
	v_add_f32_e32 v35, v35, v39
	v_add_f32_e32 v209, v95, v35
	s_waitcnt lgkmcnt(0)
	v_pk_add_f32 v[206:207], v[206:207], v[208:209]
	v_cndmask_b32_e64 v43, 0, v39, s[42:43]
	v_mov_b32_e32 v213, v206
	v_mov_b32_e32 v206, v183
	v_pk_add_f32 v[182:183], v[212:213], v[206:207]
	v_add_f32_e32 v181, v95, v43
	ds_bpermute_b32 v95, v184, v182
	v_cndmask_b32_e64 v35, 0, v211, s[42:43]
	v_add_f32_e32 v135, v35, v209
	v_cndmask_b32_e64 v35, 0, v208, s[42:43]
	v_add_f32_e32 v129, v35, v207
	s_waitcnt lgkmcnt(0)
	v_cndmask_b32_e64 v35, 0, v95, s[42:43]
	v_add_f32_e32 v121, v35, v183
	v_add_f32_e32 v35, v131, v121
	v_mov_b32_e32 v206, v33
	v_mov_b32_e32 v207, v125
	v_mul_f32_e32 v35, 0x3fb8aa3b, v35
	v_pk_add_f32 v[120:121], v[120:121], v[206:207] neg_lo:[0,1] neg_hi:[0,1]
	v_exp_f32_e32 v122, v35
	v_add_f32_e32 v33, v120, v121
	v_mov_b32_e32 v119, v121
	v_mov_b32_e32 v35, v123
	v_mul_f32_e32 v33, 0x3fb8aa3b, v33
	v_pk_add_f32 v[34:35], v[118:119], v[34:35] neg_lo:[0,1] neg_hi:[0,1]
	v_exp_f32_e32 v120, v33
	v_add_f32_e32 v33, v34, v35
	v_mul_f32_e32 v33, 0x3fb8aa3b, v33
	v_exp_f32_e32 v34, v33
	v_mov_b32_e32 v117, v35
	v_mov_b32_e32 v33, v124
	v_pk_add_f32 v[32:33], v[116:117], v[32:33] neg_lo:[0,1] neg_hi:[0,1]
	v_mov_b32_e32 v43, v167
	v_add_f32_e32 v32, v32, v33
	v_mul_f32_e32 v32, 0x3fb8aa3b, v32
	v_exp_f32_e32 v35, v32
	v_add_f32_e32 v32, v174, v129
	v_mul_f32_e32 v32, 0x3fb8aa3b, v32
	v_exp_f32_e32 v116, v32
	v_pk_add_f32 v[32:33], v[128:129], v[126:127] neg_lo:[0,1] neg_hi:[0,1]
	v_mov_b32_e32 v47, v173
	v_add_f32_e32 v32, v32, v33
	v_mul_f32_e32 v32, 0x3fb8aa3b, v32
	v_mov_b32_e32 v39, v33
	v_exp_f32_e32 v117, v32
	v_pk_add_f32 v[32:33], v[38:39], v[36:37] neg_lo:[0,1] neg_hi:[0,1]
	s_nop 0
	v_add_f32_e32 v32, v32, v33
	v_mul_f32_e32 v32, 0x3fb8aa3b, v32
	v_exp_f32_e32 v36, v32
	v_sub_f32_e32 v32, v33, v171
	v_add_f32_e32 v32, v133, v32
	v_mul_f32_e32 v32, 0x3fb8aa3b, v32
	v_exp_f32_e32 v37, v32
	v_add_f32_e32 v32, v177, v135
	v_mul_f32_e32 v32, 0x3fb8aa3b, v32
	v_exp_f32_e32 v118, v32
	v_mov_b32_e32 v32, v41
	v_mov_b32_e32 v33, v169
	v_pk_add_f32 v[32:33], v[134:135], v[32:33] neg_lo:[0,1] neg_hi:[0,1]
	v_mov_b32_e32 v41, v168
	v_add_f32_e32 v32, v32, v33
	v_mul_f32_e32 v32, 0x3fb8aa3b, v32
	v_mov_b32_e32 v133, v33
	v_exp_f32_e32 v119, v32
	v_pk_add_f32 v[32:33], v[132:133], v[42:43] neg_lo:[0,1] neg_hi:[0,1]
	s_nop 0
	v_add_f32_e32 v32, v32, v33
	v_mul_f32_e32 v32, 0x3fb8aa3b, v32
	v_mov_b32_e32 v131, v33
	v_exp_f32_e32 v42, v32
	v_pk_add_f32 v[32:33], v[130:131], v[40:41] neg_lo:[0,1] neg_hi:[0,1]
	s_nop 0
	v_add_f32_e32 v32, v32, v33
	v_mul_f32_e32 v32, 0x3fb8aa3b, v32
	v_exp_f32_e32 v40, v32
	v_add_f32_e32 v32, v190, v181
	v_mul_f32_e32 v32, 0x3fb8aa3b, v32
	v_exp_f32_e32 v41, v32
	v_mov_b32_e32 v32, v45
	v_mov_b32_e32 v33, v179
	v_pk_add_f32 v[32:33], v[180:181], v[32:33] neg_lo:[0,1] neg_hi:[0,1]
	v_mov_b32_e32 v45, v178
	v_add_f32_e32 v32, v32, v33
	v_mul_f32_e32 v32, 0x3fb8aa3b, v32
	v_mov_b32_e32 v177, v33
	v_exp_f32_e32 v43, v32
	v_pk_add_f32 v[32:33], v[176:177], v[46:47] neg_lo:[0,1] neg_hi:[0,1]
	s_nop 0
	v_add_f32_e32 v32, v32, v33
	v_mul_f32_e32 v32, 0x3fb8aa3b, v32
	v_mov_b32_e32 v171, v33
	v_exp_f32_e32 v46, v32
	v_pk_add_f32 v[32:33], v[170:171], v[44:45] neg_lo:[0,1] neg_hi:[0,1]
	v_add_f32_e32 v45, v182, v95
	v_add_f32_e32 v32, v32, v33
	v_mul_f32_e32 v32, 0x3fb8aa3b, v32
	v_exp_f32_e32 v44, v32
	v_cvt_pk_bf16_f32 v32, v35, v34
	v_cvt_pk_bf16_f32 v33, v120, v122
	v_cvt_pk_bf16_f32 v35, v117, v116
	v_cvt_pk_bf16_f32 v34, v37, v36
	s_waitcnt vmcnt(17)
	v_perm_b32 v39, v154, v144, s38
	v_perm_b32 v38, v142, v139, s38
	v_perm_b32 v37, v93, v91, s38
	v_perm_b32 v36, v89, v85, s38
	v_add_f32_e32 v95, v45, v183
	s_nop 0
	v_mfma_f32_32x32x16_bf16 v[0:15], v[32:35], v[36:39], v[0:15]
	s_waitcnt vmcnt(16)
	v_perm_b32 v39, v140, v137, s38
	v_perm_b32 v38, v136, v97, s38
	v_perm_b32 v37, v87, v83, s38
	v_perm_b32 v36, v81, v79, s38
	s_nop 1
	v_mfma_f32_32x32x16_bf16 v[16:31], v[32:35], v[36:39], v[16:31]
	v_cvt_pk_bf16_f32 v32, v40, v42
	v_cvt_pk_bf16_f32 v33, v119, v118
	v_cvt_pk_bf16_f32 v34, v44, v46
	v_cvt_pk_bf16_f32 v35, v43, v41
	s_waitcnt vmcnt(1)
	v_perm_b32 v39, v165, v164, s38
	v_perm_b32 v38, v163, v161, s38
	v_perm_b32 v37, v157, v156, s38
	v_perm_b32 v36, v155, v152, s38
	s_nop 1
	v_mfma_f32_32x32x16_bf16 v[0:15], v[32:35], v[36:39], v[0:15]
	s_waitcnt vmcnt(0)
	v_perm_b32 v39, v162, v160, s38
	v_perm_b32 v38, v159, v158, s38
	v_perm_b32 v37, v153, v143, s38
	v_perm_b32 v36, v141, v138, s38
	s_nop 1
	v_mfma_f32_32x32x16_bf16 v[16:31], v[32:35], v[36:39], v[16:31]
	v_cmp_gt_f32_e32 vcc, s34, v95
	s_cmp_lg_u64 vcc, exec
	s_cselect_b64 s[6:7], -1, 0
	s_cmp_gt_u32 s22, 63
	s_mov_b32 s22, s10
	s_cselect_b64 s[10:11], -1, 0
	s_and_b64 s[6:7], s[10:11], s[6:7]
	v_lshl_add_u64 v[112:113], v[112:113], 0, s[24:25]
	v_lshl_add_u64 v[114:115], v[114:115], 0, s[24:25]
	s_and_b64 vcc, exec, s[6:7]
	s_cbranch_vccnz .LBB0_255

.LBB0_355:
	v_add_u32_e32 v61, s8, v224
	ds_read_b64 v[68:69], v61
	v_pk_mul_f32 v[62:63], v[66:67], v[142:143] op_sel_hi:[1,0]
	v_add_u32_e32 v65, s8, v223
	v_pk_fma_f32 v[70:71], v[124:125], v[140:141], v[62:63] neg_lo:[0,0,1] neg_hi:[0,0,1]
	v_pk_fma_f32 v[62:63], v[124:125], v[140:141], v[62:63] op_sel_hi:[1,0,1]
	s_addk_i32 s8, 0x940
	v_mov_b32_e32 v71, v63
	s_waitcnt lgkmcnt(0)
	v_pk_add_f32 v[62:63], v[70:71], v[68:69]
	s_cmpk_eq_i32 s8, 0x2500
	v_cvt_pk_bf16_f32 v70, v62, v63
	v_pk_mul_f32 v[68:69], v[66:67], v[62:63] op_sel:[0,1]
	ds_write_b32 v65, v70
	v_pk_fma_f32 v[70:71], v[124:125], v[62:63], v[68:69] neg_lo:[0,0,1] neg_hi:[0,0,1]
	v_pk_fma_f32 v[62:63], v[124:125], v[62:63], v[68:69] op_sel_hi:[1,0,1]
	ds_read_b64 v[68:69], v61 offset:592
	v_mov_b32_e32 v71, v63
	s_waitcnt lgkmcnt(0)
	v_pk_add_f32 v[62:63], v[70:71], v[68:69]
	s_nop 0
	v_cvt_pk_bf16_f32 v70, v62, v63
	ds_write_b32 v65, v70 offset:592
	ds_read_b64 v[72:73], v61 offset:1184
	v_pk_mul_f32 v[68:69], v[66:67], v[62:63] op_sel:[0,1]
	s_nop 0
	v_pk_fma_f32 v[70:71], v[124:125], v[62:63], v[68:69] neg_lo:[0,0,1] neg_hi:[0,0,1]
	v_pk_fma_f32 v[62:63], v[124:125], v[62:63], v[68:69] op_sel_hi:[1,0,1]
	s_nop 0
	v_mov_b32_e32 v71, v63
	s_waitcnt lgkmcnt(0)
	v_pk_add_f32 v[62:63], v[70:71], v[72:73]
	s_nop 0
	v_cvt_pk_bf16_f32 v70, v62, v63
	ds_write_b32 v65, v70 offset:1184
	ds_read_b64 v[70:71], v61 offset:1776
	v_pk_mul_f32 v[68:69], v[66:67], v[62:63] op_sel:[0,1]
	s_nop 0
	v_pk_fma_f32 v[72:73], v[124:125], v[62:63], v[68:69] neg_lo:[0,0,1] neg_hi:[0,0,1]
	v_pk_fma_f32 v[62:63], v[124:125], v[62:63], v[68:69] op_sel_hi:[1,0,1]
	s_nop 0
	v_mov_b32_e32 v73, v63
	s_waitcnt lgkmcnt(0)
	v_pk_add_f32 v[140:141], v[72:73], v[70:71]
	s_nop 0
	v_mov_b32_e32 v142, v141
	v_cvt_pk_bf16_f32 v61, v140, v141
	ds_write_b32 v65, v61 offset:1776
	s_cbranch_scc0 .LBB0_355
	ds_read_b128 v[68:71], v60 offset:36864
	ds_read_b128 v[72:75], v60 offset:36928
	v_lshl_or_b32 v65, s10, 4, v163
	s_add_i32 s10, s10, 1
	s_cmp_eq_u32 s10, 4
	s_waitcnt lgkmcnt(1)
	v_mfma_f32_16x16x32_bf16 v[68:71], v[68:71], v[8:11], 0
	s_waitcnt lgkmcnt(0)
	v_mfma_f32_16x16x32_bf16 v[68:71], v[72:75], v[12:15], v[68:71]
	ds_read_b128 v[72:75], v60 offset:36992
	s_waitcnt lgkmcnt(0)
	v_mfma_f32_16x16x32_bf16 v[68:71], v[72:75], v[16:19], v[68:71]
	ds_read_b128 v[72:75], v60 offset:37056
	ds_read_b128 v[60:63], v60 offset:37376
	s_waitcnt lgkmcnt(1)
	v_mfma_f32_16x16x32_bf16 v[68:71], v[72:75], v[20:23], v[68:71]
	s_waitcnt lgkmcnt(0)
	v_mfma_f32_16x16x32_bf16 v[60:63], v[60:63], v[56:59], v[68:71]
	s_nop 7
	v_mul_f32_e32 v68, 0x3d372713, v60
	v_mul_f32_e32 v68, v60, v68
	v_fma_f32 v68, v60, v68, v60
	v_mul_f32_e32 v68, 0x3fcc422a, v68
	v_mul_f32_e32 v68, 0xbfb8aa3b, v68
	v_exp_f32_e32 v68, v68
	s_nop 0
	v_add_f32_e32 v68, 1.0, v68
	v_rcp_f32_e32 v68, v68
	s_nop 0
	v_mul_f32_e32 v60, v60, v68
	v_cvt_pk_bf16_f32 v60, v60, s0
	v_mad_u64_u32 v[68:69], s[8:9], v65, s3, v[64:65]
	ds_write_b16 v68, v60
	v_mul_f32_e32 v60, 0x3d372713, v61
	v_mul_f32_e32 v60, v61, v60
	v_fma_f32 v60, v61, v60, v61
	v_mul_f32_e32 v60, 0x3fcc422a, v60
	v_mul_f32_e32 v60, 0xbfb8aa3b, v60
	v_exp_f32_e32 v60, v60
	s_nop 0
	v_add_f32_e32 v60, 1.0, v60
	v_rcp_f32_e32 v60, v60
	s_nop 0
	v_mul_f32_e32 v60, v61, v60
	v_cvt_pk_bf16_f32 v60, v60, s0
	ds_write_b16 v68, v60 offset:528
	v_mul_f32_e32 v60, 0x3d372713, v62
	v_mul_f32_e32 v60, v62, v60
	v_fma_f32 v60, v62, v60, v62
	v_mul_f32_e32 v60, 0x3fcc422a, v60
	v_mul_f32_e32 v60, 0xbfb8aa3b, v60
	v_exp_f32_e32 v60, v60
	s_nop 0
	v_add_f32_e32 v60, 1.0, v60
	v_rcp_f32_e32 v60, v60
	s_nop 0
	v_mul_f32_e32 v60, v62, v60
	v_cvt_pk_bf16_f32 v60, v60, s0
	ds_write_b16 v68, v60 offset:1056
	v_mul_f32_e32 v60, 0x3d372713, v63
	v_mul_f32_e32 v60, v63, v60
	v_fma_f32 v60, v63, v60, v63
	v_mul_f32_e32 v60, 0x3fcc422a, v60
	v_mul_f32_e32 v60, 0xbfb8aa3b, v60
	v_exp_f32_e32 v60, v60
	s_nop 0
	v_add_f32_e32 v60, 1.0, v60
	v_rcp_f32_e32 v60, v60
	s_nop 0
	v_mul_f32_e32 v60, v63, v60
	v_cvt_pk_bf16_f32 v60, v60, s0
	ds_write_b16 v68, v60 offset:1584
	s_cbranch_scc0 .LBB0_352
	s_mov_b32 s8, 8
	s_mov_b64 s[24:25], 0
	s_and_b64 vcc, exec, s[6:7]
	s_cbranch_vccz .LBB0_346
	s_waitcnt lgkmcnt(0)
	s_barrier
	global_load_dword v129, v[112:113], off
	global_load_dword v128, v[114:115], off offset:3072
	global_load_dwordx4 v[76:79], v[116:117], off
	global_load_dwordx4 v[72:75], v[116:117], off offset:32
	global_load_dwordx4 v[68:71], v[116:117], off offset:64
	global_load_dwordx4 v[64:67], v[116:117], off offset:96
	global_load_dwordx4 v[60:63], v[116:117], off offset:128
	global_load_dwordx4 v[56:59], v[116:117], off offset:160
	global_load_dwordx4 v[52:55], v[116:117], off offset:192
	global_load_dwordx4 v[48:51], v[116:117], off offset:224
	global_load_dwordx4 v[44:47], v[116:117], off offset:256
	global_load_dwordx4 v[40:43], v[116:117], off offset:288
	global_load_dwordx4 v[36:39], v[116:117], off offset:320
	global_load_dwordx4 v[32:35], v[116:117], off offset:352
	global_load_dwordx4 v[28:31], v[116:117], off offset:384
	global_load_dwordx4 v[24:27], v[116:117], off offset:416
	global_load_dwordx4 v[20:23], v[116:117], off offset:448
	global_load_dwordx4 v[16:19], v[116:117], off offset:480
	s_waitcnt vmcnt(19)
	ds_read_b128 v[0:3], v229
	ds_read_b128 v[80:83], v229 offset:32
	ds_read_b128 v[84:87], v229 offset:64
	ds_read_b128 v[88:91], v229 offset:96
	s_waitcnt vmcnt(15) lgkmcnt(3)
	v_mfma_f32_32x32x16_bf16 v[0:15], v[0:3], v[76:79], 0
	s_waitcnt vmcnt(14) lgkmcnt(2)
	v_mfma_f32_32x32x16_bf16 v[0:15], v[80:83], v[72:75], v[0:15]
	s_waitcnt vmcnt(13) lgkmcnt(1)
	v_mfma_f32_32x32x16_bf16 v[0:15], v[84:87], v[68:71], v[0:15]
	s_waitcnt vmcnt(12) lgkmcnt(0)
	v_mfma_f32_32x32x16_bf16 v[0:15], v[88:91], v[64:67], v[0:15]
	ds_read_b128 v[80:83], v229 offset:128
	ds_read_b128 v[84:87], v229 offset:160
	ds_read_b128 v[88:91], v229 offset:192
	ds_read_b128 v[92:95], v229 offset:224
	s_waitcnt vmcnt(11) lgkmcnt(3)
	v_mfma_f32_32x32x16_bf16 v[0:15], v[80:83], v[60:63], v[0:15]
	s_waitcnt vmcnt(10) lgkmcnt(2)
	v_mfma_f32_32x32x16_bf16 v[0:15], v[84:87], v[56:59], v[0:15]
	s_waitcnt vmcnt(9) lgkmcnt(1)
	v_mfma_f32_32x32x16_bf16 v[0:15], v[88:91], v[52:55], v[0:15]
	s_waitcnt vmcnt(8) lgkmcnt(0)
	v_mfma_f32_32x32x16_bf16 v[0:15], v[92:95], v[48:51], v[0:15]
	ds_read_b128 v[80:83], v229 offset:256
	ds_read_b128 v[84:87], v229 offset:288
	ds_read_b128 v[88:91], v229 offset:320
	ds_read_b128 v[92:95], v229 offset:352
	s_waitcnt vmcnt(7) lgkmcnt(3)
	v_mfma_f32_32x32x16_bf16 v[0:15], v[80:83], v[44:47], v[0:15]
	s_waitcnt vmcnt(6) lgkmcnt(2)
	v_mfma_f32_32x32x16_bf16 v[0:15], v[84:87], v[40:43], v[0:15]
	s_waitcnt vmcnt(5) lgkmcnt(1)
	v_mfma_f32_32x32x16_bf16 v[0:15], v[88:91], v[36:39], v[0:15]
	s_waitcnt vmcnt(4) lgkmcnt(0)
	v_mfma_f32_32x32x16_bf16 v[0:15], v[92:95], v[32:35], v[0:15]
	ds_read_b128 v[80:83], v229 offset:384
	ds_read_b128 v[84:87], v229 offset:416
	ds_read_b128 v[88:91], v229 offset:448
	ds_read_b128 v[92:95], v229 offset:480
	s_waitcnt vmcnt(3) lgkmcnt(3)
	v_mfma_f32_32x32x16_bf16 v[0:15], v[80:83], v[28:31], v[0:15]
	s_waitcnt vmcnt(2) lgkmcnt(2)
	v_mfma_f32_32x32x16_bf16 v[0:15], v[84:87], v[24:27], v[0:15]
	s_waitcnt vmcnt(1) lgkmcnt(1)
	v_mfma_f32_32x32x16_bf16 v[0:15], v[88:91], v[20:23], v[0:15]
	s_waitcnt vmcnt(0) lgkmcnt(0)
	v_mfma_f32_32x32x16_bf16 v[0:15], v[92:95], v[16:19], v[0:15]
	s_nop 11
	v_add_f32_e32 v0, v129, v0
	v_add_f32_e32 v1, v129, v1
	v_mul_f32_e32 v0, 0xbfb8aa3b, v0
	v_mul_f32_e32 v1, 0xbfb8aa3b, v1
	v_exp_f32_e32 v0, v0
	v_exp_f32_e32 v1, v1
	ds_read_u16 v80, v230
	ds_read_u16 v81, v227
	ds_read_u16 v84, v227 offset:528
	ds_read_u16 v85, v227 offset:1056
	ds_read_u16 v88, v227 offset:3696
	ds_read_u16 v89, v227 offset:4224
	ds_read_u16 v92, v227 offset:4752
	ds_read_u16 v93, v227 offset:5280
	s_waitcnt lgkmcnt(6)
	v_lshlrev_b32_e32 v81, 16, v81
	v_add_f32_e32 v0, 1.0, v0
	v_add_f32_e32 v1, 1.0, v1
	v_rcp_f32_e32 v0, v0
	v_rcp_f32_e32 v1, v1
	v_lshlrev_b32_e32 v80, 16, v80
	v_add_f32_e32 v2, v129, v2
	v_mul_f32_e32 v2, 0xbfb8aa3b, v2
	v_pk_mul_f32 v[80:81], v[0:1], v[80:81]
	s_waitcnt lgkmcnt(4)
	v_lshlrev_b32_e32 v85, 16, v85
	v_pk_mul_f32 v[0:1], v[80:81], v[80:81]
	ds_bpermute_b32 v0, v185, v0
	ds_bpermute_b32 v1, v185, v1
	v_lshlrev_b32_e32 v84, 16, v84
	v_add_f32_e32 v6, v129, v6
	v_mul_f32_e32 v6, 0xbfb8aa3b, v6
	s_waitcnt lgkmcnt(4)
	v_lshlrev_b32_e32 v89, 16, v89
	s_waitcnt lgkmcnt(0)
	v_pk_fma_f32 v[0:1], v[80:81], v[80:81], v[0:1]
	s_nop 1
	v_mov_b32_dpp v82, v0 row_ror:8 row_mask:0xf bank_mask:0xf
	s_nop 0
	v_mov_b32_dpp v83, v1 row_ror:8 row_mask:0xf bank_mask:0xf
	v_lshlrev_b32_e32 v88, 16, v88
	v_lshlrev_b32_e32 v93, 16, v93
	v_lshlrev_b32_e32 v92, 16, v92
	v_add_f32_e32 v8, v129, v8
	s_waitcnt lgkmcnt(0)
	v_pk_add_f32 v[0:1], v[0:1], v[82:83]
	v_exp_f32_e32 v82, v2
	v_add_f32_e32 v2, v129, v3
	v_mul_f32_e32 v2, 0xbfb8aa3b, v2
	v_exp_f32_e32 v3, v2
	v_add_f32_e32 v82, 1.0, v82
	v_mov_b32_dpp v2, v0 row_half_mirror row_mask:0xf bank_mask:0xf
	s_nop 1
	v_mov_b32_dpp v2, v2 quad_perm:[3,2,1,0] row_mask:0xf bank_mask:0xf
	v_rcp_f32_e32 v82, v82
	v_add_f32_e32 v3, 1.0, v3
	v_rcp_f32_e32 v83, v3
	s_nop 0
	v_mov_b32_dpp v3, v1 row_half_mirror row_mask:0xf bank_mask:0xf
	s_nop 1
	v_mov_b32_dpp v3, v3 quad_perm:[3,2,1,0] row_mask:0xf bank_mask:0xf
	v_add_f32_e32 v9, v129, v9
	v_mul_f32_e32 v8, 0xbfb8aa3b, v8
	v_pk_mul_f32 v[82:83], v[82:83], v[84:85]
	v_mul_f32_e32 v9, 0xbfb8aa3b, v9
	v_pk_mul_f32 v[84:85], v[82:83], v[82:83]
	s_waitcnt lgkmcnt(0)
	v_pk_add_f32 v[0:1], v[0:1], v[2:3]
	ds_bpermute_b32 v84, v185, v84
	ds_bpermute_b32 v85, v185, v85
	v_mov_b32_dpp v2, v0 quad_perm:[2,3,0,1] row_mask:0xf bank_mask:0xf
	v_mov_b32_dpp v3, v1 quad_perm:[2,3,0,1] row_mask:0xf bank_mask:0xf
	v_exp_f32_e32 v8, v8
	v_exp_f32_e32 v9, v9
	s_waitcnt lgkmcnt(0)
	v_pk_fma_f32 v[84:85], v[82:83], v[82:83], v[84:85]
	s_nop 1
	v_mov_b32_dpp v86, v84 row_ror:8 row_mask:0xf bank_mask:0xf
	s_waitcnt lgkmcnt(0)
	v_pk_add_f32 v[0:1], v[0:1], v[2:3]
	v_add_f32_e32 v3, v129, v4
	v_mov_b32_dpp v87, v85 row_ror:8 row_mask:0xf bank_mask:0xf
	v_mul_f32_e32 v3, 0xbfb8aa3b, v3
	v_add_f32_e32 v4, v129, v5
	v_exp_f32_e32 v3, v3
	v_mul_f32_e32 v4, 0xbfb8aa3b, v4
	v_exp_f32_e32 v5, v4
	s_waitcnt lgkmcnt(0)
	v_pk_add_f32 v[86:87], v[84:85], v[86:87]
	v_add_f32_e32 v3, 1.0, v3
	s_nop 0
	v_mov_b32_dpp v4, v86 row_half_mirror row_mask:0xf bank_mask:0xf
	s_nop 1
	v_mov_b32_dpp v4, v4 quad_perm:[3,2,1,0] row_mask:0xf bank_mask:0xf
	v_rcp_f32_e32 v84, v3
	v_add_f32_e32 v3, 1.0, v5
	v_mov_b32_dpp v5, v87 row_half_mirror row_mask:0xf bank_mask:0xf
	s_nop 1
	v_mov_b32_dpp v5, v5 quad_perm:[3,2,1,0] row_mask:0xf bank_mask:0xf
	v_rcp_f32_e32 v85, v3
	v_add_f32_e32 v8, 1.0, v8
	v_add_f32_e32 v9, 1.0, v9
	v_rcp_f32_e32 v8, v8
	s_waitcnt lgkmcnt(0)
	v_pk_add_f32 v[4:5], v[86:87], v[4:5]
	v_exp_f32_e32 v86, v6
	v_add_f32_e32 v6, v129, v7
	v_mul_f32_e32 v6, 0xbfb8aa3b, v6
	v_pk_mul_f32 v[84:85], v[84:85], v[88:89]
	v_exp_f32_e32 v7, v6
	v_pk_mul_f32 v[88:89], v[84:85], v[84:85]
	ds_bpermute_b32 v88, v185, v88
	ds_bpermute_b32 v89, v185, v89
	v_add_f32_e32 v86, 1.0, v86
	v_add_f32_e32 v7, 1.0, v7
	v_rcp_f32_e32 v86, v86
	v_rcp_f32_e32 v87, v7
	s_waitcnt lgkmcnt(0)
	v_pk_fma_f32 v[88:89], v[84:85], v[84:85], v[88:89]
	s_nop 1
	v_mov_b32_dpp v6, v88 row_ror:8 row_mask:0xf bank_mask:0xf
	s_nop 0
	v_mov_b32_dpp v7, v89 row_ror:8 row_mask:0xf bank_mask:0xf
	v_mov_b32_dpp v90, v4 quad_perm:[2,3,0,1] row_mask:0xf bank_mask:0xf
	v_mov_b32_dpp v91, v5 quad_perm:[2,3,0,1] row_mask:0xf bank_mask:0xf
	v_pk_mul_f32 v[86:87], v[86:87], v[92:93]
	v_rcp_f32_e32 v9, v9
	v_pk_mul_f32 v[92:93], v[86:87], v[86:87]
	ds_bpermute_b32 v92, v185, v92
	ds_bpermute_b32 v93, v185, v93
	s_waitcnt lgkmcnt(0)
	v_pk_add_f32 v[88:89], v[88:89], v[6:7]
	s_waitcnt lgkmcnt(0)
	v_pk_add_f32 v[4:5], v[4:5], v[90:91]
	v_mov_b32_dpp v90, v88 row_half_mirror row_mask:0xf bank_mask:0xf
	s_nop 1
	v_mov_b32_dpp v90, v90 quad_perm:[3,2,1,0] row_mask:0xf bank_mask:0xf
	v_mov_b32_dpp v91, v89 row_half_mirror row_mask:0xf bank_mask:0xf
	s_nop 1
	v_mov_b32_dpp v91, v91 quad_perm:[3,2,1,0] row_mask:0xf bank_mask:0xf
	s_waitcnt lgkmcnt(0)
	v_pk_fma_f32 v[92:93], v[86:87], v[86:87], v[92:93]
	s_nop 1
	v_mov_b32_dpp v94, v92 row_ror:8 row_mask:0xf bank_mask:0xf
	s_nop 0
	v_mov_b32_dpp v95, v93 row_ror:8 row_mask:0xf bank_mask:0xf
	v_add_f32_e32 v10, v129, v10
	s_waitcnt lgkmcnt(0)
	v_pk_add_f32 v[90:91], v[88:89], v[90:91]
	ds_read_u16 v88, v227 offset:7920
	ds_read_u16 v89, v227 offset:8448
	ds_read_u16 v120, v227 offset:8976
	ds_read_u16 v121, v227 offset:9504
	ds_read_u16 v124, v227 offset:12144
	ds_read_u16 v125, v227 offset:12672
	ds_read_u16 v126, v227 offset:13200
	ds_read_u16 v127, v227 offset:13728
	s_waitcnt lgkmcnt(0)
	v_lshlrev_b32_e32 v89, 16, v89
	v_lshlrev_b32_e32 v88, 16, v88
	v_pk_mul_f32 v[88:89], v[8:9], v[88:89]
	v_pk_add_f32 v[92:93], v[92:93], v[94:95]
	v_pk_mul_f32 v[8:9], v[88:89], v[88:89]
	v_add_f32_e32 v11, v129, v11
	v_mov_b32_dpp v94, v92 row_half_mirror row_mask:0xf bank_mask:0xf
	s_nop 1
	v_mov_b32_dpp v94, v94 quad_perm:[3,2,1,0] row_mask:0xf bank_mask:0xf
	v_mov_b32_dpp v95, v93 row_half_mirror row_mask:0xf bank_mask:0xf
	s_nop 1
	v_mov_b32_dpp v95, v95 quad_perm:[3,2,1,0] row_mask:0xf bank_mask:0xf
	ds_bpermute_b32 v8, v185, v8
	ds_bpermute_b32 v9, v185, v9
	v_mul_f32_e32 v10, 0xbfb8aa3b, v10
	v_mul_f32_e32 v11, 0xbfb8aa3b, v11
	v_exp_f32_e32 v10, v10
	v_exp_f32_e32 v11, v11
	v_mov_b32_dpp v96, v90 quad_perm:[2,3,0,1] row_mask:0xf bank_mask:0xf
	v_mov_b32_dpp v97, v91 quad_perm:[2,3,0,1] row_mask:0xf bank_mask:0xf
	s_waitcnt lgkmcnt(0)
	v_pk_add_f32 v[92:93], v[92:93], v[94:95]
	s_waitcnt lgkmcnt(0)
	v_pk_fma_f32 v[100:101], v[88:89], v[88:89], v[8:9]
	v_add_f32_e32 v10, 1.0, v10
	v_add_f32_e32 v11, 1.0, v11
	v_mov_b32_dpp v94, v92 quad_perm:[2,3,0,1] row_mask:0xf bank_mask:0xf
	v_mov_b32_dpp v95, v93 quad_perm:[2,3,0,1] row_mask:0xf bank_mask:0xf
	v_mov_b32_dpp v102, v100 row_ror:8 row_mask:0xf bank_mask:0xf
	v_mov_b32_dpp v103, v101 row_ror:8 row_mask:0xf bank_mask:0xf
	v_rcp_f32_e32 v10, v10
	v_rcp_f32_e32 v11, v11
	s_waitcnt lgkmcnt(0)
	v_pk_add_f32 v[8:9], v[90:91], v[96:97]
	v_lshlrev_b32_e32 v91, 16, v121
	v_lshlrev_b32_e32 v90, 16, v120
	v_pk_mul_f32 v[90:91], v[10:11], v[90:91]
	s_waitcnt lgkmcnt(0)
	v_pk_add_f32 v[98:99], v[92:93], v[94:95]
	s_waitcnt lgkmcnt(0)
	v_pk_add_f32 v[92:93], v[100:101], v[102:103]
	v_pk_mul_f32 v[10:11], v[90:91], v[90:91]
	s_nop 0
	v_mov_b32_dpp v94, v92 row_half_mirror row_mask:0xf bank_mask:0xf
	s_nop 1
	v_mov_b32_dpp v94, v94 quad_perm:[3,2,1,0] row_mask:0xf bank_mask:0xf
	v_mov_b32_dpp v95, v93 row_half_mirror row_mask:0xf bank_mask:0xf
	s_nop 1
	v_mov_b32_dpp v95, v95 quad_perm:[3,2,1,0] row_mask:0xf bank_mask:0xf
	ds_bpermute_b32 v100, v185, v10
	ds_bpermute_b32 v101, v185, v11
	v_add_f32_e32 v12, v129, v12
	v_mul_f32_e32 v12, 0xbfb8aa3b, v12
	s_waitcnt lgkmcnt(0)
	v_pk_add_f32 v[92:93], v[92:93], v[94:95]
	s_nop 1
	v_mov_b32_dpp v94, v92 quad_perm:[2,3,0,1] row_mask:0xf bank_mask:0xf
	s_waitcnt lgkmcnt(0)
	v_pk_fma_f32 v[120:121], v[90:91], v[90:91], v[100:101]
	v_mov_b32_dpp v95, v93 quad_perm:[2,3,0,1] row_mask:0xf bank_mask:0xf
	s_nop 0
	v_mov_b32_dpp v122, v120 row_ror:8 row_mask:0xf bank_mask:0xf
	v_mov_b32_dpp v123, v121 row_ror:8 row_mask:0xf bank_mask:0xf
	v_add_f32_e32 v14, v129, v14
	v_mul_f32_e32 v14, 0xbfb8aa3b, v14
	s_waitcnt lgkmcnt(0)
	v_pk_add_f32 v[100:101], v[92:93], v[94:95]
	v_mov_b32_dpp v2, v0 quad_perm:[1,0,3,2] row_mask:0xf bank_mask:0xf
	s_waitcnt lgkmcnt(0)
	v_pk_add_f32 v[92:93], v[120:121], v[122:123]
	v_exp_f32_e32 v120, v12
	v_add_f32_e32 v12, v129, v13
	v_mov_b32_dpp v94, v92 row_half_mirror row_mask:0xf bank_mask:0xf
	s_nop 1
	v_mov_b32_dpp v94, v94 quad_perm:[3,2,1,0] row_mask:0xf bank_mask:0xf
	v_mov_b32_dpp v95, v93 row_half_mirror row_mask:0xf bank_mask:0xf
	s_nop 1
	v_mov_b32_dpp v95, v95 quad_perm:[3,2,1,0] row_mask:0xf bank_mask:0xf
	v_mul_f32_e32 v12, 0xbfb8aa3b, v12
	v_exp_f32_e32 v121, v12
	v_mov_b32_dpp v3, v1 quad_perm:[1,0,3,2] row_mask:0xf bank_mask:0xf
	v_mov_b32_dpp v6, v4 quad_perm:[1,0,3,2] row_mask:0xf bank_mask:0xf
	s_waitcnt lgkmcnt(0)
	v_pk_add_f32 v[12:13], v[92:93], v[94:95]
	v_add_f32_e32 v92, 1.0, v120
	v_add_f32_e32 v93, 1.0, v121
	v_rcp_f32_e32 v92, v92
	v_rcp_f32_e32 v93, v93
	v_exp_f32_e32 v121, v14
	v_add_f32_e32 v14, v129, v15
	v_mul_f32_e32 v14, 0xbfb8aa3b, v14
	v_exp_f32_e32 v15, v14
	v_lshlrev_b32_e32 v95, 16, v125
	v_lshlrev_b32_e32 v94, 16, v124
	v_pk_mul_f32 v[92:93], v[92:93], v[94:95]
	v_add_f32_e32 v15, 1.0, v15
	v_pk_mul_f32 v[94:95], v[92:93], v[92:93]
	ds_bpermute_b32 v14, v185, v94
	v_add_f32_e32 v94, 1.0, v121
	v_rcp_f32_e32 v122, v94
	v_rcp_f32_e32 v123, v15
	ds_bpermute_b32 v15, v185, v95
	v_lshlrev_b32_e32 v95, 16, v127
	v_lshlrev_b32_e32 v94, 16, v126
	v_pk_mul_f32 v[94:95], v[122:123], v[94:95]
	v_mov_b32_dpp v120, v12 quad_perm:[2,3,0,1] row_mask:0xf bank_mask:0xf
	v_pk_mul_f32 v[122:123], v[94:95], v[94:95]
	ds_bpermute_b32 v122, v185, v122
	ds_bpermute_b32 v123, v185, v123
	s_waitcnt lgkmcnt(0)
	v_pk_fma_f32 v[14:15], v[92:93], v[92:93], v[14:15]
	v_mov_b32_dpp v121, v13 quad_perm:[2,3,0,1] row_mask:0xf bank_mask:0xf
	s_nop 0
	v_mov_b32_dpp v124, v14 row_ror:8 row_mask:0xf bank_mask:0xf
	v_mov_b32_dpp v125, v15 row_ror:8 row_mask:0xf bank_mask:0xf
	s_waitcnt lgkmcnt(0)
	v_pk_fma_f32 v[122:123], v[94:95], v[94:95], v[122:123]
	s_nop 1
	v_mov_b32_dpp v126, v122 row_ror:8 row_mask:0xf bank_mask:0xf
	s_nop 0
	v_mov_b32_dpp v127, v123 row_ror:8 row_mask:0xf bank_mask:0xf
	s_waitcnt lgkmcnt(0)
	v_pk_add_f32 v[12:13], v[12:13], v[120:121]
	s_waitcnt lgkmcnt(0)
	v_pk_add_f32 v[120:121], v[14:15], v[124:125]
	s_nop 1
	v_mov_b32_dpp v124, v120 row_half_mirror row_mask:0xf bank_mask:0xf
	s_nop 1
	v_mov_b32_dpp v124, v124 quad_perm:[3,2,1,0] row_mask:0xf bank_mask:0xf
	v_mov_b32_dpp v125, v121 row_half_mirror row_mask:0xf bank_mask:0xf
	s_nop 1
	v_mov_b32_dpp v125, v125 quad_perm:[3,2,1,0] row_mask:0xf bank_mask:0xf
	s_waitcnt lgkmcnt(0)
	v_pk_add_f32 v[122:123], v[122:123], v[126:127]
	s_nop 1
	v_mov_b32_dpp v126, v122 row_half_mirror row_mask:0xf bank_mask:0xf
	s_nop 1
	v_mov_b32_dpp v126, v126 quad_perm:[3,2,1,0] row_mask:0xf bank_mask:0xf
	v_mov_b32_dpp v127, v123 row_half_mirror row_mask:0xf bank_mask:0xf
	s_nop 1
	v_mov_b32_dpp v127, v127 quad_perm:[3,2,1,0] row_mask:0xf bank_mask:0xf
	v_mov_b32_dpp v7, v5 quad_perm:[1,0,3,2] row_mask:0xf bank_mask:0xf
	s_waitcnt lgkmcnt(0)
	v_pk_add_f32 v[120:121], v[120:121], v[124:125]
	s_nop 1
	v_mov_b32_dpp v124, v120 quad_perm:[2,3,0,1] row_mask:0xf bank_mask:0xf
	s_nop 0
	v_mov_b32_dpp v125, v121 quad_perm:[2,3,0,1] row_mask:0xf bank_mask:0xf
	s_waitcnt lgkmcnt(0)
	v_pk_add_f32 v[126:127], v[122:123], v[126:127]
	s_nop 1
	v_mov_b32_dpp v130, v126 quad_perm:[2,3,0,1] row_mask:0xf bank_mask:0xf
	s_nop 0
	v_mov_b32_dpp v131, v127 quad_perm:[2,3,0,1] row_mask:0xf bank_mask:0xf
	v_mov_b32_dpp v96, v8 quad_perm:[1,0,3,2] row_mask:0xf bank_mask:0xf
	s_waitcnt lgkmcnt(0)
	v_pk_add_f32 v[120:121], v[120:121], v[124:125]
	v_mov_b32_dpp v97, v9 quad_perm:[1,0,3,2] row_mask:0xf bank_mask:0xf
	v_mov_b32_dpp v10, v98 quad_perm:[1,0,3,2] row_mask:0xf bank_mask:0xf
	s_waitcnt lgkmcnt(0)
	v_pk_add_f32 v[124:125], v[126:127], v[130:131]
	v_mov_b32_dpp v11, v99 quad_perm:[1,0,3,2] row_mask:0xf bank_mask:0xf
	v_mov_b32_dpp v102, v100 quad_perm:[1,0,3,2] row_mask:0xf bank_mask:0xf
	v_mov_b32_dpp v103, v101 quad_perm:[1,0,3,2] row_mask:0xf bank_mask:0xf
	v_mov_b32_dpp v14, v12 quad_perm:[1,0,3,2] row_mask:0xf bank_mask:0xf
	v_mov_b32_dpp v15, v13 quad_perm:[1,0,3,2] row_mask:0xf bank_mask:0xf
	v_mov_b32_dpp v122, v120 quad_perm:[1,0,3,2] row_mask:0xf bank_mask:0xf
	v_mov_b32_dpp v123, v121 quad_perm:[1,0,3,2] row_mask:0xf bank_mask:0xf
	v_mov_b32_dpp v126, v124 quad_perm:[1,0,3,2] row_mask:0xf bank_mask:0xf
	v_mov_b32_dpp v127, v125 quad_perm:[1,0,3,2] row_mask:0xf bank_mask:0xf
	s_and_saveexec_b64 s[6:7], s[48:49]
	s_cbranch_execz .LBB0_360
	v_pk_add_f32 v[0:1], v[0:1], v[2:3]
	v_pk_add_f32 v[2:3], v[4:5], v[6:7]
	ds_write_b128 v231, v[0:3] offset:33792
	s_waitcnt lgkmcnt(11)
	v_pk_add_f32 v[0:1], v[8:9], v[96:97]
	s_waitcnt lgkmcnt(9)
	v_pk_add_f32 v[2:3], v[98:99], v[10:11]
	ds_write_b128 v231, v[0:3] offset:33824
	s_waitcnt lgkmcnt(8)
	v_pk_add_f32 v[0:1], v[100:101], v[102:103]
	s_waitcnt lgkmcnt(6)
	v_pk_add_f32 v[2:3], v[12:13], v[14:15]
	ds_write_b128 v231, v[0:3] offset:33856
	s_waitcnt lgkmcnt(5)
	v_pk_add_f32 v[0:1], v[120:121], v[122:123]
	s_waitcnt lgkmcnt(3)
	v_pk_add_f32 v[2:3], v[124:125], v[126:127]
	ds_write_b128 v231, v[0:3] offset:33888
.LBB0_360:
	s_or_b64 exec, exec, s[6:7]
	ds_read_b128 v[0:3], v229 offset:16896
	s_waitcnt lgkmcnt(11)
	ds_read_b128 v[96:99], v229 offset:16928
	s_waitcnt lgkmcnt(8)
	ds_read_b128 v[100:103], v229 offset:16960
	s_waitcnt lgkmcnt(5)
	ds_read_b128 v[120:123], v229 offset:16992
	s_waitcnt lgkmcnt(3)
	v_mfma_f32_32x32x16_bf16 v[0:15], v[0:3], v[76:79], 0
	s_waitcnt lgkmcnt(2)
	v_mfma_f32_32x32x16_bf16 v[0:15], v[96:99], v[72:75], v[0:15]
	s_waitcnt lgkmcnt(1)
	v_mfma_f32_32x32x16_bf16 v[0:15], v[100:103], v[68:71], v[0:15]
	s_waitcnt lgkmcnt(0)
	v_mfma_f32_32x32x16_bf16 v[0:15], v[120:123], v[64:67], v[0:15]
	ds_read_b128 v[64:67], v229 offset:17024
	ds_read_b128 v[68:71], v229 offset:17056
	ds_read_b128 v[72:75], v229 offset:17088
	ds_read_b128 v[76:79], v229 offset:17120
	s_waitcnt lgkmcnt(3)
	v_mfma_f32_32x32x16_bf16 v[0:15], v[64:67], v[60:63], v[0:15]
	s_waitcnt lgkmcnt(2)
	v_mfma_f32_32x32x16_bf16 v[0:15], v[68:71], v[56:59], v[0:15]
	s_waitcnt lgkmcnt(1)
	v_mfma_f32_32x32x16_bf16 v[0:15], v[72:75], v[52:55], v[0:15]
	s_waitcnt lgkmcnt(0)
	v_mfma_f32_32x32x16_bf16 v[0:15], v[76:79], v[48:51], v[0:15]
	ds_read_b128 v[48:51], v229 offset:17152
	ds_read_b128 v[52:55], v229 offset:17184
	ds_read_b128 v[56:59], v229 offset:17216
	ds_read_b128 v[60:63], v229 offset:17248
	s_waitcnt lgkmcnt(3)
	v_mfma_f32_32x32x16_bf16 v[0:15], v[48:51], v[44:47], v[0:15]
	s_waitcnt lgkmcnt(2)
	v_mfma_f32_32x32x16_bf16 v[0:15], v[52:55], v[40:43], v[0:15]
	s_waitcnt lgkmcnt(1)
	v_mfma_f32_32x32x16_bf16 v[0:15], v[56:59], v[36:39], v[0:15]
	s_waitcnt lgkmcnt(0)
	v_mfma_f32_32x32x16_bf16 v[0:15], v[60:63], v[32:35], v[0:15]
	ds_read_b128 v[32:35], v229 offset:17280
	ds_read_b128 v[36:39], v229 offset:17312
	ds_read_b128 v[40:43], v229 offset:17344
	ds_read_b128 v[44:47], v229 offset:17376
	s_waitcnt lgkmcnt(3)
	v_mfma_f32_32x32x16_bf16 v[0:15], v[32:35], v[28:31], v[0:15]
	s_waitcnt lgkmcnt(2)
	v_mfma_f32_32x32x16_bf16 v[0:15], v[36:39], v[24:27], v[0:15]
	s_waitcnt lgkmcnt(1)
	v_mfma_f32_32x32x16_bf16 v[0:15], v[40:43], v[20:23], v[0:15]
	s_waitcnt lgkmcnt(0)
	v_mfma_f32_32x32x16_bf16 v[0:15], v[44:47], v[16:19], v[0:15]
	s_nop 11
	v_add_f32_e32 v0, v129, v0
	v_add_f32_e32 v1, v129, v1
	v_mul_f32_e32 v0, 0xbfb8aa3b, v0
	v_mul_f32_e32 v1, 0xbfb8aa3b, v1
	v_exp_f32_e32 v0, v0
	v_exp_f32_e32 v1, v1
	ds_read_u16 v16, v228
	ds_read_u16 v17, v230 offset:17424
	ds_read_u16 v20, v230 offset:17952
	ds_read_u16 v21, v230 offset:18480
	ds_read_u16 v27, v230 offset:21120
	ds_read_u16 v28, v230 offset:21648
	ds_read_u16 v30, v230 offset:22176
	ds_read_u16 v29, v230 offset:22704
	ds_read_u16 v33, v230 offset:25344
	s_waitcnt lgkmcnt(7)
	v_lshlrev_b32_e32 v17, 16, v17
	v_add_f32_e32 v0, 1.0, v0
	v_add_f32_e32 v1, 1.0, v1
	v_rcp_f32_e32 v0, v0
	v_rcp_f32_e32 v1, v1
	v_lshlrev_b32_e32 v16, 16, v16
	v_add_f32_e32 v2, v129, v2
	v_mul_f32_e32 v2, 0xbfb8aa3b, v2
	v_pk_mul_f32 v[16:17], v[0:1], v[16:17]
	s_waitcnt lgkmcnt(5)
	v_lshlrev_b32_e32 v21, 16, v21
	v_pk_mul_f32 v[0:1], v[16:17], v[16:17]
	ds_bpermute_b32 v0, v185, v0
	ds_bpermute_b32 v1, v185, v1
	v_lshlrev_b32_e32 v20, 16, v20
	v_add_f32_e32 v6, v129, v6
	v_mul_f32_e32 v6, 0xbfb8aa3b, v6
	s_waitcnt lgkmcnt(3)
	v_lshlrev_b32_e32 v29, 16, v29
	s_waitcnt lgkmcnt(0)
	v_pk_fma_f32 v[0:1], v[16:17], v[16:17], v[0:1]
	s_nop 1
	v_mov_b32_dpp v18, v0 row_ror:8 row_mask:0xf bank_mask:0xf
	s_nop 0
	v_mov_b32_dpp v19, v1 row_ror:8 row_mask:0xf bank_mask:0xf
	ds_read_u16 v44, v230 offset:31152
	ds_read_u16 v34, v230 offset:25872
	ds_read_u16 v40, v230 offset:26400
	ds_read_u16 v41, v230 offset:26928
	ds_read_u16 v45, v230 offset:29568
	ds_read_u16 v46, v230 offset:30096
	ds_read_u16 v47, v230 offset:30624
	v_add_f32_e32 v12, v129, v12
	v_mul_f32_e32 v12, 0xbfb8aa3b, v12
	s_waitcnt lgkmcnt(0)
	v_pk_add_f32 v[0:1], v[0:1], v[18:19]
	v_exp_f32_e32 v18, v2
	v_add_f32_e32 v2, v129, v3
	v_mul_f32_e32 v2, 0xbfb8aa3b, v2
	v_exp_f32_e32 v3, v2
	s_nop 0
	v_mov_b32_dpp v2, v0 row_half_mirror row_mask:0xf bank_mask:0xf
	s_nop 1
	v_mov_b32_dpp v2, v2 quad_perm:[3,2,1,0] row_mask:0xf bank_mask:0xf
	v_add_f32_e32 v18, 1.0, v18
	v_rcp_f32_e32 v18, v18
	v_add_f32_e32 v3, 1.0, v3
	v_rcp_f32_e32 v19, v3
	s_nop 0
	v_mov_b32_dpp v3, v1 row_half_mirror row_mask:0xf bank_mask:0xf
	s_nop 1
	v_mov_b32_dpp v3, v3 quad_perm:[3,2,1,0] row_mask:0xf bank_mask:0xf
	v_add_f32_e32 v14, v129, v14
	v_mul_f32_e32 v14, 0xbfb8aa3b, v14
	v_pk_mul_f32 v[18:19], v[18:19], v[20:21]
	s_waitcnt lgkmcnt(0)
	v_pk_add_f32 v[0:1], v[0:1], v[2:3]
	s_nop 1
	v_mov_b32_dpp v2, v0 quad_perm:[2,3,0,1] row_mask:0xf bank_mask:0xf
	s_nop 0
	v_mov_b32_dpp v3, v1 quad_perm:[2,3,0,1] row_mask:0xf bank_mask:0xf
	v_pk_mul_f32 v[20:21], v[18:19], v[18:19]
	ds_bpermute_b32 v20, v185, v20
	ds_bpermute_b32 v21, v185, v21
	s_waitcnt lgkmcnt(0)
	v_pk_add_f32 v[24:25], v[0:1], v[2:3]
	v_add_f32_e32 v2, v129, v4
	v_mul_f32_e32 v2, 0xbfb8aa3b, v2
	v_exp_f32_e32 v3, v2
	v_add_f32_e32 v2, v129, v5
	v_mul_f32_e32 v2, 0xbfb8aa3b, v2
	v_exp_f32_e32 v5, v2
	s_waitcnt lgkmcnt(0)
	v_pk_fma_f32 v[20:21], v[18:19], v[18:19], v[20:21]
	s_nop 1
	v_mov_b32_dpp v22, v20 row_ror:8 row_mask:0xf bank_mask:0xf
	s_nop 0
	v_mov_b32_dpp v23, v21 row_ror:8 row_mask:0xf bank_mask:0xf
	v_add_f32_e32 v3, 1.0, v3
	v_rcp_f32_e32 v4, v3
	v_add_f32_e32 v3, 1.0, v5
	v_rcp_f32_e32 v5, v3
	s_waitcnt lgkmcnt(0)
	v_pk_add_f32 v[0:1], v[20:21], v[22:23]
	v_lshlrev_b32_e32 v21, 16, v28
	v_lshlrev_b32_e32 v20, 16, v27
	v_pk_mul_f32 v[20:21], v[4:5], v[20:21]
	v_exp_f32_e32 v22, v6
	v_add_f32_e32 v6, v129, v7
	v_pk_mul_f32 v[4:5], v[20:21], v[20:21]
	v_mul_f32_e32 v6, 0xbfb8aa3b, v6
	v_mov_b32_dpp v2, v0 row_half_mirror row_mask:0xf bank_mask:0xf
	s_nop 1
	v_mov_b32_dpp v2, v2 quad_perm:[3,2,1,0] row_mask:0xf bank_mask:0xf
	v_mov_b32_dpp v3, v1 row_half_mirror row_mask:0xf bank_mask:0xf
	s_nop 1
	v_mov_b32_dpp v3, v3 quad_perm:[3,2,1,0] row_mask:0xf bank_mask:0xf
	ds_bpermute_b32 v4, v185, v4
	ds_bpermute_b32 v5, v185, v5
	v_exp_f32_e32 v7, v6
	v_add_f32_e32 v22, 1.0, v22
	s_waitcnt lgkmcnt(0)
	v_pk_add_f32 v[0:1], v[0:1], v[2:3]
	v_rcp_f32_e32 v22, v22
	v_add_f32_e32 v7, 1.0, v7
	s_waitcnt lgkmcnt(0)
	v_pk_fma_f32 v[4:5], v[20:21], v[20:21], v[4:5]
	v_rcp_f32_e32 v23, v7
	v_mov_b32_dpp v2, v0 quad_perm:[2,3,0,1] row_mask:0xf bank_mask:0xf
	v_mov_b32_dpp v3, v1 quad_perm:[2,3,0,1] row_mask:0xf bank_mask:0xf
	v_mov_b32_dpp v6, v4 row_ror:8 row_mask:0xf bank_mask:0xf
	v_mov_b32_dpp v7, v5 row_ror:8 row_mask:0xf bank_mask:0xf
	v_lshlrev_b32_e32 v28, 16, v30
	v_pk_mul_f32 v[22:23], v[22:23], v[28:29]
	v_mov_b32_dpp v26, v24 quad_perm:[1,0,3,2] row_mask:0xf bank_mask:0xf
	v_pk_mul_f32 v[28:29], v[22:23], v[22:23]
	ds_bpermute_b32 v30, v185, v28
	ds_bpermute_b32 v31, v185, v29
	s_waitcnt lgkmcnt(0)
	v_pk_add_f32 v[28:29], v[0:1], v[2:3]
	s_waitcnt lgkmcnt(0)
	v_pk_add_f32 v[0:1], v[4:5], v[6:7]
	s_nop 1
	v_mov_b32_dpp v2, v0 row_half_mirror row_mask:0xf bank_mask:0xf
	s_nop 1
	v_mov_b32_dpp v2, v2 quad_perm:[3,2,1,0] row_mask:0xf bank_mask:0xf
	v_mov_b32_dpp v3, v1 row_half_mirror row_mask:0xf bank_mask:0xf
	s_nop 1
	v_mov_b32_dpp v3, v3 quad_perm:[3,2,1,0] row_mask:0xf bank_mask:0xf
	s_waitcnt lgkmcnt(0)
	v_pk_fma_f32 v[4:5], v[22:23], v[22:23], v[30:31]
	s_nop 1
	v_mov_b32_dpp v6, v4 row_ror:8 row_mask:0xf bank_mask:0xf
	s_nop 0
	v_mov_b32_dpp v7, v5 row_ror:8 row_mask:0xf bank_mask:0xf
	v_mov_b32_dpp v27, v25 quad_perm:[1,0,3,2] row_mask:0xf bank_mask:0xf
	s_waitcnt lgkmcnt(0)
	v_pk_add_f32 v[2:3], v[0:1], v[2:3]
	v_add_f32_e32 v0, v129, v8
	v_add_f32_e32 v1, v129, v9
	v_mul_f32_e32 v0, 0xbfb8aa3b, v0
	v_mul_f32_e32 v1, 0xbfb8aa3b, v1
	v_exp_f32_e32 v0, v0
	v_exp_f32_e32 v1, v1
	v_lshlrev_b32_e32 v9, 16, v34
	v_lshlrev_b32_e32 v8, 16, v33
	v_add_f32_e32 v0, 1.0, v0
	v_add_f32_e32 v1, 1.0, v1
	v_rcp_f32_e32 v0, v0
	v_rcp_f32_e32 v1, v1
	v_mov_b32_dpp v32, v2 quad_perm:[2,3,0,1] row_mask:0xf bank_mask:0xf
	v_mov_b32_dpp v33, v3 quad_perm:[2,3,0,1] row_mask:0xf bank_mask:0xf
	s_waitcnt lgkmcnt(0)
	v_pk_add_f32 v[4:5], v[4:5], v[6:7]
	v_pk_mul_f32 v[0:1], v[0:1], v[8:9]
	s_nop 0
	v_mov_b32_dpp v6, v4 row_half_mirror row_mask:0xf bank_mask:0xf
	s_nop 1
	v_mov_b32_dpp v6, v6 quad_perm:[3,2,1,0] row_mask:0xf bank_mask:0xf
	v_pk_mul_f32 v[8:9], v[0:1], v[0:1]
	ds_bpermute_b32 v8, v185, v8
	ds_bpermute_b32 v9, v185, v9
	v_mov_b32_dpp v7, v5 row_half_mirror row_mask:0xf bank_mask:0xf
	s_nop 1
	v_mov_b32_dpp v7, v7 quad_perm:[3,2,1,0] row_mask:0xf bank_mask:0xf
	v_mov_b32_dpp v30, v28 quad_perm:[1,0,3,2] row_mask:0xf bank_mask:0xf
	v_mov_b32_dpp v31, v29 quad_perm:[1,0,3,2] row_mask:0xf bank_mask:0xf
	s_waitcnt lgkmcnt(0)
	v_pk_fma_f32 v[36:37], v[0:1], v[0:1], v[8:9]
	v_pk_add_f32 v[8:9], v[2:3], v[32:33]
	v_add_f32_e32 v2, v129, v10
	v_add_f32_e32 v3, v129, v11
	v_mul_f32_e32 v2, 0xbfb8aa3b, v2
	v_mul_f32_e32 v3, 0xbfb8aa3b, v3
	v_exp_f32_e32 v2, v2
	v_exp_f32_e32 v3, v3
	s_waitcnt lgkmcnt(0)
	v_pk_add_f32 v[4:5], v[4:5], v[6:7]
	s_nop 1
	v_mov_b32_dpp v6, v4 quad_perm:[2,3,0,1] row_mask:0xf bank_mask:0xf
	v_add_f32_e32 v2, 1.0, v2
	v_add_f32_e32 v3, 1.0, v3
	v_mov_b32_dpp v7, v5 quad_perm:[2,3,0,1] row_mask:0xf bank_mask:0xf
	v_mov_b32_dpp v38, v36 row_ror:8 row_mask:0xf bank_mask:0xf
	v_mov_b32_dpp v39, v37 row_ror:8 row_mask:0xf bank_mask:0xf
	v_rcp_f32_e32 v2, v2
	v_rcp_f32_e32 v3, v3
	v_lshlrev_b32_e32 v11, 16, v41
	v_lshlrev_b32_e32 v10, 16, v40
	s_waitcnt lgkmcnt(0)
	v_pk_add_f32 v[34:35], v[4:5], v[6:7]
	v_pk_mul_f32 v[2:3], v[2:3], v[10:11]
	s_waitcnt lgkmcnt(0)
	v_pk_add_f32 v[4:5], v[36:37], v[38:39]
	v_pk_mul_f32 v[10:11], v[2:3], v[2:3]
	s_nop 0
	v_mov_b32_dpp v6, v4 row_half_mirror row_mask:0xf bank_mask:0xf
	s_nop 1
	v_mov_b32_dpp v6, v6 quad_perm:[3,2,1,0] row_mask:0xf bank_mask:0xf
	v_mov_b32_dpp v7, v5 row_half_mirror row_mask:0xf bank_mask:0xf
	s_nop 1
	v_mov_b32_dpp v7, v7 quad_perm:[3,2,1,0] row_mask:0xf bank_mask:0xf
	ds_bpermute_b32 v36, v185, v10
	ds_bpermute_b32 v37, v185, v11
	v_mov_b32_dpp v32, v8 quad_perm:[1,0,3,2] row_mask:0xf bank_mask:0xf
	v_mov_b32_dpp v33, v9 quad_perm:[1,0,3,2] row_mask:0xf bank_mask:0xf
	s_waitcnt lgkmcnt(0)
	v_pk_add_f32 v[4:5], v[4:5], v[6:7]
	s_nop 1
	v_mov_b32_dpp v6, v4 quad_perm:[2,3,0,1] row_mask:0xf bank_mask:0xf
	s_waitcnt lgkmcnt(0)
	v_pk_fma_f32 v[40:41], v[2:3], v[2:3], v[36:37]
	v_mov_b32_dpp v7, v5 quad_perm:[2,3,0,1] row_mask:0xf bank_mask:0xf
	s_nop 0
	v_mov_b32_dpp v42, v40 row_ror:8 row_mask:0xf bank_mask:0xf
	v_mov_b32_dpp v43, v41 row_ror:8 row_mask:0xf bank_mask:0xf
	v_mov_b32_dpp v10, v34 quad_perm:[1,0,3,2] row_mask:0xf bank_mask:0xf
	v_mov_b32_dpp v11, v35 quad_perm:[1,0,3,2] row_mask:0xf bank_mask:0xf
	s_waitcnt lgkmcnt(0)
	v_pk_add_f32 v[36:37], v[4:5], v[6:7]
	s_nop 1
	v_mov_b32_dpp v38, v36 quad_perm:[1,0,3,2] row_mask:0xf bank_mask:0xf
	s_waitcnt lgkmcnt(0)
	v_pk_add_f32 v[4:5], v[40:41], v[42:43]
	v_exp_f32_e32 v40, v12
	v_add_f32_e32 v12, v129, v13
	v_mov_b32_dpp v6, v4 row_half_mirror row_mask:0xf bank_mask:0xf
	s_nop 1
	v_mov_b32_dpp v6, v6 quad_perm:[3,2,1,0] row_mask:0xf bank_mask:0xf
	v_mov_b32_dpp v7, v5 row_half_mirror row_mask:0xf bank_mask:0xf
	s_nop 1
	v_mov_b32_dpp v7, v7 quad_perm:[3,2,1,0] row_mask:0xf bank_mask:0xf
	v_mul_f32_e32 v12, 0xbfb8aa3b, v12
	v_exp_f32_e32 v41, v12
	v_mov_b32_dpp v39, v37 quad_perm:[1,0,3,2] row_mask:0xf bank_mask:0xf
	s_waitcnt lgkmcnt(0)
	v_pk_add_f32 v[12:13], v[4:5], v[6:7]
	v_add_f32_e32 v4, 1.0, v40
	v_add_f32_e32 v5, 1.0, v41
	v_rcp_f32_e32 v4, v4
	v_rcp_f32_e32 v5, v5
	v_exp_f32_e32 v41, v14
	v_add_f32_e32 v14, v129, v15
	v_mul_f32_e32 v14, 0xbfb8aa3b, v14
	v_lshlrev_b32_e32 v7, 16, v46
	v_lshlrev_b32_e32 v6, 16, v45
	v_exp_f32_e32 v15, v14
	v_pk_mul_f32 v[4:5], v[4:5], v[6:7]
	v_mov_b32_dpp v40, v12 quad_perm:[2,3,0,1] row_mask:0xf bank_mask:0xf
	v_pk_mul_f32 v[6:7], v[4:5], v[4:5]
	ds_bpermute_b32 v14, v185, v6
	v_add_f32_e32 v6, 1.0, v41
	v_rcp_f32_e32 v42, v6
	v_add_f32_e32 v6, 1.0, v15
	v_rcp_f32_e32 v43, v6
	ds_bpermute_b32 v15, v185, v7
	v_lshlrev_b32_e32 v7, 16, v44
	v_lshlrev_b32_e32 v6, 16, v47
	v_pk_mul_f32 v[6:7], v[42:43], v[6:7]
	v_mov_b32_dpp v41, v13 quad_perm:[2,3,0,1] row_mask:0xf bank_mask:0xf
	v_pk_mul_f32 v[42:43], v[6:7], v[6:7]
	ds_bpermute_b32 v42, v185, v42
	ds_bpermute_b32 v43, v185, v43
	s_waitcnt lgkmcnt(0)
	v_pk_fma_f32 v[14:15], v[4:5], v[4:5], v[14:15]
	s_nop 1
	v_mov_b32_dpp v44, v14 row_ror:8 row_mask:0xf bank_mask:0xf
	s_nop 0
	v_mov_b32_dpp v45, v15 row_ror:8 row_mask:0xf bank_mask:0xf
	s_waitcnt lgkmcnt(0)
	v_pk_add_f32 v[12:13], v[12:13], v[40:41]
	s_waitcnt lgkmcnt(0)
	v_pk_fma_f32 v[42:43], v[6:7], v[6:7], v[42:43]
	s_nop 1
	v_mov_b32_dpp v46, v42 row_ror:8 row_mask:0xf bank_mask:0xf
	s_nop 0
	v_mov_b32_dpp v47, v43 row_ror:8 row_mask:0xf bank_mask:0xf
	s_waitcnt lgkmcnt(0)
	v_pk_add_f32 v[40:41], v[14:15], v[44:45]
	s_nop 1
	v_mov_b32_dpp v44, v40 row_half_mirror row_mask:0xf bank_mask:0xf
	s_nop 1
	v_mov_b32_dpp v44, v44 quad_perm:[3,2,1,0] row_mask:0xf bank_mask:0xf
	v_mov_b32_dpp v45, v41 row_half_mirror row_mask:0xf bank_mask:0xf
	s_nop 1
	v_mov_b32_dpp v45, v45 quad_perm:[3,2,1,0] row_mask:0xf bank_mask:0xf
	v_mov_b32_dpp v14, v12 quad_perm:[1,0,3,2] row_mask:0xf bank_mask:0xf
	s_waitcnt lgkmcnt(0)
	v_pk_add_f32 v[42:43], v[42:43], v[46:47]
	s_nop 1
	v_mov_b32_dpp v46, v42 row_half_mirror row_mask:0xf bank_mask:0xf
	s_nop 1
	v_mov_b32_dpp v46, v46 quad_perm:[3,2,1,0] row_mask:0xf bank_mask:0xf
	v_mov_b32_dpp v47, v43 row_half_mirror row_mask:0xf bank_mask:0xf
	s_nop 1
	v_mov_b32_dpp v47, v47 quad_perm:[3,2,1,0] row_mask:0xf bank_mask:0xf
	s_waitcnt lgkmcnt(0)
	v_pk_add_f32 v[40:41], v[40:41], v[44:45]
	s_nop 1
	v_mov_b32_dpp v44, v40 quad_perm:[2,3,0,1] row_mask:0xf bank_mask:0xf
	s_nop 0
	v_mov_b32_dpp v45, v41 quad_perm:[2,3,0,1] row_mask:0xf bank_mask:0xf
	v_mov_b32_dpp v15, v13 quad_perm:[1,0,3,2] row_mask:0xf bank_mask:0xf
	s_waitcnt lgkmcnt(0)
	v_pk_add_f32 v[46:47], v[42:43], v[46:47]
	s_nop 1
	v_mov_b32_dpp v48, v46 quad_perm:[2,3,0,1] row_mask:0xf bank_mask:0xf
	s_nop 0
	v_mov_b32_dpp v49, v47 quad_perm:[2,3,0,1] row_mask:0xf bank_mask:0xf
	s_waitcnt lgkmcnt(0)
	v_pk_add_f32 v[40:41], v[40:41], v[44:45]
	s_nop 1
	v_mov_b32_dpp v42, v40 quad_perm:[1,0,3,2] row_mask:0xf bank_mask:0xf
	s_nop 0
	v_mov_b32_dpp v43, v41 quad_perm:[1,0,3,2] row_mask:0xf bank_mask:0xf
	s_waitcnt lgkmcnt(0)
	v_pk_add_f32 v[44:45], v[46:47], v[48:49]
	s_nop 1
	v_mov_b32_dpp v46, v44 quad_perm:[1,0,3,2] row_mask:0xf bank_mask:0xf
	s_nop 0
	v_mov_b32_dpp v47, v45 quad_perm:[1,0,3,2] row_mask:0xf bank_mask:0xf
	s_and_saveexec_b64 s[6:7], s[48:49]
	s_cbranch_execz .LBB0_362
	v_pk_add_f32 v[8:9], v[8:9], v[32:33]
	v_pk_add_f32 v[10:11], v[34:35], v[10:11]
	ds_write_b128 v231, v[8:11] offset:33952
	v_pk_add_f32 v[8:9], v[36:37], v[38:39]
	v_pk_add_f32 v[10:11], v[12:13], v[14:15]
	v_pk_add_f32 v[24:25], v[24:25], v[26:27]
	v_pk_add_f32 v[26:27], v[28:29], v[30:31]
	ds_write_b128 v231, v[8:11] offset:33984
	s_waitcnt lgkmcnt(4)
	v_pk_add_f32 v[8:9], v[40:41], v[42:43]
	s_waitcnt lgkmcnt(2)
	v_pk_add_f32 v[10:11], v[44:45], v[46:47]
	ds_write_b128 v231, v[24:27] offset:33920
	ds_write_b128 v231, v[8:11] offset:34016

.LBB0_532:
	s_add_i32 s8, s11, s8
	s_ashr_i32 s9, s8, 31
	s_lshr_b32 s9, s9, 27
	s_add_i32 s9, s8, s9
	s_ashr_i32 s10, s9, 5
	s_andn2_b32 s9, s9, 31
	s_sub_i32 s8, s8, s9
	s_lshl_b32 s9, s10, 3
	s_sub_i32 s10, 64, s9
	s_min_i32 s10, s10, 8
	s_abs_i32 s18, s10
	v_cvt_f32_u32_e32 v0, s18
	s_sub_i32 s19, 0, s18
	s_abs_i32 s17, s8
	s_xor_b32 s11, s8, s10
	v_rcp_iflag_f32_e32 v0, v0
	s_ashr_i32 s11, s11, 31
	s_barrier
	v_mul_f32_e32 v0, 0x4f7ffffe, v0
	v_cvt_u32_f32_e32 v0, v0
	v_mov_b32_e32 v135, v145
	v_readfirstlane_b32 s20, v0
	s_mul_i32 s19, s19, s20
	s_mul_hi_u32 s19, s20, s19
	s_add_i32 s20, s20, s19
	s_mul_hi_u32 s19, s17, s20
	s_mul_i32 s20, s19, s18
	s_sub_i32 s17, s17, s20
	s_add_i32 s20, s19, 1
	s_sub_i32 s21, s17, s18
	s_cmp_ge_u32 s17, s18
	s_cselect_b32 s19, s20, s19
	s_cselect_b32 s17, s21, s17
	s_add_i32 s20, s19, 1
	s_cmp_ge_u32 s17, s18
	s_cselect_b32 s17, s20, s19
	s_xor_b32 s17, s17, s11
	s_sub_i32 s11, s17, s11
	s_mul_i32 s10, s11, s10
	s_sub_i32 s8, s8, s10
	s_add_i32 s9, s9, s8
	s_ashr_i32 s17, s9, 4
	v_lshl_add_u32 v0, s17, 8, v128
	v_ashrrev_i32_e32 v1, 31, v0
	s_lshl_b32 s8, s11, 8
	s_lshl_b32 s10, s9, 8
	v_lshlrev_b64 v[0:1], 12, v[0:1]
	s_ashr_i32 s9, s8, 31
	v_lshl_add_u64 v[0:1], s[6:7], 0, v[0:1]
	s_lshl_b64 s[8:9], s[8:9], 1
	v_lshl_add_u64 v[0:1], v[0:1], 0, s[8:9]
	v_lshl_add_u64 v[16:17], v[0:1], 0, v[144:145]
	global_load_dwordx4 v[0:3], v[16:17], off offset:48
	global_load_dwordx4 v[4:7], v[16:17], off offset:32
	global_load_dwordx4 v[8:11], v[16:17], off offset:16
	global_load_dwordx4 v[12:15], v[16:17], off
	s_waitcnt vmcnt(0)
	ds_write_b128 v142, v[12:15]
	ds_write_b128 v142, v[8:11] offset:16
	ds_write_b128 v142, v[4:7] offset:32
	ds_write_b128 v142, v[0:3] offset:48
	global_load_dwordx4 v[0:3], v[16:17], off offset:112
	global_load_dwordx4 v[4:7], v[16:17], off offset:96
	global_load_dwordx4 v[8:11], v[16:17], off offset:80
	global_load_dwordx4 v[12:15], v[16:17], off offset:64
	s_waitcnt vmcnt(0)
	ds_write_b128 v142, v[12:15] offset:64
	ds_write_b128 v142, v[8:11] offset:80
	ds_write_b128 v142, v[4:7] offset:96
	ds_write_b128 v142, v[0:3] offset:112
	global_load_dwordx4 v[0:3], v[16:17], off offset:176
	global_load_dwordx4 v[4:7], v[16:17], off offset:160
	global_load_dwordx4 v[8:11], v[16:17], off offset:144
	global_load_dwordx4 v[12:15], v[16:17], off offset:128
	s_waitcnt vmcnt(0)
	ds_write_b128 v142, v[12:15] offset:128
	ds_write_b128 v142, v[8:11] offset:144
	ds_write_b128 v142, v[4:7] offset:160
	ds_write_b128 v142, v[0:3] offset:176
	global_load_dwordx4 v[0:3], v[16:17], off offset:240
	global_load_dwordx4 v[4:7], v[16:17], off offset:224
	global_load_dwordx4 v[8:11], v[16:17], off offset:208
	global_load_dwordx4 v[12:15], v[16:17], off offset:192
	s_waitcnt vmcnt(0)
	ds_write_b128 v142, v[12:15] offset:192
	ds_write_b128 v142, v[8:11] offset:208
	ds_write_b128 v142, v[4:7] offset:224
	ds_write_b128 v142, v[0:3] offset:240
	v_add_u32_e32 v0, s10, v141
	v_or_b32_e32 v0, v0, v140
	v_ashrrev_i32_e32 v1, 31, v0
	v_lshlrev_b64 v[0:1], 11, v[0:1]
	v_lshl_add_u64 v[0:1], s[92:93], 0, v[0:1]
	v_lshl_add_u64 v[0:1], v[0:1], 0, s[8:9]
	v_lshl_add_u64 v[136:137], v[0:1], 0, v[134:135]
	s_waitcnt lgkmcnt(0)
	s_barrier
	global_load_dwordx4 v[0:3], v[136:137], off
	global_load_dwordx4 v[160:163], v[136:137], off offset:32
	global_load_dwordx4 v[164:167], v[136:137], off offset:64
	global_load_dwordx4 v[168:171], v[136:137], off offset:96
	ds_read_b128 v[4:7], v129
	ds_read_b128 v[8:11], v129 offset:32
	ds_read_b128 v[12:15], v129 offset:64
	ds_read_b128 v[16:19], v129 offset:96
	s_waitcnt vmcnt(3) lgkmcnt(3)
	v_mfma_f32_32x32x16_bf16 v[112:127], v[4:7], v[0:3], 0
	s_waitcnt vmcnt(2) lgkmcnt(2)
	v_mfma_f32_32x32x16_bf16 v[112:127], v[8:11], v[160:163], v[112:127]
	s_waitcnt vmcnt(1) lgkmcnt(1)
	v_mfma_f32_32x32x16_bf16 v[112:127], v[12:15], v[164:167], v[112:127]
	s_waitcnt vmcnt(0) lgkmcnt(0)
	v_mfma_f32_32x32x16_bf16 v[112:127], v[16:19], v[168:171], v[112:127]
	ds_read_b128 v[4:7], v129 offset:16896
	ds_read_b128 v[8:11], v129 offset:16928
	ds_read_b128 v[12:15], v129 offset:16960
	ds_read_b128 v[16:19], v129 offset:16992
	s_waitcnt lgkmcnt(3)
	v_mfma_f32_32x32x16_bf16 v[96:111], v[4:7], v[0:3], 0
	s_waitcnt lgkmcnt(2)
	v_mfma_f32_32x32x16_bf16 v[96:111], v[8:11], v[160:163], v[96:111]
	s_waitcnt lgkmcnt(1)
	v_mfma_f32_32x32x16_bf16 v[96:111], v[12:15], v[164:167], v[96:111]
	s_waitcnt lgkmcnt(0)
	v_mfma_f32_32x32x16_bf16 v[96:111], v[16:19], v[168:171], v[96:111]
	ds_read_b128 v[4:7], v129 offset:33792
	ds_read_b128 v[8:11], v129 offset:33824
	ds_read_b128 v[12:15], v129 offset:33856
	ds_read_b128 v[16:19], v129 offset:33888
	s_waitcnt lgkmcnt(3)
	v_mfma_f32_32x32x16_bf16 v[80:95], v[4:7], v[0:3], 0
	s_waitcnt lgkmcnt(2)
	v_mfma_f32_32x32x16_bf16 v[80:95], v[8:11], v[160:163], v[80:95]
	s_waitcnt lgkmcnt(1)
	v_mfma_f32_32x32x16_bf16 v[80:95], v[12:15], v[164:167], v[80:95]
	s_waitcnt lgkmcnt(0)
	v_mfma_f32_32x32x16_bf16 v[80:95], v[16:19], v[168:171], v[80:95]
	ds_read_b128 v[4:7], v129 offset:50688
	ds_read_b128 v[8:11], v129 offset:50720
	ds_read_b128 v[12:15], v129 offset:50752
	ds_read_b128 v[16:19], v129 offset:50784
	s_waitcnt lgkmcnt(3)
	v_mfma_f32_32x32x16_bf16 v[64:79], v[4:7], v[0:3], 0
	s_waitcnt lgkmcnt(2)
	v_mfma_f32_32x32x16_bf16 v[64:79], v[8:11], v[160:163], v[64:79]
	s_waitcnt lgkmcnt(1)
	v_mfma_f32_32x32x16_bf16 v[64:79], v[12:15], v[164:167], v[64:79]
	s_waitcnt lgkmcnt(0)
	v_mfma_f32_32x32x16_bf16 v[64:79], v[16:19], v[168:171], v[64:79]
	ds_read_b128 v[4:7], v156
	ds_read_b128 v[8:11], v156 offset:32
	ds_read_b128 v[12:15], v156 offset:64
	ds_read_b128 v[16:19], v156 offset:96
	s_waitcnt lgkmcnt(3)
	v_mfma_f32_32x32x16_bf16 v[48:63], v[4:7], v[0:3], 0
	s_waitcnt lgkmcnt(2)
	v_mfma_f32_32x32x16_bf16 v[48:63], v[8:11], v[160:163], v[48:63]
	s_waitcnt lgkmcnt(1)
	v_mfma_f32_32x32x16_bf16 v[48:63], v[12:15], v[164:167], v[48:63]
	s_waitcnt lgkmcnt(0)
	v_mfma_f32_32x32x16_bf16 v[48:63], v[16:19], v[168:171], v[48:63]
	ds_read_b128 v[4:7], v157
	ds_read_b128 v[8:11], v157 offset:32
	ds_read_b128 v[12:15], v157 offset:64
	ds_read_b128 v[16:19], v157 offset:96
	s_waitcnt lgkmcnt(3)
	v_mfma_f32_32x32x16_bf16 v[32:47], v[4:7], v[0:3], 0
	s_waitcnt lgkmcnt(2)
	v_mfma_f32_32x32x16_bf16 v[32:47], v[8:11], v[160:163], v[32:47]
	s_waitcnt lgkmcnt(1)
	v_mfma_f32_32x32x16_bf16 v[32:47], v[12:15], v[164:167], v[32:47]
	s_waitcnt lgkmcnt(0)
	v_mfma_f32_32x32x16_bf16 v[32:47], v[16:19], v[168:171], v[32:47]
	ds_read_b128 v[4:7], v158
	ds_read_b128 v[8:11], v158 offset:32
	ds_read_b128 v[12:15], v158 offset:64
	ds_read_b128 v[176:179], v158 offset:96
	s_waitcnt lgkmcnt(3)
	v_mfma_f32_32x32x16_bf16 v[16:31], v[4:7], v[0:3], 0
	s_waitcnt lgkmcnt(2)
	v_mfma_f32_32x32x16_bf16 v[16:31], v[8:11], v[160:163], v[16:31]
	s_waitcnt lgkmcnt(1)
	v_mfma_f32_32x32x16_bf16 v[16:31], v[12:15], v[164:167], v[16:31]
	s_waitcnt lgkmcnt(0)
	v_mfma_f32_32x32x16_bf16 v[16:31], v[176:179], v[168:171], v[16:31]
	ds_read_b128 v[4:7], v159
	ds_read_b128 v[176:179], v159 offset:32
	ds_read_b128 v[180:183], v159 offset:64
	ds_read_b128 v[206:209], v159 offset:96
	s_waitcnt lgkmcnt(3)
	v_mfma_f32_32x32x16_bf16 v[0:15], v[4:7], v[0:3], 0
	s_waitcnt lgkmcnt(2)
	v_mfma_f32_32x32x16_bf16 v[0:15], v[176:179], v[160:163], v[0:15]
	s_waitcnt lgkmcnt(1)
	v_mfma_f32_32x32x16_bf16 v[0:15], v[180:183], v[164:167], v[0:15]
	s_waitcnt lgkmcnt(0)
	v_mfma_f32_32x32x16_bf16 v[0:15], v[206:209], v[168:171], v[0:15]
	global_load_dwordx4 v[160:163], v[136:137], off offset:128
	global_load_dwordx4 v[164:167], v[136:137], off offset:160
	global_load_dwordx4 v[168:171], v[136:137], off offset:192
	global_load_dwordx4 v[176:179], v[136:137], off offset:224
	ds_read_b128 v[180:183], v129 offset:128
	ds_read_b128 v[206:209], v129 offset:160
	ds_read_b128 v[210:213], v129 offset:192
	ds_read_b128 v[214:217], v129 offset:224
	s_waitcnt vmcnt(3) lgkmcnt(3)
	v_mfma_f32_32x32x16_bf16 v[112:127], v[180:183], v[160:163], v[112:127]
	s_waitcnt vmcnt(2) lgkmcnt(2)
	v_mfma_f32_32x32x16_bf16 v[112:127], v[206:209], v[164:167], v[112:127]
	s_waitcnt vmcnt(1) lgkmcnt(1)
	v_mfma_f32_32x32x16_bf16 v[112:127], v[210:213], v[168:171], v[112:127]
	s_waitcnt vmcnt(0) lgkmcnt(0)
	v_mfma_f32_32x32x16_bf16 v[112:127], v[214:217], v[176:179], v[112:127]
	ds_read_b128 v[180:183], v129 offset:17024
	ds_read_b128 v[206:209], v129 offset:17056
	ds_read_b128 v[210:213], v129 offset:17088
	ds_read_b128 v[214:217], v129 offset:17120
	s_waitcnt lgkmcnt(3)
	v_mfma_f32_32x32x16_bf16 v[96:111], v[180:183], v[160:163], v[96:111]
	s_waitcnt lgkmcnt(2)
	v_mfma_f32_32x32x16_bf16 v[96:111], v[206:209], v[164:167], v[96:111]
	s_waitcnt lgkmcnt(1)
	v_mfma_f32_32x32x16_bf16 v[96:111], v[210:213], v[168:171], v[96:111]
	s_waitcnt lgkmcnt(0)
	v_mfma_f32_32x32x16_bf16 v[96:111], v[214:217], v[176:179], v[96:111]
	ds_read_b128 v[180:183], v129 offset:33920
	ds_read_b128 v[206:209], v129 offset:33952
	ds_read_b128 v[210:213], v129 offset:33984
	ds_read_b128 v[214:217], v129 offset:34016
	s_waitcnt lgkmcnt(3)
	v_mfma_f32_32x32x16_bf16 v[80:95], v[180:183], v[160:163], v[80:95]
	s_waitcnt lgkmcnt(2)
	v_mfma_f32_32x32x16_bf16 v[80:95], v[206:209], v[164:167], v[80:95]
	s_waitcnt lgkmcnt(1)
	v_mfma_f32_32x32x16_bf16 v[80:95], v[210:213], v[168:171], v[80:95]
	s_waitcnt lgkmcnt(0)
	v_mfma_f32_32x32x16_bf16 v[80:95], v[214:217], v[176:179], v[80:95]
	ds_read_b128 v[180:183], v129 offset:50816
	ds_read_b128 v[206:209], v129 offset:50848
	ds_read_b128 v[210:213], v129 offset:50880
	ds_read_b128 v[214:217], v129 offset:50912
	s_waitcnt lgkmcnt(3)
	v_mfma_f32_32x32x16_bf16 v[64:79], v[180:183], v[160:163], v[64:79]
	s_waitcnt lgkmcnt(2)
	v_mfma_f32_32x32x16_bf16 v[64:79], v[206:209], v[164:167], v[64:79]
	s_waitcnt lgkmcnt(1)
	v_mfma_f32_32x32x16_bf16 v[64:79], v[210:213], v[168:171], v[64:79]
	s_waitcnt lgkmcnt(0)
	v_mfma_f32_32x32x16_bf16 v[64:79], v[214:217], v[176:179], v[64:79]
	ds_read_b128 v[180:183], v156 offset:128
	ds_read_b128 v[206:209], v156 offset:160
	ds_read_b128 v[210:213], v156 offset:192
	ds_read_b128 v[214:217], v156 offset:224
	s_waitcnt lgkmcnt(3)
	v_mfma_f32_32x32x16_bf16 v[48:63], v[180:183], v[160:163], v[48:63]
	s_waitcnt lgkmcnt(2)
	v_mfma_f32_32x32x16_bf16 v[48:63], v[206:209], v[164:167], v[48:63]
	s_waitcnt lgkmcnt(1)
	v_mfma_f32_32x32x16_bf16 v[48:63], v[210:213], v[168:171], v[48:63]
	s_waitcnt lgkmcnt(0)
	v_mfma_f32_32x32x16_bf16 v[48:63], v[214:217], v[176:179], v[48:63]
	ds_read_b128 v[180:183], v157 offset:128
	ds_read_b128 v[206:209], v157 offset:160
	ds_read_b128 v[210:213], v157 offset:192
	ds_read_b128 v[214:217], v157 offset:224
	s_waitcnt lgkmcnt(3)
	v_mfma_f32_32x32x16_bf16 v[32:47], v[180:183], v[160:163], v[32:47]
	s_waitcnt lgkmcnt(2)
	v_mfma_f32_32x32x16_bf16 v[32:47], v[206:209], v[164:167], v[32:47]
	s_waitcnt lgkmcnt(1)
	v_mfma_f32_32x32x16_bf16 v[32:47], v[210:213], v[168:171], v[32:47]
	s_waitcnt lgkmcnt(0)
	v_mfma_f32_32x32x16_bf16 v[32:47], v[214:217], v[176:179], v[32:47]
	ds_read_b128 v[180:183], v158 offset:128
	ds_read_b128 v[206:209], v158 offset:160
	ds_read_b128 v[210:213], v158 offset:192
	ds_read_b128 v[214:217], v158 offset:224
	s_waitcnt lgkmcnt(3)
	v_mfma_f32_32x32x16_bf16 v[16:31], v[180:183], v[160:163], v[16:31]
	s_waitcnt lgkmcnt(2)
	v_mfma_f32_32x32x16_bf16 v[16:31], v[206:209], v[164:167], v[16:31]
	s_waitcnt lgkmcnt(1)
	v_mfma_f32_32x32x16_bf16 v[16:31], v[210:213], v[168:171], v[16:31]
	s_waitcnt lgkmcnt(0)
	v_mfma_f32_32x32x16_bf16 v[16:31], v[214:217], v[176:179], v[16:31]
	ds_read_b128 v[180:183], v159 offset:128
	ds_read_b128 v[206:209], v159 offset:160
	ds_read_b128 v[210:213], v159 offset:192
	ds_read_b128 v[214:217], v159 offset:224
	s_waitcnt lgkmcnt(3)
	v_mfma_f32_32x32x16_bf16 v[0:15], v[180:183], v[160:163], v[0:15]
	s_waitcnt lgkmcnt(2)
	v_mfma_f32_32x32x16_bf16 v[0:15], v[206:209], v[164:167], v[0:15]
	s_waitcnt lgkmcnt(1)
	v_mfma_f32_32x32x16_bf16 v[0:15], v[210:213], v[168:171], v[0:15]
	s_waitcnt lgkmcnt(0)
	v_mfma_f32_32x32x16_bf16 v[0:15], v[214:217], v[176:179], v[0:15]
	global_load_dwordx4 v[160:163], v[136:137], off offset:256
	global_load_dwordx4 v[164:167], v[136:137], off offset:288
	global_load_dwordx4 v[168:171], v[136:137], off offset:320
	global_load_dwordx4 v[176:179], v[136:137], off offset:352
	ds_read_b128 v[180:183], v129 offset:256
	ds_read_b128 v[206:209], v129 offset:288
	ds_read_b128 v[210:213], v129 offset:320
	ds_read_b128 v[214:217], v129 offset:352
	s_waitcnt vmcnt(3) lgkmcnt(3)
	v_mfma_f32_32x32x16_bf16 v[112:127], v[180:183], v[160:163], v[112:127]
	s_waitcnt vmcnt(2) lgkmcnt(2)
	v_mfma_f32_32x32x16_bf16 v[112:127], v[206:209], v[164:167], v[112:127]
	s_waitcnt vmcnt(1) lgkmcnt(1)
	v_mfma_f32_32x32x16_bf16 v[112:127], v[210:213], v[168:171], v[112:127]
	s_waitcnt vmcnt(0) lgkmcnt(0)
	v_mfma_f32_32x32x16_bf16 v[112:127], v[214:217], v[176:179], v[112:127]
	ds_read_b128 v[180:183], v129 offset:17152
	ds_read_b128 v[206:209], v129 offset:17184
	ds_read_b128 v[210:213], v129 offset:17216
	ds_read_b128 v[214:217], v129 offset:17248
	s_waitcnt lgkmcnt(3)
	v_mfma_f32_32x32x16_bf16 v[96:111], v[180:183], v[160:163], v[96:111]
	s_waitcnt lgkmcnt(2)
	v_mfma_f32_32x32x16_bf16 v[96:111], v[206:209], v[164:167], v[96:111]
	s_waitcnt lgkmcnt(1)
	v_mfma_f32_32x32x16_bf16 v[96:111], v[210:213], v[168:171], v[96:111]
	s_waitcnt lgkmcnt(0)
	v_mfma_f32_32x32x16_bf16 v[96:111], v[214:217], v[176:179], v[96:111]
	ds_read_b128 v[180:183], v129 offset:34048
	ds_read_b128 v[206:209], v129 offset:34080
	ds_read_b128 v[210:213], v129 offset:34112
	ds_read_b128 v[214:217], v129 offset:34144
	s_waitcnt lgkmcnt(3)
	v_mfma_f32_32x32x16_bf16 v[80:95], v[180:183], v[160:163], v[80:95]
	s_waitcnt lgkmcnt(2)
	v_mfma_f32_32x32x16_bf16 v[80:95], v[206:209], v[164:167], v[80:95]
	s_waitcnt lgkmcnt(1)
	v_mfma_f32_32x32x16_bf16 v[80:95], v[210:213], v[168:171], v[80:95]
	s_waitcnt lgkmcnt(0)
	v_mfma_f32_32x32x16_bf16 v[80:95], v[214:217], v[176:179], v[80:95]
	ds_read_b128 v[180:183], v129 offset:50944
	ds_read_b128 v[206:209], v129 offset:50976
	ds_read_b128 v[210:213], v129 offset:51008
	ds_read_b128 v[214:217], v129 offset:51040
	s_waitcnt lgkmcnt(3)
	v_mfma_f32_32x32x16_bf16 v[64:79], v[180:183], v[160:163], v[64:79]
	s_waitcnt lgkmcnt(2)
	v_mfma_f32_32x32x16_bf16 v[64:79], v[206:209], v[164:167], v[64:79]
	s_waitcnt lgkmcnt(1)
	v_mfma_f32_32x32x16_bf16 v[64:79], v[210:213], v[168:171], v[64:79]
	s_waitcnt lgkmcnt(0)
	v_mfma_f32_32x32x16_bf16 v[64:79], v[214:217], v[176:179], v[64:79]
	ds_read_b128 v[180:183], v156 offset:256
	ds_read_b128 v[206:209], v156 offset:288
	ds_read_b128 v[210:213], v156 offset:320
	ds_read_b128 v[214:217], v156 offset:352
	s_waitcnt lgkmcnt(3)
	v_mfma_f32_32x32x16_bf16 v[48:63], v[180:183], v[160:163], v[48:63]
	s_waitcnt lgkmcnt(2)
	v_mfma_f32_32x32x16_bf16 v[48:63], v[206:209], v[164:167], v[48:63]
	s_waitcnt lgkmcnt(1)
	v_mfma_f32_32x32x16_bf16 v[48:63], v[210:213], v[168:171], v[48:63]
	s_waitcnt lgkmcnt(0)
	v_mfma_f32_32x32x16_bf16 v[48:63], v[214:217], v[176:179], v[48:63]
	ds_read_b128 v[180:183], v157 offset:256
	ds_read_b128 v[206:209], v157 offset:288
	ds_read_b128 v[210:213], v157 offset:320
	ds_read_b128 v[214:217], v157 offset:352
	s_waitcnt lgkmcnt(3)
	v_mfma_f32_32x32x16_bf16 v[32:47], v[180:183], v[160:163], v[32:47]
	s_waitcnt lgkmcnt(2)
	v_mfma_f32_32x32x16_bf16 v[32:47], v[206:209], v[164:167], v[32:47]
	s_waitcnt lgkmcnt(1)
	v_mfma_f32_32x32x16_bf16 v[32:47], v[210:213], v[168:171], v[32:47]
	s_waitcnt lgkmcnt(0)
	v_mfma_f32_32x32x16_bf16 v[32:47], v[214:217], v[176:179], v[32:47]
	ds_read_b128 v[180:183], v158 offset:256
	ds_read_b128 v[206:209], v158 offset:288
	ds_read_b128 v[210:213], v158 offset:320
	ds_read_b128 v[214:217], v158 offset:352
	s_waitcnt lgkmcnt(3)
	v_mfma_f32_32x32x16_bf16 v[16:31], v[180:183], v[160:163], v[16:31]
	s_waitcnt lgkmcnt(2)
	v_mfma_f32_32x32x16_bf16 v[16:31], v[206:209], v[164:167], v[16:31]
	s_waitcnt lgkmcnt(1)
	v_mfma_f32_32x32x16_bf16 v[16:31], v[210:213], v[168:171], v[16:31]
	s_waitcnt lgkmcnt(0)
	v_mfma_f32_32x32x16_bf16 v[16:31], v[214:217], v[176:179], v[16:31]
	ds_read_b128 v[180:183], v159 offset:256
	ds_read_b128 v[206:209], v159 offset:288
	ds_read_b128 v[210:213], v159 offset:320
	ds_read_b128 v[214:217], v159 offset:352
	s_waitcnt lgkmcnt(3)
	v_mfma_f32_32x32x16_bf16 v[0:15], v[180:183], v[160:163], v[0:15]
	s_waitcnt lgkmcnt(2)
	v_mfma_f32_32x32x16_bf16 v[0:15], v[206:209], v[164:167], v[0:15]
	s_waitcnt lgkmcnt(1)
	v_mfma_f32_32x32x16_bf16 v[0:15], v[210:213], v[168:171], v[0:15]
	s_waitcnt lgkmcnt(0)
	v_mfma_f32_32x32x16_bf16 v[0:15], v[214:217], v[176:179], v[0:15]
	global_load_dwordx4 v[160:163], v[136:137], off offset:384
	global_load_dwordx4 v[164:167], v[136:137], off offset:416
	global_load_dwordx4 v[168:171], v[136:137], off offset:448
	s_nop 0
	global_load_dwordx4 v[136:139], v[136:137], off offset:480
	ds_read_b128 v[176:179], v129 offset:384
	ds_read_b128 v[180:183], v129 offset:416
	ds_read_b128 v[206:209], v129 offset:448
	ds_read_b128 v[210:213], v129 offset:480
	s_waitcnt vmcnt(3) lgkmcnt(3)
	v_mfma_f32_32x32x16_bf16 v[112:127], v[176:179], v[160:163], v[112:127]
	s_waitcnt vmcnt(2) lgkmcnt(2)
	v_mfma_f32_32x32x16_bf16 v[112:127], v[180:183], v[164:167], v[112:127]
	s_waitcnt vmcnt(1) lgkmcnt(1)
	v_mfma_f32_32x32x16_bf16 v[112:127], v[206:209], v[168:171], v[112:127]
	s_waitcnt vmcnt(0) lgkmcnt(0)
	v_mfma_f32_32x32x16_bf16 v[112:127], v[210:213], v[136:139], v[112:127]
	ds_read_b128 v[176:179], v129 offset:17280
	ds_read_b128 v[180:183], v129 offset:17312
	ds_read_b128 v[206:209], v129 offset:17344
	ds_read_b128 v[210:213], v129 offset:17376
	s_waitcnt lgkmcnt(3)
	v_mfma_f32_32x32x16_bf16 v[96:111], v[176:179], v[160:163], v[96:111]
	s_waitcnt lgkmcnt(2)
	v_mfma_f32_32x32x16_bf16 v[96:111], v[180:183], v[164:167], v[96:111]
	s_waitcnt lgkmcnt(1)
	v_mfma_f32_32x32x16_bf16 v[96:111], v[206:209], v[168:171], v[96:111]
	s_waitcnt lgkmcnt(0)
	v_mfma_f32_32x32x16_bf16 v[96:111], v[210:213], v[136:139], v[96:111]
	ds_read_b128 v[176:179], v129 offset:34176
	ds_read_b128 v[180:183], v129 offset:34208
	ds_read_b128 v[206:209], v129 offset:34240
	ds_read_b128 v[210:213], v129 offset:34272
	s_waitcnt lgkmcnt(3)
	v_mfma_f32_32x32x16_bf16 v[80:95], v[176:179], v[160:163], v[80:95]
	s_waitcnt lgkmcnt(2)
	v_mfma_f32_32x32x16_bf16 v[80:95], v[180:183], v[164:167], v[80:95]
	s_waitcnt lgkmcnt(1)
	v_mfma_f32_32x32x16_bf16 v[80:95], v[206:209], v[168:171], v[80:95]
	s_waitcnt lgkmcnt(0)
	v_mfma_f32_32x32x16_bf16 v[80:95], v[210:213], v[136:139], v[80:95]
	ds_read_b128 v[176:179], v129 offset:51072
	ds_read_b128 v[180:183], v129 offset:51104
	ds_read_b128 v[206:209], v129 offset:51136
	ds_read_b128 v[210:213], v129 offset:51168
	s_waitcnt lgkmcnt(3)
	v_mfma_f32_32x32x16_bf16 v[64:79], v[176:179], v[160:163], v[64:79]
	s_waitcnt lgkmcnt(2)
	v_mfma_f32_32x32x16_bf16 v[64:79], v[180:183], v[164:167], v[64:79]
	s_waitcnt lgkmcnt(1)
	v_mfma_f32_32x32x16_bf16 v[64:79], v[206:209], v[168:171], v[64:79]
	s_waitcnt lgkmcnt(0)
	v_mfma_f32_32x32x16_bf16 v[64:79], v[210:213], v[136:139], v[64:79]
	ds_read_b128 v[176:179], v156 offset:384
	ds_read_b128 v[180:183], v156 offset:416
	ds_read_b128 v[206:209], v156 offset:448
	ds_read_b128 v[210:213], v156 offset:480
	s_waitcnt lgkmcnt(3)
	v_mfma_f32_32x32x16_bf16 v[48:63], v[176:179], v[160:163], v[48:63]
	s_waitcnt lgkmcnt(2)
	v_mfma_f32_32x32x16_bf16 v[48:63], v[180:183], v[164:167], v[48:63]
	s_waitcnt lgkmcnt(1)
	v_mfma_f32_32x32x16_bf16 v[48:63], v[206:209], v[168:171], v[48:63]
	s_waitcnt lgkmcnt(0)
	v_mfma_f32_32x32x16_bf16 v[48:63], v[210:213], v[136:139], v[48:63]
	ds_read_b128 v[176:179], v157 offset:384
	ds_read_b128 v[180:183], v157 offset:416
	ds_read_b128 v[206:209], v157 offset:448
	ds_read_b128 v[210:213], v157 offset:480
	s_waitcnt lgkmcnt(3)
	v_mfma_f32_32x32x16_bf16 v[32:47], v[176:179], v[160:163], v[32:47]
	s_waitcnt lgkmcnt(2)
	v_mfma_f32_32x32x16_bf16 v[32:47], v[180:183], v[164:167], v[32:47]
	s_waitcnt lgkmcnt(1)
	v_mfma_f32_32x32x16_bf16 v[32:47], v[206:209], v[168:171], v[32:47]
	s_waitcnt lgkmcnt(0)
	v_mfma_f32_32x32x16_bf16 v[32:47], v[210:213], v[136:139], v[32:47]
	ds_read_b128 v[176:179], v158 offset:384
	ds_read_b128 v[180:183], v158 offset:416
	ds_read_b128 v[206:209], v158 offset:448
	ds_read_b128 v[210:213], v158 offset:480
	s_waitcnt lgkmcnt(3)
	v_mfma_f32_32x32x16_bf16 v[16:31], v[176:179], v[160:163], v[16:31]
	s_waitcnt lgkmcnt(2)
	v_mfma_f32_32x32x16_bf16 v[16:31], v[180:183], v[164:167], v[16:31]
	s_waitcnt lgkmcnt(1)
	v_mfma_f32_32x32x16_bf16 v[16:31], v[206:209], v[168:171], v[16:31]
	s_waitcnt lgkmcnt(0)
	v_mfma_f32_32x32x16_bf16 v[16:31], v[210:213], v[136:139], v[16:31]
	ds_read_b128 v[176:179], v159 offset:384
	ds_read_b128 v[180:183], v159 offset:416
	ds_read_b128 v[206:209], v159 offset:448
	ds_read_b128 v[210:213], v159 offset:480
	s_waitcnt lgkmcnt(3)
	v_mfma_f32_32x32x16_bf16 v[0:15], v[176:179], v[160:163], v[0:15]
	s_waitcnt lgkmcnt(2)
	v_mfma_f32_32x32x16_bf16 v[0:15], v[180:183], v[164:167], v[0:15]
	s_waitcnt lgkmcnt(1)
	v_mfma_f32_32x32x16_bf16 v[0:15], v[206:209], v[168:171], v[0:15]
	s_waitcnt lgkmcnt(0)
	v_mfma_f32_32x32x16_bf16 v[0:15], v[210:213], v[136:139], v[0:15]
	v_max_f32_e32 v135, v113, v113
	v_max_f32_e32 v136, v112, v112
	v_max_f32_e32 v135, v136, v135
	v_max3_f32 v135, v135, v114, v115
	v_max3_f32 v135, v135, v116, v117
	v_max3_f32 v135, v135, v118, v119
	v_max3_f32 v135, v135, v120, v121
	v_max3_f32 v135, v135, v122, v123
	v_max3_f32 v135, v135, v124, v125
	v_max3_f32 v135, v135, v126, v127
	v_max3_f32 v135, v135, v96, v97
	v_max3_f32 v135, v135, v98, v99
	v_max3_f32 v135, v135, v100, v101
	v_max3_f32 v135, v135, v102, v103
	v_max3_f32 v135, v135, v104, v105
	v_max3_f32 v135, v135, v106, v107
	v_max3_f32 v135, v135, v108, v109
	v_max3_f32 v135, v135, v110, v111
	v_max3_f32 v135, v135, v80, v81
	v_max3_f32 v135, v135, v82, v83
	v_max3_f32 v135, v135, v84, v85
	v_max3_f32 v135, v135, v86, v87
	v_max3_f32 v135, v135, v88, v89
	v_max3_f32 v135, v135, v90, v91
	v_max3_f32 v135, v135, v92, v93
	v_max3_f32 v135, v135, v94, v95
	v_max3_f32 v135, v135, v64, v65
	v_max3_f32 v135, v135, v66, v67
	v_max3_f32 v135, v135, v68, v69
	v_max3_f32 v135, v135, v70, v71
	v_max3_f32 v135, v135, v72, v73
	v_max3_f32 v135, v135, v74, v75
	v_max3_f32 v135, v135, v76, v77
	v_max3_f32 v135, v135, v78, v79
	v_max3_f32 v135, v135, v48, v49
	v_max3_f32 v135, v135, v50, v51
	v_max3_f32 v135, v135, v52, v53
	v_max3_f32 v135, v135, v54, v55
	v_max3_f32 v135, v135, v56, v57
	v_max3_f32 v135, v135, v58, v59
	v_max3_f32 v135, v135, v60, v61
	v_max3_f32 v135, v135, v62, v63
	v_max3_f32 v135, v135, v32, v33
	v_max3_f32 v135, v135, v34, v35
	v_max3_f32 v135, v135, v36, v37
	v_max3_f32 v135, v135, v38, v39
	v_max3_f32 v135, v135, v40, v41
	v_max3_f32 v135, v135, v42, v43
	v_max3_f32 v135, v135, v44, v45
	v_max3_f32 v135, v135, v46, v47
	v_max3_f32 v135, v135, v16, v17
	v_max3_f32 v135, v135, v18, v19
	v_max3_f32 v135, v135, v20, v21
	v_max3_f32 v135, v135, v22, v23
	v_max3_f32 v135, v135, v24, v25
	v_max3_f32 v135, v135, v26, v27
	v_max3_f32 v135, v135, v28, v29
	v_max3_f32 v135, v135, v30, v31
	v_max3_f32 v135, v135, v0, v1
	v_max3_f32 v135, v135, v2, v3
	v_max3_f32 v135, v135, v4, v5
	v_max3_f32 v135, v135, v6, v7
	v_max3_f32 v135, v135, v8, v9
	v_max3_f32 v135, v135, v10, v11
	v_max3_f32 v135, v135, v12, v13
	v_max3_f32 v135, v135, v14, v15
	ds_bpermute_b32 v136, v184, v135
	s_lshl_b32 s17, s17, 2
	s_waitcnt lgkmcnt(0)
	s_barrier
	v_max_f32_e32 v136, v136, v136
	v_max_f32_e32 v160, v135, v136
	v_sub_f32_e32 v112, v112, v160
	v_mul_f32_e32 v112, 0x3d800000, v112
	v_mul_f32_e32 v112, 0x3fb8aa3b, v112
	v_exp_f32_e32 v135, v112
	v_sub_f32_e32 v112, v113, v160
	v_mul_f32_e32 v112, 0x3d800000, v112
	v_sub_f32_e32 v113, v114, v160
	v_mul_f32_e32 v112, 0x3fb8aa3b, v112
	v_mul_f32_e32 v113, 0x3d800000, v113
	v_sub_f32_e32 v114, v115, v160
	v_exp_f32_e32 v112, v112
	v_mul_f32_e32 v113, 0x3fb8aa3b, v113
	v_mul_f32_e32 v114, 0x3d800000, v114
	v_sub_f32_e32 v115, v116, v160
	v_exp_f32_e32 v113, v113
	v_mul_f32_e32 v114, 0x3fb8aa3b, v114
	v_mul_f32_e32 v115, 0x3d800000, v115
	v_sub_f32_e32 v116, v117, v160
	v_sub_f32_e32 v119, v119, v160
	v_exp_f32_e32 v114, v114
	v_mul_f32_e32 v115, 0x3fb8aa3b, v115
	v_mul_f32_e32 v116, 0x3d800000, v116
	v_sub_f32_e32 v117, v118, v160
	v_mul_f32_e32 v119, 0x3d800000, v119
	v_add_f32_e32 v136, 0, v135
	v_exp_f32_e32 v115, v115
	v_mul_f32_e32 v116, 0x3fb8aa3b, v116
	v_mul_f32_e32 v117, 0x3d800000, v117
	v_mul_f32_e32 v119, 0x3fb8aa3b, v119
	v_add_f32_e32 v136, v112, v136
	v_exp_f32_e32 v116, v116
	v_mul_f32_e32 v117, 0x3fb8aa3b, v117
	v_exp_f32_e32 v161, v119
	v_sub_f32_e32 v119, v120, v160
	v_add_f32_e32 v136, v113, v136
	v_exp_f32_e32 v117, v117
	v_mul_f32_e32 v119, 0x3d800000, v119
	v_add_f32_e32 v136, v114, v136
	v_mul_f32_e32 v119, 0x3fb8aa3b, v119
	v_add_f32_e32 v136, v115, v136
	v_exp_f32_e32 v162, v119
	v_add_f32_e32 v136, v116, v136
	v_add_f32_e32 v118, v117, v136
	v_add_f32_e32 v118, v161, v118
	v_add_f32_e32 v119, v162, v118
	v_sub_f32_e32 v118, v121, v160
	v_mul_f32_e32 v118, 0x3d800000, v118
	v_mul_f32_e32 v118, 0x3fb8aa3b, v118
	v_exp_f32_e32 v118, v118
	v_sub_f32_e32 v96, v96, v160
	v_mul_f32_e32 v96, 0x3d800000, v96
	v_mul_f32_e32 v96, 0x3fb8aa3b, v96
	v_add_f32_e32 v120, v118, v119
	v_sub_f32_e32 v119, v122, v160
	v_mul_f32_e32 v119, 0x3d800000, v119
	v_mul_f32_e32 v119, 0x3fb8aa3b, v119
	v_exp_f32_e32 v119, v119
	v_exp_f32_e32 v164, v96
	v_sub_f32_e32 v96, v97, v160
	v_mul_f32_e32 v96, 0x3d800000, v96
	v_add_f32_e32 v121, v119, v120
	v_sub_f32_e32 v120, v123, v160
	v_mul_f32_e32 v120, 0x3d800000, v120
	v_mul_f32_e32 v120, 0x3fb8aa3b, v120
	v_exp_f32_e32 v120, v120
	v_sub_f32_e32 v97, v98, v160
	v_mul_f32_e32 v96, 0x3fb8aa3b, v96
	v_mul_f32_e32 v97, 0x3d800000, v97
	v_add_f32_e32 v122, v120, v121
	v_sub_f32_e32 v121, v124, v160
	v_mul_f32_e32 v121, 0x3d800000, v121
	v_mul_f32_e32 v121, 0x3fb8aa3b, v121
	v_exp_f32_e32 v121, v121
	v_sub_f32_e32 v98, v99, v160
	v_exp_f32_e32 v96, v96
	v_mul_f32_e32 v97, 0x3fb8aa3b, v97
	v_add_f32_e32 v123, v121, v122
	v_sub_f32_e32 v122, v125, v160
	v_mul_f32_e32 v122, 0x3d800000, v122
	v_mul_f32_e32 v122, 0x3fb8aa3b, v122
	v_exp_f32_e32 v122, v122
	v_sub_f32_e32 v125, v127, v160
	v_mul_f32_e32 v125, 0x3d800000, v125
	v_mul_f32_e32 v125, 0x3fb8aa3b, v125
	v_add_f32_e32 v124, v122, v123
	v_sub_f32_e32 v123, v126, v160
	v_mul_f32_e32 v123, 0x3d800000, v123
	v_mul_f32_e32 v123, 0x3fb8aa3b, v123
	v_exp_f32_e32 v123, v123
	v_exp_f32_e32 v163, v125
	v_mul_f32_e32 v98, 0x3d800000, v98
	v_sub_f32_e32 v99, v100, v160
	v_add_f32_e32 v124, v123, v124
	v_exp_f32_e32 v97, v97
	v_mul_f32_e32 v98, 0x3fb8aa3b, v98
	v_mul_f32_e32 v99, 0x3d800000, v99
	v_sub_f32_e32 v100, v101, v160
	v_sub_f32_e32 v103, v103, v160
	v_add_f32_e32 v124, v163, v124
	v_exp_f32_e32 v98, v98
	v_mul_f32_e32 v99, 0x3fb8aa3b, v99
	v_mul_f32_e32 v100, 0x3d800000, v100
	v_sub_f32_e32 v101, v102, v160
	v_mul_f32_e32 v103, 0x3d800000, v103
	v_add_f32_e32 v124, v164, v124
	v_exp_f32_e32 v99, v99
	v_mul_f32_e32 v100, 0x3fb8aa3b, v100
	v_mul_f32_e32 v101, 0x3d800000, v101
	v_mul_f32_e32 v103, 0x3fb8aa3b, v103
	v_add_f32_e32 v124, v96, v124
	v_exp_f32_e32 v100, v100
	v_mul_f32_e32 v101, 0x3fb8aa3b, v101
	v_exp_f32_e32 v165, v103
	v_sub_f32_e32 v103, v104, v160
	v_add_f32_e32 v124, v97, v124
	v_exp_f32_e32 v101, v101
	v_mul_f32_e32 v103, 0x3d800000, v103
	v_add_f32_e32 v124, v98, v124
	v_mul_f32_e32 v103, 0x3fb8aa3b, v103
	v_add_f32_e32 v124, v99, v124
	v_exp_f32_e32 v166, v103
	v_add_f32_e32 v124, v100, v124
	v_add_f32_e32 v102, v101, v124
	v_add_f32_e32 v102, v165, v102
	v_add_f32_e32 v103, v166, v102
	v_sub_f32_e32 v102, v105, v160
	v_mul_f32_e32 v102, 0x3d800000, v102
	v_mul_f32_e32 v102, 0x3fb8aa3b, v102
	v_exp_f32_e32 v102, v102
	v_sub_f32_e32 v80, v80, v160
	v_mul_f32_e32 v80, 0x3d800000, v80
	v_mul_f32_e32 v80, 0x3fb8aa3b, v80
	v_add_f32_e32 v104, v102, v103
	v_sub_f32_e32 v103, v106, v160
	v_mul_f32_e32 v103, 0x3d800000, v103
	v_mul_f32_e32 v103, 0x3fb8aa3b, v103
	v_exp_f32_e32 v103, v103
	v_exp_f32_e32 v168, v80
	v_sub_f32_e32 v80, v81, v160
	v_mul_f32_e32 v80, 0x3d800000, v80
	v_add_f32_e32 v105, v103, v104
	v_sub_f32_e32 v104, v107, v160
	v_mul_f32_e32 v104, 0x3d800000, v104
	v_mul_f32_e32 v104, 0x3fb8aa3b, v104
	v_exp_f32_e32 v104, v104
	v_sub_f32_e32 v81, v82, v160
	v_mul_f32_e32 v80, 0x3fb8aa3b, v80
	v_mul_f32_e32 v81, 0x3d800000, v81
	v_add_f32_e32 v106, v104, v105
	v_sub_f32_e32 v105, v108, v160
	v_mul_f32_e32 v105, 0x3d800000, v105
	v_mul_f32_e32 v105, 0x3fb8aa3b, v105
	v_exp_f32_e32 v105, v105
	v_sub_f32_e32 v82, v83, v160
	v_exp_f32_e32 v80, v80
	v_mul_f32_e32 v81, 0x3fb8aa3b, v81
	v_add_f32_e32 v107, v105, v106
	v_sub_f32_e32 v106, v109, v160
	v_mul_f32_e32 v106, 0x3d800000, v106
	v_mul_f32_e32 v106, 0x3fb8aa3b, v106
	v_exp_f32_e32 v106, v106
	v_sub_f32_e32 v109, v111, v160
	v_mul_f32_e32 v109, 0x3d800000, v109
	v_mul_f32_e32 v109, 0x3fb8aa3b, v109
	v_add_f32_e32 v108, v106, v107
	v_sub_f32_e32 v107, v110, v160
	v_mul_f32_e32 v107, 0x3d800000, v107
	v_mul_f32_e32 v107, 0x3fb8aa3b, v107
	v_exp_f32_e32 v107, v107
	v_exp_f32_e32 v167, v109
	v_mul_f32_e32 v82, 0x3d800000, v82
	v_sub_f32_e32 v83, v84, v160
	v_add_f32_e32 v108, v107, v108
	v_exp_f32_e32 v81, v81
	v_mul_f32_e32 v82, 0x3fb8aa3b, v82
	v_mul_f32_e32 v83, 0x3d800000, v83
	v_sub_f32_e32 v84, v85, v160
	v_sub_f32_e32 v87, v87, v160
	v_add_f32_e32 v108, v167, v108
	v_exp_f32_e32 v82, v82
	v_mul_f32_e32 v83, 0x3fb8aa3b, v83
	v_mul_f32_e32 v84, 0x3d800000, v84
	v_sub_f32_e32 v85, v86, v160
	v_mul_f32_e32 v87, 0x3d800000, v87
	v_add_f32_e32 v108, v168, v108
	v_exp_f32_e32 v83, v83
	v_mul_f32_e32 v84, 0x3fb8aa3b, v84
	v_mul_f32_e32 v85, 0x3d800000, v85
	v_mul_f32_e32 v87, 0x3fb8aa3b, v87
	v_add_f32_e32 v108, v80, v108
	v_exp_f32_e32 v84, v84
	v_mul_f32_e32 v85, 0x3fb8aa3b, v85
	v_exp_f32_e32 v169, v87
	v_sub_f32_e32 v87, v88, v160
	v_add_f32_e32 v108, v81, v108
	v_exp_f32_e32 v85, v85
	v_mul_f32_e32 v87, 0x3d800000, v87
	v_add_f32_e32 v108, v82, v108
	v_mul_f32_e32 v87, 0x3fb8aa3b, v87
	v_add_f32_e32 v108, v83, v108
	v_exp_f32_e32 v170, v87
	v_add_f32_e32 v108, v84, v108
	v_add_f32_e32 v86, v85, v108
	v_add_f32_e32 v86, v169, v86
	v_add_f32_e32 v87, v170, v86
	v_sub_f32_e32 v86, v89, v160
	v_mul_f32_e32 v86, 0x3d800000, v86
	v_mul_f32_e32 v86, 0x3fb8aa3b, v86
	v_exp_f32_e32 v86, v86
	v_sub_f32_e32 v64, v64, v160
	v_mul_f32_e32 v64, 0x3d800000, v64
	v_mul_f32_e32 v64, 0x3fb8aa3b, v64
	v_add_f32_e32 v88, v86, v87
	v_sub_f32_e32 v87, v90, v160
	v_mul_f32_e32 v87, 0x3d800000, v87
	v_mul_f32_e32 v87, 0x3fb8aa3b, v87
	v_exp_f32_e32 v87, v87
	v_exp_f32_e32 v172, v64
	v_sub_f32_e32 v64, v65, v160
	v_mul_f32_e32 v64, 0x3d800000, v64
	v_add_f32_e32 v89, v87, v88
	v_sub_f32_e32 v88, v91, v160
	v_mul_f32_e32 v88, 0x3d800000, v88
	v_mul_f32_e32 v88, 0x3fb8aa3b, v88
	v_exp_f32_e32 v88, v88
	v_sub_f32_e32 v65, v66, v160
	v_mul_f32_e32 v64, 0x3fb8aa3b, v64
	v_mul_f32_e32 v65, 0x3d800000, v65
	v_add_f32_e32 v90, v88, v89
	v_sub_f32_e32 v89, v92, v160
	v_mul_f32_e32 v89, 0x3d800000, v89
	v_mul_f32_e32 v89, 0x3fb8aa3b, v89
	v_exp_f32_e32 v89, v89
	v_sub_f32_e32 v66, v67, v160
	v_exp_f32_e32 v64, v64
	v_mul_f32_e32 v65, 0x3fb8aa3b, v65
	v_add_f32_e32 v91, v89, v90
	v_sub_f32_e32 v90, v93, v160
	v_mul_f32_e32 v90, 0x3d800000, v90
	v_mul_f32_e32 v90, 0x3fb8aa3b, v90
	v_exp_f32_e32 v90, v90
	v_sub_f32_e32 v93, v95, v160
	v_mul_f32_e32 v93, 0x3d800000, v93
	v_mul_f32_e32 v93, 0x3fb8aa3b, v93
	v_add_f32_e32 v92, v90, v91
	v_sub_f32_e32 v91, v94, v160
	v_mul_f32_e32 v91, 0x3d800000, v91
	v_mul_f32_e32 v91, 0x3fb8aa3b, v91
	v_exp_f32_e32 v91, v91
	v_exp_f32_e32 v171, v93
	v_mul_f32_e32 v66, 0x3d800000, v66
	v_sub_f32_e32 v67, v68, v160
	v_add_f32_e32 v92, v91, v92
	v_exp_f32_e32 v65, v65
	v_mul_f32_e32 v66, 0x3fb8aa3b, v66
	v_mul_f32_e32 v67, 0x3d800000, v67
	v_sub_f32_e32 v68, v69, v160
	v_sub_f32_e32 v71, v71, v160
	v_add_f32_e32 v92, v171, v92
	v_exp_f32_e32 v66, v66
	v_mul_f32_e32 v67, 0x3fb8aa3b, v67
	v_mul_f32_e32 v68, 0x3d800000, v68
	v_sub_f32_e32 v69, v70, v160
	v_mul_f32_e32 v71, 0x3d800000, v71
	v_add_f32_e32 v92, v172, v92
	v_exp_f32_e32 v67, v67
	v_mul_f32_e32 v68, 0x3fb8aa3b, v68
	v_mul_f32_e32 v69, 0x3d800000, v69
	v_mul_f32_e32 v71, 0x3fb8aa3b, v71
	v_add_f32_e32 v92, v64, v92
	v_exp_f32_e32 v68, v68
	v_mul_f32_e32 v69, 0x3fb8aa3b, v69
	v_exp_f32_e32 v173, v71
	v_sub_f32_e32 v71, v72, v160
	v_add_f32_e32 v92, v65, v92
	v_exp_f32_e32 v69, v69
	v_mul_f32_e32 v71, 0x3d800000, v71
	v_add_f32_e32 v92, v66, v92
	v_mul_f32_e32 v71, 0x3fb8aa3b, v71
	v_add_f32_e32 v92, v67, v92
	v_exp_f32_e32 v174, v71
	v_add_f32_e32 v92, v68, v92
	v_add_f32_e32 v70, v69, v92
	v_add_f32_e32 v70, v173, v70
	v_add_f32_e32 v71, v174, v70
	v_sub_f32_e32 v70, v73, v160
	v_mul_f32_e32 v70, 0x3d800000, v70
	v_mul_f32_e32 v70, 0x3fb8aa3b, v70
	v_exp_f32_e32 v70, v70
	v_sub_f32_e32 v48, v48, v160
	v_mul_f32_e32 v48, 0x3d800000, v48
	v_mul_f32_e32 v48, 0x3fb8aa3b, v48
	v_add_f32_e32 v72, v70, v71
	v_sub_f32_e32 v71, v74, v160
	v_mul_f32_e32 v71, 0x3d800000, v71
	v_mul_f32_e32 v71, 0x3fb8aa3b, v71
	v_exp_f32_e32 v71, v71
	v_exp_f32_e32 v177, v48
	v_sub_f32_e32 v48, v49, v160
	v_mul_f32_e32 v48, 0x3d800000, v48
	v_add_f32_e32 v73, v71, v72
	v_sub_f32_e32 v72, v75, v160
	v_mul_f32_e32 v72, 0x3d800000, v72
	v_mul_f32_e32 v72, 0x3fb8aa3b, v72
	v_exp_f32_e32 v72, v72
	v_sub_f32_e32 v49, v50, v160
	v_mul_f32_e32 v48, 0x3fb8aa3b, v48
	v_mul_f32_e32 v49, 0x3d800000, v49
	v_add_f32_e32 v74, v72, v73
	v_sub_f32_e32 v73, v76, v160
	v_mul_f32_e32 v73, 0x3d800000, v73
	v_mul_f32_e32 v73, 0x3fb8aa3b, v73
	v_exp_f32_e32 v73, v73
	v_sub_f32_e32 v50, v51, v160
	v_exp_f32_e32 v48, v48
	v_mul_f32_e32 v49, 0x3fb8aa3b, v49
	v_add_f32_e32 v75, v73, v74
	v_sub_f32_e32 v74, v77, v160
	v_mul_f32_e32 v74, 0x3d800000, v74
	v_mul_f32_e32 v74, 0x3fb8aa3b, v74
	v_exp_f32_e32 v74, v74
	v_sub_f32_e32 v77, v79, v160
	v_mul_f32_e32 v77, 0x3d800000, v77
	v_mul_f32_e32 v77, 0x3fb8aa3b, v77
	v_add_f32_e32 v76, v74, v75
	v_sub_f32_e32 v75, v78, v160
	v_mul_f32_e32 v75, 0x3d800000, v75
	v_mul_f32_e32 v75, 0x3fb8aa3b, v75
	v_exp_f32_e32 v75, v75
	v_exp_f32_e32 v176, v77
	v_mul_f32_e32 v50, 0x3d800000, v50
	v_sub_f32_e32 v51, v52, v160
	v_add_f32_e32 v76, v75, v76
	v_exp_f32_e32 v49, v49
	v_mul_f32_e32 v50, 0x3fb8aa3b, v50
	v_mul_f32_e32 v51, 0x3d800000, v51
	v_sub_f32_e32 v52, v53, v160
	v_sub_f32_e32 v55, v55, v160
	v_add_f32_e32 v76, v176, v76
	v_exp_f32_e32 v50, v50
	v_mul_f32_e32 v51, 0x3fb8aa3b, v51
	v_mul_f32_e32 v52, 0x3d800000, v52
	v_sub_f32_e32 v53, v54, v160
	v_mul_f32_e32 v55, 0x3d800000, v55
	v_add_f32_e32 v76, v177, v76
	v_exp_f32_e32 v51, v51
	v_mul_f32_e32 v52, 0x3fb8aa3b, v52
	v_mul_f32_e32 v53, 0x3d800000, v53
	v_mul_f32_e32 v55, 0x3fb8aa3b, v55
	v_add_f32_e32 v76, v48, v76
	v_exp_f32_e32 v52, v52
	v_mul_f32_e32 v53, 0x3fb8aa3b, v53
	v_exp_f32_e32 v178, v55
	v_sub_f32_e32 v55, v56, v160
	v_add_f32_e32 v76, v49, v76
	v_exp_f32_e32 v53, v53
	v_mul_f32_e32 v55, 0x3d800000, v55
	v_add_f32_e32 v76, v50, v76
	v_mul_f32_e32 v55, 0x3fb8aa3b, v55
	v_add_f32_e32 v76, v51, v76
	v_exp_f32_e32 v179, v55
	v_add_f32_e32 v76, v52, v76
	v_add_f32_e32 v54, v53, v76
	v_add_f32_e32 v54, v178, v54
	v_add_f32_e32 v55, v179, v54
	v_sub_f32_e32 v54, v57, v160
	v_mul_f32_e32 v54, 0x3d800000, v54
	v_mul_f32_e32 v54, 0x3fb8aa3b, v54
	v_exp_f32_e32 v54, v54
	v_sub_f32_e32 v32, v32, v160
	v_mul_f32_e32 v32, 0x3d800000, v32
	v_mul_f32_e32 v32, 0x3fb8aa3b, v32
	v_add_f32_e32 v56, v54, v55
	v_sub_f32_e32 v55, v58, v160
	v_mul_f32_e32 v55, 0x3d800000, v55
	v_mul_f32_e32 v55, 0x3fb8aa3b, v55
	v_exp_f32_e32 v55, v55
	v_exp_f32_e32 v181, v32
	v_sub_f32_e32 v33, v33, v160
	v_mul_f32_e32 v33, 0x3d800000, v33
	v_add_f32_e32 v57, v55, v56
	v_sub_f32_e32 v56, v59, v160
	v_mul_f32_e32 v56, 0x3d800000, v56
	v_mul_f32_e32 v56, 0x3fb8aa3b, v56
	v_exp_f32_e32 v56, v56
	v_mul_f32_e32 v33, 0x3fb8aa3b, v33
	v_sub_f32_e32 v17, v17, v160
	v_mul_f32_e32 v17, 0x3d800000, v17
	v_add_f32_e32 v58, v56, v57
	v_sub_f32_e32 v57, v60, v160
	v_mul_f32_e32 v57, 0x3d800000, v57
	v_mul_f32_e32 v57, 0x3fb8aa3b, v57
	v_exp_f32_e32 v57, v57
	v_mul_f32_e32 v17, 0x3fb8aa3b, v17
	v_exp_f32_e32 v108, v17
	v_sub_f32_e32 v17, v18, v160
	v_add_f32_e32 v59, v57, v58
	v_sub_f32_e32 v58, v61, v160
	v_mul_f32_e32 v58, 0x3d800000, v58
	v_mul_f32_e32 v58, 0x3fb8aa3b, v58
	v_exp_f32_e32 v58, v58
	v_sub_f32_e32 v61, v63, v160
	v_mul_f32_e32 v61, 0x3d800000, v61
	v_mul_f32_e32 v61, 0x3fb8aa3b, v61
	v_add_f32_e32 v60, v58, v59
	v_sub_f32_e32 v59, v62, v160
	v_mul_f32_e32 v59, 0x3d800000, v59
	v_mul_f32_e32 v59, 0x3fb8aa3b, v59
	v_exp_f32_e32 v59, v59
	v_exp_f32_e32 v180, v61
	v_mul_f32_e32 v17, 0x3d800000, v17
	v_mul_f32_e32 v17, 0x3fb8aa3b, v17
	v_add_f32_e32 v60, v59, v60
	v_add_f32_e32 v60, v180, v60
	v_add_f32_e32 v32, v181, v60
	v_exp_f32_e32 v60, v33
	v_sub_f32_e32 v33, v34, v160
	v_mul_f32_e32 v33, 0x3d800000, v33
	v_mul_f32_e32 v33, 0x3fb8aa3b, v33
	v_exp_f32_e32 v61, v33
	v_sub_f32_e32 v33, v35, v160
	v_mul_f32_e32 v33, 0x3d800000, v33
	v_mul_f32_e32 v33, 0x3fb8aa3b, v33
	v_exp_f32_e32 v62, v33
	v_sub_f32_e32 v33, v36, v160
	v_mul_f32_e32 v33, 0x3d800000, v33
	v_mul_f32_e32 v33, 0x3fb8aa3b, v33
	v_exp_f32_e32 v63, v33
	v_sub_f32_e32 v33, v37, v160
	v_mul_f32_e32 v33, 0x3d800000, v33
	v_mul_f32_e32 v33, 0x3fb8aa3b, v33
	v_exp_f32_e32 v76, v33
	v_sub_f32_e32 v33, v38, v160
	v_mul_f32_e32 v33, 0x3d800000, v33
	v_mul_f32_e32 v33, 0x3fb8aa3b, v33
	v_exp_f32_e32 v77, v33
	v_sub_f32_e32 v33, v39, v160
	v_mul_f32_e32 v33, 0x3d800000, v33
	v_mul_f32_e32 v33, 0x3fb8aa3b, v33
	v_exp_f32_e32 v182, v33
	v_sub_f32_e32 v33, v40, v160
	v_mul_f32_e32 v33, 0x3d800000, v33
	v_exp_f32_e32 v109, v17
	v_sub_f32_e32 v17, v19, v160
	v_mul_f32_e32 v33, 0x3fb8aa3b, v33
	v_mul_f32_e32 v17, 0x3d800000, v17
	v_exp_f32_e32 v183, v33
	v_sub_f32_e32 v33, v41, v160
	v_mul_f32_e32 v17, 0x3fb8aa3b, v17
	v_mul_f32_e32 v33, 0x3d800000, v33
	v_exp_f32_e32 v110, v17
	v_sub_f32_e32 v17, v20, v160
	v_mul_f32_e32 v33, 0x3fb8aa3b, v33
	v_mul_f32_e32 v17, 0x3d800000, v17
	v_exp_f32_e32 v78, v33
	v_sub_f32_e32 v33, v42, v160
	v_mul_f32_e32 v17, 0x3fb8aa3b, v17
	v_mul_f32_e32 v33, 0x3d800000, v33
	v_exp_f32_e32 v111, v17
	v_sub_f32_e32 v17, v21, v160
	v_mul_f32_e32 v33, 0x3fb8aa3b, v33
	v_mul_f32_e32 v17, 0x3d800000, v17
	v_exp_f32_e32 v79, v33
	v_sub_f32_e32 v33, v43, v160
	v_mul_f32_e32 v17, 0x3fb8aa3b, v17
	v_mul_f32_e32 v33, 0x3d800000, v33
	v_exp_f32_e32 v124, v17
	v_sub_f32_e32 v17, v22, v160
	v_mul_f32_e32 v33, 0x3fb8aa3b, v33
	v_mul_f32_e32 v17, 0x3d800000, v17
	v_exp_f32_e32 v92, v33
	v_sub_f32_e32 v33, v44, v160
	v_mul_f32_e32 v17, 0x3fb8aa3b, v17
	v_mul_f32_e32 v33, 0x3d800000, v33
	v_exp_f32_e32 v125, v17
	v_sub_f32_e32 v17, v23, v160
	v_add_f32_e32 v32, v60, v32
	v_mul_f32_e32 v33, 0x3fb8aa3b, v33
	v_mul_f32_e32 v17, 0x3d800000, v17
	v_add_f32_e32 v32, v61, v32
	v_exp_f32_e32 v93, v33
	v_sub_f32_e32 v33, v45, v160
	v_mul_f32_e32 v17, 0x3fb8aa3b, v17
	v_add_f32_e32 v32, v62, v32
	v_mul_f32_e32 v33, 0x3d800000, v33
	v_exp_f32_e32 v206, v17
	v_sub_f32_e32 v17, v24, v160
	v_add_f32_e32 v32, v63, v32
	v_mul_f32_e32 v33, 0x3fb8aa3b, v33
	v_mul_f32_e32 v17, 0x3d800000, v17
	v_add_f32_e32 v32, v76, v32
	v_exp_f32_e32 v94, v33
	v_sub_f32_e32 v33, v46, v160
	v_mul_f32_e32 v17, 0x3fb8aa3b, v17
	v_add_f32_e32 v32, v77, v32
	v_mul_f32_e32 v33, 0x3d800000, v33
	v_exp_f32_e32 v207, v17
	v_sub_f32_e32 v17, v25, v160
	v_add_f32_e32 v32, v182, v32
	v_mul_f32_e32 v33, 0x3fb8aa3b, v33
	v_mul_f32_e32 v17, 0x3d800000, v17
	v_add_f32_e32 v32, v183, v32
	v_exp_f32_e32 v95, v33
	v_sub_f32_e32 v33, v47, v160
	v_mul_f32_e32 v17, 0x3fb8aa3b, v17
	v_add_f32_e32 v32, v78, v32
	v_mul_f32_e32 v33, 0x3d800000, v33
	v_sub_f32_e32 v16, v16, v160
	v_exp_f32_e32 v126, v17
	v_sub_f32_e32 v17, v26, v160
	v_add_f32_e32 v32, v79, v32
	v_mul_f32_e32 v33, 0x3fb8aa3b, v33
	v_mul_f32_e32 v16, 0x3d800000, v16
	v_mul_f32_e32 v17, 0x3d800000, v17
	v_add_f32_e32 v32, v92, v32
	v_exp_f32_e32 v190, v33
	v_mul_f32_e32 v16, 0x3fb8aa3b, v16
	v_mul_f32_e32 v17, 0x3fb8aa3b, v17
	v_add_f32_e32 v32, v93, v32
	v_exp_f32_e32 v195, v16
	v_exp_f32_e32 v127, v17
	v_sub_f32_e32 v17, v27, v160
	v_add_f32_e32 v32, v94, v32
	v_mul_f32_e32 v17, 0x3d800000, v17
	v_add_f32_e32 v32, v95, v32
	v_mul_f32_e32 v17, 0x3fb8aa3b, v17
	v_add_f32_e32 v32, v190, v32
	v_exp_f32_e32 v136, v17
	v_sub_f32_e32 v17, v28, v160
	v_add_f32_e32 v16, v195, v32
	v_mul_f32_e32 v17, 0x3d800000, v17
	v_add_f32_e32 v16, v108, v16
	v_mul_f32_e32 v17, 0x3fb8aa3b, v17
	v_add_f32_e32 v16, v109, v16
	v_exp_f32_e32 v137, v17
	v_sub_f32_e32 v17, v29, v160
	v_add_f32_e32 v16, v110, v16
	v_mul_f32_e32 v17, 0x3d800000, v17
	v_add_f32_e32 v16, v111, v16
	v_mul_f32_e32 v17, 0x3fb8aa3b, v17
	v_add_f32_e32 v16, v124, v16
	v_exp_f32_e32 v138, v17
	v_sub_f32_e32 v17, v30, v160
	v_add_f32_e32 v16, v125, v16
	v_mul_f32_e32 v17, 0x3d800000, v17
	v_add_f32_e32 v16, v206, v16
	v_mul_f32_e32 v17, 0x3fb8aa3b, v17
	v_sub_f32_e32 v0, v0, v160
	v_add_f32_e32 v16, v207, v16
	v_exp_f32_e32 v139, v17
	v_sub_f32_e32 v17, v31, v160
	v_mul_f32_e32 v0, 0x3d800000, v0
	v_add_f32_e32 v16, v126, v16
	v_mul_f32_e32 v17, 0x3d800000, v17
	v_mul_f32_e32 v0, 0x3fb8aa3b, v0
	v_add_f32_e32 v16, v127, v16
	v_mul_f32_e32 v17, 0x3fb8aa3b, v17
	v_exp_f32_e32 v209, v0
	v_sub_f32_e32 v0, v1, v160
	v_add_f32_e32 v16, v136, v16
	v_exp_f32_e32 v208, v17
	v_mul_f32_e32 v0, 0x3d800000, v0
	v_sub_f32_e32 v1, v2, v160
	v_add_f32_e32 v16, v137, v16
	v_mul_f32_e32 v0, 0x3fb8aa3b, v0
	v_mul_f32_e32 v1, 0x3d800000, v1
	v_sub_f32_e32 v2, v3, v160
	v_add_f32_e32 v16, v138, v16
	v_exp_f32_e32 v0, v0
	v_mul_f32_e32 v1, 0x3fb8aa3b, v1
	v_mul_f32_e32 v2, 0x3d800000, v2
	v_sub_f32_e32 v3, v4, v160
	v_add_f32_e32 v16, v139, v16
	v_exp_f32_e32 v1, v1
	v_mul_f32_e32 v2, 0x3fb8aa3b, v2
	v_mul_f32_e32 v3, 0x3d800000, v3
	v_sub_f32_e32 v4, v5, v160
	v_sub_f32_e32 v7, v7, v160
	v_add_f32_e32 v16, v208, v16
	v_exp_f32_e32 v2, v2
	v_mul_f32_e32 v3, 0x3fb8aa3b, v3
	v_mul_f32_e32 v4, 0x3d800000, v4
	v_sub_f32_e32 v5, v6, v160
	v_mul_f32_e32 v7, 0x3d800000, v7
	v_add_f32_e32 v16, v209, v16
	v_exp_f32_e32 v3, v3
	v_mul_f32_e32 v4, 0x3fb8aa3b, v4
	v_mul_f32_e32 v5, 0x3d800000, v5
	v_mul_f32_e32 v7, 0x3fb8aa3b, v7
	v_add_f32_e32 v16, v0, v16
	v_exp_f32_e32 v4, v4
	v_mul_f32_e32 v5, 0x3fb8aa3b, v5
	v_exp_f32_e32 v210, v7
	v_sub_f32_e32 v7, v8, v160
	v_add_f32_e32 v16, v1, v16
	v_exp_f32_e32 v5, v5
	v_mul_f32_e32 v7, 0x3d800000, v7
	v_add_f32_e32 v16, v2, v16
	v_mul_f32_e32 v7, 0x3fb8aa3b, v7
	v_add_f32_e32 v16, v3, v16
	v_exp_f32_e32 v211, v7
	v_add_f32_e32 v16, v4, v16
	v_add_f32_e32 v6, v5, v16
	v_add_f32_e32 v6, v210, v6
	v_add_f32_e32 v7, v211, v6
	v_sub_f32_e32 v6, v9, v160
	v_mul_f32_e32 v6, 0x3d800000, v6
	v_mul_f32_e32 v6, 0x3fb8aa3b, v6
	v_exp_f32_e32 v6, v6
	s_nop 0
	v_add_f32_e32 v8, v6, v7
	v_sub_f32_e32 v7, v10, v160
	v_mul_f32_e32 v7, 0x3d800000, v7
	v_mul_f32_e32 v7, 0x3fb8aa3b, v7
	v_exp_f32_e32 v7, v7
	s_nop 0
	v_add_f32_e32 v9, v7, v8
	v_sub_f32_e32 v8, v11, v160
	v_mul_f32_e32 v8, 0x3d800000, v8
	v_mul_f32_e32 v8, 0x3fb8aa3b, v8
	v_exp_f32_e32 v8, v8
	s_nop 0
	v_add_f32_e32 v10, v8, v9
	v_sub_f32_e32 v9, v12, v160
	v_mul_f32_e32 v9, 0x3d800000, v9
	v_mul_f32_e32 v9, 0x3fb8aa3b, v9
	v_exp_f32_e32 v9, v9
	s_nop 0
	v_add_f32_e32 v11, v9, v10
	v_sub_f32_e32 v10, v13, v160
	v_mul_f32_e32 v10, 0x3d800000, v10
	v_mul_f32_e32 v10, 0x3fb8aa3b, v10
	v_exp_f32_e32 v10, v10
	v_sub_f32_e32 v13, v15, v160
	v_mul_f32_e32 v13, 0x3d800000, v13
	v_mul_f32_e32 v13, 0x3fb8aa3b, v13
	v_add_f32_e32 v12, v10, v11
	v_sub_f32_e32 v11, v14, v160
	v_mul_f32_e32 v11, 0x3d800000, v11
	v_mul_f32_e32 v11, 0x3fb8aa3b, v11
	v_exp_f32_e32 v11, v11
	v_exp_f32_e32 v13, v13
	v_add_f32_e32 v12, v11, v12
	v_add_f32_e32 v12, v13, v12
	ds_bpermute_b32 v14, v184, v12
	s_waitcnt lgkmcnt(0)
	v_add_f32_e32 v12, v12, v14
	v_div_scale_f32 v14, s[18:19], v12, v12, 1.0
	v_rcp_f32_e32 v15, v14
	s_add_i32 s18, s17, s11
	s_ashr_i32 s19, s18, 31
	s_lshl_b64 s[18:19], s[18:19], 17
	v_fma_f32 v16, -v14, v15, 1.0
	v_fmac_f32_e32 v15, v16, v15
	v_div_scale_f32 v16, vcc, 1.0, v12, 1.0
	v_mul_f32_e32 v17, v16, v15
	v_fma_f32 v18, -v14, v17, v16
	v_fmac_f32_e32 v17, v18, v15
	v_fma_f32 v14, -v14, v17, v16
	v_div_fmas_f32 v14, v14, v15, v17
	v_div_fixup_f32 v12, v14, v12, 1.0
	v_mul_f32_e32 v14, v135, v12
	v_cvt_pk_bf16_f32 v16, v14, s0
	v_pk_mul_f32 v[14:15], v[112:113], v[12:13] op_sel_hi:[1,0]
	v_pk_mul_f32 v[0:1], v[0:1], v[12:13] op_sel_hi:[1,0]
	v_cvt_pk_bf16_f32 v17, v14, v15
	v_pk_mul_f32 v[14:15], v[114:115], v[12:13] op_sel_hi:[1,0]
	v_perm_b32 v16, v17, v16, s40
	v_cvt_pk_bf16_f32 v18, v14, v15
	v_pk_mul_f32 v[14:15], v[116:117], v[12:13] op_sel_hi:[1,0]
	v_alignbit_b32 v17, v18, v17, 16
	v_cvt_pk_bf16_f32 v14, v14, v15
	v_mul_f32_e32 v15, v161, v12
	v_cvt_pk_bf16_f32 v15, v15, s0
	v_alignbit_b32 v18, v14, v18, 16
	v_alignbit_b32 v19, v15, v14, 16
	v_mul_f32_e32 v14, v162, v12
	v_cvt_pk_bf16_f32 v20, v14, s0
	v_pk_mul_f32 v[14:15], v[118:119], v[12:13] op_sel_hi:[1,0]
	s_nop 0
	v_cvt_pk_bf16_f32 v21, v14, v15
	v_pk_mul_f32 v[14:15], v[120:121], v[12:13] op_sel_hi:[1,0]
	v_perm_b32 v20, v21, v20, s40
	v_cvt_pk_bf16_f32 v22, v14, v15
	v_pk_mul_f32 v[14:15], v[122:123], v[12:13] op_sel_hi:[1,0]
	v_alignbit_b32 v21, v22, v21, 16
	v_cvt_pk_bf16_f32 v14, v14, v15
	v_mul_f32_e32 v15, v163, v12
	v_cvt_pk_bf16_f32 v15, v15, s0
	v_alignbit_b32 v22, v14, v22, 16
	v_alignbit_b32 v23, v15, v14, 16
	v_mul_f32_e32 v14, v164, v12
	v_cvt_pk_bf16_f32 v24, v14, s0
	v_pk_mul_f32 v[14:15], v[96:97], v[12:13] op_sel_hi:[1,0]
	s_nop 0
	v_cvt_pk_bf16_f32 v25, v14, v15
	v_pk_mul_f32 v[14:15], v[98:99], v[12:13] op_sel_hi:[1,0]
	v_perm_b32 v24, v25, v24, s40
	v_cvt_pk_bf16_f32 v26, v14, v15
	v_pk_mul_f32 v[14:15], v[100:101], v[12:13] op_sel_hi:[1,0]
	v_alignbit_b32 v25, v26, v25, 16
	v_cvt_pk_bf16_f32 v14, v14, v15
	v_mul_f32_e32 v15, v165, v12
	v_cvt_pk_bf16_f32 v15, v15, s0
	v_alignbit_b32 v26, v14, v26, 16
	v_alignbit_b32 v27, v15, v14, 16
	v_mul_f32_e32 v14, v166, v12
	v_cvt_pk_bf16_f32 v28, v14, s0
	v_pk_mul_f32 v[14:15], v[102:103], v[12:13] op_sel_hi:[1,0]
	s_nop 0
	v_cvt_pk_bf16_f32 v29, v14, v15
	v_pk_mul_f32 v[14:15], v[104:105], v[12:13] op_sel_hi:[1,0]
	v_perm_b32 v28, v29, v28, s40
	v_cvt_pk_bf16_f32 v30, v14, v15
	v_pk_mul_f32 v[14:15], v[106:107], v[12:13] op_sel_hi:[1,0]
	v_alignbit_b32 v29, v30, v29, 16
	v_cvt_pk_bf16_f32 v14, v14, v15
	v_mul_f32_e32 v15, v167, v12
	v_cvt_pk_bf16_f32 v15, v15, s0
	v_alignbit_b32 v30, v14, v30, 16
	v_alignbit_b32 v31, v15, v14, 16
	v_mul_f32_e32 v14, v168, v12
	v_cvt_pk_bf16_f32 v32, v14, s0
	v_pk_mul_f32 v[14:15], v[80:81], v[12:13] op_sel_hi:[1,0]
	v_lshl_add_u64 v[80:81], v[130:131], 0, s[18:19]
	v_cvt_pk_bf16_f32 v33, v14, v15
	v_pk_mul_f32 v[14:15], v[82:83], v[12:13] op_sel_hi:[1,0]
	v_perm_b32 v32, v33, v32, s40
	v_cvt_pk_bf16_f32 v34, v14, v15
	v_pk_mul_f32 v[14:15], v[84:85], v[12:13] op_sel_hi:[1,0]
	v_alignbit_b32 v33, v34, v33, 16
	v_cvt_pk_bf16_f32 v14, v14, v15
	v_mul_f32_e32 v15, v169, v12
	v_cvt_pk_bf16_f32 v15, v15, s0
	v_alignbit_b32 v34, v14, v34, 16
	v_alignbit_b32 v35, v15, v14, 16
	v_mul_f32_e32 v14, v170, v12
	v_cvt_pk_bf16_f32 v36, v14, s0
	v_pk_mul_f32 v[14:15], v[86:87], v[12:13] op_sel_hi:[1,0]
	s_nop 0
	v_cvt_pk_bf16_f32 v37, v14, v15
	v_pk_mul_f32 v[14:15], v[88:89], v[12:13] op_sel_hi:[1,0]
	v_perm_b32 v36, v37, v36, s40
	v_cvt_pk_bf16_f32 v38, v14, v15
	v_pk_mul_f32 v[14:15], v[90:91], v[12:13] op_sel_hi:[1,0]
	v_alignbit_b32 v37, v38, v37, 16
	v_cvt_pk_bf16_f32 v14, v14, v15
	v_mul_f32_e32 v15, v171, v12
	v_cvt_pk_bf16_f32 v15, v15, s0
	v_alignbit_b32 v38, v14, v38, 16
	v_alignbit_b32 v39, v15, v14, 16
	v_mul_f32_e32 v14, v172, v12
	v_cvt_pk_bf16_f32 v40, v14, s0
	v_pk_mul_f32 v[14:15], v[64:65], v[12:13] op_sel_hi:[1,0]
	v_mov_b32_e32 v88, v143
	v_cvt_pk_bf16_f32 v41, v14, v15
	v_pk_mul_f32 v[14:15], v[66:67], v[12:13] op_sel_hi:[1,0]
	v_perm_b32 v40, v41, v40, s40
	v_cvt_pk_bf16_f32 v42, v14, v15
	v_pk_mul_f32 v[14:15], v[68:69], v[12:13] op_sel_hi:[1,0]
	v_alignbit_b32 v41, v42, v41, 16
	v_cvt_pk_bf16_f32 v14, v14, v15
	v_mul_f32_e32 v15, v173, v12
	v_cvt_pk_bf16_f32 v15, v15, s0
	v_alignbit_b32 v42, v14, v42, 16
	v_alignbit_b32 v43, v15, v14, 16
	v_mul_f32_e32 v14, v174, v12
	v_cvt_pk_bf16_f32 v44, v14, s0
	v_pk_mul_f32 v[14:15], v[70:71], v[12:13] op_sel_hi:[1,0]
	s_nop 0
	v_cvt_pk_bf16_f32 v45, v14, v15
	v_pk_mul_f32 v[14:15], v[72:73], v[12:13] op_sel_hi:[1,0]
	v_perm_b32 v44, v45, v44, s40
	v_cvt_pk_bf16_f32 v46, v14, v15
	v_pk_mul_f32 v[14:15], v[74:75], v[12:13] op_sel_hi:[1,0]
	v_alignbit_b32 v45, v46, v45, 16
	v_cvt_pk_bf16_f32 v14, v14, v15
	v_mul_f32_e32 v15, v176, v12
	v_cvt_pk_bf16_f32 v15, v15, s0
	v_alignbit_b32 v46, v14, v46, 16
	v_alignbit_b32 v47, v15, v14, 16
	v_mul_f32_e32 v14, v177, v12
	v_cvt_pk_bf16_f32 v64, v14, s0
	v_pk_mul_f32 v[14:15], v[48:49], v[12:13] op_sel_hi:[1,0]
	s_nop 0
	v_cvt_pk_bf16_f32 v49, v14, v15
	v_pk_mul_f32 v[14:15], v[50:51], v[12:13] op_sel_hi:[1,0]
	v_perm_b32 v48, v49, v64, s40
	v_cvt_pk_bf16_f32 v50, v14, v15
	v_pk_mul_f32 v[14:15], v[52:53], v[12:13] op_sel_hi:[1,0]
	v_alignbit_b32 v49, v50, v49, 16
	v_cvt_pk_bf16_f32 v14, v14, v15
	v_mul_f32_e32 v15, v178, v12
	v_cvt_pk_bf16_f32 v15, v15, s0
	v_alignbit_b32 v50, v14, v50, 16
	v_alignbit_b32 v51, v15, v14, 16
	v_mul_f32_e32 v14, v179, v12
	v_cvt_pk_bf16_f32 v52, v14, s0
	v_pk_mul_f32 v[14:15], v[54:55], v[12:13] op_sel_hi:[1,0]
	s_nop 0
	v_cvt_pk_bf16_f32 v53, v14, v15
	v_pk_mul_f32 v[14:15], v[56:57], v[12:13] op_sel_hi:[1,0]
	v_perm_b32 v52, v53, v52, s40
	v_cvt_pk_bf16_f32 v54, v14, v15
	v_pk_mul_f32 v[14:15], v[58:59], v[12:13] op_sel_hi:[1,0]
	v_alignbit_b32 v53, v54, v53, 16
	v_cvt_pk_bf16_f32 v14, v14, v15
	v_mul_f32_e32 v15, v180, v12
	v_cvt_pk_bf16_f32 v15, v15, s0
	v_alignbit_b32 v54, v14, v54, 16
	v_alignbit_b32 v55, v15, v14, 16
	v_mul_f32_e32 v14, v181, v12
	v_cvt_pk_bf16_f32 v56, v14, s0
	v_pk_mul_f32 v[14:15], v[60:61], v[12:13] op_sel_hi:[1,0]
	s_nop 0
	v_cvt_pk_bf16_f32 v57, v14, v15
	v_pk_mul_f32 v[14:15], v[62:63], v[12:13] op_sel_hi:[1,0]
	v_perm_b32 v56, v57, v56, s40
	v_cvt_pk_bf16_f32 v58, v14, v15
	v_pk_mul_f32 v[14:15], v[76:77], v[12:13] op_sel_hi:[1,0]
	v_alignbit_b32 v57, v58, v57, 16
	v_cvt_pk_bf16_f32 v14, v14, v15
	v_mul_f32_e32 v15, v182, v12
	v_cvt_pk_bf16_f32 v15, v15, s0
	v_alignbit_b32 v58, v14, v58, 16
	v_alignbit_b32 v59, v15, v14, 16
	v_mul_f32_e32 v14, v183, v12
	v_cvt_pk_bf16_f32 v60, v14, s0
	v_pk_mul_f32 v[14:15], v[78:79], v[12:13] op_sel_hi:[1,0]
	s_nop 0
	v_cvt_pk_bf16_f32 v61, v14, v15
	v_pk_mul_f32 v[14:15], v[92:93], v[12:13] op_sel_hi:[1,0]
	v_perm_b32 v60, v61, v60, s40
	v_cvt_pk_bf16_f32 v62, v14, v15
	v_pk_mul_f32 v[14:15], v[94:95], v[12:13] op_sel_hi:[1,0]
	v_alignbit_b32 v61, v62, v61, 16
	v_cvt_pk_bf16_f32 v14, v14, v15
	v_mul_f32_e32 v15, v190, v12
	v_cvt_pk_bf16_f32 v15, v15, s0
	v_alignbit_b32 v62, v14, v62, 16
	v_alignbit_b32 v63, v15, v14, 16
	v_mul_f32_e32 v14, v195, v12
	v_cvt_pk_bf16_f32 v64, v14, s0
	v_pk_mul_f32 v[14:15], v[108:109], v[12:13] op_sel_hi:[1,0]
	s_nop 0
	v_cvt_pk_bf16_f32 v65, v14, v15
	v_pk_mul_f32 v[14:15], v[110:111], v[12:13] op_sel_hi:[1,0]
	v_perm_b32 v64, v65, v64, s40
	v_cvt_pk_bf16_f32 v66, v14, v15
	v_pk_mul_f32 v[14:15], v[124:125], v[12:13] op_sel_hi:[1,0]
	v_alignbit_b32 v65, v66, v65, 16
	v_cvt_pk_bf16_f32 v14, v14, v15
	v_mul_f32_e32 v15, v206, v12
	v_cvt_pk_bf16_f32 v15, v15, s0
	v_alignbit_b32 v66, v14, v66, 16
	v_alignbit_b32 v67, v15, v14, 16
	v_mul_f32_e32 v14, v207, v12
	v_cvt_pk_bf16_f32 v68, v14, s0
	v_pk_mul_f32 v[14:15], v[126:127], v[12:13] op_sel_hi:[1,0]
	s_nop 0
	v_cvt_pk_bf16_f32 v69, v14, v15
	v_pk_mul_f32 v[14:15], v[136:137], v[12:13] op_sel_hi:[1,0]
	v_perm_b32 v68, v69, v68, s40
	v_cvt_pk_bf16_f32 v70, v14, v15
	v_pk_mul_f32 v[14:15], v[138:139], v[12:13] op_sel_hi:[1,0]
	v_alignbit_b32 v69, v70, v69, 16
	v_cvt_pk_bf16_f32 v14, v14, v15
	v_mul_f32_e32 v15, v208, v12
	v_cvt_pk_bf16_f32 v15, v15, s0
	v_alignbit_b32 v71, v15, v14, 16
	v_cvt_pk_bf16_f32 v15, v0, v1
	v_pk_mul_f32 v[0:1], v[2:3], v[12:13] op_sel_hi:[1,0]
	v_alignbit_b32 v70, v14, v70, 16
	v_cvt_pk_bf16_f32 v2, v0, v1
	v_pk_mul_f32 v[0:1], v[4:5], v[12:13] op_sel_hi:[1,0]
	v_alignbit_b32 v73, v2, v15, 16
	v_cvt_pk_bf16_f32 v0, v0, v1
	v_mul_f32_e32 v1, v210, v12
	v_cvt_pk_bf16_f32 v1, v1, s0
	v_alignbit_b32 v74, v0, v2, 16
	v_alignbit_b32 v75, v1, v0, 16
	v_mul_f32_e32 v0, v211, v12
	v_cvt_pk_bf16_f32 v2, v0, s0
	v_pk_mul_f32 v[0:1], v[6:7], v[12:13] op_sel_hi:[1,0]
	v_mul_f32_e32 v14, v209, v12
	v_cvt_pk_bf16_f32 v3, v0, v1
	v_pk_mul_f32 v[0:1], v[8:9], v[12:13] op_sel_hi:[1,0]
	v_perm_b32 v76, v3, v2, s40
	v_cvt_pk_bf16_f32 v2, v0, v1
	v_pk_mul_f32 v[0:1], v[10:11], v[12:13] op_sel_hi:[1,0]
	v_cvt_pk_bf16_f32 v14, v14, s0
	v_cvt_pk_bf16_f32 v0, v0, v1
	v_mul_f32_e32 v1, v13, v12
	v_cvt_pk_bf16_f32 v1, v1, s0
	v_perm_b32 v72, v15, v14, s40
	v_alignbit_b32 v77, v2, v3, 16
	v_alignbit_b32 v78, v0, v2, 16
	v_alignbit_b32 v79, v1, v0, 16
	global_load_dwordx4 v[0:3], v[80:81], off offset:48
	global_load_dwordx4 v[4:7], v[80:81], off offset:32
	global_load_dwordx4 v[8:11], v[80:81], off offset:16
	global_load_dwordx4 v[12:15], v[80:81], off
	s_waitcnt vmcnt(0)
	ds_write_b128 v142, v[12:15]
	ds_write_b128 v142, v[8:11] offset:16
	ds_write_b128 v142, v[4:7] offset:32
	ds_write_b128 v142, v[0:3] offset:48
	global_load_dwordx4 v[0:3], v[80:81], off offset:112
	global_load_dwordx4 v[4:7], v[80:81], off offset:96
	global_load_dwordx4 v[8:11], v[80:81], off offset:80
	global_load_dwordx4 v[12:15], v[80:81], off offset:64
	s_waitcnt vmcnt(0)
	ds_write_b128 v142, v[12:15] offset:64
	ds_write_b128 v142, v[8:11] offset:80
	ds_write_b128 v142, v[4:7] offset:96
	ds_write_b128 v142, v[0:3] offset:112
	global_load_dwordx4 v[0:3], v[80:81], off offset:176
	global_load_dwordx4 v[4:7], v[80:81], off offset:160
	global_load_dwordx4 v[8:11], v[80:81], off offset:144
	global_load_dwordx4 v[12:15], v[80:81], off offset:128
	s_waitcnt vmcnt(0)
	ds_write_b128 v142, v[12:15] offset:128
	ds_write_b128 v142, v[8:11] offset:144
	ds_write_b128 v142, v[4:7] offset:160
	ds_write_b128 v142, v[0:3] offset:176
	global_load_dwordx4 v[0:3], v[80:81], off offset:240
	global_load_dwordx4 v[4:7], v[80:81], off offset:224
	global_load_dwordx4 v[8:11], v[80:81], off offset:208
	global_load_dwordx4 v[12:15], v[80:81], off offset:192
	s_waitcnt vmcnt(0)
	ds_write_b128 v142, v[12:15] offset:192
	ds_write_b128 v142, v[8:11] offset:208
	ds_write_b128 v142, v[4:7] offset:224
	ds_write_b128 v142, v[0:3] offset:240
	v_add_u32_e32 v0, s10, v152
	v_ashrrev_i32_e32 v1, 31, v0
	v_lshlrev_b64 v[0:1], 11, v[0:1]
	v_lshl_add_u64 v[0:1], v[0:1], 0, s[8:9]
	v_lshl_add_u64 v[80:81], v[132:133], 0, v[0:1]
	v_add_u32_e32 v0, s10, v153
	v_ashrrev_i32_e32 v1, 31, v0
	v_lshlrev_b64 v[0:1], 11, v[0:1]
	v_lshl_add_u64 v[0:1], v[0:1], 0, s[8:9]
	v_lshl_add_u64 v[82:83], v[132:133], 0, v[0:1]
	v_add_u32_e32 v0, s10, v154
	v_ashrrev_i32_e32 v1, 31, v0
	v_lshlrev_b64 v[0:1], 11, v[0:1]
	v_lshl_add_u64 v[0:1], v[0:1], 0, s[8:9]
	v_lshl_add_u64 v[84:85], v[132:133], 0, v[0:1]
	v_add_u32_e32 v0, s10, v155
	v_ashrrev_i32_e32 v1, 31, v0
	v_lshlrev_b64 v[0:1], 11, v[0:1]
	v_lshl_add_u64 v[0:1], v[0:1], 0, s[8:9]
	v_lshl_add_u64 v[86:87], v[132:133], 0, v[0:1]
	s_mov_b64 s[8:9], 0
	s_waitcnt lgkmcnt(0)
	s_barrier
.LBB0_533:
	ds_read_b128 v[0:3], v88
	ds_read_b128 v[90:93], v88 offset:32
	ds_read_b128 v[94:97], v88 offset:64
	ds_read_b128 v[98:101], v88 offset:96
	s_waitcnt lgkmcnt(3)
	v_mfma_f32_32x32x16_bf16 v[0:15], v[16:19], v[0:3], 0
	s_waitcnt lgkmcnt(2)
	v_mfma_f32_32x32x16_bf16 v[0:15], v[20:23], v[90:93], v[0:15]
	s_waitcnt lgkmcnt(1)
	v_mfma_f32_32x32x16_bf16 v[0:15], v[24:27], v[94:97], v[0:15]
	s_waitcnt lgkmcnt(0)
	v_mfma_f32_32x32x16_bf16 v[0:15], v[28:31], v[98:101], v[0:15]
	ds_read_b128 v[90:93], v88 offset:128
	ds_read_b128 v[94:97], v88 offset:160
	ds_read_b128 v[98:101], v88 offset:192
	ds_read_b128 v[102:105], v88 offset:224
	s_waitcnt lgkmcnt(3)
	v_mfma_f32_32x32x16_bf16 v[0:15], v[32:35], v[90:93], v[0:15]
	s_waitcnt lgkmcnt(2)
	v_mfma_f32_32x32x16_bf16 v[0:15], v[36:39], v[94:97], v[0:15]
	s_waitcnt lgkmcnt(1)
	v_mfma_f32_32x32x16_bf16 v[0:15], v[40:43], v[98:101], v[0:15]
	s_waitcnt lgkmcnt(0)
	v_mfma_f32_32x32x16_bf16 v[0:15], v[44:47], v[102:105], v[0:15]
	ds_read_b128 v[90:93], v88 offset:256
	ds_read_b128 v[94:97], v88 offset:288
	ds_read_b128 v[98:101], v88 offset:320
	ds_read_b128 v[102:105], v88 offset:352
	s_waitcnt lgkmcnt(3)
	v_mfma_f32_32x32x16_bf16 v[0:15], v[48:51], v[90:93], v[0:15]
	s_waitcnt lgkmcnt(2)
	v_mfma_f32_32x32x16_bf16 v[0:15], v[52:55], v[94:97], v[0:15]
	s_waitcnt lgkmcnt(1)
	v_mfma_f32_32x32x16_bf16 v[0:15], v[56:59], v[98:101], v[0:15]
	s_waitcnt lgkmcnt(0)
	v_mfma_f32_32x32x16_bf16 v[0:15], v[60:63], v[102:105], v[0:15]
	ds_read_b128 v[90:93], v88 offset:384
	ds_read_b128 v[94:97], v88 offset:416
	ds_read_b128 v[98:101], v88 offset:448
	ds_read_b128 v[102:105], v88 offset:480
	s_waitcnt lgkmcnt(3)
	v_mfma_f32_32x32x16_bf16 v[0:15], v[64:67], v[90:93], v[0:15]
	s_waitcnt lgkmcnt(2)
	v_mfma_f32_32x32x16_bf16 v[0:15], v[68:71], v[94:97], v[0:15]
	s_waitcnt lgkmcnt(1)
	v_mfma_f32_32x32x16_bf16 v[0:15], v[72:75], v[98:101], v[0:15]
	s_waitcnt lgkmcnt(0)
	v_mfma_f32_32x32x16_bf16 v[0:15], v[76:79], v[102:105], v[0:15]
	v_lshl_add_u64 v[90:91], v[80:81], 0, s[8:9]
	v_add_co_u32_e32 v92, vcc, s41, v90
	s_nop 9
	v_cvt_pk_bf16_f32 v0, v0, s0
	v_addc_co_u32_e32 v93, vcc, 0, v91, vcc
	v_add_co_u32_e32 v90, vcc, s73, v90
	v_cvt_pk_bf16_f32 v4, v4, s0
	s_nop 0
	v_addc_co_u32_e32 v91, vcc, 0, v91, vcc
	global_store_short v[90:91], v0, off offset:-4096
	v_cvt_pk_bf16_f32 v0, v1, s0
	global_store_short v[92:93], v0, off offset:2048
	v_cvt_pk_bf16_f32 v0, v2, s0
	global_store_short v[90:91], v0, off
	v_cvt_pk_bf16_f32 v0, v3, s0
	global_store_short v[90:91], v0, off offset:2048
	v_lshl_add_u64 v[0:1], v[84:85], 0, s[8:9]
	v_add_co_u32_e32 v2, vcc, s41, v0
	v_add_u32_e32 v88, 0x4200, v88
	s_nop 0
	v_addc_co_u32_e32 v3, vcc, 0, v1, vcc
	v_add_co_u32_e32 v0, vcc, s73, v0
	s_nop 1
	v_addc_co_u32_e32 v1, vcc, 0, v1, vcc
	global_store_short v[0:1], v4, off offset:-4096
	v_cvt_pk_bf16_f32 v4, v5, s0
	global_store_short v[2:3], v4, off offset:2048
	v_cvt_pk_bf16_f32 v2, v6, s0
	global_store_short v[0:1], v2, off
	v_cvt_pk_bf16_f32 v2, v7, s0
	global_store_short v[0:1], v2, off offset:2048
	v_lshl_add_u64 v[0:1], v[86:87], 0, s[8:9]
	v_add_co_u32_e32 v2, vcc, s41, v0
	v_cvt_pk_bf16_f32 v4, v8, s0
	s_nop 0
	v_addc_co_u32_e32 v3, vcc, 0, v1, vcc
	v_add_co_u32_e32 v0, vcc, s73, v0
	s_nop 1
	v_addc_co_u32_e32 v1, vcc, 0, v1, vcc
	global_store_short v[0:1], v4, off offset:-4096
	v_cvt_pk_bf16_f32 v4, v9, s0
	global_store_short v[2:3], v4, off offset:2048
	v_cvt_pk_bf16_f32 v2, v10, s0
	global_store_short v[0:1], v2, off
	v_cvt_pk_bf16_f32 v2, v11, s0
	global_store_short v[0:1], v2, off offset:2048
	v_lshl_add_u64 v[0:1], v[82:83], 0, s[8:9]
	v_add_co_u32_e32 v2, vcc, s41, v0
	v_cvt_pk_bf16_f32 v4, v12, s0
	s_nop 0
	v_addc_co_u32_e32 v3, vcc, 0, v1, vcc
	v_add_co_u32_e32 v0, vcc, s73, v0
	s_add_u32 s8, s8, 64
	s_nop 0
	v_addc_co_u32_e32 v1, vcc, 0, v1, vcc
	global_store_short v[0:1], v4, off offset:-4096
	v_cvt_pk_bf16_f32 v4, v13, s0
	global_store_short v[2:3], v4, off offset:2048
	v_cvt_pk_bf16_f32 v2, v14, s0
	s_addc_u32 s9, s9, 0
	global_store_short v[0:1], v2, off
	v_cvt_pk_bf16_f32 v2, v15, s0
	s_cmpk_lg_i32 s8, 0x200
	global_store_short v[0:1], v2, off offset:2048
	s_cbranch_scc1 .LBB0_533
	s_add_i32 s16, s16, 1
	s_mov_b64 s[10:11], 0
	s_branch .LBB0_526

.LBB0_704:
	v_cndmask_b32_e64 v0, 0, 1, s[6:7]
	s_lshl_b32 s36, s8, 8
	v_cmp_ne_u32_e32 vcc, 1, v0
	v_lshl_add_u64 v[0:1], v[178:179], 0, s[36:37]
	global_load_dwordx4 v[44:47], v[0:1], off
	global_load_dwordx4 v[40:43], v[0:1], off offset:32
	global_load_dwordx4 v[36:39], v[0:1], off offset:64
	global_load_dwordx4 v[32:35], v[0:1], off offset:96
	global_load_dwordx4 v[28:31], v[0:1], off offset:128
	global_load_dwordx4 v[24:27], v[0:1], off offset:160
	global_load_dwordx4 v[20:23], v[0:1], off offset:192
	global_load_dwordx4 v[16:19], v[0:1], off offset:224
	v_lshl_or_b32 v180, s8, 7, v209
	v_ashrrev_i32_e32 v181, 31, v180
	v_lshlrev_b64 v[0:1], 8, v[180:181]
	v_lshl_add_u64 v[60:61], v[64:65], 0, v[0:1]
	global_load_dwordx4 v[0:3], v[60:61], off
	global_load_dwordx4 v[48:51], v[60:61], off offset:32
	global_load_dwordx4 v[52:55], v[60:61], off offset:64
	global_load_dwordx4 v[56:59], v[60:61], off offset:96
	s_waitcnt vmcnt(0)
	v_mfma_f32_32x32x16_bf16 v[0:15], v[0:3], v[44:47], 0
	v_mfma_f32_32x32x16_bf16 v[0:15], v[48:51], v[40:43], v[0:15]
	v_mfma_f32_32x32x16_bf16 v[0:15], v[52:55], v[36:39], v[0:15]
	v_mfma_f32_32x32x16_bf16 v[0:15], v[56:59], v[32:35], v[0:15]
	global_load_dwordx4 v[48:51], v[60:61], off offset:128
	global_load_dwordx4 v[52:55], v[60:61], off offset:160
	global_load_dwordx4 v[56:59], v[60:61], off offset:192
	s_nop 0
	global_load_dwordx4 v[60:63], v[60:61], off offset:224
	s_waitcnt vmcnt(3)
	v_mfma_f32_32x32x16_bf16 v[0:15], v[48:51], v[28:31], v[0:15]
	s_waitcnt vmcnt(2)
	v_mfma_f32_32x32x16_bf16 v[0:15], v[52:55], v[24:27], v[0:15]
	s_waitcnt vmcnt(1)
	v_mfma_f32_32x32x16_bf16 v[0:15], v[56:59], v[20:23], v[0:15]
	s_waitcnt vmcnt(0)
	v_mfma_f32_32x32x16_bf16 v[0:15], v[60:63], v[16:19], v[0:15]
	v_or_b32_e32 v49, 1, v66
	v_xor_b32_e32 v51, 0x7e, v66
	s_nop 9
	v_cmp_gt_i32_e64 s[6:7], 0, v1
	v_xor_b32_e32 v48, 0x7f, v66
	v_and_b32_e32 v1, 0xffffff80, v1
	v_cndmask_b32_e64 v49, v51, v49, s[6:7]
	v_cmp_gt_i32_e64 s[6:7], 0, v0
	v_and_b32_e32 v0, 0xffffff80, v0
	v_or_b32_e32 v210, v49, v1
	v_cndmask_b32_e64 v48, v48, v66, s[6:7]
	v_or_b32_e32 v211, v48, v0
	v_or_b32_e32 v48, 32, v180
	v_ashrrev_i32_e32 v49, 31, v48
	v_lshlrev_b64 v[48:49], 8, v[48:49]
	v_lshl_add_u64 v[182:183], v[64:65], 0, v[48:49]
	global_load_dwordx4 v[60:63], v[182:183], off
	global_load_dwordx4 v[56:59], v[182:183], off offset:32
	global_load_dwordx4 v[52:55], v[182:183], off offset:64
	global_load_dwordx4 v[48:51], v[182:183], off offset:96
	v_or_b32_e32 v1, 3, v66
	v_xor_b32_e32 v173, 0x7c, v66
	v_cmp_gt_i32_e64 s[6:7], 0, v3
	v_or_b32_e32 v0, 2, v66
	v_xor_b32_e32 v190, 0x7d, v66
	v_cndmask_b32_e64 v1, v173, v1, s[6:7]
	v_cmp_gt_i32_e64 s[6:7], 0, v2
	v_and_b32_e32 v3, 0xffffff80, v3
	v_and_b32_e32 v2, 0xffffff80, v2
	v_cndmask_b32_e64 v0, v190, v0, s[6:7]
	v_or_b32_e32 v173, v1, v3
	v_or_b32_e32 v1, 9, v66
	v_xor_b32_e32 v3, 0x76, v66
	v_cmp_gt_i32_e64 s[6:7], 0, v5
	v_or_b32_e32 v212, v0, v2
	v_or_b32_e32 v0, 8, v66
	v_cndmask_b32_e64 v1, v3, v1, s[6:7]
	v_xor_b32_e32 v2, 0x77, v66
	v_cmp_gt_i32_e64 s[6:7], 0, v4
	v_and_b32_e32 v3, 0xffffff80, v4
	s_nop 0
	v_cndmask_b32_e64 v0, v2, v0, s[6:7]
	v_and_b32_e32 v2, 0xffffff80, v5
	v_or_b32_e32 v213, v1, v2
	v_or_b32_e32 v214, v0, v3
	v_or_b32_e32 v1, 11, v66
	v_xor_b32_e32 v3, 0x74, v66
	v_cmp_gt_i32_e64 s[6:7], 0, v7
	v_or_b32_e32 v0, 10, v66
	v_xor_b32_e32 v2, 0x75, v66
	v_cndmask_b32_e64 v1, v3, v1, s[6:7]
	v_cmp_gt_i32_e64 s[6:7], 0, v6
	v_and_b32_e32 v3, 0xffffff80, v6
	s_nop 0
	v_cndmask_b32_e64 v0, v2, v0, s[6:7]
	v_and_b32_e32 v2, 0xffffff80, v7
	v_or_b32_e32 v215, v1, v2
	v_or_b32_e32 v216, v0, v3
	v_or_b32_e32 v1, 17, v66
	v_xor_b32_e32 v3, 0x6e, v66
	v_cmp_gt_i32_e64 s[6:7], 0, v9
	v_or_b32_e32 v0, 16, v66
	v_xor_b32_e32 v2, 0x6f, v66
	v_cndmask_b32_e64 v1, v3, v1, s[6:7]
	v_cmp_gt_i32_e64 s[6:7], 0, v8
	v_and_b32_e32 v3, 0xffffff80, v8
	s_nop 0
	v_cndmask_b32_e64 v0, v2, v0, s[6:7]
	v_and_b32_e32 v2, 0xffffff80, v9
	v_or_b32_e32 v217, v1, v2
	v_or_b32_e32 v218, v0, v3
	v_or_b32_e32 v1, 19, v66
	v_xor_b32_e32 v3, 0x6c, v66
	v_cmp_gt_i32_e64 s[6:7], 0, v11
	v_or_b32_e32 v0, 18, v66
	v_xor_b32_e32 v2, 0x6d, v66
	v_cndmask_b32_e64 v1, v3, v1, s[6:7]
	v_cmp_gt_i32_e64 s[6:7], 0, v10
	v_and_b32_e32 v3, 0xffffff80, v10
	s_nop 0
	v_cndmask_b32_e64 v0, v2, v0, s[6:7]
	v_and_b32_e32 v2, 0xffffff80, v11
	v_or_b32_e32 v219, v1, v2
	v_or_b32_e32 v220, v0, v3
	v_or_b32_e32 v1, 25, v66
	v_xor_b32_e32 v3, 0x66, v66
	v_cmp_gt_i32_e64 s[6:7], 0, v13
	v_or_b32_e32 v0, 24, v66
	v_xor_b32_e32 v2, 0x67, v66
	v_cndmask_b32_e64 v1, v3, v1, s[6:7]
	v_cmp_gt_i32_e64 s[6:7], 0, v12
	v_and_b32_e32 v3, 0xffffff80, v12
	s_nop 0
	v_cndmask_b32_e64 v0, v2, v0, s[6:7]
	v_and_b32_e32 v2, 0xffffff80, v13
	v_or_b32_e32 v221, v1, v2
	v_or_b32_e32 v1, 27, v66
	v_cmp_gt_i32_e64 s[6:7], 0, v15
	v_or_b32_e32 v222, v0, v3
	v_and_b32_e32 v2, 0xffffff80, v15
	v_cndmask_b32_e64 v0, v67, v1, s[6:7]
	v_cmp_gt_i32_e64 s[6:7], 0, v14
	v_and_b32_e32 v3, 0xffffff80, v14
	v_or_b32_e32 v223, v0, v2
	v_cndmask_b32_e64 v1, v70, v68, s[6:7]
	v_or_b32_e32 v224, v1, v3
	s_waitcnt vmcnt(3)
	v_mfma_f32_32x32x16_bf16 v[0:15], v[60:63], v[44:47], 0
	s_waitcnt vmcnt(2)
	v_mfma_f32_32x32x16_bf16 v[0:15], v[56:59], v[40:43], v[0:15]
	s_waitcnt vmcnt(1)
	v_mfma_f32_32x32x16_bf16 v[0:15], v[52:55], v[36:39], v[0:15]
	s_waitcnt vmcnt(0)
	v_mfma_f32_32x32x16_bf16 v[0:15], v[48:51], v[32:35], v[0:15]
	global_load_dwordx4 v[48:51], v[182:183], off offset:128
	global_load_dwordx4 v[52:55], v[182:183], off offset:160
	global_load_dwordx4 v[56:59], v[182:183], off offset:192
	global_load_dwordx4 v[60:63], v[182:183], off offset:224
	s_waitcnt vmcnt(3)
	v_mfma_f32_32x32x16_bf16 v[0:15], v[48:51], v[28:31], v[0:15]
	s_waitcnt vmcnt(2)
	v_mfma_f32_32x32x16_bf16 v[0:15], v[52:55], v[24:27], v[0:15]
	s_waitcnt vmcnt(1)
	v_mfma_f32_32x32x16_bf16 v[0:15], v[56:59], v[20:23], v[0:15]
	s_waitcnt vmcnt(0)
	v_mfma_f32_32x32x16_bf16 v[0:15], v[60:63], v[16:19], v[0:15]
	v_or_b32_e32 v48, 64, v180
	v_ashrrev_i32_e32 v49, 31, v48
	v_lshlrev_b64 v[48:49], 8, v[48:49]
	v_lshl_add_u64 v[182:183], v[64:65], 0, v[48:49]
	global_load_dwordx4 v[60:63], v[182:183], off
	global_load_dwordx4 v[56:59], v[182:183], off offset:32
	global_load_dwordx4 v[52:55], v[182:183], off offset:64
	global_load_dwordx4 v[48:51], v[182:183], off offset:96
	s_nop 3
	v_cmp_gt_i32_e64 s[6:7], 0, v1
	v_and_b32_e32 v1, 0xffffff80, v1
	s_nop 0
	v_cndmask_b32_e64 v181, v71, v69, s[6:7]
	v_cmp_gt_i32_e64 s[6:7], 0, v0
	v_and_b32_e32 v0, 0xffffff80, v0
	v_or_b32_e32 v225, v181, v1
	v_cndmask_b32_e64 v190, v74, v72, s[6:7]
	v_cmp_gt_i32_e64 s[6:7], 0, v3
	v_or_b32_e32 v226, v190, v0
	v_and_b32_e32 v3, 0xffffff80, v3
	v_cndmask_b32_e64 v0, v75, v73, s[6:7]
	v_cmp_gt_i32_e64 s[6:7], 0, v2
	v_and_b32_e32 v2, 0xffffff80, v2
	v_or_b32_e32 v227, v0, v3
	v_cndmask_b32_e64 v1, v78, v76, s[6:7]
	v_cmp_gt_i32_e64 s[6:7], 0, v5
	v_or_b32_e32 v228, v1, v2
	v_and_b32_e32 v2, 0xffffff80, v5
	v_cndmask_b32_e64 v0, v79, v77, s[6:7]
	v_cmp_gt_i32_e64 s[6:7], 0, v4
	v_and_b32_e32 v3, 0xffffff80, v4
	v_or_b32_e32 v229, v0, v2
	v_cndmask_b32_e64 v1, v82, v80, s[6:7]
	v_cmp_gt_i32_e64 s[6:7], 0, v7
	v_or_b32_e32 v230, v1, v3
	v_and_b32_e32 v2, 0xffffff80, v7
	v_cndmask_b32_e64 v0, v83, v81, s[6:7]
	v_cmp_gt_i32_e64 s[6:7], 0, v6
	v_and_b32_e32 v3, 0xffffff80, v6
	v_or_b32_e32 v231, v0, v2
	v_cndmask_b32_e64 v1, v86, v84, s[6:7]
	v_cmp_gt_i32_e64 s[6:7], 0, v9
	v_or_b32_e32 v232, v1, v3
	v_and_b32_e32 v2, 0xffffff80, v9
	v_cndmask_b32_e64 v0, v87, v85, s[6:7]
	v_cmp_gt_i32_e64 s[6:7], 0, v8
	v_and_b32_e32 v3, 0xffffff80, v8
	v_or_b32_e32 v233, v0, v2
	v_cndmask_b32_e64 v1, v90, v88, s[6:7]
	v_cmp_gt_i32_e64 s[6:7], 0, v11
	v_or_b32_e32 v234, v1, v3
	v_and_b32_e32 v2, 0xffffff80, v11
	v_cndmask_b32_e64 v0, v91, v89, s[6:7]
	v_cmp_gt_i32_e64 s[6:7], 0, v10
	v_and_b32_e32 v3, 0xffffff80, v10
	v_or_b32_e32 v235, v0, v2
	v_cndmask_b32_e64 v1, v94, v92, s[6:7]
	v_cmp_gt_i32_e64 s[6:7], 0, v13
	v_or_b32_e32 v236, v1, v3
	v_and_b32_e32 v2, 0xffffff80, v13
	v_cndmask_b32_e64 v0, v95, v93, s[6:7]
	v_cmp_gt_i32_e64 s[6:7], 0, v12
	v_and_b32_e32 v3, 0xffffff80, v12
	v_or_b32_e32 v237, v0, v2
	v_cndmask_b32_e64 v1, v98, v96, s[6:7]
	v_cmp_gt_i32_e64 s[6:7], 0, v15
	v_or_b32_e32 v238, v1, v3
	v_and_b32_e32 v2, 0xffffff80, v15
	v_cndmask_b32_e64 v0, v99, v97, s[6:7]
	v_cmp_gt_i32_e64 s[6:7], 0, v14
	v_and_b32_e32 v3, 0xffffff80, v14
	v_or_b32_e32 v239, v0, v2
	v_cndmask_b32_e64 v1, v102, v100, s[6:7]
	v_or_b32_e32 v240, v1, v3
	s_waitcnt vmcnt(3)
	v_mfma_f32_32x32x16_bf16 v[0:15], v[60:63], v[44:47], 0
	s_waitcnt vmcnt(2)
	v_mfma_f32_32x32x16_bf16 v[0:15], v[56:59], v[40:43], v[0:15]
	s_waitcnt vmcnt(1)
	v_mfma_f32_32x32x16_bf16 v[0:15], v[52:55], v[36:39], v[0:15]
	s_waitcnt vmcnt(0)
	v_mfma_f32_32x32x16_bf16 v[0:15], v[48:51], v[32:35], v[0:15]
	global_load_dwordx4 v[48:51], v[182:183], off offset:128
	global_load_dwordx4 v[52:55], v[182:183], off offset:160
	global_load_dwordx4 v[56:59], v[182:183], off offset:192
	global_load_dwordx4 v[60:63], v[182:183], off offset:224
	s_waitcnt vmcnt(3)
	v_mfma_f32_32x32x16_bf16 v[0:15], v[48:51], v[28:31], v[0:15]
	s_waitcnt vmcnt(2)
	v_mfma_f32_32x32x16_bf16 v[0:15], v[52:55], v[24:27], v[0:15]
	s_waitcnt vmcnt(1)
	v_mfma_f32_32x32x16_bf16 v[0:15], v[56:59], v[20:23], v[0:15]
	s_waitcnt vmcnt(0)
	v_mfma_f32_32x32x16_bf16 v[0:15], v[60:63], v[16:19], v[0:15]
	v_or_b32_e32 v48, 0x60, v180
	v_ashrrev_i32_e32 v49, 31, v48
	v_lshlrev_b64 v[48:49], 8, v[48:49]
	v_lshl_add_u64 v[180:181], v[64:65], 0, v[48:49]
	global_load_dwordx4 v[60:63], v[180:181], off
	global_load_dwordx4 v[56:59], v[180:181], off offset:32
	global_load_dwordx4 v[52:55], v[180:181], off offset:64
	global_load_dwordx4 v[48:51], v[180:181], off offset:96
	s_nop 3
	v_cmp_gt_i32_e64 s[6:7], 0, v1
	v_and_b32_e32 v1, 0xffffff80, v1
	s_nop 0
	v_cndmask_b32_e64 v182, v103, v101, s[6:7]
	v_cmp_gt_i32_e64 s[6:7], 0, v0
	v_and_b32_e32 v0, 0xffffff80, v0
	v_or_b32_e32 v182, v182, v1
	v_cndmask_b32_e64 v183, v106, v104, s[6:7]
	v_cmp_gt_i32_e64 s[6:7], 0, v3
	v_or_b32_e32 v183, v183, v0
	v_and_b32_e32 v3, 0xffffff80, v3
	v_cndmask_b32_e64 v0, v107, v105, s[6:7]
	v_cmp_gt_i32_e64 s[6:7], 0, v2
	v_and_b32_e32 v2, 0xffffff80, v2
	v_or_b32_e32 v241, v0, v3
	v_cndmask_b32_e64 v1, v110, v108, s[6:7]
	v_cmp_gt_i32_e64 s[6:7], 0, v5
	v_or_b32_e32 v242, v1, v2
	v_and_b32_e32 v2, 0xffffff80, v5
	v_cndmask_b32_e64 v0, v111, v109, s[6:7]
	v_cmp_gt_i32_e64 s[6:7], 0, v4
	v_and_b32_e32 v3, 0xffffff80, v4
	v_or_b32_e32 v243, v0, v2
	v_cndmask_b32_e64 v1, v114, v112, s[6:7]
	v_cmp_gt_i32_e64 s[6:7], 0, v7
	v_or_b32_e32 v244, v1, v3
	v_and_b32_e32 v2, 0xffffff80, v7
	v_cndmask_b32_e64 v0, v115, v113, s[6:7]
	v_cmp_gt_i32_e64 s[6:7], 0, v6
	v_and_b32_e32 v3, 0xffffff80, v6
	v_or_b32_e32 v245, v0, v2
	v_cndmask_b32_e64 v1, v118, v116, s[6:7]
	v_cmp_gt_i32_e64 s[6:7], 0, v9
	v_or_b32_e32 v246, v1, v3
	v_and_b32_e32 v2, 0xffffff80, v9
	v_cndmask_b32_e64 v0, v119, v117, s[6:7]
	v_cmp_gt_i32_e64 s[6:7], 0, v8
	v_and_b32_e32 v3, 0xffffff80, v8
	v_or_b32_e32 v247, v0, v2
	v_cndmask_b32_e64 v1, v122, v120, s[6:7]
	v_cmp_gt_i32_e64 s[6:7], 0, v11
	v_or_b32_e32 v248, v1, v3
	v_and_b32_e32 v2, 0xffffff80, v11
	v_cndmask_b32_e64 v0, v123, v121, s[6:7]
	v_cmp_gt_i32_e64 s[6:7], 0, v10
	v_and_b32_e32 v3, 0xffffff80, v10
	v_or_b32_e32 v249, v0, v2
	v_cndmask_b32_e64 v1, v126, v124, s[6:7]
	v_cmp_gt_i32_e64 s[6:7], 0, v13
	v_or_b32_e32 v250, v1, v3
	v_and_b32_e32 v2, 0xffffff80, v13
	v_cndmask_b32_e64 v0, v127, v125, s[6:7]
	v_cmp_gt_i32_e64 s[6:7], 0, v12
	v_and_b32_e32 v3, 0xffffff80, v12
	v_or_b32_e32 v251, v0, v2
	v_cndmask_b32_e64 v1, v130, v128, s[6:7]
	v_cmp_gt_i32_e64 s[6:7], 0, v15
	v_or_b32_e32 v252, v1, v3
	v_and_b32_e32 v2, 0xffffff80, v15
	v_cndmask_b32_e64 v0, v131, v129, s[6:7]
	v_cmp_gt_i32_e64 s[6:7], 0, v14
	v_and_b32_e32 v3, 0xffffff80, v14
	v_or_b32_e32 v190, v0, v2
	v_cndmask_b32_e64 v1, v134, v132, s[6:7]
	v_or_b32_e32 v195, v1, v3
	s_waitcnt vmcnt(3)
	v_mfma_f32_32x32x16_bf16 v[0:15], v[60:63], v[44:47], 0
	s_waitcnt vmcnt(2)
	v_mfma_f32_32x32x16_bf16 v[0:15], v[56:59], v[40:43], v[0:15]
	s_waitcnt vmcnt(1)
	v_mfma_f32_32x32x16_bf16 v[0:15], v[52:55], v[36:39], v[0:15]
	s_waitcnt vmcnt(0)
	v_mfma_f32_32x32x16_bf16 v[0:15], v[48:51], v[32:35], v[0:15]
	global_load_dwordx4 v[32:35], v[180:181], off offset:128
	global_load_dwordx4 v[36:39], v[180:181], off offset:160
	global_load_dwordx4 v[40:43], v[180:181], off offset:192
	global_load_dwordx4 v[44:47], v[180:181], off offset:224
	s_waitcnt vmcnt(3)
	v_mfma_f32_32x32x16_bf16 v[0:15], v[32:35], v[28:31], v[0:15]
	s_waitcnt vmcnt(2)
	v_mfma_f32_32x32x16_bf16 v[0:15], v[36:39], v[24:27], v[0:15]
	s_waitcnt vmcnt(1)
	v_mfma_f32_32x32x16_bf16 v[0:15], v[40:43], v[20:23], v[0:15]
	s_waitcnt vmcnt(0)
	v_mfma_f32_32x32x16_bf16 v[0:15], v[44:47], v[16:19], v[0:15]
	s_nop 11
	v_cmp_gt_i32_e64 s[6:7], 0, v1
	v_and_b32_e32 v1, 0xffffff80, v1
	v_and_b32_e32 v18, 0xffffff80, v0
	v_cndmask_b32_e64 v16, v135, v133, s[6:7]
	v_cmp_gt_i32_e64 s[6:7], 0, v0
	v_or_b32_e32 v0, v16, v1
	s_nop 0
	v_cndmask_b32_e64 v17, v138, v136, s[6:7]
	v_cmp_gt_i32_e64 s[6:7], 0, v3
	v_or_b32_e32 v1, v17, v18
	v_and_b32_e32 v3, 0xffffff80, v3
	v_cndmask_b32_e64 v16, v139, v137, s[6:7]
	v_cmp_gt_i32_e64 s[6:7], 0, v2
	v_and_b32_e32 v18, 0xffffff80, v2
	v_or_b32_e32 v2, v16, v3
	v_cndmask_b32_e64 v17, v142, v140, s[6:7]
	v_cmp_gt_i32_e64 s[6:7], 0, v5
	v_or_b32_e32 v3, v17, v18
	v_and_b32_e32 v5, 0xffffff80, v5
	v_cndmask_b32_e64 v16, v143, v141, s[6:7]
	v_cmp_gt_i32_e64 s[6:7], 0, v4
	v_and_b32_e32 v18, 0xffffff80, v4
	v_or_b32_e32 v4, v16, v5
	v_cndmask_b32_e64 v17, v154, v152, s[6:7]
	v_cmp_gt_i32_e64 s[6:7], 0, v7
	v_or_b32_e32 v5, v17, v18
	v_and_b32_e32 v7, 0xffffff80, v7
	v_cndmask_b32_e64 v16, v155, v153, s[6:7]
	v_cmp_gt_i32_e64 s[6:7], 0, v6
	v_and_b32_e32 v18, 0xffffff80, v6
	v_or_b32_e32 v6, v16, v7
	v_cndmask_b32_e64 v17, v158, v156, s[6:7]
	v_cmp_gt_i32_e64 s[6:7], 0, v9
	v_or_b32_e32 v7, v17, v18
	v_and_b32_e32 v9, 0xffffff80, v9
	v_cndmask_b32_e64 v16, v159, v157, s[6:7]
	v_cmp_gt_i32_e64 s[6:7], 0, v8
	v_and_b32_e32 v18, 0xffffff80, v8
	v_or_b32_e32 v8, v16, v9
	v_cndmask_b32_e64 v17, v162, v160, s[6:7]
	v_cmp_gt_i32_e64 s[6:7], 0, v11
	v_or_b32_e32 v9, v17, v18
	v_and_b32_e32 v11, 0xffffff80, v11
	v_cndmask_b32_e64 v16, v163, v161, s[6:7]
	v_cmp_gt_i32_e64 s[6:7], 0, v10
	v_and_b32_e32 v18, 0xffffff80, v10
	v_or_b32_e32 v10, v16, v11
	v_cndmask_b32_e64 v17, v166, v164, s[6:7]
	v_cmp_gt_i32_e64 s[6:7], 0, v13
	v_or_b32_e32 v11, v17, v18
	v_and_b32_e32 v13, 0xffffff80, v13
	v_cndmask_b32_e64 v16, v167, v165, s[6:7]
	v_cmp_gt_i32_e64 s[6:7], 0, v12
	v_and_b32_e32 v18, 0xffffff80, v12
	v_or_b32_e32 v12, v16, v13
	v_cndmask_b32_e64 v17, v170, v168, s[6:7]
	v_cmp_gt_i32_e64 s[6:7], 0, v15
	v_or_b32_e32 v16, v17, v18
	v_and_b32_e32 v15, 0xffffff80, v15
	v_cndmask_b32_e64 v13, v171, v169, s[6:7]
	v_cmp_gt_i32_e64 s[6:7], 0, v14
	v_and_b32_e32 v14, 0xffffff80, v14
	v_or_b32_e32 v25, v13, v15
	v_cndmask_b32_e64 v17, v174, v172, s[6:7]
	v_or_b32_e32 v28, v17, v14
	v_max_f32_e32 v13, v211, v210
	v_min_f32_e32 v14, v211, v210
	v_min_f32_e32 v15, v212, v173
	v_max_f32_e32 v17, v212, v173
	v_max_f32_e32 v18, v214, v213
	v_min_f32_e32 v19, v214, v213
	v_min_f32_e32 v20, v216, v215
	v_max_f32_e32 v21, v216, v215
	v_max_f32_e32 v22, v218, v217
	v_min_f32_e32 v23, v218, v217
	v_min_f32_e32 v24, v220, v219
	v_max_f32_e32 v26, v220, v219
	v_max_f32_e32 v27, v222, v221
	v_min_f32_e32 v29, v222, v221
	v_min_f32_e32 v30, v224, v223
	v_max_f32_e32 v31, v224, v223
	v_max_f32_e32 v32, v13, v15
	v_min_f32_e32 v13, v13, v15
	v_max_f32_e32 v15, v14, v17
	v_min_f32_e32 v14, v14, v17
	v_min_f32_e32 v17, v18, v20
	v_max_f32_e32 v18, v18, v20
	v_min_f32_e32 v20, v19, v21
	v_max_f32_e32 v19, v19, v21
	v_max_f32_e32 v21, v22, v24
	v_min_f32_e32 v22, v22, v24
	v_max_f32_e32 v24, v23, v26
	v_min_f32_e32 v23, v23, v26
	v_min_f32_e32 v26, v27, v30
	v_max_f32_e32 v27, v27, v30
	v_min_f32_e32 v30, v29, v31
	v_max_f32_e32 v29, v29, v31
	v_max_f32_e32 v31, v32, v15
	v_min_f32_e32 v15, v32, v15
	v_max_f32_e32 v32, v13, v14
	v_min_f32_e32 v13, v13, v14
	v_min_f32_e32 v14, v17, v20
	v_max_f32_e32 v17, v17, v20
	v_min_f32_e32 v20, v18, v19
	v_max_f32_e32 v18, v18, v19
	v_max_f32_e32 v19, v21, v24
	v_min_f32_e32 v21, v21, v24
	v_max_f32_e32 v24, v22, v23
	v_min_f32_e32 v22, v22, v23
	v_min_f32_e32 v23, v26, v30
	v_max_f32_e32 v26, v26, v30
	v_min_f32_e32 v30, v27, v29
	v_max_f32_e32 v27, v27, v29
	v_max_f32_e32 v29, v31, v14
	v_min_f32_e32 v14, v31, v14
	v_max_f32_e32 v31, v15, v17
	v_min_f32_e32 v15, v15, v17
	v_max_f32_e32 v17, v32, v20
	v_min_f32_e32 v20, v32, v20
	v_max_f32_e32 v32, v13, v18
	v_min_f32_e32 v13, v13, v18
	v_min_f32_e32 v18, v19, v23
	v_max_f32_e32 v19, v19, v23
	v_min_f32_e32 v23, v21, v26
	v_max_f32_e32 v21, v21, v26
	v_min_f32_e32 v26, v24, v30
	v_max_f32_e32 v24, v24, v30
	v_min_f32_e32 v30, v22, v27
	v_max_f32_e32 v22, v22, v27
	v_max_f32_e32 v27, v29, v17
	v_min_f32_e32 v17, v29, v17
	v_max_f32_e32 v29, v31, v32
	v_min_f32_e32 v31, v31, v32
	v_max_f32_e32 v32, v14, v20
	v_min_f32_e32 v14, v14, v20
	v_max_f32_e32 v20, v15, v13
	v_min_f32_e32 v13, v15, v13
	v_min_f32_e32 v15, v18, v26
	v_max_f32_e32 v18, v18, v26
	v_min_f32_e32 v26, v23, v30
	v_max_f32_e32 v23, v23, v30
	v_min_f32_e32 v30, v19, v24
	v_max_f32_e32 v19, v19, v24
	v_min_f32_e32 v24, v21, v22
	v_max_f32_e32 v21, v21, v22
	v_max_f32_e32 v22, v27, v29
	v_min_f32_e32 v27, v27, v29
	v_max_f32_e32 v29, v17, v31
	v_min_f32_e32 v17, v17, v31
	v_max_f32_e32 v31, v32, v20
	v_min_f32_e32 v20, v32, v20
	v_max_f32_e32 v32, v14, v13
	v_min_f32_e32 v13, v14, v13
	v_min_f32_e32 v14, v15, v26
	v_max_f32_e32 v15, v15, v26
	v_min_f32_e32 v26, v18, v23
	v_max_f32_e32 v18, v18, v23
	v_min_f32_e32 v23, v30, v24
	v_max_f32_e32 v24, v30, v24
	v_min_f32_e32 v30, v19, v21
	v_max_f32_e32 v19, v19, v21
	v_max_f32_e32 v21, v22, v14
	v_min_f32_e32 v14, v22, v14
	v_max_f32_e32 v22, v27, v15
	v_min_f32_e32 v15, v27, v15
	v_max_f32_e32 v27, v29, v26
	v_min_f32_e32 v26, v29, v26
	v_max_f32_e32 v29, v17, v18
	v_min_f32_e32 v17, v17, v18
	v_max_f32_e32 v18, v31, v23
	v_min_f32_e32 v23, v31, v23
	v_max_f32_e32 v31, v20, v24
	v_min_f32_e32 v20, v20, v24
	v_max_f32_e32 v24, v32, v30
	v_min_f32_e32 v30, v32, v30
	v_max_f32_e32 v32, v13, v19
	v_min_f32_e32 v13, v13, v19
	v_max_f32_e32 v19, v21, v18
	v_min_f32_e32 v18, v21, v18
	v_max_f32_e32 v21, v22, v31
	v_min_f32_e32 v22, v22, v31
	v_max_f32_e32 v31, v27, v24
	v_min_f32_e32 v24, v27, v24
	v_max_f32_e32 v27, v29, v32
	v_min_f32_e32 v29, v29, v32
	v_max_f32_e32 v32, v14, v23
	v_min_f32_e32 v14, v14, v23
	v_max_f32_e32 v23, v15, v20
	v_min_f32_e32 v15, v15, v20
	v_max_f32_e32 v20, v26, v30
	v_min_f32_e32 v26, v26, v30
	v_max_f32_e32 v30, v17, v13
	v_min_f32_e32 v13, v17, v13
	v_max_f32_e32 v17, v19, v31
	v_min_f32_e32 v19, v19, v31
	v_max_f32_e32 v33, v21, v27
	v_min_f32_e32 v21, v21, v27
	v_max_f32_e32 v34, v18, v24
	v_min_f32_e32 v18, v18, v24
	v_max_f32_e32 v24, v22, v29
	v_min_f32_e32 v22, v22, v29
	v_max_f32_e32 v35, v32, v20
	v_min_f32_e32 v32, v32, v20
	v_max_f32_e32 v20, v23, v30
	v_min_f32_e32 v36, v23, v30
	v_max_f32_e32 v37, v14, v26
	v_min_f32_e32 v38, v14, v26
	v_max_f32_e32 v14, v15, v13
	v_min_f32_e32 v13, v15, v13
	v_max_f32_e32 v31, v17, v33
	v_min_f32_e32 v29, v17, v33
	v_max_f32_e32 v30, v19, v21
	v_min_f32_e32 v26, v19, v21
	v_max_f32_e32 v27, v34, v24
	v_min_f32_e32 v23, v34, v24
	v_max_f32_e32 v24, v18, v22
	v_min_f32_e32 v21, v18, v22
	v_max_f32_e32 v22, v35, v20
	v_min_f32_e32 v19, v35, v20
	v_max_f32_e32 v20, v32, v36
	v_min_f32_e32 v17, v32, v36
	v_max_f32_e32 v18, v37, v14
	v_min_f32_e32 v14, v37, v14
	v_max_f32_e32 v15, v38, v13
	v_min_f32_e32 v13, v38, v13
	v_max_f32_e32 v32, v226, v225
	v_min_f32_e32 v33, v226, v225
	v_min_f32_e32 v34, v228, v227
	v_max_f32_e32 v35, v228, v227
	v_max_f32_e32 v36, v230, v229
	v_min_f32_e32 v37, v230, v229
	v_min_f32_e32 v38, v232, v231
	v_max_f32_e32 v39, v232, v231
	v_max_f32_e32 v40, v234, v233
	v_min_f32_e32 v41, v234, v233
	v_min_f32_e32 v42, v236, v235
	v_max_f32_e32 v43, v236, v235
	v_max_f32_e32 v44, v238, v237
	v_min_f32_e32 v45, v238, v237
	v_min_f32_e32 v46, v240, v239
	v_max_f32_e32 v47, v240, v239
	v_max_f32_e32 v48, v32, v34
	v_min_f32_e32 v32, v32, v34
	v_max_f32_e32 v34, v33, v35
	v_min_f32_e32 v33, v33, v35
	v_min_f32_e32 v35, v36, v38
	v_max_f32_e32 v36, v36, v38
	v_min_f32_e32 v38, v37, v39
	v_max_f32_e32 v37, v37, v39
	v_max_f32_e32 v39, v40, v42
	v_min_f32_e32 v40, v40, v42
	v_max_f32_e32 v42, v41, v43
	v_min_f32_e32 v41, v41, v43
	v_min_f32_e32 v43, v44, v46
	v_max_f32_e32 v44, v44, v46
	v_min_f32_e32 v46, v45, v47
	v_max_f32_e32 v45, v45, v47
	v_max_f32_e32 v47, v48, v34
	v_min_f32_e32 v34, v48, v34
	v_max_f32_e32 v48, v32, v33
	v_min_f32_e32 v32, v32, v33
	v_min_f32_e32 v33, v35, v38
	v_max_f32_e32 v35, v35, v38
	v_min_f32_e32 v38, v36, v37
	v_max_f32_e32 v36, v36, v37
	v_max_f32_e32 v37, v39, v42
	v_min_f32_e32 v39, v39, v42
	v_max_f32_e32 v42, v40, v41
	v_min_f32_e32 v40, v40, v41
	v_min_f32_e32 v41, v43, v46
	v_max_f32_e32 v43, v43, v46
	v_min_f32_e32 v46, v44, v45
	v_max_f32_e32 v44, v44, v45
	v_max_f32_e32 v45, v47, v33
	v_min_f32_e32 v33, v47, v33
	v_max_f32_e32 v47, v34, v35
	v_min_f32_e32 v34, v34, v35
	v_max_f32_e32 v35, v48, v38
	v_min_f32_e32 v38, v48, v38
	v_max_f32_e32 v48, v32, v36
	v_min_f32_e32 v32, v32, v36
	v_min_f32_e32 v36, v37, v41
	v_max_f32_e32 v37, v37, v41
	v_min_f32_e32 v41, v39, v43
	v_max_f32_e32 v39, v39, v43
	v_min_f32_e32 v43, v42, v46
	v_max_f32_e32 v42, v42, v46
	v_min_f32_e32 v46, v40, v44
	v_max_f32_e32 v40, v40, v44
	v_max_f32_e32 v44, v45, v35
	v_min_f32_e32 v35, v45, v35
	v_max_f32_e32 v45, v47, v48
	v_min_f32_e32 v47, v47, v48
	v_max_f32_e32 v48, v33, v38
	v_min_f32_e32 v33, v33, v38
	v_max_f32_e32 v38, v34, v32
	v_min_f32_e32 v32, v34, v32
	v_min_f32_e32 v34, v36, v43
	v_max_f32_e32 v36, v36, v43
	v_min_f32_e32 v43, v41, v46
	v_max_f32_e32 v41, v41, v46
	v_min_f32_e32 v46, v37, v42
	v_max_f32_e32 v37, v37, v42
	v_min_f32_e32 v42, v39, v40
	v_max_f32_e32 v39, v39, v40
	v_max_f32_e32 v40, v44, v45
	v_min_f32_e32 v44, v44, v45
	v_max_f32_e32 v45, v35, v47
	v_min_f32_e32 v35, v35, v47
	v_max_f32_e32 v47, v48, v38
	v_min_f32_e32 v38, v48, v38
	v_max_f32_e32 v48, v33, v32
	v_min_f32_e32 v32, v33, v32
	v_min_f32_e32 v33, v34, v43
	v_max_f32_e32 v34, v34, v43
	v_min_f32_e32 v43, v36, v41
	v_max_f32_e32 v36, v36, v41
	v_min_f32_e32 v41, v46, v42
	v_max_f32_e32 v42, v46, v42
	v_min_f32_e32 v46, v37, v39
	v_max_f32_e32 v37, v37, v39
	v_max_f32_e32 v39, v40, v33
	v_min_f32_e32 v33, v40, v33
	v_max_f32_e32 v40, v44, v34
	v_min_f32_e32 v34, v44, v34
	v_max_f32_e32 v44, v45, v43
	v_min_f32_e32 v43, v45, v43
	v_max_f32_e32 v45, v35, v36
	v_min_f32_e32 v35, v35, v36
	v_max_f32_e32 v36, v47, v41
	v_min_f32_e32 v41, v47, v41
	v_max_f32_e32 v47, v38, v42
	v_min_f32_e32 v38, v38, v42
	v_max_f32_e32 v42, v48, v46
	v_min_f32_e32 v46, v48, v46
	v_max_f32_e32 v48, v32, v37
	v_min_f32_e32 v32, v32, v37
	v_max_f32_e32 v37, v39, v36
	v_min_f32_e32 v36, v39, v36
	v_max_f32_e32 v39, v40, v47
	v_min_f32_e32 v40, v40, v47
	v_max_f32_e32 v47, v44, v42
	v_min_f32_e32 v42, v44, v42
	v_max_f32_e32 v44, v45, v48
	v_min_f32_e32 v45, v45, v48
	v_max_f32_e32 v48, v33, v41
	v_min_f32_e32 v33, v33, v41
	v_max_f32_e32 v41, v34, v38
	v_min_f32_e32 v34, v34, v38
	v_max_f32_e32 v38, v43, v46
	v_min_f32_e32 v43, v43, v46
	v_max_f32_e32 v46, v35, v32
	v_min_f32_e32 v32, v35, v32
	v_max_f32_e32 v35, v37, v47
	v_min_f32_e32 v37, v37, v47
	v_max_f32_e32 v47, v39, v44
	v_min_f32_e32 v39, v39, v44
	v_max_f32_e32 v44, v36, v42
	v_min_f32_e32 v42, v36, v42
	v_max_f32_e32 v49, v40, v45
	v_min_f32_e32 v40, v40, v45
	v_max_f32_e32 v45, v48, v38
	v_min_f32_e32 v48, v48, v38
	v_max_f32_e32 v50, v41, v46
	v_min_f32_e32 v41, v41, v46
	v_max_f32_e32 v46, v33, v43
	v_min_f32_e32 v43, v33, v43
	v_max_f32_e32 v51, v34, v32
	v_min_f32_e32 v52, v34, v32
	v_max_f32_e32 v32, v35, v47
	v_min_f32_e32 v33, v35, v47
	v_max_f32_e32 v34, v37, v39
	v_min_f32_e32 v35, v37, v39
	v_max_f32_e32 v36, v44, v49
	v_min_f32_e32 v37, v44, v49
	v_max_f32_e32 v38, v42, v40
	v_min_f32_e32 v39, v42, v40
	v_max_f32_e32 v40, v45, v50
	v_min_f32_e32 v42, v45, v50
	v_max_f32_e32 v44, v48, v41
	v_min_f32_e32 v41, v48, v41
	v_max_f32_e32 v45, v46, v51
	v_min_f32_e32 v46, v46, v51
	v_max_f32_e32 v47, v43, v52
	v_min_f32_e32 v43, v43, v52
	v_max_f32_e32 v48, v183, v182
	v_min_f32_e32 v49, v183, v182
	v_min_f32_e32 v50, v242, v241
	v_max_f32_e32 v51, v242, v241
	v_max_f32_e32 v52, v244, v243
	v_min_f32_e32 v53, v244, v243
	v_min_f32_e32 v54, v246, v245
	v_max_f32_e32 v55, v246, v245
	v_max_f32_e32 v56, v248, v247
	v_min_f32_e32 v57, v248, v247
	v_min_f32_e32 v58, v250, v249
	v_max_f32_e32 v59, v250, v249
	v_max_f32_e32 v60, v252, v251
	v_min_f32_e32 v61, v252, v251
	v_min_f32_e32 v62, v195, v190
	v_max_f32_e32 v63, v195, v190
	v_max_f32_e32 v173, v48, v50
	v_min_f32_e32 v48, v48, v50
	v_max_f32_e32 v50, v49, v51
	v_min_f32_e32 v49, v49, v51
	v_min_f32_e32 v51, v52, v54
	v_max_f32_e32 v52, v52, v54
	v_min_f32_e32 v54, v53, v55
	v_max_f32_e32 v53, v53, v55
	v_max_f32_e32 v55, v56, v58
	v_min_f32_e32 v56, v56, v58
	v_max_f32_e32 v58, v57, v59
	v_min_f32_e32 v57, v57, v59
	v_min_f32_e32 v59, v60, v62
	v_max_f32_e32 v60, v60, v62
	v_min_f32_e32 v62, v61, v63
	v_max_f32_e32 v61, v61, v63
	v_max_f32_e32 v63, v173, v50
	v_min_f32_e32 v50, v173, v50
	v_max_f32_e32 v173, v48, v49
	v_min_f32_e32 v48, v48, v49
	v_min_f32_e32 v49, v51, v54
	v_max_f32_e32 v51, v51, v54
	v_min_f32_e32 v54, v52, v53
	v_max_f32_e32 v52, v52, v53
	v_max_f32_e32 v53, v55, v58
	v_min_f32_e32 v55, v55, v58
	v_max_f32_e32 v58, v56, v57
	v_min_f32_e32 v56, v56, v57
	v_min_f32_e32 v57, v59, v62
	v_max_f32_e32 v59, v59, v62
	v_min_f32_e32 v62, v60, v61
	v_max_f32_e32 v60, v60, v61
	v_max_f32_e32 v61, v63, v49
	v_min_f32_e32 v49, v63, v49
	v_max_f32_e32 v63, v50, v51
	v_min_f32_e32 v50, v50, v51
	v_max_f32_e32 v51, v173, v54
	v_min_f32_e32 v54, v173, v54
	v_max_f32_e32 v173, v48, v52
	v_min_f32_e32 v48, v48, v52
	v_min_f32_e32 v52, v53, v57
	v_max_f32_e32 v53, v53, v57
	v_min_f32_e32 v57, v55, v59
	v_max_f32_e32 v55, v55, v59
	v_min_f32_e32 v59, v58, v62
	v_max_f32_e32 v58, v58, v62
	v_min_f32_e32 v62, v56, v60
	v_max_f32_e32 v56, v56, v60
	v_max_f32_e32 v60, v61, v51
	v_min_f32_e32 v51, v61, v51
	v_max_f32_e32 v61, v63, v173
	v_min_f32_e32 v63, v63, v173
	v_max_f32_e32 v173, v49, v54
	v_min_f32_e32 v49, v49, v54
	v_max_f32_e32 v54, v50, v48
	v_min_f32_e32 v48, v50, v48
	v_min_f32_e32 v50, v52, v59
	v_max_f32_e32 v52, v52, v59
	v_min_f32_e32 v59, v57, v62
	v_max_f32_e32 v57, v57, v62
	v_min_f32_e32 v62, v53, v58
	v_max_f32_e32 v53, v53, v58
	v_min_f32_e32 v58, v55, v56
	v_max_f32_e32 v55, v55, v56
	v_max_f32_e32 v56, v60, v61
	v_min_f32_e32 v60, v60, v61
	v_max_f32_e32 v61, v51, v63
	v_min_f32_e32 v51, v51, v63
	v_max_f32_e32 v63, v173, v54
	v_min_f32_e32 v54, v173, v54
	v_max_f32_e32 v173, v49, v48
	v_min_f32_e32 v48, v49, v48
	v_min_f32_e32 v49, v50, v59
	v_max_f32_e32 v50, v50, v59
	v_min_f32_e32 v59, v52, v57
	v_max_f32_e32 v52, v52, v57
	v_min_f32_e32 v57, v62, v58
	v_max_f32_e32 v58, v62, v58
	v_min_f32_e32 v62, v53, v55
	v_max_f32_e32 v53, v53, v55
	v_max_f32_e32 v55, v56, v49
	v_min_f32_e32 v49, v56, v49
	v_max_f32_e32 v56, v60, v50
	v_min_f32_e32 v50, v60, v50
	v_max_f32_e32 v60, v61, v59
	v_min_f32_e32 v59, v61, v59
	v_max_f32_e32 v61, v51, v52
	v_min_f32_e32 v51, v51, v52
	v_max_f32_e32 v52, v63, v57
	v_min_f32_e32 v57, v63, v57
	v_max_f32_e32 v63, v54, v58
	v_min_f32_e32 v54, v54, v58
	v_max_f32_e32 v58, v173, v62
	v_min_f32_e32 v62, v173, v62
	v_max_f32_e32 v173, v48, v53
	v_min_f32_e32 v48, v48, v53
	v_max_f32_e32 v53, v55, v52
	v_min_f32_e32 v52, v55, v52
	v_max_f32_e32 v55, v56, v63
	v_min_f32_e32 v56, v56, v63
	v_max_f32_e32 v63, v60, v58
	v_min_f32_e32 v58, v60, v58
	v_max_f32_e32 v60, v61, v173
	v_min_f32_e32 v61, v61, v173
	v_max_f32_e32 v173, v49, v57
	v_min_f32_e32 v49, v49, v57
	v_max_f32_e32 v57, v50, v54
	v_min_f32_e32 v50, v50, v54
	v_max_f32_e32 v54, v59, v62
	v_min_f32_e32 v59, v59, v62
	v_max_f32_e32 v62, v51, v48
	v_min_f32_e32 v48, v51, v48
	v_max_f32_e32 v51, v53, v63
	v_min_f32_e32 v53, v53, v63
	v_max_f32_e32 v63, v55, v60
	v_min_f32_e32 v55, v55, v60
	v_max_f32_e32 v60, v52, v58
	v_min_f32_e32 v52, v52, v58
	v_max_f32_e32 v58, v56, v61
	v_min_f32_e32 v56, v56, v61
	v_max_f32_e32 v61, v173, v54
	v_min_f32_e32 v54, v173, v54
	v_max_f32_e32 v173, v57, v62
	v_min_f32_e32 v57, v57, v62
	v_max_f32_e32 v62, v49, v59
	v_min_f32_e32 v49, v49, v59
	v_max_f32_e32 v59, v50, v48
	v_min_f32_e32 v48, v50, v48
	v_max_f32_e32 v50, v51, v63
	v_min_f32_e32 v51, v51, v63
	v_max_f32_e32 v63, v53, v55
	v_min_f32_e32 v53, v53, v55
	v_max_f32_e32 v55, v60, v58
	v_min_f32_e32 v58, v60, v58
	v_max_f32_e32 v60, v52, v56
	v_min_f32_e32 v52, v52, v56
	v_max_f32_e32 v56, v61, v173
	v_min_f32_e32 v61, v61, v173
	v_max_f32_e32 v173, v54, v57
	v_min_f32_e32 v54, v54, v57
	v_max_f32_e32 v57, v62, v59
	v_min_f32_e32 v59, v62, v59
	v_max_f32_e32 v62, v49, v48
	v_min_f32_e32 v48, v49, v48
	v_max_f32_e32 v49, v1, v0
	v_min_f32_e32 v0, v1, v0
	v_min_f32_e32 v1, v3, v2
	v_max_f32_e32 v2, v3, v2
	v_max_f32_e32 v3, v5, v4
	v_min_f32_e32 v4, v5, v4
	v_min_f32_e32 v5, v7, v6
	v_max_f32_e32 v6, v7, v6
	v_max_f32_e32 v7, v9, v8
	v_min_f32_e32 v8, v9, v8
	v_min_f32_e32 v9, v11, v10
	v_max_f32_e32 v10, v11, v10
	v_max_f32_e32 v11, v16, v12
	v_min_f32_e32 v12, v16, v12
	v_min_f32_e32 v16, v28, v25
	v_max_f32_e32 v25, v28, v25
	v_max_f32_e32 v28, v49, v1
	v_min_f32_e32 v1, v49, v1
	v_max_f32_e32 v49, v0, v2
	v_min_f32_e32 v0, v0, v2
	v_min_f32_e32 v2, v3, v5
	v_max_f32_e32 v3, v3, v5
	v_min_f32_e32 v5, v4, v6
	v_max_f32_e32 v4, v4, v6
	v_max_f32_e32 v6, v7, v9
	v_min_f32_e32 v7, v7, v9
	v_max_f32_e32 v9, v8, v10
	v_min_f32_e32 v8, v8, v10
	v_min_f32_e32 v10, v11, v16
	v_max_f32_e32 v11, v11, v16
	v_min_f32_e32 v16, v12, v25
	v_max_f32_e32 v12, v12, v25
	v_max_f32_e32 v25, v28, v49
	v_min_f32_e32 v28, v28, v49
	v_max_f32_e32 v49, v1, v0
	v_min_f32_e32 v0, v1, v0
	v_min_f32_e32 v1, v2, v5
	v_max_f32_e32 v2, v2, v5
	v_min_f32_e32 v5, v3, v4
	v_max_f32_e32 v3, v3, v4
	v_max_f32_e32 v4, v6, v9
	v_min_f32_e32 v6, v6, v9
	v_max_f32_e32 v9, v7, v8
	v_min_f32_e32 v7, v7, v8
	v_min_f32_e32 v8, v10, v16
	v_max_f32_e32 v10, v10, v16
	v_min_f32_e32 v16, v11, v12
	v_max_f32_e32 v11, v11, v12
	v_max_f32_e32 v12, v25, v1
	v_min_f32_e32 v1, v25, v1
	v_max_f32_e32 v25, v28, v2
	v_min_f32_e32 v2, v28, v2
	v_max_f32_e32 v28, v49, v5
	v_min_f32_e32 v5, v49, v5
	v_max_f32_e32 v49, v0, v3
	v_min_f32_e32 v0, v0, v3
	v_min_f32_e32 v3, v4, v8
	v_max_f32_e32 v4, v4, v8
	v_min_f32_e32 v8, v6, v10
	v_max_f32_e32 v6, v6, v10
	v_min_f32_e32 v10, v9, v16
	v_max_f32_e32 v9, v9, v16
	v_min_f32_e32 v16, v7, v11
	v_max_f32_e32 v7, v7, v11
	v_max_f32_e32 v11, v12, v28
	v_min_f32_e32 v12, v12, v28
	v_max_f32_e32 v28, v25, v49
	v_min_f32_e32 v25, v25, v49
	v_max_f32_e32 v49, v1, v5
	v_min_f32_e32 v1, v1, v5
	v_max_f32_e32 v5, v2, v0
	v_min_f32_e32 v0, v2, v0
	v_min_f32_e32 v2, v3, v10
	v_max_f32_e32 v3, v3, v10
	v_min_f32_e32 v10, v8, v16
	v_max_f32_e32 v8, v8, v16
	v_min_f32_e32 v16, v4, v9
	v_max_f32_e32 v4, v4, v9
	v_min_f32_e32 v9, v6, v7
	v_max_f32_e32 v6, v6, v7
	v_max_f32_e32 v7, v11, v28
	v_min_f32_e32 v11, v11, v28
	v_max_f32_e32 v28, v12, v25
	v_min_f32_e32 v12, v12, v25
	v_max_f32_e32 v25, v49, v5
	v_min_f32_e32 v5, v49, v5
	v_max_f32_e32 v49, v1, v0
	v_min_f32_e32 v0, v1, v0
	v_min_f32_e32 v1, v2, v10
	v_max_f32_e32 v2, v2, v10
	v_min_f32_e32 v10, v3, v8
	v_max_f32_e32 v3, v3, v8
	v_min_f32_e32 v8, v16, v9
	v_max_f32_e32 v9, v16, v9
	v_min_f32_e32 v16, v4, v6
	v_max_f32_e32 v4, v4, v6
	v_max_f32_e32 v6, v7, v1
	v_min_f32_e32 v1, v7, v1
	v_max_f32_e32 v7, v11, v2
	v_min_f32_e32 v2, v11, v2
	v_max_f32_e32 v11, v28, v10
	v_min_f32_e32 v10, v28, v10
	v_max_f32_e32 v28, v12, v3
	v_min_f32_e32 v3, v12, v3
	v_max_f32_e32 v12, v25, v8
	v_min_f32_e32 v8, v25, v8
	v_max_f32_e32 v25, v5, v9
	v_min_f32_e32 v5, v5, v9
	v_max_f32_e32 v9, v49, v16
	v_min_f32_e32 v16, v49, v16
	v_max_f32_e32 v49, v0, v4
	v_min_f32_e32 v0, v0, v4
	v_max_f32_e32 v4, v6, v12
	v_min_f32_e32 v6, v6, v12
	v_max_f32_e32 v12, v7, v25
	v_min_f32_e32 v7, v7, v25
	v_max_f32_e32 v25, v11, v9
	v_min_f32_e32 v9, v11, v9
	v_max_f32_e32 v11, v28, v49
	v_min_f32_e32 v28, v28, v49
	v_max_f32_e32 v49, v1, v8
	v_min_f32_e32 v1, v1, v8
	v_max_f32_e32 v8, v2, v5
	v_min_f32_e32 v2, v2, v5
	v_max_f32_e32 v5, v10, v16
	v_min_f32_e32 v10, v10, v16
	v_max_f32_e32 v16, v3, v0
	v_min_f32_e32 v0, v3, v0
	v_max_f32_e32 v3, v4, v25
	v_min_f32_e32 v4, v4, v25
	v_max_f32_e32 v25, v12, v11
	v_min_f32_e32 v11, v12, v11
	v_max_f32_e32 v12, v6, v9
	v_min_f32_e32 v6, v6, v9
	v_max_f32_e32 v9, v7, v28
	v_min_f32_e32 v7, v7, v28
	v_max_f32_e32 v28, v49, v5
	v_min_f32_e32 v5, v49, v5
	v_max_f32_e32 v49, v8, v16
	v_min_f32_e32 v8, v8, v16
	v_max_f32_e32 v16, v1, v10
	v_min_f32_e32 v1, v1, v10
	v_max_f32_e32 v10, v2, v0
	v_min_f32_e32 v0, v2, v0
	v_max_f32_e32 v2, v3, v25
	v_min_f32_e32 v3, v3, v25
	v_max_f32_e32 v25, v4, v11
	v_min_f32_e32 v4, v4, v11
	v_max_f32_e32 v11, v12, v9
	v_min_f32_e32 v9, v12, v9
	v_max_f32_e32 v12, v6, v7
	v_min_f32_e32 v6, v6, v7
	v_max_f32_e32 v7, v28, v49
	v_min_f32_e32 v28, v28, v49
	v_max_f32_e32 v49, v5, v8
	v_min_f32_e32 v5, v5, v8
	v_max_f32_e32 v8, v16, v10
	v_min_f32_e32 v10, v16, v10
	v_max_f32_e32 v16, v1, v0
	v_min_f32_e32 v0, v1, v0
	v_max_f32_e32 v1, v31, v43
	v_max_f32_e32 v29, v29, v47
	v_max_f32_e32 v30, v30, v46
	v_max_f32_e32 v26, v26, v45
	v_max_f32_e32 v27, v27, v41
	v_max_f32_e32 v23, v23, v44
	v_max_f32_e32 v24, v24, v42
	v_max_f32_e32 v21, v21, v40
	v_max_f32_e32 v22, v22, v39
	v_max_f32_e32 v19, v19, v38
	v_max_f32_e32 v20, v20, v37
	v_max_f32_e32 v17, v17, v36
	v_max_f32_e32 v18, v18, v35
	v_max_f32_e32 v14, v14, v34
	v_max_f32_e32 v15, v15, v33
	v_max_f32_e32 v13, v13, v32
	v_max_f32_e32 v31, v1, v22
	v_min_f32_e32 v1, v1, v22
	v_max_f32_e32 v22, v29, v19
	v_min_f32_e32 v19, v29, v19
	v_max_f32_e32 v29, v30, v20
	v_min_f32_e32 v20, v30, v20
	v_max_f32_e32 v30, v26, v17
	v_min_f32_e32 v17, v26, v17
	v_max_f32_e32 v26, v27, v18
	v_min_f32_e32 v18, v27, v18
	v_max_f32_e32 v27, v23, v14
	v_min_f32_e32 v14, v23, v14
	v_max_f32_e32 v23, v24, v15
	v_min_f32_e32 v15, v24, v15
	v_max_f32_e32 v24, v21, v13
	v_min_f32_e32 v13, v21, v13
	v_max_f32_e32 v21, v31, v26
	v_min_f32_e32 v26, v31, v26
	v_max_f32_e32 v31, v22, v27
	v_min_f32_e32 v22, v22, v27
	v_max_f32_e32 v27, v29, v23
	v_min_f32_e32 v23, v29, v23
	v_max_f32_e32 v29, v30, v24
	v_min_f32_e32 v24, v30, v24
	v_max_f32_e32 v30, v1, v18
	v_min_f32_e32 v1, v1, v18
	v_max_f32_e32 v18, v19, v14
	v_min_f32_e32 v14, v19, v14
	v_max_f32_e32 v19, v20, v15
	v_min_f32_e32 v15, v20, v15
	v_max_f32_e32 v20, v17, v13
	v_min_f32_e32 v13, v17, v13
	v_max_f32_e32 v17, v21, v27
	v_min_f32_e32 v21, v21, v27
	v_max_f32_e32 v27, v31, v29
	v_min_f32_e32 v29, v31, v29
	v_max_f32_e32 v31, v26, v23
	v_min_f32_e32 v23, v26, v23
	v_max_f32_e32 v26, v22, v24
	v_min_f32_e32 v22, v22, v24
	v_max_f32_e32 v24, v30, v19
	v_min_f32_e32 v19, v30, v19
	v_max_f32_e32 v30, v18, v20
	v_min_f32_e32 v18, v18, v20
	v_max_f32_e32 v20, v1, v15
	v_min_f32_e32 v1, v1, v15
	v_max_f32_e32 v15, v14, v13
	v_min_f32_e32 v13, v14, v13
	v_max_f32_e32 v14, v17, v27
	v_min_f32_e32 v17, v17, v27
	v_max_f32_e32 v27, v21, v29
	v_min_f32_e32 v21, v21, v29
	v_max_f32_e32 v29, v31, v26
	v_min_f32_e32 v26, v31, v26
	v_max_f32_e32 v31, v23, v22
	v_min_f32_e32 v22, v23, v22
	v_max_f32_e32 v23, v24, v30
	v_min_f32_e32 v24, v24, v30
	v_max_f32_e32 v30, v19, v18
	v_min_f32_e32 v18, v19, v18
	v_max_f32_e32 v19, v20, v15
	v_min_f32_e32 v15, v20, v15
	v_max_f32_e32 v20, v1, v13
	v_min_f32_e32 v1, v1, v13
	v_max_f32_e32 v0, v50, v0
	v_max_f32_e32 v13, v51, v16
	v_max_f32_e32 v10, v63, v10
	v_max_f32_e32 v8, v53, v8
	v_max_f32_e32 v5, v55, v5
	v_max_f32_e32 v16, v58, v49
	v_max_f32_e32 v28, v60, v28
	v_max_f32_e32 v7, v52, v7
	v_max_f32_e32 v6, v56, v6
	v_max_f32_e32 v12, v61, v12
	v_max_f32_e32 v9, v173, v9
	v_max_f32_e32 v11, v54, v11
	v_max_f32_e32 v4, v57, v4
	v_max_f32_e32 v25, v59, v25
	v_max_f32_e32 v3, v62, v3
	v_max_f32_e32 v2, v48, v2
	v_max_f32_e32 v32, v0, v6
	v_min_f32_e32 v0, v0, v6
	v_max_f32_e32 v6, v13, v12
	v_min_f32_e32 v12, v13, v12
	v_max_f32_e32 v13, v10, v9
	v_min_f32_e32 v9, v10, v9
	v_max_f32_e32 v10, v8, v11
	v_min_f32_e32 v8, v8, v11
	v_max_f32_e32 v11, v5, v4
	v_min_f32_e32 v4, v5, v4
	v_max_f32_e32 v5, v16, v25
	v_min_f32_e32 v16, v16, v25
	v_max_f32_e32 v25, v28, v3
	v_min_f32_e32 v3, v28, v3
	v_max_f32_e32 v28, v7, v2
	v_min_f32_e32 v2, v7, v2
	v_max_f32_e32 v7, v32, v11
	v_min_f32_e32 v11, v32, v11
	v_max_f32_e32 v32, v6, v5
	v_min_f32_e32 v5, v6, v5
	v_max_f32_e32 v6, v13, v25
	v_min_f32_e32 v13, v13, v25
	v_max_f32_e32 v25, v10, v28
	v_min_f32_e32 v10, v10, v28
	v_max_f32_e32 v28, v0, v4
	v_min_f32_e32 v0, v0, v4
	v_max_f32_e32 v4, v12, v16
	v_min_f32_e32 v12, v12, v16
	v_max_f32_e32 v16, v9, v3
	v_min_f32_e32 v3, v9, v3
	v_max_f32_e32 v9, v8, v2
	v_min_f32_e32 v2, v8, v2
	v_max_f32_e32 v8, v7, v6
	v_min_f32_e32 v6, v7, v6
	v_max_f32_e32 v7, v32, v25
	v_min_f32_e32 v25, v32, v25
	v_max_f32_e32 v32, v11, v13
	v_min_f32_e32 v11, v11, v13
	v_max_f32_e32 v13, v5, v10
	v_min_f32_e32 v5, v5, v10
	v_max_f32_e32 v10, v28, v16
	v_min_f32_e32 v16, v28, v16
	v_max_f32_e32 v28, v4, v9
	v_min_f32_e32 v4, v4, v9
	v_max_f32_e32 v9, v0, v3
	v_min_f32_e32 v0, v0, v3
	v_max_f32_e32 v3, v12, v2
	v_min_f32_e32 v2, v12, v2
	v_max_f32_e32 v12, v8, v7
	v_min_f32_e32 v7, v8, v7
	v_max_f32_e32 v8, v6, v25
	v_min_f32_e32 v6, v6, v25
	v_max_f32_e32 v25, v32, v13
	v_min_f32_e32 v13, v32, v13
	v_max_f32_e32 v32, v11, v5
	v_min_f32_e32 v5, v11, v5
	v_max_f32_e32 v11, v10, v28
	v_min_f32_e32 v10, v10, v28
	v_max_f32_e32 v28, v16, v4
	v_min_f32_e32 v4, v16, v4
	v_max_f32_e32 v16, v9, v3
	v_min_f32_e32 v3, v9, v3
	v_max_f32_e32 v9, v0, v2
	v_min_f32_e32 v0, v0, v2
	v_max_f32_e32 v0, v14, v0
	v_max_f32_e32 v2, v17, v9
	v_max_f32_e32 v3, v27, v3
	v_max_f32_e32 v9, v21, v16
	v_max_f32_e32 v4, v29, v4
	v_max_f32_e32 v14, v26, v28
	v_max_f32_e32 v10, v31, v10
	v_max_f32_e32 v11, v22, v11
	v_max_f32_e32 v5, v23, v5
	v_max_f32_e32 v16, v24, v32
	v_max_f32_e32 v13, v30, v13
	v_max_f32_e32 v17, v18, v25
	v_max_f32_e32 v6, v19, v6
	v_max_f32_e32 v8, v15, v8
	v_max_f32_e32 v7, v20, v7
	v_max_f32_e32 v1, v1, v12
	v_max_f32_e32 v12, v0, v5
	v_min_f32_e32 v0, v0, v5
	v_max_f32_e32 v5, v2, v16
	v_min_f32_e32 v2, v2, v16
	v_max_f32_e32 v15, v3, v13
	v_min_f32_e32 v3, v3, v13
	v_max_f32_e32 v13, v9, v17
	v_min_f32_e32 v9, v9, v17
	v_max_f32_e32 v16, v4, v6
	v_min_f32_e32 v4, v4, v6
	v_max_f32_e32 v6, v14, v8
	v_min_f32_e32 v8, v14, v8
	v_max_f32_e32 v14, v10, v7
	v_min_f32_e32 v7, v10, v7
	v_max_f32_e32 v10, v11, v1
	v_min_f32_e32 v1, v11, v1
	v_max_f32_e32 v11, v12, v16
	v_min_f32_e32 v12, v12, v16
	v_max_f32_e32 v16, v5, v6
	v_min_f32_e32 v5, v5, v6
	v_max_f32_e32 v6, v15, v14
	v_min_f32_e32 v14, v15, v14
	v_max_f32_e32 v15, v13, v10
	v_min_f32_e32 v10, v13, v10
	v_max_f32_e32 v13, v0, v4
	v_min_f32_e32 v0, v0, v4
	v_max_f32_e32 v4, v2, v8
	v_min_f32_e32 v2, v2, v8
	v_max_f32_e32 v8, v3, v7
	v_min_f32_e32 v3, v3, v7
	v_max_f32_e32 v7, v9, v1
	v_min_f32_e32 v1, v9, v1
	v_max_f32_e32 v9, v11, v6
	v_min_f32_e32 v6, v11, v6
	v_max_f32_e32 v11, v16, v15
	v_min_f32_e32 v15, v16, v15
	v_max_f32_e32 v16, v12, v14
	v_min_f32_e32 v12, v12, v14
	v_max_f32_e32 v14, v5, v10
	v_min_f32_e32 v5, v5, v10
	v_max_f32_e32 v10, v13, v8
	v_min_f32_e32 v8, v13, v8
	v_max_f32_e32 v13, v4, v7
	v_min_f32_e32 v4, v4, v7
	v_max_f32_e32 v7, v0, v3
	v_min_f32_e32 v0, v0, v3
	v_max_f32_e32 v3, v2, v1
	v_min_f32_e32 v1, v2, v1
	v_max_f32_e32 v2, v9, v11
	v_min_f32_e32 v9, v9, v11
	v_max_f32_e32 v11, v6, v15
	v_min_f32_e32 v6, v6, v15
	v_max_f32_e32 v15, v16, v14
	v_min_f32_e32 v14, v16, v14
	v_max_f32_e32 v16, v12, v5
	v_min_f32_e32 v5, v12, v5
	v_max_f32_e32 v12, v10, v13
	v_min_f32_e32 v10, v10, v13
	v_max_f32_e32 v13, v8, v4
	v_min_f32_e32 v4, v8, v4
	v_max_f32_e32 v8, v7, v3
	v_min_f32_e32 v3, v7, v3
	v_max_f32_e32 v7, v0, v1
	v_min_f32_e32 v0, v0, v1
	v_mov_b32_e32 v27, v0
	s_nop 1
	v_permlane32_swap_b32 v27, v27
	v_mov_b32_e32 v29, v7
	s_nop 1
	v_permlane32_swap_b32 v29, v29
	v_mov_b32_e32 v31, v3
	s_nop 1
	v_permlane32_swap_b32 v31, v31
	v_mov_b32_e32 v30, v8
	s_nop 1
	v_permlane32_swap_b32 v30, v30
	v_mov_b32_e32 v28, v4
	s_nop 1
	v_permlane32_swap_b32 v28, v28
	v_mov_b32_e32 v26, v13
	s_nop 1
	v_permlane32_swap_b32 v26, v26
	s_waitcnt lgkmcnt(5)
	v_mov_b32_e32 v1, v2
	s_nop 1
	v_permlane32_swap_b32 v1, v1
	v_mov_b32_e32 v25, v10
	s_nop 1
	v_permlane32_swap_b32 v25, v25
	v_max_f32_e32 v2, v2, v27
	s_waitcnt lgkmcnt(6)
	v_mov_b32_e32 v17, v9
	s_nop 1
	v_permlane32_swap_b32 v17, v17
	v_mov_b32_e32 v24, v12
	s_nop 1
	v_permlane32_swap_b32 v24, v24
	v_max_f32_e32 v9, v9, v29
	s_waitcnt lgkmcnt(7)
	v_mov_b32_e32 v18, v11
	s_nop 1
	v_permlane32_swap_b32 v18, v18
	v_mov_b32_e32 v23, v5
	s_nop 1
	v_permlane32_swap_b32 v23, v23
	v_max_f32_e32 v11, v11, v31
	s_waitcnt lgkmcnt(8)
	v_mov_b32_e32 v19, v6
	s_nop 1
	v_permlane32_swap_b32 v19, v19
	v_mov_b32_e32 v22, v16
	s_nop 1
	v_permlane32_swap_b32 v22, v22
	v_max_f32_e32 v6, v6, v30
	s_waitcnt lgkmcnt(9)
	v_mov_b32_e32 v20, v15
	s_nop 1
	v_permlane32_swap_b32 v20, v20
	v_mov_b32_e32 v21, v14
	s_nop 1
	v_permlane32_swap_b32 v21, v21
	v_max_f32_e32 v15, v15, v28
	s_waitcnt lgkmcnt(10)
	v_max_f32_e32 v14, v14, v26
	s_waitcnt lgkmcnt(8)
	v_max_f32_e32 v16, v16, v25
	s_waitcnt lgkmcnt(6)
	v_max_f32_e32 v5, v5, v24
	s_waitcnt lgkmcnt(4)
	v_max_f32_e32 v12, v12, v23
	s_waitcnt lgkmcnt(2)
	v_max_f32_e32 v10, v10, v22
	s_waitcnt lgkmcnt(0)
	v_max_f32_e32 v13, v13, v21
	v_max_f32_e32 v4, v4, v20
	v_max_f32_e32 v8, v8, v19
	v_max_f32_e32 v3, v3, v18
	v_max_f32_e32 v7, v7, v17
	v_max_f32_e32 v0, v0, v1
	v_max_f32_e32 v1, v2, v12
	v_min_f32_e32 v2, v2, v12
	v_max_f32_e32 v12, v9, v10
	v_min_f32_e32 v9, v9, v10
	v_max_f32_e32 v10, v11, v13
	v_min_f32_e32 v11, v11, v13
	v_max_f32_e32 v13, v6, v4
	v_min_f32_e32 v4, v6, v4
	v_max_f32_e32 v6, v15, v8
	v_min_f32_e32 v8, v15, v8
	v_max_f32_e32 v15, v14, v3
	v_min_f32_e32 v3, v14, v3
	v_max_f32_e32 v14, v16, v7
	v_min_f32_e32 v7, v16, v7
	v_max_f32_e32 v16, v5, v0
	v_min_f32_e32 v0, v5, v0
	v_max_f32_e32 v5, v1, v6
	v_min_f32_e32 v1, v1, v6
	v_max_f32_e32 v6, v12, v15
	v_min_f32_e32 v12, v12, v15
	v_max_f32_e32 v15, v10, v14
	v_min_f32_e32 v10, v10, v14
	v_max_f32_e32 v14, v13, v16
	v_min_f32_e32 v13, v13, v16
	v_max_f32_e32 v16, v2, v8
	v_min_f32_e32 v2, v2, v8
	v_max_f32_e32 v8, v9, v3
	v_min_f32_e32 v3, v9, v3
	v_max_f32_e32 v9, v11, v7
	v_min_f32_e32 v7, v11, v7
	v_max_f32_e32 v11, v4, v0
	v_min_f32_e32 v0, v4, v0
	v_max_f32_e32 v4, v5, v15
	v_min_f32_e32 v5, v5, v15
	v_max_f32_e32 v15, v6, v14
	v_min_f32_e32 v6, v6, v14
	v_max_f32_e32 v14, v1, v10
	v_min_f32_e32 v1, v1, v10
	v_max_f32_e32 v10, v12, v13
	v_min_f32_e32 v12, v12, v13
	v_max_f32_e32 v13, v16, v9
	v_min_f32_e32 v9, v16, v9
	v_max_f32_e32 v16, v8, v11
	v_min_f32_e32 v8, v8, v11
	v_max_f32_e32 v11, v2, v7
	v_min_f32_e32 v2, v2, v7
	v_max_f32_e32 v7, v3, v0
	v_min_f32_e32 v0, v3, v0
	v_max_f32_e32 v3, v4, v15
	v_min_f32_e32 v4, v4, v15
	v_max_f32_e32 v15, v5, v6
	v_min_f32_e32 v5, v5, v6
	v_max_f32_e32 v6, v14, v10
	v_min_f32_e32 v10, v14, v10
	v_max_f32_e32 v14, v1, v12
	v_min_f32_e32 v1, v1, v12
	v_max_f32_e32 v12, v13, v16
	v_min_f32_e32 v13, v13, v16
	v_max_f32_e32 v16, v9, v8
	v_min_f32_e32 v8, v9, v8
	v_max_f32_e32 v9, v11, v7
	v_min_f32_e32 v7, v11, v7
	v_max_f32_e32 v11, v2, v0
	v_min_f32_e32 v0, v2, v0
	v_lshl_add_u32 v2, s8, 12, v207
	ds_write2st64_b32 v2, v3, v4 offset1:1
	ds_write2st64_b32 v2, v15, v5 offset0:2 offset1:3
	ds_write2st64_b32 v2, v6, v10 offset0:4 offset1:5
	ds_write2st64_b32 v2, v14, v1 offset0:6 offset1:7
	ds_write2st64_b32 v2, v12, v13 offset0:8 offset1:9
	ds_write2st64_b32 v2, v16, v8 offset0:10 offset1:11
	ds_write2st64_b32 v2, v9, v7 offset0:12 offset1:13
	ds_write2st64_b32 v2, v11, v0 offset0:14 offset1:15
	s_mov_b64 s[6:7], 0
	s_mov_b32 s8, 1
	s_cbranch_vccz .LBB0_704
	ds_read2st64_b32 v[0:1], v207 offset1:1
	ds_read2st64_b32 v[2:3], v207 offset0:2 offset1:3
	ds_read2st64_b32 v[4:5], v207 offset0:4 offset1:5
	ds_read2st64_b32 v[6:7], v207 offset0:6 offset1:7
	ds_read2st64_b32 v[16:17], v207 offset0:16 offset1:17
	ds_read2st64_b32 v[18:19], v207 offset0:18 offset1:19
	ds_read2st64_b32 v[20:21], v207 offset0:20 offset1:21
	ds_read2st64_b32 v[22:23], v207 offset0:22 offset1:23
	ds_read2st64_b32 v[8:9], v207 offset0:8 offset1:9
	ds_read2st64_b32 v[10:11], v207 offset0:10 offset1:11
	ds_read2st64_b32 v[12:13], v207 offset0:12 offset1:13
	ds_read2st64_b32 v[14:15], v207 offset0:14 offset1:15
	ds_read2st64_b32 v[24:25], v207 offset0:24 offset1:25
	ds_read2st64_b32 v[26:27], v207 offset0:26 offset1:27
	ds_read2st64_b32 v[28:29], v207 offset0:28 offset1:29
	ds_read2st64_b32 v[30:31], v207 offset0:30 offset1:31
	s_and_saveexec_b64 s[8:9], s[38:39]
	s_cbranch_execz .LBB0_696
	s_waitcnt lgkmcnt(0)
	v_and_b32_e32 v49, 0xffffff80, v30
	v_and_b32_e32 v48, 0xffffff80, v0
	v_and_b32_e32 v39, 0xffffff80, v19
	v_and_b32_e32 v38, 0xffffff80, v20
	v_pk_add_f32 v[52:53], v[38:39], v[48:49] op_sel:[1,0] op_sel_hi:[0,1]
	v_cmp_gt_i32_e32 vcc, 0, v52
	v_bfrev_b32_e32 v43, 0.5
	s_movk_i32 s12, 0xff00
	v_cndmask_b32_e64 v43, v43, 3, vcc
	v_and_b32_e32 v42, 0xffffff80, v23
	v_and_or_b32 v56, v52, s12, v43
	v_mov_b32_e32 v43, v38
	v_pk_add_f32 v[52:53], v[48:49], v[42:43] op_sel_hi:[0,1]
	v_cmp_gt_i32_e32 vcc, 0, v53
	v_mov_b32_e32 v54, 0xfb
	v_and_b32_e32 v41, 0xffffff80, v22
	v_cndmask_b32_e64 v54, v54, 4, vcc
	v_and_b32_e32 v40, 0xffffff80, v21
	v_and_or_b32 v53, v53, s12, v54
	v_cmp_gt_i32_e32 vcc, 0, v52
	v_mov_b32_e32 v54, 0xf8
	v_mov_b32_e32 v58, 0xf9
	v_cndmask_b32_e64 v57, v54, 7, vcc
	v_pk_add_f32 v[54:55], v[48:49], v[40:41] op_sel_hi:[0,1]
	v_cmp_gt_i32_e32 vcc, 0, v55
	v_mov_b32_e32 v59, 0xfa
	v_and_b32_e32 v55, 0xffffff00, v55
	v_cndmask_b32_e64 v58, v58, 6, vcc
	v_cmp_gt_i32_e32 vcc, 0, v54
	v_and_b32_e32 v54, 0xffffff00, v54
	v_and_b32_e32 v52, 0xffffff00, v52
	v_cndmask_b32_e64 v59, v59, 5, vcc
	v_or_b32_e32 v55, v58, v55
	v_or_b32_e32 v54, v59, v54
	v_or_b32_e32 v52, v57, v52
	v_writelane_b32 v255, s8, 44
	v_min_f32_e32 v57, v55, v52
	v_max_f32_e32 v58, v53, v54
	v_min_f32_e32 v53, v53, v54
	v_max_f32_e32 v52, v55, v52
	v_writelane_b32 v255, s9, 45
	v_and_b32_e32 v45, 0xffffff80, v24
	v_and_b32_e32 v44, 0xffffff80, v27
	v_min_f32_e32 v59, v58, v57
	v_min_f32_e32 v54, v53, v52
	v_max_f32_e32 v57, v58, v57
	v_max_f32_e32 v52, v53, v52
	v_pk_add_f32 v[44:45], v[48:49], v[44:45] op_sel_hi:[0,1]
	v_and_b32_e32 v47, 0xffffff80, v26
	v_min_f32_e32 v58, v57, v52
	v_max_f32_e32 v57, v57, v52
	v_cmp_gt_i32_e32 vcc, 0, v45
	v_mov_b32_e32 v52, 0xf7
	v_and_b32_e32 v46, 0xffffff80, v25
	v_cndmask_b32_e64 v52, v52, 8, vcc
	v_and_or_b32 v45, v45, s12, v52
	v_cmp_gt_i32_e32 vcc, 0, v44
	v_mov_b32_e32 v52, 0xf4
	v_pk_add_f32 v[46:47], v[48:49], v[46:47] op_sel_hi:[0,1]
	v_cndmask_b32_e64 v52, v52, 11, vcc
	v_cmp_gt_i32_e32 vcc, 0, v47
	v_mov_b32_e32 v53, 0xf5
	v_min_f32_e32 v55, v59, v54
	v_max_f32_e32 v59, v59, v54
	v_cndmask_b32_e64 v53, v53, 10, vcc
	v_cmp_gt_i32_e32 vcc, 0, v46
	v_mov_b32_e32 v54, 0xf6
	v_and_b32_e32 v47, 0xffffff00, v47
	v_cndmask_b32_e64 v54, v54, 9, vcc
	v_and_b32_e32 v46, 0xffffff00, v46
	v_and_b32_e32 v44, 0xffffff00, v44
	v_or_b32_e32 v47, v53, v47
	v_or_b32_e32 v46, v54, v46
	v_or_b32_e32 v44, v52, v44
	v_and_b32_e32 v51, 0xffffff80, v29
	v_and_b32_e32 v50, 0xffffff80, v28
	v_writelane_b32 v255, s11, 46
	v_min_f32_e32 v52, v47, v44
	v_max_f32_e32 v53, v45, v46
	v_min_f32_e32 v46, v45, v46
	v_max_f32_e32 v47, v47, v44
	v_pk_add_f32 v[44:45], v[48:49], v[50:51] op_sel_hi:[0,1]
	v_cmp_gt_i32_e64 s[10:11], 0, v45
	v_mov_b32_e32 v50, 0xf2
	v_mov_b32_e32 v51, 0xf3
	v_cndmask_b32_e64 v50, v50, 13, s[10:11]
	v_cmp_gt_i32_e64 s[10:11], 0, v44
	v_and_b32_e32 v45, 0xffffff00, v45
	v_and_b32_e32 v44, 0xffffff00, v44
	v_cndmask_b32_e64 v51, v51, 12, s[10:11]
	v_or_b32_e32 v50, v50, v45
	v_or_b32_e32 v51, v51, v44
	v_and_b32_e32 v45, 0xffffff80, v31
	v_mov_b32_e32 v44, v49
	v_pk_add_f32 v[44:45], v[48:49], v[44:45] op_sel_hi:[0,1]
	v_cmp_gt_i32_e64 s[42:43], 0, v45
	v_mov_b32_e32 v249, 0xf0
	v_mov_b32_e32 v173, 0xf1
	v_cndmask_b32_e64 v63, v249, 15, s[42:43]
	v_cmp_gt_i32_e64 s[42:43], 0, v44
	v_and_b32_e32 v45, 0xffffff00, v45
	v_and_b32_e32 v44, 0xffffff00, v44
	v_cndmask_b32_e64 v173, v173, 14, s[42:43]
	v_or_b32_e32 v45, v63, v45
	v_or_b32_e32 v44, v173, v44
	v_max_f32_e32 v62, v51, v50
	v_min_f32_e32 v63, v44, v45
	v_min_f32_e32 v50, v51, v50
	v_max_f32_e32 v44, v44, v45
	v_max_f32_e32 v54, v53, v52
	v_max_f32_e32 v60, v46, v47
	v_min_f32_e32 v173, v62, v63
	v_min_f32_e32 v45, v50, v44
	v_min_f32_e32 v51, v53, v52
	v_min_f32_e32 v46, v46, v47
	v_max_f32_e32 v52, v62, v63
	v_max_f32_e32 v44, v50, v44
	v_max_f32_e32 v61, v54, v60
	v_min_f32_e32 v178, v173, v45
	v_max_f32_e32 v47, v51, v46
	v_min_f32_e32 v50, v52, v44
	v_min_f32_e32 v54, v54, v60
	v_max_f32_e32 v45, v173, v45
	v_min_f32_e32 v46, v51, v46
	v_max_f32_e32 v44, v52, v44
	v_min_f32_e32 v179, v61, v178
	v_min_f32_e32 v53, v47, v50
	v_min_f32_e32 v60, v54, v45
	v_min_f32_e32 v52, v46, v44
	v_max_f32_e32 v61, v61, v178
	v_max_f32_e32 v47, v47, v50
	v_max_f32_e32 v45, v54, v45
	v_max_f32_e32 v44, v46, v44
	v_min_f32_e32 v62, v179, v53
	v_min_f32_e32 v63, v60, v52
	v_min_f32_e32 v50, v61, v47
	v_min_f32_e32 v46, v45, v44
	v_max_f32_e32 v53, v179, v53
	v_max_f32_e32 v52, v60, v52
	v_max_f32_e32 v47, v61, v47
	v_max_f32_e32 v44, v45, v44
	v_min_f32_e32 v60, v53, v52
	v_min_f32_e32 v61, v47, v44
	v_max_f32_e32 v52, v53, v52
	v_max_f32_e32 v53, v47, v44
	v_and_b32_e32 v44, 0xffffff80, v1
	v_add_f32_e32 v45, v39, v44
	v_min_f32_e32 v51, v62, v63
	v_min_f32_e32 v173, v50, v46
	v_max_f32_e32 v62, v62, v63
	v_max_f32_e32 v63, v50, v46
	v_cmp_gt_i32_e32 vcc, 0, v45
	v_mov_b32_e32 v46, 0xec
	v_mov_b32_e32 v47, 0xe9
	v_cndmask_b32_e64 v46, v46, 19, vcc
	v_and_or_b32 v45, v45, s12, v46
	v_pk_add_f32 v[42:43], v[44:45], v[42:43] op_sel_hi:[0,1]
	v_cmp_gt_i32_e32 vcc, 0, v43
	v_mov_b32_e32 v46, 0xeb
	v_pk_add_f32 v[40:41], v[44:45], v[40:41] op_sel_hi:[0,1]
	v_cndmask_b32_e64 v46, v46, 20, vcc
	v_and_or_b32 v43, v43, s12, v46
	v_cmp_gt_i32_e32 vcc, 0, v42
	v_mov_b32_e32 v46, 0xe8
	v_mov_b32_e32 v50, 0xea
	v_cndmask_b32_e64 v46, v46, 23, vcc
	v_cmp_gt_i32_e32 vcc, 0, v41
	v_and_b32_e32 v41, 0xffffff00, v41
	v_and_b32_e32 v42, 0xffffff00, v42
	v_cndmask_b32_e64 v47, v47, 22, vcc
	v_cmp_gt_i32_e32 vcc, 0, v40
	v_and_b32_e32 v40, 0xffffff00, v40
	v_or_b32_e32 v41, v47, v41
	v_cndmask_b32_e64 v50, v50, 21, vcc
	v_or_b32_e32 v40, v50, v40
	v_or_b32_e32 v42, v46, v42
	v_and_b32_e32 v182, 0xffffff80, v3
	v_min_f32_e32 v46, v41, v42
	v_max_f32_e32 v47, v43, v40
	v_min_f32_e32 v40, v43, v40
	v_max_f32_e32 v41, v41, v42
	v_and_b32_e32 v37, 0xffffff80, v4
	v_max_f32_e32 v43, v47, v46
	v_min_f32_e32 v42, v40, v41
	v_max_f32_e32 v40, v40, v41
	v_min_f32_e32 v50, v47, v46
	v_and_b32_e32 v46, 0xffffff80, v2
	v_and_b32_e32 v36, 0xffffff80, v18
	v_min_f32_e32 v179, v43, v40
	v_max_f32_e32 v180, v43, v40
	v_pk_add_f32 v[40:41], v[46:47], v[38:39] op_sel_hi:[0,1]
	v_cmp_gt_i32_e32 vcc, 0, v41
	v_mov_b32_e32 v38, 0xdc
	v_and_b32_e32 v35, 0xffffff80, v7
	v_cndmask_b32_e64 v38, v38, 35, vcc
	v_and_or_b32 v41, v41, s12, v38
	v_cmp_gt_i32_e32 vcc, 0, v40
	v_mov_b32_e32 v38, 0xdb
	v_and_b32_e32 v34, 0xffffff80, v17
	v_cndmask_b32_e64 v38, v38, 36, vcc
	v_and_or_b32 v181, v40, s12, v38
	v_add_f32_e32 v38, v39, v182
	v_cmp_gt_i32_e32 vcc, 0, v38
	v_mov_b32_e32 v39, 0xcc
	s_nop 0
	v_cndmask_b32_e64 v39, v39, 51, vcc
	v_and_or_b32 v54, v38, s12, v39
	v_pk_add_f32 v[38:39], v[48:49], v[36:37]
	v_min_f32_e32 v178, v50, v42
	v_cmp_gt_i32_e32 vcc, 0, v38
	v_bfrev_b32_e32 v39, -0.5
	v_max_f32_e32 v50, v50, v42
	v_cndmask_b32_e64 v39, v39, 2, vcc
	v_and_or_b32 v38, v38, s12, v39
	v_mov_b32_e32 v39, 0xed
	v_and_b32_e32 v43, 0xffffff80, v6
	v_min_f32_e32 v183, v38, v56
	v_max_f32_e32 v56, v38, v56
	v_add_f32_e32 v38, v36, v44
	v_cmp_gt_i32_e32 vcc, 0, v38
	v_and_b32_e32 v42, 0xffffff80, v5
	v_and_b32_e32 v33, 0xffffff80, v14
	v_cndmask_b32_e64 v39, v39, 18, vcc
	v_and_or_b32 v38, v38, s12, v39
	v_mov_b32_e32 v39, 0xdd
	v_and_b32_e32 v32, 0xffffff80, v16
	v_min_f32_e32 v190, v38, v45
	v_max_f32_e32 v195, v38, v45
	v_add_f32_e32 v38, v36, v46
	v_cmp_gt_i32_e32 vcc, 0, v38
	v_mov_b32_e32 v45, 0x61
	v_mov_b32_e32 v234, 0xef
	v_cndmask_b32_e64 v39, v39, 34, vcc
	v_and_or_b32 v38, v38, s12, v39
	v_mov_b32_e32 v39, 0xcd
	v_mov_b32_e32 v241, 0xdf
	v_min_f32_e32 v209, v38, v41
	v_max_f32_e32 v210, v38, v41
	v_add_f32_e32 v38, v36, v182
	v_cmp_gt_i32_e32 vcc, 0, v38
	v_mov_b32_e32 v41, 0x42
	v_mov_b32_e32 v244, 0xcf
	v_cndmask_b32_e64 v39, v39, 50, vcc
	v_and_or_b32 v40, v38, s12, v39
	v_pk_add_f32 v[38:39], v[36:37], v[36:37] op_sel:[1,0] op_sel_hi:[0,1]
	v_cmp_gt_i32_e32 vcc, 0, v38
	v_mov_b32_e32 v39, 0xbd
	v_and_b32_e32 v47, 0xffffff80, v8
	v_cndmask_b32_e32 v39, v39, v41, vcc
	v_and_or_b32 v41, v38, s12, v39
	v_pk_add_f32 v[38:39], v[48:49], v[34:35]
	v_pk_add_f32 v[48:49], v[48:49], v[32:33]
	v_cmp_gt_i32_e32 vcc, 0, v38
	v_mov_b32_e32 v39, 0xfe
	s_mov_b32 s28, 0xff61b1e6
	v_cndmask_b32_e64 v39, v39, 1, vcc
	v_and_or_b32 v211, v38, s12, v39
	v_add_f32_e32 v38, v34, v44
	v_cmp_gt_i32_e32 vcc, 0, v38
	v_mov_b32_e32 v39, 0xee
	v_add_f32_e32 v44, v32, v44
	v_cndmask_b32_e64 v39, v39, 17, vcc
	v_and_or_b32 v212, v38, s12, v39
	v_add_f32_e32 v38, v34, v46
	v_cmp_gt_i32_e32 vcc, 0, v38
	v_mov_b32_e32 v39, 0xde
	v_add_f32_e32 v46, v32, v46
	v_cndmask_b32_e64 v39, v39, 33, vcc
	v_and_or_b32 v213, v38, s12, v39
	v_add_f32_e32 v38, v34, v182
	v_cmp_gt_i32_e32 vcc, 0, v38
	v_mov_b32_e32 v39, 0xce
	v_add_f32_e32 v182, v32, v182
	v_cndmask_b32_e64 v39, v39, 49, vcc
	v_and_or_b32 v38, v38, s12, v39
	v_cmp_gt_i32_e64 s[74:75], 0, v46
	v_cmp_gt_i32_e64 s[84:85], 0, v182
	v_min_f32_e32 v219, v38, v40
	v_max_f32_e32 v220, v38, v40
	v_pk_add_f32 v[38:39], v[36:37], v[34:35] op_sel:[1,0] op_sel_hi:[0,1]
	v_cmp_gt_i32_e32 vcc, 0, v38
	v_mov_b32_e32 v39, 0xbe
	v_mov_b32_e32 v40, 0x41
	v_cndmask_b32_e32 v39, v39, v40, vcc
	v_and_or_b32 v38, v38, s12, v39
	v_mov_b32_e32 v40, v35
	v_cndmask_b32_e64 v241, v241, 32, s[74:75]
	v_min_f32_e32 v215, v38, v41
	v_max_f32_e32 v216, v38, v41
	v_pk_add_f32 v[38:39], v[34:35], v[42:43]
	v_mov_b32_e32 v41, v43
	v_pk_add_f32 v[40:41], v[34:35], v[40:41] op_sel_hi:[0,1]
	v_cmp_gt_i32_e32 vcc, 0, v38
	v_mov_b32_e32 v34, 0xae
	v_mov_b32_e32 v39, 0x51
	v_cndmask_b32_e32 v34, v34, v39, vcc
	v_cmp_gt_i32_e32 vcc, 0, v41
	v_mov_b32_e32 v39, 0x9e
	v_and_b32_e32 v38, 0xffffff00, v38
	v_cndmask_b32_e32 v39, v39, v45, vcc
	v_or_b32_e32 v218, v34, v38
	v_cmp_gt_i32_e32 vcc, 0, v40
	v_mov_b32_e32 v34, 0x8e
	v_mov_b32_e32 v38, 0x71
	v_cndmask_b32_e32 v34, v34, v38, vcc
	v_and_or_b32 v214, v40, s12, v34
	v_cmp_gt_i32_e32 vcc, 0, v48
	v_mov_b32_e32 v34, 0xff
	v_cndmask_b32_e64 v244, v244, 48, s[84:85]
	v_cndmask_b32_e64 v34, v34, 0, vcc
	v_and_or_b32 v34, v48, s12, v34
	v_and_or_b32 v46, v46, s12, v241
	v_and_or_b32 v182, v182, s12, v244
	v_max_f32_e32 v48, v34, v211
	v_min_f32_e32 v34, v34, v211
	v_max_f32_e32 v49, v48, v183
	v_max_f32_e32 v211, v34, v56
	v_min_f32_e32 v48, v48, v183
	v_min_f32_e32 v34, v34, v56
	v_max_f32_e32 v221, v49, v211
	v_max_f32_e32 v56, v48, v34
	v_min_f32_e32 v49, v49, v211
	v_min_f32_e32 v34, v48, v34
	v_max_f32_e32 v222, v221, v55
	v_max_f32_e32 v183, v56, v58
	v_max_f32_e32 v211, v49, v59
	v_max_f32_e32 v48, v34, v57
	v_min_f32_e32 v55, v221, v55
	v_min_f32_e32 v56, v56, v58
	v_min_f32_e32 v49, v49, v59
	v_min_f32_e32 v34, v34, v57
	v_max_f32_e32 v241, v46, v213
	v_max_f32_e32 v58, v55, v56
	v_max_f32_e32 v57, v49, v34
	v_min_f32_e32 v55, v55, v56
	v_min_f32_e32 v34, v49, v34
	v_min_f32_e32 v46, v46, v213
	v_max_f32_e32 v244, v181, v182
	v_max_f32_e32 v49, v55, v34
	v_min_f32_e32 v34, v55, v34
	v_cmp_gt_i32_e64 s[6:7], 0, v44
	v_min_f32_e32 v181, v181, v182
	s_nop 0
	v_cndmask_b32_e64 v234, v234, 16, s[6:7]
	v_and_or_b32 v44, v44, s12, v234
	v_max_f32_e32 v234, v44, v212
	v_min_f32_e32 v44, v44, v212
	v_max_f32_e32 v235, v234, v190
	v_max_f32_e32 v212, v44, v195
	v_min_f32_e32 v190, v234, v190
	v_min_f32_e32 v44, v44, v195
	v_max_f32_e32 v242, v241, v209
	v_max_f32_e32 v213, v46, v210
	v_min_f32_e32 v245, v244, v219
	v_min_f32_e32 v182, v181, v220
	v_min_f32_e32 v209, v241, v209
	v_min_f32_e32 v46, v46, v210
	v_max_f32_e32 v219, v244, v219
	v_max_f32_e32 v181, v181, v220
	v_max_f32_e32 v59, v58, v57
	v_min_f32_e32 v57, v58, v57
	v_max_f32_e32 v236, v235, v212
	v_max_f32_e32 v195, v190, v44
	v_min_f32_e32 v212, v235, v212
	v_min_f32_e32 v44, v190, v44
	v_max_f32_e32 v243, v242, v213
	v_min_f32_e32 v246, v245, v182
	v_max_f32_e32 v210, v209, v46
	v_min_f32_e32 v220, v219, v181
	v_min_f32_e32 v213, v242, v213
	v_max_f32_e32 v182, v245, v182
	v_min_f32_e32 v46, v209, v46
	v_max_f32_e32 v181, v219, v181
	v_max_f32_e32 v237, v236, v178
	v_max_f32_e32 v234, v195, v179
	v_max_f32_e32 v235, v212, v50
	v_max_f32_e32 v190, v44, v180
	v_min_f32_e32 v247, v243, v246
	v_min_f32_e32 v241, v210, v220
	v_min_f32_e32 v242, v213, v182
	v_min_f32_e32 v209, v46, v181
	v_min_f32_e32 v178, v236, v178
	v_min_f32_e32 v179, v195, v179
	v_min_f32_e32 v50, v212, v50
	v_min_f32_e32 v44, v44, v180
	v_max_f32_e32 v236, v243, v246
	v_max_f32_e32 v210, v210, v220
	v_max_f32_e32 v182, v213, v182
	v_max_f32_e32 v46, v46, v181
	v_max_f32_e32 v223, v222, v183
	v_max_f32_e32 v224, v211, v48
	v_min_f32_e32 v183, v222, v183
	v_min_f32_e32 v48, v211, v48
	v_max_f32_e32 v238, v237, v234
	v_max_f32_e32 v239, v235, v190
	v_min_f32_e32 v244, v247, v241
	v_min_f32_e32 v219, v242, v209
	v_max_f32_e32 v195, v178, v179
	v_max_f32_e32 v180, v50, v44
	v_min_f32_e32 v220, v236, v210
	v_min_f32_e32 v181, v182, v46
	v_min_f32_e32 v234, v237, v234
	v_min_f32_e32 v190, v235, v190
	v_max_f32_e32 v237, v247, v241
	v_max_f32_e32 v209, v242, v209
	v_min_f32_e32 v178, v178, v179
	v_min_f32_e32 v44, v50, v44
	v_max_f32_e32 v50, v236, v210
	v_max_f32_e32 v46, v182, v46
	v_max_f32_e32 v225, v223, v224
	v_max_f32_e32 v211, v183, v48
	v_min_f32_e32 v223, v223, v224
	v_min_f32_e32 v48, v183, v48
	v_max_f32_e32 v240, v238, v239
	v_min_f32_e32 v245, v244, v219
	v_max_f32_e32 v212, v195, v180
	v_min_f32_e32 v213, v220, v181
	v_max_f32_e32 v235, v234, v190
	v_min_f32_e32 v241, v237, v209
	v_max_f32_e32 v179, v178, v44
	v_min_f32_e32 v182, v50, v46
	v_min_f32_e32 v238, v238, v239
	v_max_f32_e32 v219, v244, v219
	v_min_f32_e32 v180, v195, v180
	v_max_f32_e32 v181, v220, v181
	v_min_f32_e32 v190, v234, v190
	v_max_f32_e32 v209, v237, v209
	v_min_f32_e32 v44, v178, v44
	v_max_f32_e32 v46, v50, v46
	v_max_f32_e32 v226, v225, v51
	v_max_f32_e32 v221, v59, v173
	v_max_f32_e32 v222, v211, v60
	v_max_f32_e32 v56, v49, v61
	v_max_f32_e32 v224, v223, v62
	v_max_f32_e32 v58, v57, v63
	v_max_f32_e32 v183, v48, v52
	v_max_f32_e32 v55, v34, v53
	v_min_f32_e32 v248, v240, v245
	v_min_f32_e32 v243, v212, v213
	v_min_f32_e32 v242, v235, v241
	v_min_f32_e32 v210, v179, v182
	v_min_f32_e32 v239, v238, v219
	v_min_f32_e32 v195, v180, v181
	v_min_f32_e32 v234, v190, v209
	v_min_f32_e32 v178, v44, v46
	v_max_f32_e32 v227, v226, v221
	v_max_f32_e32 v228, v222, v56
	v_max_f32_e32 v230, v224, v58
	v_max_f32_e32 v231, v183, v55
	v_min_f32_e32 v246, v248, v243
	v_min_f32_e32 v236, v242, v210
	v_min_f32_e32 v220, v239, v195
	v_min_f32_e32 v237, v234, v178
	v_max_f32_e32 v229, v227, v228
	v_max_f32_e32 v232, v230, v231
	v_min_f32_e32 v247, v246, v236
	v_min_f32_e32 v244, v220, v237
	v_min_f32_e32 v51, v225, v51
	v_min_f32_e32 v59, v59, v173
	v_min_f32_e32 v60, v211, v60
	v_min_f32_e32 v61, v49, v61
	v_min_f32_e32 v62, v223, v62
	v_min_f32_e32 v57, v57, v63
	v_min_f32_e32 v48, v48, v52
	v_min_f32_e32 v34, v34, v53
	v_max_f32_e32 v63, v240, v245
	v_max_f32_e32 v212, v212, v213
	v_max_f32_e32 v235, v235, v241
	v_max_f32_e32 v179, v179, v182
	v_max_f32_e32 v219, v238, v219
	v_max_f32_e32 v180, v180, v181
	v_max_f32_e32 v190, v190, v209
	v_max_f32_e32 v44, v44, v46
	v_max_f32_e32 v233, v229, v232
	v_min_f32_e32 v50, v247, v244
	v_max_f32_e32 v173, v51, v59
	v_max_f32_e32 v211, v60, v61
	v_max_f32_e32 v223, v62, v57
	v_max_f32_e32 v53, v48, v34
	v_min_f32_e32 v213, v63, v212
	v_min_f32_e32 v182, v235, v179
	v_min_f32_e32 v181, v219, v180
	v_min_f32_e32 v46, v190, v44
	v_min_f32_e32 v227, v227, v228
	v_min_f32_e32 v228, v230, v231
	v_max_f32_e32 v230, v246, v236
	v_max_f32_e32 v220, v220, v237
	v_max_f32_e32 v50, v233, v50
	v_max_f32_e32 v44, v190, v44
	v_max_f32_e32 v225, v173, v211
	v_max_f32_e32 v233, v223, v53
	v_min_f32_e32 v240, v213, v182
	v_min_f32_e32 v209, v181, v46
	v_min_f32_e32 v221, v226, v221
	v_min_f32_e32 v222, v222, v56
	v_min_f32_e32 v224, v224, v58
	v_min_f32_e32 v183, v183, v55
	v_max_f32_e32 v241, v248, v243
	v_max_f32_e32 v210, v242, v210
	v_max_f32_e32 v195, v239, v195
	v_max_f32_e32 v234, v234, v178
	v_min_f32_e32 v51, v51, v59
	v_min_f32_e32 v59, v60, v61
	v_min_f32_e32 v57, v62, v57
	v_min_f32_e32 v34, v48, v34
	v_max_f32_e32 v60, v63, v212
	v_max_f32_e32 v62, v235, v179
	v_max_f32_e32 v58, v227, v228
	v_min_f32_e32 v63, v230, v220
	v_min_f32_e32 v211, v173, v211
	v_min_f32_e32 v223, v223, v53
	v_max_f32_e32 v213, v213, v182
	v_max_f32_e32 v46, v181, v46
	v_max_f32_e32 v226, v221, v222
	v_max_f32_e32 v238, v224, v183
	v_max_f32_e32 v243, v51, v59
	v_max_f32_e32 v245, v57, v34
	v_min_f32_e32 v179, v60, v62
	v_max_f32_e32 v63, v58, v63
	v_max_f32_e32 v53, v211, v223
	v_min_f32_e32 v58, v213, v46
	v_min_f32_e32 v181, v221, v222
	v_min_f32_e32 v221, v224, v183
	v_max_f32_e32 v222, v241, v210
	v_max_f32_e32 v224, v195, v234
	v_min_f32_e32 v51, v51, v59
	v_min_f32_e32 v59, v57, v34
	v_max_f32_e32 v231, v60, v62
	v_min_f32_e32 v57, v229, v232
	v_max_f32_e32 v62, v247, v244
	v_min_f32_e32 v239, v195, v234
	v_min_f32_e32 v242, v241, v210
	v_max_f32_e32 v212, v219, v180
	v_max_f32_e32 v178, v53, v58
	v_max_f32_e32 v53, v181, v221
	v_min_f32_e32 v173, v222, v224
	v_max_f32_e32 v183, v57, v62
	v_min_f32_e32 v57, v225, v233
	v_max_f32_e32 v62, v240, v209
	v_min_f32_e32 v219, v212, v44
	v_max_f32_e32 v180, v53, v173
	v_max_f32_e32 v190, v57, v62
	v_min_f32_e32 v57, v226, v238
	v_max_f32_e32 v173, v242, v239
	v_max_f32_e32 v55, v226, v238
	v_min_f32_e32 v56, v242, v239
	v_max_f32_e32 v210, v230, v220
	v_max_f32_e32 v195, v57, v173
	v_min_f32_e32 v57, v243, v245
	v_max_f32_e32 v173, v179, v219
	v_max_f32_e32 v55, v55, v56
	v_min_f32_e32 v56, v179, v219
	v_min_f32_e32 v179, v227, v228
	v_min_f32_e32 v52, v240, v209
	v_max_f32_e32 v209, v57, v173
	v_max_f32_e32 v46, v213, v46
	v_max_f32_e32 v44, v212, v44
	v_max_f32_e32 v210, v179, v210
	v_min_f32_e32 v179, v211, v223
	v_max_f32_e32 v211, v179, v46
	v_min_f32_e32 v46, v181, v221
	v_max_f32_e32 v181, v222, v224
	v_min_f32_e32 v53, v231, v44
	v_max_f32_e32 v44, v231, v44
	v_max_f32_e32 v212, v46, v181
	v_min_f32_e32 v46, v51, v59
	v_max_f32_e32 v34, v51, v59
	v_pk_add_f32 v[36:37], v[36:37], v[32:33] op_sel:[1,0] op_sel_hi:[0,1]
	v_mov_b32_e32 v37, 0xbf
	v_max_f32_e32 v213, v46, v44
	v_cmp_gt_i32_e32 vcc, 0, v36
	v_mov_b32_e32 v221, 0x50
	v_and_b32_e32 v41, 0xffffff00, v41
	v_cndmask_b32_e64 v37, v37, 64, vcc
	v_and_or_b32 v36, v36, s12, v37
	v_or_b32_e32 v217, v39, v41
	v_max_f32_e32 v49, v225, v233
	v_max_f32_e32 v44, v54, v36
	v_min_f32_e32 v54, v54, v36
	v_pk_add_f32 v[36:37], v[32:33], v[42:43] op_sel_hi:[0,1]
	v_cmp_gt_i32_e64 s[68:69], 0, v37
	v_mov_b32_e32 v42, 0x9f
	v_mov_b32_e32 v43, 0x60
	v_cndmask_b32_e64 v42, v42, v43, s[68:69]
	v_cmp_gt_i32_e64 s[68:69], 0, v36
	v_mov_b32_e32 v43, 0xaf
	v_and_b32_e32 v37, 0xffffff00, v37
	v_cndmask_b32_e64 v43, v43, v221, s[68:69]
	v_and_b32_e32 v36, 0xffffff00, v36
	v_or_b32_e32 v37, v42, v37
	v_or_b32_e32 v36, v43, v36
	v_min_f32_e32 v42, v37, v217
	v_max_f32_e32 v43, v36, v218
	v_max_f32_e32 v37, v37, v217
	v_min_f32_e32 v36, v36, v218
	v_max_f32_e32 v46, v44, v215
	v_max_f32_e32 v219, v54, v216
	v_min_f32_e32 v221, v43, v42
	v_min_f32_e32 v217, v36, v37
	v_max_f32_e32 v42, v43, v42
	v_max_f32_e32 v36, v36, v37
	v_max_f32_e32 v220, v46, v219
	v_min_f32_e32 v44, v44, v215
	v_min_f32_e32 v54, v54, v216
	v_min_f32_e32 v219, v46, v219
	v_mov_b32_e32 v46, v35
	v_min_f32_e32 v216, v42, v36
	v_max_f32_e32 v225, v42, v36
	v_pk_add_f32 v[36:37], v[32:33], v[46:47] op_sel_hi:[0,1]
	v_and_b32_e32 v45, 0xffffff80, v9
	v_max_f32_e32 v215, v44, v54
	v_min_f32_e32 v54, v44, v54
	v_mov_b32_e32 v44, v35
	v_cmp_gt_i32_e32 vcc, 0, v37
	v_mov_b32_e32 v35, 0x7f
	v_pk_add_f32 v[42:43], v[32:33], v[44:45] op_sel_hi:[0,1]
	v_cndmask_b32_e32 v35, v35, v196, vcc
	v_cmp_gt_i32_e32 vcc, 0, v36
	v_mov_b32_e32 v47, 0x8f
	v_mov_b32_e32 v45, 0x6f
	v_cndmask_b32_e32 v44, v47, v198, vcc
	v_cmp_gt_i32_e32 vcc, 0, v43
	v_mov_b32_e32 v46, 0x90
	v_and_b32_e32 v37, 0xffffff00, v37
	v_and_b32_e32 v36, 0xffffff00, v36
	v_cndmask_b32_e32 v45, v45, v46, vcc
	v_and_b32_e32 v43, 0xffffff00, v43
	v_cmp_gt_i32_e32 vcc, 0, v42
	v_or_b32_e32 v35, v35, v37
	v_or_b32_e32 v36, v44, v36
	v_or_b32_e32 v37, v45, v43
	v_and_b32_e32 v41, 0xffffff80, v10
	v_and_b32_e32 v40, 0xffffff80, v13
	v_cndmask_b32_e32 v46, v47, v198, vcc
	v_cmp_lt_f32_e32 vcc, v37, v35
	v_cmp_lt_f32_e64 s[8:9], v214, v36
	v_and_b32_e32 v39, 0xffffff80, v12
	v_cndmask_b32_e32 v43, v35, v37, vcc
	v_cndmask_b32_e64 v45, v36, v214, s[8:9]
	v_cndmask_b32_e32 v35, v37, v35, vcc
	v_pk_add_f32 v[36:37], v[32:33], v[40:41] op_sel_hi:[0,1]
	v_cmp_gt_i32_e64 s[80:81], 0, v37
	v_mov_b32_e32 v40, 0x5f
	v_mov_b32_e32 v41, 0xa0
	v_and_b32_e32 v38, 0xffffff80, v11
	v_cndmask_b32_e64 v40, v40, v41, s[80:81]
	v_and_b32_e32 v42, 0xffffff00, v42
	v_and_or_b32 v37, v37, s12, v40
	v_cmp_gt_i32_e64 s[80:81], 0, v36
	v_mov_b32_e32 v40, 0xd0
	v_pk_add_f32 v[38:39], v[32:33], v[38:39] op_sel_hi:[0,1]
	v_or_b32_e32 v42, v46, v42
	v_cndmask_b32_e64 v40, 47, v40, s[80:81]
	v_cmp_gt_i32_e64 s[80:81], 0, v39
	v_mov_b32_e32 v41, 0xc0
	v_cndmask_b32_e64 v42, v214, v42, s[8:9]
	v_cndmask_b32_e64 v41, 63, v41, s[80:81]
	v_cmp_gt_i32_e64 s[80:81], 0, v38
	v_mov_b32_e32 v214, 0x4f
	v_mov_b32_e32 v229, 0xb0
	v_cndmask_b32_e64 v214, v214, v229, s[80:81]
	v_and_b32_e32 v39, 0xffffff00, v39
	v_and_b32_e32 v38, 0xffffff00, v38
	v_and_b32_e32 v36, 0xffffff00, v36
	v_or_b32_e32 v39, v41, v39
	v_or_b32_e32 v38, v214, v38
	v_or_b32_e32 v36, v40, v36
	v_min_f32_e32 v40, v39, v36
	v_max_f32_e32 v41, v37, v38
	v_min_f32_e32 v37, v37, v38
	v_max_f32_e32 v36, v39, v36
	v_max_f32_e32 v44, v42, v43
	v_max_f32_e32 v46, v45, v35
	v_min_f32_e32 v214, v41, v40
	v_min_f32_e32 v38, v37, v36
	v_min_f32_e32 v42, v42, v43
	v_min_f32_e32 v35, v45, v35
	v_max_f32_e32 v40, v41, v40
	v_max_f32_e32 v36, v37, v36
	v_max_f32_e32 v47, v44, v46
	v_min_f32_e32 v39, v214, v38
	v_max_f32_e32 v43, v42, v35
	v_min_f32_e32 v37, v40, v36
	v_min_f32_e32 v44, v44, v46
	v_max_f32_e32 v38, v214, v38
	v_min_f32_e32 v35, v42, v35
	v_max_f32_e32 v36, v40, v36
	v_min_f32_e32 v218, v221, v217
	v_max_f32_e32 v217, v221, v217
	v_min_f32_e32 v229, v47, v39
	v_min_f32_e32 v41, v43, v37
	v_min_f32_e32 v46, v44, v38
	v_min_f32_e32 v40, v35, v36
	v_max_f32_e32 v39, v47, v39
	v_max_f32_e32 v37, v43, v37
	v_max_f32_e32 v38, v44, v38
	v_max_f32_e32 v35, v35, v36
	v_max_f32_e32 v222, v220, v218
	v_max_f32_e32 v223, v215, v216
	v_max_f32_e32 v221, v219, v217
	v_max_f32_e32 v226, v54, v225
	v_min_f32_e32 v218, v220, v218
	v_min_f32_e32 v215, v215, v216
	v_min_f32_e32 v217, v219, v217
	v_min_f32_e32 v54, v54, v225
	v_min_f32_e32 v43, v39, v37
	v_min_f32_e32 v36, v38, v35
	v_max_f32_e32 v37, v39, v37
	v_max_f32_e32 v35, v38, v35
	v_max_f32_e32 v216, v218, v215
	v_max_f32_e32 v219, v217, v54
	v_min_f32_e32 v44, v43, v36
	v_min_f32_e32 v215, v218, v215
	v_min_f32_e32 v54, v217, v54
	v_min_f32_e32 v38, v37, v35
	v_max_f32_e32 v43, v43, v36
	v_max_f32_e32 v35, v37, v35
	v_and_b32_e32 v37, 0xffffff80, v15
	v_mov_b32_e32 v36, v33
	v_pk_add_f32 v[32:33], v[32:33], v[36:37] op_sel_hi:[0,1]
	v_mov_b32_e32 v37, 0xe0
	v_max_f32_e32 v217, v215, v54
	v_min_f32_e32 v54, v215, v54
	v_cmp_gt_i32_e64 s[76:77], 0, v33
	v_and_b32_e32 v33, 0xffffff00, v33
	s_nop 0
	v_cndmask_b32_e64 v36, 15, v249, s[76:77]
	v_cmp_gt_i32_e64 s[76:77], 0, v32
	v_and_b32_e32 v32, 0xffffff00, v32
	v_or_b32_e32 v33, v36, v33
	v_cndmask_b32_e64 v37, 31, v37, s[76:77]
	v_or_b32_e32 v32, v37, v32
	v_max_f32_e32 v36, v32, v33
	v_min_f32_e32 v32, v32, v33
	v_max_f32_e32 v37, v36, v36
	v_max_f32_e32 v33, v32, v32
	v_max_f32_e32 v37, 0xff61b1e6, v37
	v_max_f32_e32 v33, 0xff61b1e6, v33
	v_max_f32_e32 v224, v222, v223
	v_max_f32_e32 v233, v37, v33
	v_min_f32_e32 v33, v37, v33
	v_max_f32_e32 v234, 0xff61b1e6, v233
	v_max_f32_e32 v37, 0xff61b1e6, v33
	v_cmp_nlt_f32_e32 vcc, s28, v33
	v_max_f32_e32 v227, v221, v226
	v_max_f32_e32 v235, v234, v37
	v_cmp_nlt_f32_e64 s[88:89], s28, v235
	v_cndmask_b32_e32 v33, v199, v33, vcc
	v_min_f32_e32 v45, v229, v41
	v_cndmask_b32_e64 v236, v199, v235, s[88:89]
	v_cmp_nlt_f32_e64 s[88:89], s28, v233
	v_min_f32_e32 v42, v46, v40
	v_min_f32_e32 v222, v222, v223
	v_cndmask_b32_e64 v233, v199, v233, s[88:89]
	v_cmp_nlt_f32_e64 s[88:89], s28, v36
	v_min_f32_e32 v221, v221, v226
	v_max_f32_e32 v41, v229, v41
	v_cndmask_b32_e64 v36, v199, v36, s[88:89]
	v_cmp_nlt_f32_e64 s[88:89], s28, v32
	v_max_f32_e32 v40, v46, v40
	s_nop 0
	v_cndmask_b32_e64 v32, v199, v32, s[88:89]
	v_max_f32_e32 v237, v36, v32
	v_min_f32_e32 v32, v36, v32
	v_max_f32_e32 v238, v233, v237
	v_max_f32_e32 v36, v33, v32
	v_max_f32_e32 v228, v224, v227
	v_min_f32_e32 v214, v45, v42
	v_max_f32_e32 v220, v216, v219
	v_max_f32_e32 v223, v222, v221
	v_min_f32_e32 v46, v41, v40
	v_min_f32_e32 v224, v224, v227
	v_max_f32_e32 v42, v45, v42
	v_min_f32_e32 v216, v216, v219
	v_min_f32_e32 v221, v222, v221
	v_max_f32_e32 v40, v41, v40
	v_max_f32_e32 v239, v238, v36
	v_min_f32_e32 v233, v233, v237
	v_min_f32_e32 v32, v33, v32
	v_min_f32_e32 v37, v234, v37
	v_min_f32_e32 v36, v238, v36
	v_max_f32_e32 v52, v49, v52
	s_mov_b64 s[6:7], s[96:97]
	v_cmp_nlt_f32_e64 s[88:89], s28, v239
	v_cmp_nlt_f32_e64 s[76:77], s28, v37
	v_cmp_nlt_f32_e64 s[14:15], s28, v36
	v_max_f32_e32 v230, v228, v214
	v_max_f32_e32 v47, v220, v44
	v_max_f32_e32 v226, v223, v46
	v_max_f32_e32 v39, v217, v38
	v_max_f32_e32 v45, v224, v42
	v_max_f32_e32 v219, v216, v43
	v_max_f32_e32 v41, v221, v40
	v_max_f32_e32 v215, v54, v35
	v_cndmask_b32_e64 v240, v199, v239, s[88:89]
	v_max_f32_e32 v33, v233, v32
	v_cndmask_b32_e64 v234, v199, v37, s[76:77]
	v_cndmask_b32_e64 v238, v199, v36, s[14:15]
	v_min_f32_e32 v32, v233, v32
	v_cmp_nlt_f32_e64 s[88:89], s28, v33
	v_cmp_nlt_f32_e32 vcc, s28, v32
	v_max_f32_e32 v48, v243, v245
	v_max_f32_e32 v225, v230, v47
	v_max_f32_e32 v218, v226, v39
	v_max_f32_e32 v227, v45, v219
	v_max_f32_e32 v222, v41, v215
	v_min_f32_e32 v241, v236, v240
	v_cndmask_b32_e64 v237, v199, v33, s[88:89]
	v_min_f32_e32 v243, v234, v238
	v_cndmask_b32_e32 v233, v199, v32, vcc
	v_max_f32_e32 v229, v225, v218
	v_max_f32_e32 v231, v227, v222
	v_min_f32_e32 v242, v241, v237
	v_min_f32_e32 v244, v243, v233
	v_min_f32_e32 v214, v228, v214
	v_max_f32_e32 v232, v229, v231
	v_min_f32_e32 v245, v242, v244
	v_max_f32_e32 v228, 0xff61b1e6, v235
	v_max_f32_e32 v235, v239, v239
	v_max_f32_e32 v36, v36, v36
	v_min_f32_e32 v44, v220, v44
	v_min_f32_e32 v46, v223, v46
	v_min_f32_e32 v38, v217, v38
	v_min_f32_e32 v42, v224, v42
	v_min_f32_e32 v43, v216, v43
	v_min_f32_e32 v40, v221, v40
	v_min_f32_e32 v35, v54, v35
	v_max_f32_e32 v235, 0xff61b1e6, v235
	v_max_f32_e32 v33, v33, v33
	v_max_f32_e32 v37, 0xff61b1e6, v37
	v_max_f32_e32 v36, 0xff61b1e6, v36
	v_max_f32_e32 v32, v32, v32
	v_max_f32_e32 v232, v232, v245
	s_mov_b32 s36, s18
	v_max_f32_e32 v33, 0xff61b1e6, v33
	v_max_f32_e32 v32, 0xff61b1e6, v32
	v_max_f32_e32 v220, v214, v44
	v_max_f32_e32 v217, v46, v38
	v_max_f32_e32 v216, v42, v43
	v_max_f32_e32 v54, v40, v35
	v_min_f32_e32 v239, v228, v235
	v_min_f32_e32 v245, 0xff61b1e6, v33
	v_min_f32_e32 v247, v37, v36
	v_min_f32_e32 v248, 0xff61b1e6, v32
	v_max_f32_e32 v223, v220, v217
	v_max_f32_e32 v221, v216, v54
	v_min_f32_e32 v246, v239, v245
	v_min_f32_e32 v249, v247, v248
	v_min_f32_e32 v47, v230, v47
	v_max_f32_e32 v230, v236, v240
	v_cmp_ngt_f32_e64 s[16:17], s28, v237
	v_max_f32_e32 v234, v234, v238
	v_cmp_ngt_f32_e64 s[14:15], s28, v233
	v_min_f32_e32 v44, v214, v44
	v_min_f32_e32 v38, v46, v38
	v_min_f32_e32 v42, v42, v43
	v_min_f32_e32 v35, v40, v35
	v_max_f32_e32 v214, v228, v235
	v_max_f32_e32 v36, v37, v36
	v_max_f32_e32 v224, v223, v221
	v_min_f32_e32 v250, v246, v249
	v_min_f32_e32 v39, v226, v39
	v_min_f32_e32 v45, v45, v219
	v_min_f32_e32 v41, v41, v215
	v_cndmask_b32_e64 v236, v199, v237, s[16:17]
	v_cndmask_b32_e64 v238, v199, v233, s[14:15]
	v_max_f32_e32 v46, v44, v38
	v_max_f32_e32 v40, v42, v35
	v_min_f32_e32 v228, v214, v33
	v_min_f32_e32 v37, v36, v32
	v_max_f32_e32 v224, v224, v250
	v_max_f32_e32 v226, v47, v39
	v_max_f32_e32 v215, v45, v41
	v_min_f32_e32 v240, v230, v236
	v_min_f32_e32 v250, v234, v238
	v_min_f32_e32 v218, v225, v218
	v_min_f32_e32 v222, v227, v222
	v_max_f32_e32 v237, v241, v237
	v_max_f32_e32 v233, v243, v233
	v_min_f32_e32 v39, v47, v39
	v_min_f32_e32 v41, v45, v41
	v_max_f32_e32 v47, v230, v236
	v_max_f32_e32 v230, v234, v238
	v_max_f32_e32 v43, v46, v40
	v_min_f32_e32 v235, v228, v37
	v_min_f32_e32 v217, v220, v217
	v_min_f32_e32 v54, v216, v54
	v_max_f32_e32 v239, v239, v245
	v_max_f32_e32 v243, v247, v248
	v_min_f32_e32 v38, v44, v38
	v_min_f32_e32 v35, v42, v35
	v_max_f32_e32 v33, v214, v33
	v_max_f32_e32 v32, v36, v32
	v_max_f32_e32 v219, v226, v215
	v_max_f32_e32 v227, v218, v222
	v_min_f32_e32 v241, v237, v233
	v_max_f32_e32 v45, v39, v41
	v_min_f32_e32 v234, v47, v230
	v_min_f32_e32 v229, v229, v231
	v_max_f32_e32 v231, v242, v244
	v_min_f32_e32 v215, v226, v215
	v_max_f32_e32 v226, v240, v250
	v_min_f32_e32 v251, v240, v250
	v_max_f32_e32 v43, v43, v235
	v_max_f32_e32 v216, v217, v54
	v_min_f32_e32 v245, v239, v243
	v_max_f32_e32 v42, v38, v35
	v_min_f32_e32 v36, v33, v32
	v_min_f32_e32 v221, v223, v221
	v_max_f32_e32 v223, v246, v249
	v_min_f32_e32 v40, v46, v40
	v_max_f32_e32 v37, v228, v37
	v_min_f32_e32 v218, v218, v222
	v_max_f32_e32 v222, v237, v233
	v_min_f32_e32 v54, v217, v54
	v_max_f32_e32 v217, v239, v243
	v_min_f32_e32 v39, v39, v41
	v_max_f32_e32 v41, v47, v230
	v_min_f32_e32 v35, v38, v35
	v_max_f32_e32 v32, v33, v32
	v_max_f32_e32 v227, v227, v241
	v_max_f32_e32 v45, v45, v234
	v_max_f32_e32 v229, v229, v231
	v_max_f32_e32 v215, v215, v226
	v_max_f32_e32 v61, v48, v56
	v_max_f32_e32 v182, v34, v53
	v_max_f32_e32 v219, v219, v251
	v_max_f32_e32 v216, v216, v245
	v_max_f32_e32 v36, v42, v36
	v_max_f32_e32 v221, v221, v223
	v_max_f32_e32 v37, v40, v37
	v_max_f32_e32 v218, v218, v222
	v_max_f32_e32 v217, v54, v217
	v_max_f32_e32 v39, v39, v41
	v_max_f32_e32 v32, v35, v32
	v_max_f32_e32 v49, v50, v52
	v_max_f32_e32 v56, v55, v61
	v_max_f32_e32 v58, v63, v178
	v_max_f32_e32 v60, v180, v182
	v_max_f32_e32 v62, v183, v190
	v_max_f32_e32 v173, v195, v209
	v_max_f32_e32 v179, v210, v211
	v_max_f32_e32 v181, v212, v213
	v_min_f32_e32 v225, v232, v224
	v_min_f32_e32 v241, v219, v43
	v_min_f32_e32 v245, v227, v216
	v_min_f32_e32 v42, v45, v36
	v_min_f32_e32 v223, v229, v221
	v_min_f32_e32 v40, v215, v37
	v_min_f32_e32 v222, v218, v217
	v_min_f32_e32 v33, v39, v32
	v_max_f32_e32 v48, v49, v56
	v_max_f32_e32 v53, v58, v60
	v_max_f32_e32 v57, v62, v173
	v_max_f32_e32 v59, v179, v181
	v_min_f32_e32 v220, v225, v241
	v_min_f32_e32 v44, v245, v42
	v_min_f32_e32 v46, v223, v40
	v_min_f32_e32 v35, v222, v33
	v_max_f32_e32 v34, v48, v53
	v_max_f32_e32 v51, v57, v59
	v_min_f32_e32 v214, v220, v44
	v_min_f32_e32 v38, v46, v35
	v_min_f32_e32 v47, v55, v61
	v_max_f32_e32 v235, v34, v51
	v_min_f32_e32 v41, v214, v38
	v_min_f32_e32 v61, v63, v178
	v_min_f32_e32 v63, v180, v182
	v_max_f32_e32 v54, v235, v41
	v_min_f32_e32 v41, v50, v52
	v_min_f32_e32 v182, v183, v190
	v_min_f32_e32 v183, v195, v209
	v_min_f32_e32 v190, v210, v211
	v_min_f32_e32 v209, v212, v213
	v_max_f32_e32 v212, v232, v224
	v_max_f32_e32 v43, v219, v43
	v_max_f32_e32 v216, v227, v216
	v_max_f32_e32 v36, v45, v36
	v_max_f32_e32 v221, v229, v221
	v_max_f32_e32 v37, v215, v37
	v_max_f32_e32 v217, v218, v217
	v_max_f32_e32 v32, v39, v32
	v_min_f32_e32 v49, v49, v56
	v_min_f32_e32 v224, v58, v60
	v_min_f32_e32 v62, v62, v173
	v_min_f32_e32 v173, v179, v181
	v_max_f32_e32 v181, v225, v241
	v_max_f32_e32 v42, v245, v42
	v_max_f32_e32 v40, v223, v40
	v_max_f32_e32 v33, v222, v33
	v_max_f32_e32 v50, v41, v47
	v_max_f32_e32 v178, v61, v63
	v_max_f32_e32 v195, v182, v183
	v_min_f32_e32 v213, v212, v43
	v_min_f32_e32 v45, v216, v36
	v_min_f32_e32 v215, v221, v37
	v_min_f32_e32 v39, v217, v32
	v_max_f32_e32 v226, v49, v224
	v_max_f32_e32 v179, v62, v173
	v_min_f32_e32 v225, v181, v42
	v_min_f32_e32 v222, v40, v33
	v_min_f32_e32 v41, v41, v47
	v_min_f32_e32 v47, v61, v63
	v_min_f32_e32 v63, v182, v183
	v_min_f32_e32 v182, v190, v209
	v_max_f32_e32 v43, v212, v43
	v_max_f32_e32 v36, v216, v36
	v_max_f32_e32 v37, v221, v37
	v_max_f32_e32 v32, v217, v32
	v_cmp_gt_f32_e64 s[24:25], v63, v182
	v_max_f32_e32 v210, v190, v209
	v_max_f32_e32 v56, v226, v179
	v_min_f32_e32 v58, v225, v222
	v_max_f32_e32 v223, v41, v47
	v_cndmask_b32_e64 v183, v182, v63, s[24:25]
	v_min_f32_e32 v209, v43, v36
	v_min_f32_e32 v212, v37, v32
	v_max_f32_e32 v56, v56, v58
	v_max_f32_e32 v58, v223, v183
	v_min_f32_e32 v60, v209, v212
	v_min_f32_e32 v48, v48, v53
	v_min_f32_e32 v217, v57, v59
	v_max_f32_e32 v44, v220, v44
	v_max_f32_e32 v35, v46, v35
	v_max_f32_e32 v58, v58, v60
	v_max_f32_e32 v53, v48, v217
	v_min_f32_e32 v46, v44, v35
	v_max_f32_e32 v180, v50, v178
	v_min_f32_e32 v219, v213, v45
	v_min_f32_e32 v218, v215, v39
	v_max_f32_e32 v59, v53, v46
	v_min_f32_e32 v46, v50, v178
	v_min_f32_e32 v50, v195, v210
	v_max_f32_e32 v45, v213, v45
	v_max_f32_e32 v39, v215, v39
	v_min_f32_e32 v49, v49, v224
	v_max_f32_e32 v53, v46, v50
	v_min_f32_e32 v57, v45, v39
	v_min_f32_e32 v213, v62, v173
	v_max_f32_e32 v42, v181, v42
	v_max_f32_e32 v33, v40, v33
	v_max_f32_e32 v60, v53, v57
	v_cmp_gt_f32_e64 s[20:21], v49, v213
	v_max_f32_e32 v211, v195, v210
	s_nop 0
	v_cndmask_b32_e64 v57, v213, v49, s[20:21]
	v_min_f32_e32 v40, v42, v33
	v_max_f32_e32 v36, v43, v36
	v_max_f32_e32 v32, v37, v32
	v_max_f32_e32 v61, v57, v40
	v_min_f32_e32 v40, v41, v47
	v_cndmask_b32_e64 v41, v63, v182, s[24:25]
	v_cmp_gt_f32_e64 s[14:15], v40, v41
	v_min_f32_e32 v34, v34, v51
	s_nop 0
	v_cndmask_b32_e64 v47, v41, v40, s[14:15]
	v_min_f32_e32 v37, v36, v32
	s_mov_b64 s[96:97], s[6:7]
	v_max_f32_e32 v62, v47, v37
	v_max_f32_e32 v37, v214, v38
	v_max_f32_e32 v35, v44, v35
	v_min_f32_e32 v55, v219, v218
	v_max_f32_e32 v63, v34, v37
	v_min_f32_e32 v34, v180, v211
	v_max_f32_e32 v37, v219, v218
	v_max_f32_e32 v52, v180, v211
	v_max_f32_e32 v33, v42, v33
	v_max_f32_e32 v173, v34, v37
	v_min_f32_e32 v34, v226, v179
	v_max_f32_e32 v37, v225, v222
	v_max_f32_e32 v32, v36, v32
	v_max_f32_e32 v178, v34, v37
	v_min_f32_e32 v34, v223, v183
	v_max_f32_e32 v37, v209, v212
	v_max_f32_e32 v55, v52, v55
	v_max_f32_e32 v179, v34, v37
	v_min_f32_e32 v34, v48, v217
	v_max_f32_e32 v180, v34, v35
	v_min_f32_e32 v34, v46, v50
	v_max_f32_e32 v35, v45, v39
	v_max_f32_e32 v181, v34, v35
	v_cndmask_b32_e64 v34, v49, v213, s[20:21]
	v_max_f32_e32 v182, v34, v33
	v_cndmask_b32_e64 v33, v40, v41, s[14:15]
	v_min_f32_e32 v52, v54, v55
	v_min_f32_e32 v190, v56, v58
	v_max_f32_e32 v183, v33, v32
	v_min_f32_e32 v53, v59, v60
	v_min_f32_e32 v57, v61, v62
	v_min_f32_e32 v195, v63, v173
	v_min_f32_e32 v209, v178, v179
	v_min_f32_e32 v210, v180, v181
	v_min_f32_e32 v211, v182, v183
	v_min_f32_e32 v216, v52, v190
	v_min_f32_e32 v215, v53, v57
	v_min_f32_e32 v51, v195, v209
	v_min_f32_e32 v50, v210, v211
	s_movk_i32 s10, 0xff
	v_min_f32_e32 v220, v216, v215
	v_min_f32_e32 v212, v51, v50
	s_movk_i32 s8, 0x7f
	v_bitop3_b32 v35, v31, s8, v31 bitop3:0xc
	v_min_f32_e32 v32, v220, v212
	v_and_b32_e32 v33, 0xff, v32
	v_bitop3_b32 v34, v32, s10, v32 bitop3:0xc
	v_cmp_gt_i32_e64 s[6:7], 0, v32
	v_readlane_b32 s94, v255, 39
	v_readlane_b32 s95, v255, 40
	v_cndmask_b32_e64 v213, v34, v33, s[6:7]
	v_and_b32_e32 v33, 0x7f, v31
	v_cmp_gt_i32_e64 s[6:7], 0, v31
	v_and_b32_e32 v34, 15, v213
	v_lshrrev_b32_e32 v214, 4, v213
	v_cndmask_b32_e64 v31, v35, v33, s[6:7]
	v_and_b32_e32 v33, 0x7f, v30
	v_bitop3_b32 v35, v30, s8, v30 bitop3:0xc
	v_cmp_gt_i32_e64 s[6:7], 0, v30
	v_readlane_b32 s86, v255, 31
	v_readlane_b32 s82, v255, 33
	v_cndmask_b32_e64 v30, v35, v33, s[6:7]
	v_and_b32_e32 v33, 0x7f, v29
	v_bitop3_b32 v35, v29, s8, v29 bitop3:0xc
	v_cmp_gt_i32_e64 s[6:7], 0, v29
	v_readlane_b32 s84, v255, 25
	v_readlane_b32 s87, v255, 32
	v_cndmask_b32_e64 v29, v35, v33, s[6:7]
	v_and_b32_e32 v33, 0x7f, v28
	v_bitop3_b32 v35, v28, s8, v28 bitop3:0xc
	v_cmp_gt_i32_e64 s[6:7], 0, v28
	v_readlane_b32 s92, v255, 35
	v_readlane_b32 s88, v255, 29
	v_cndmask_b32_e64 v28, v35, v33, s[6:7]
	v_and_b32_e32 v33, 0x7f, v27
	v_bitop3_b32 v35, v27, s8, v27 bitop3:0xc
	v_cmp_gt_i32_e64 s[6:7], 0, v27
	v_readlane_b32 s90, v255, 27
	v_readlane_b32 s78, v255, 13
	v_cndmask_b32_e64 v27, v35, v33, s[6:7]
	v_and_b32_e32 v33, 0x7f, v26
	v_bitop3_b32 v35, v26, s8, v26 bitop3:0xc
	v_cmp_gt_i32_e64 s[6:7], 0, v26
	v_readlane_b32 s83, v255, 34
	v_readlane_b32 s74, v255, 9
	v_cndmask_b32_e64 v26, v35, v33, s[6:7]
	v_and_b32_e32 v33, 0x7f, v25
	v_bitop3_b32 v35, v25, s8, v25 bitop3:0xc
	v_cmp_gt_i32_e64 s[6:7], 0, v25
	v_readlane_b32 s85, v255, 26
	v_readlane_b32 s76, v255, 11
	v_cndmask_b32_e64 v25, v35, v33, s[6:7]
	v_and_b32_e32 v33, 0x7f, v24
	v_bitop3_b32 v35, v24, s8, v24 bitop3:0xc
	v_cmp_gt_i32_e64 s[6:7], 0, v24
	v_readlane_b32 s22, v255, 23
	v_readlane_b32 s34, v255, 17
	v_cndmask_b32_e64 v24, v35, v33, s[6:7]
	v_and_b32_e32 v33, 0x7f, v23
	v_bitop3_b32 v35, v23, s8, v23 bitop3:0xc
	v_cmp_gt_i32_e64 s[6:7], 0, v23
	v_readlane_b32 s30, v255, 15
	v_readlane_b32 s81, v255, 41
	v_cndmask_b32_e64 v23, v35, v33, s[6:7]
	v_and_b32_e32 v33, 0x7f, v22
	v_bitop3_b32 v35, v22, s8, v22 bitop3:0xc
	v_cmp_gt_i32_e64 s[6:7], 0, v22
	s_movk_i32 s87, 0x4000
	v_readlane_b32 s93, v255, 36
	v_cndmask_b32_e64 v22, v35, v33, s[6:7]
	v_and_b32_e32 v33, 0x7f, v21
	v_bitop3_b32 v35, v21, s8, v21 bitop3:0xc
	v_cmp_gt_i32_e64 s[6:7], 0, v21
	v_readlane_b32 s89, v255, 30
	v_readlane_b32 s91, v255, 28
	v_cndmask_b32_e64 v21, v35, v33, s[6:7]
	v_and_b32_e32 v33, 0x7f, v20
	v_bitop3_b32 v35, v20, s8, v20 bitop3:0xc
	v_cmp_gt_i32_e64 s[6:7], 0, v20
	v_readlane_b32 s79, v255, 14
	v_readlane_b32 s83, v255, 37
	v_cndmask_b32_e64 v20, v35, v33, s[6:7]
	v_and_b32_e32 v33, 0x7f, v19
	v_bitop3_b32 v35, v19, s8, v19 bitop3:0xc
	v_cmp_gt_i32_e64 s[6:7], 0, v19
	v_readlane_b32 s75, v255, 10
	v_readlane_b32 s85, v255, 38
	v_cndmask_b32_e64 v19, v35, v33, s[6:7]
	v_and_b32_e32 v33, 0x7f, v18
	v_bitop3_b32 v35, v18, s8, v18 bitop3:0xc
	v_cmp_gt_i32_e64 s[6:7], 0, v18
	v_readlane_b32 s77, v255, 12
	v_readlane_b32 s23, v255, 24
	v_cndmask_b32_e64 v18, v35, v33, s[6:7]
	v_and_b32_e32 v33, 0x7f, v17
	v_bitop3_b32 v35, v17, s8, v17 bitop3:0xc
	v_cmp_gt_i32_e64 s[6:7], 0, v17
	s_mov_b32 s18, s36
	s_movk_i32 s27, 0x1200
	v_cndmask_b32_e64 v17, v35, v33, s[6:7]
	v_and_b32_e32 v33, 0x7f, v16
	v_bitop3_b32 v35, v16, s8, v16 bitop3:0xc
	v_cmp_gt_i32_e64 s[6:7], 0, v16
	v_readlane_b32 s35, v255, 18
	v_readlane_b32 s31, v255, 16
	v_cndmask_b32_e64 v33, v35, v33, s[6:7]
	v_lshl_add_u32 v252, v34, 8, v207
	ds_read_b32 v16, v252 offset:4096
	v_bitop3_b32 v35, v15, s8, v15 bitop3:0xc
	s_nop 0
	s_nop 1
	s_nop 1
	s_nop 1
	s_nop 1
	s_nop 1
	s_nop 1
	s_nop 1
	s_nop 1
	s_nop 1
	s_nop 1
	s_nop 1
	s_nop 1
	s_nop 1
	s_nop 1
	v_and_b32_e32 v34, 0x7f, v15
	s_nop 0
	s_waitcnt lgkmcnt(0)
	v_and_b32_e32 v252, 0x7f, v16
	v_cmp_gt_i32_e64 s[6:7], 0, v16
	v_xor_b32_e32 v16, 0x7f, v252
	s_nop 0
	v_cndmask_b32_e64 v16, v16, v252, s[6:7]
	v_cmp_gt_i32_e64 s[6:7], 0, v15
	v_and_b32_e32 v15, 0x7f, v14
	s_nop 0
	v_cndmask_b32_e64 v34, v35, v34, s[6:7]
	v_bitop3_b32 v35, v14, s8, v14 bitop3:0xc
	v_cmp_gt_i32_e64 s[6:7], 0, v14
	v_and_b32_e32 v14, 0x7f, v13
	s_nop 0
	v_cndmask_b32_e64 v35, v35, v15, s[6:7]
	v_bitop3_b32 v15, v13, s8, v13 bitop3:0xc
	v_cmp_gt_i32_e64 s[6:7], 0, v13
	v_and_b32_e32 v13, 0x7f, v12
	s_nop 0
	v_cndmask_b32_e64 v36, v15, v14, s[6:7]
	v_bitop3_b32 v14, v12, s8, v12 bitop3:0xc
	v_cmp_gt_i32_e64 s[6:7], 0, v12
	v_and_b32_e32 v12, 0x7f, v11
	v_max_f32_e32 v15, v59, v60
	v_cndmask_b32_e64 v37, v14, v13, s[6:7]
	v_bitop3_b32 v13, v11, s8, v11 bitop3:0xc
	v_cmp_gt_i32_e64 s[6:7], 0, v11
	v_and_b32_e32 v11, 0x7f, v10
	v_max_f32_e32 v14, v56, v58
	v_cndmask_b32_e64 v38, v13, v12, s[6:7]
	v_bitop3_b32 v12, v10, s8, v10 bitop3:0xc
	v_cmp_gt_i32_e64 s[6:7], 0, v10
	v_and_b32_e32 v10, 0x7f, v9
	v_max_f32_e32 v59, v61, v62
	v_cndmask_b32_e64 v39, v12, v11, s[6:7]
	v_bitop3_b32 v11, v9, s8, v9 bitop3:0xc
	v_cmp_gt_i32_e64 s[6:7], 0, v9
	v_and_b32_e32 v9, 0x7f, v8
	v_max_f32_e32 v60, v63, v173
	v_cndmask_b32_e64 v40, v11, v10, s[6:7]
	v_bitop3_b32 v10, v8, s8, v8 bitop3:0xc
	v_cmp_gt_i32_e64 s[6:7], 0, v8
	v_and_b32_e32 v8, 0x7f, v7
	v_max_f32_e32 v61, v178, v179
	v_cndmask_b32_e64 v41, v10, v9, s[6:7]
	v_bitop3_b32 v9, v7, s8, v7 bitop3:0xc
	v_cmp_gt_i32_e64 s[6:7], 0, v7
	v_and_b32_e32 v7, 0x7f, v6
	v_max_f32_e32 v62, v180, v181
	v_cndmask_b32_e64 v42, v9, v8, s[6:7]
	v_bitop3_b32 v8, v6, s8, v6 bitop3:0xc
	v_cmp_gt_i32_e64 s[6:7], 0, v6
	v_and_b32_e32 v6, 0x7f, v5
	v_max_f32_e32 v9, v210, v211
	v_cndmask_b32_e64 v43, v8, v7, s[6:7]
	v_bitop3_b32 v7, v5, s8, v5 bitop3:0xc
	v_cmp_gt_i32_e64 s[6:7], 0, v5
	v_and_b32_e32 v5, 0x7f, v4
	v_max_f32_e32 v8, v195, v209
	v_cndmask_b32_e64 v44, v7, v6, s[6:7]
	v_bitop3_b32 v6, v4, s8, v4 bitop3:0xc
	v_cmp_gt_i32_e64 s[6:7], 0, v4
	v_and_b32_e32 v4, 0x7f, v3
	v_max_f32_e32 v63, v182, v183
	v_cndmask_b32_e64 v45, v6, v5, s[6:7]
	v_bitop3_b32 v5, v3, s8, v3 bitop3:0xc
	v_cmp_gt_i32_e64 s[6:7], 0, v3
	v_and_b32_e32 v3, 0x7f, v2
	s_nop 0
	v_cndmask_b32_e64 v46, v5, v4, s[6:7]
	v_bitop3_b32 v4, v2, s8, v2 bitop3:0xc
	v_cmp_gt_i32_e64 s[6:7], 0, v2
	v_and_b32_e32 v2, 0x7f, v1
	s_nop 0
	v_cndmask_b32_e64 v47, v4, v3, s[6:7]
	v_bitop3_b32 v3, v1, s8, v1 bitop3:0xc
	v_cmp_gt_i32_e64 s[6:7], 0, v1
	v_and_b32_e32 v1, 0x7f, v0
	v_max_f32_e32 v4, v51, v50
	v_cndmask_b32_e64 v48, v3, v2, s[6:7]
	v_bitop3_b32 v2, v0, s8, v0 bitop3:0xc
	v_cmp_gt_i32_e64 s[6:7], 0, v0
	v_min_f32_e32 v56, v60, v61
	s_nop 0
	v_cndmask_b32_e64 v49, v2, v1, s[6:7]
	v_lshl_add_u32 v252, v214, 8, v207
	ds_read_b32 v0, v252
	v_min_f32_e32 v58, v62, v63
	s_nop 0
	v_max_f32_e32 v60, v60, v61
	v_max_f32_e32 v61, v62, v63
	v_readlane_b32 s46, v255, 21
	v_readlane_b32 s44, v255, 19
	v_readlane_b32 s47, v255, 22
	v_readlane_b32 s45, v255, 20
	s_nop 1
	s_nop 1
	s_nop 1
	s_nop 1
	s_nop 1
	s_nop 1
	s_nop 1
	s_nop 1
	s_nop 1
	s_nop 1
	s_nop 1
	s_nop 1
	s_waitcnt lgkmcnt(0)
	v_and_b32_e32 v252, 0x7f, v0
	v_cmp_gt_i32_e64 s[6:7], 0, v0
	v_xor_b32_e32 v0, 0x7f, v252
	s_nop 0
	v_cndmask_b32_e64 v3, v0, v252, s[6:7]
	v_max_f32_e32 v0, v220, v212
	v_and_b32_e32 v1, 0xff, v0
	v_bitop3_b32 v2, v0, s10, v0 bitop3:0xc
	v_cmp_gt_i32_e64 s[6:7], 0, v0
	v_and_b32_e32 v12, 0xffffff00, v0
	v_lshl_add_u32 v3, v3, 7, v16
	v_cndmask_b32_e64 v0, v2, v1, s[6:7]
	v_lshrrev_b32_e32 v1, 4, v0
	v_lshl_add_u32 v252, v1, 8, v207
	ds_read_b32 v2, v252
	v_and_b32_e32 v0, 15, v0
	s_nop 0
	s_nop 1
	s_nop 1
	s_nop 1
	s_nop 1
	s_nop 1
	s_nop 1
	s_nop 1
	s_nop 1
	s_nop 1
	s_nop 1
	s_nop 1
	s_nop 1
	s_nop 1
	s_nop 1
	s_nop 1
	s_waitcnt lgkmcnt(0)
	v_and_b32_e32 v252, 0x7f, v2
	v_cmp_gt_i32_e64 s[6:7], 0, v2
	v_xor_b32_e32 v2, 0x7f, v252
	s_nop 0
	v_cndmask_b32_e64 v1, v2, v252, s[6:7]
	v_lshl_add_u32 v252, v0, 8, v207
	ds_read_b32 v2, v252 offset:4096
	s_nop 1
	s_nop 1
	s_nop 1
	s_nop 1
	s_nop 1
	s_nop 1
	s_nop 1
	s_nop 1
	s_nop 1
	s_nop 1
	s_nop 1
	s_nop 1
	s_nop 1
	s_nop 1
	s_nop 1
	s_nop 1
	s_waitcnt lgkmcnt(0)
	v_and_b32_e32 v252, 0x7f, v2
	v_cmp_gt_i32_e64 s[6:7], 0, v2
	v_xor_b32_e32 v2, 0x7f, v252
	s_nop 0
	v_cndmask_b32_e64 v0, v2, v252, s[6:7]
	v_lshl_add_u32 v2, v1, 7, v0
	v_max_f32_e32 v0, v216, v215
	v_min_f32_e32 v1, v0, v4
	v_and_b32_e32 v5, 0xff, v1
	v_bitop3_b32 v6, v1, s10, v1 bitop3:0xc
	v_cmp_gt_i32_e64 s[8:9], 0, v1
	v_and_b32_e32 v50, 0xffffff00, v1
	v_max_f32_e32 v0, v0, v4
	v_cndmask_b32_e64 v1, v6, v5, s[8:9]
	v_lshrrev_b32_e32 v5, 4, v1
	v_lshl_add_u32 v252, v5, 8, v207
	ds_read_b32 v6, v252
	v_and_b32_e32 v1, 15, v1
	v_and_b32_e32 v4, 0xff, v0
	v_cmp_gt_i32_e64 s[6:7], 0, v0
	v_and_b32_e32 v51, 0xffffff00, v0
	s_nop 1
	s_nop 1
	s_nop 1
	s_nop 1
	s_nop 1
	s_nop 1
	s_nop 1
	s_nop 1
	s_nop 1
	s_nop 1
	s_nop 1
	s_nop 1
	s_nop 1
	s_nop 1
	s_waitcnt lgkmcnt(0)
	v_and_b32_e32 v252, 0x7f, v6
	v_cmp_gt_i32_e64 s[8:9], 0, v6
	v_xor_b32_e32 v6, 0x7f, v252
	s_nop 0
	v_cndmask_b32_e64 v5, v6, v252, s[8:9]
	v_lshl_add_u32 v252, v1, 8, v207
	ds_read_b32 v6, v252 offset:4096
	s_nop 1
	s_nop 1
	s_nop 1
	s_nop 1
	s_nop 1
	s_nop 1
	s_nop 1
	s_nop 1
	s_nop 1
	s_nop 1
	s_nop 1
	s_nop 1
	s_nop 1
	s_nop 1
	s_nop 1
	s_nop 1
	s_waitcnt lgkmcnt(0)
	v_and_b32_e32 v252, 0x7f, v6
	v_cmp_gt_i32_e64 s[8:9], 0, v6
	v_xor_b32_e32 v6, 0x7f, v252
	s_nop 0
	v_cndmask_b32_e64 v1, v6, v252, s[8:9]
	v_lshl_add_u32 v1, v5, 7, v1
	v_bitop3_b32 v5, v0, s10, v0 bitop3:0xc
	v_cndmask_b32_e64 v0, v5, v4, s[6:7]
	v_lshrrev_b32_e32 v4, 4, v0
	v_lshl_add_u32 v252, v4, 8, v207
	ds_read_b32 v5, v252
	v_and_b32_e32 v0, 15, v0
	s_nop 0
	s_nop 1
	s_nop 1
	s_nop 1
	s_nop 1
	s_nop 1
	s_nop 1
	s_nop 1
	s_nop 1
	s_nop 1
	s_nop 1
	s_nop 1
	s_nop 1
	s_nop 1
	s_nop 1
	s_nop 1
	s_waitcnt lgkmcnt(0)
	v_and_b32_e32 v252, 0x7f, v5
	v_cmp_gt_i32_e64 s[6:7], 0, v5
	v_xor_b32_e32 v5, 0x7f, v252
	s_nop 0
	v_cndmask_b32_e64 v4, v5, v252, s[6:7]
	v_lshl_add_u32 v252, v0, 8, v207
	ds_read_b32 v5, v252 offset:4096
	s_nop 1
	s_nop 1
	s_nop 1
	s_nop 1
	s_nop 1
	s_nop 1
	s_nop 1
	s_nop 1
	s_nop 1
	s_nop 1
	s_nop 1
	s_nop 1
	s_nop 1
	s_nop 1
	s_nop 1
	s_nop 1
	s_waitcnt lgkmcnt(0)
	v_and_b32_e32 v252, 0x7f, v5
	v_cmp_gt_i32_e64 s[6:7], 0, v5
	v_xor_b32_e32 v5, 0x7f, v252
	s_nop 0
	v_cndmask_b32_e64 v0, v5, v252, s[6:7]
	v_lshl_add_u32 v0, v4, 7, v0
	v_max_f32_e32 v4, v52, v190
	v_max_f32_e32 v5, v53, v57
	v_min_f32_e32 v6, v4, v5
	v_min_f32_e32 v10, v8, v9
	v_max_f32_e32 v4, v4, v5
	v_max_f32_e32 v8, v8, v9
	v_min_f32_e32 v7, v6, v10
	v_and_b32_e32 v11, 0xff, v7
	v_bitop3_b32 v13, v7, s10, v7 bitop3:0xc
	v_cmp_gt_i32_e64 s[8:9], 0, v7
	v_and_b32_e32 v52, 0xffffff00, v7
	v_max_f32_e32 v6, v6, v10
	v_cndmask_b32_e64 v7, v13, v11, s[8:9]
	v_lshrrev_b32_e32 v11, 4, v7
	v_lshl_add_u32 v252, v11, 8, v207
	ds_read_b32 v13, v252
	v_and_b32_e32 v7, 15, v7
	v_and_b32_e32 v10, 0xff, v6
	v_cmp_gt_i32_e64 s[6:7], 0, v6
	v_and_b32_e32 v53, 0xffffff00, v6
	s_nop 1
	s_nop 1
	s_nop 1
	s_nop 1
	s_nop 1
	s_nop 1
	s_nop 1
	s_nop 1
	s_nop 1
	s_nop 1
	s_nop 1
	s_nop 1
	s_nop 1
	s_nop 1
	s_waitcnt lgkmcnt(0)
	v_and_b32_e32 v252, 0x7f, v13
	v_cmp_gt_i32_e64 s[8:9], 0, v13
	v_xor_b32_e32 v13, 0x7f, v252
	s_nop 0
	v_cndmask_b32_e64 v11, v13, v252, s[8:9]
	v_lshl_add_u32 v252, v7, 8, v207
	ds_read_b32 v13, v252 offset:4096
	s_nop 1
	s_nop 1
	s_nop 1
	s_nop 1
	s_nop 1
	s_nop 1
	s_nop 1
	s_nop 1
	s_nop 1
	s_nop 1
	s_nop 1
	s_nop 1
	s_nop 1
	s_nop 1
	s_nop 1
	s_nop 1
	s_waitcnt lgkmcnt(0)
	v_and_b32_e32 v252, 0x7f, v13
	v_cmp_gt_i32_e64 s[8:9], 0, v13
	v_xor_b32_e32 v13, 0x7f, v252
	s_nop 0
	v_cndmask_b32_e64 v7, v13, v252, s[8:9]
	v_lshl_add_u32 v7, v11, 7, v7
	v_bitop3_b32 v11, v6, s10, v6 bitop3:0xc
	v_cndmask_b32_e64 v6, v11, v10, s[6:7]
	v_lshrrev_b32_e32 v10, 4, v6
	v_lshl_add_u32 v252, v10, 8, v207
	ds_read_b32 v11, v252
	v_and_b32_e32 v6, 15, v6
	v_max_f32_e32 v13, v54, v55
	v_min_f32_e32 v55, v56, v58
	s_nop 0
	v_max_f32_e32 v58, v56, v58
	s_nop 0
	s_nop 1
	s_nop 1
	s_nop 1
	s_nop 1
	s_nop 1
	s_nop 1
	s_nop 1
	s_nop 1
	s_nop 1
	s_nop 1
	s_nop 1
	s_nop 1
	s_nop 1
	s_waitcnt lgkmcnt(0)
	v_and_b32_e32 v252, 0x7f, v11
	v_cmp_gt_i32_e64 s[6:7], 0, v11
	v_xor_b32_e32 v11, 0x7f, v252
	s_nop 0
	v_cndmask_b32_e64 v10, v11, v252, s[6:7]
	v_lshl_add_u32 v252, v6, 8, v207
	ds_read_b32 v11, v252 offset:4096
	s_nop 1
	s_nop 1
	s_nop 1
	s_nop 1
	s_nop 1
	s_nop 1
	s_nop 1
	s_nop 1
	s_nop 1
	s_nop 1
	s_nop 1
	s_nop 1
	s_nop 1
	s_nop 1
	s_nop 1
	s_nop 1
	s_waitcnt lgkmcnt(0)
	v_and_b32_e32 v252, 0x7f, v11
	v_cmp_gt_i32_e64 s[6:7], 0, v11
	v_xor_b32_e32 v11, 0x7f, v252
	s_nop 0
	v_cndmask_b32_e64 v6, v11, v252, s[6:7]
	v_lshl_add_u32 v6, v10, 7, v6
	v_min_f32_e32 v5, v4, v8
	v_and_b32_e32 v9, 0xff, v5
	v_bitop3_b32 v10, v5, s10, v5 bitop3:0xc
	v_cmp_gt_i32_e64 s[8:9], 0, v5
	v_and_b32_e32 v57, 0xffffff00, v5
	v_max_f32_e32 v4, v4, v8
	v_cndmask_b32_e64 v5, v10, v9, s[8:9]
	v_lshrrev_b32_e32 v9, 4, v5
	v_lshl_add_u32 v252, v9, 8, v207
	ds_read_b32 v10, v252
	v_and_b32_e32 v5, 15, v5
	v_and_b32_e32 v8, 0xff, v4
	v_cmp_gt_i32_e64 s[6:7], 0, v4
	v_and_b32_e32 v209, 0xffffff00, v4
	s_nop 1
	s_nop 1
	s_nop 1
	s_nop 1
	s_nop 1
	s_nop 1
	s_nop 1
	s_nop 1
	s_nop 1
	s_nop 1
	s_nop 1
	s_nop 1
	s_nop 1
	s_nop 1
	s_waitcnt lgkmcnt(0)
	v_and_b32_e32 v252, 0x7f, v10
	v_cmp_gt_i32_e64 s[8:9], 0, v10
	v_xor_b32_e32 v10, 0x7f, v252
	s_nop 0
	v_cndmask_b32_e64 v9, v10, v252, s[8:9]
	v_lshl_add_u32 v252, v5, 8, v207
	ds_read_b32 v10, v252 offset:4096
	s_nop 1
	s_nop 1
	s_nop 1
	s_nop 1
	s_nop 1
	s_nop 1
	s_nop 1
	s_nop 1
	s_nop 1
	s_nop 1
	s_nop 1
	s_nop 1
	s_nop 1
	s_nop 1
	s_nop 1
	s_nop 1
	s_waitcnt lgkmcnt(0)
	v_and_b32_e32 v252, 0x7f, v10
	v_cmp_gt_i32_e64 s[8:9], 0, v10
	v_xor_b32_e32 v10, 0x7f, v252
	s_nop 0
	v_cndmask_b32_e64 v5, v10, v252, s[8:9]
	v_lshl_add_u32 v5, v9, 7, v5
	v_bitop3_b32 v9, v4, s10, v4 bitop3:0xc
	v_cndmask_b32_e64 v4, v9, v8, s[6:7]
	v_lshrrev_b32_e32 v8, 4, v4
	v_lshl_add_u32 v252, v8, 8, v207
	ds_read_b32 v9, v252
	v_and_b32_e32 v4, 15, v4
	s_nop 0
	s_nop 1
	s_nop 1
	s_nop 1
	s_nop 1
	s_nop 1
	s_nop 1
	s_nop 1
	s_nop 1
	s_nop 1
	s_nop 1
	s_nop 1
	s_nop 1
	s_nop 1
	s_nop 1
	s_nop 1
	s_waitcnt lgkmcnt(0)
	v_and_b32_e32 v252, 0x7f, v9
	v_cmp_gt_i32_e64 s[6:7], 0, v9
	v_xor_b32_e32 v9, 0x7f, v252
	s_nop 0
	v_cndmask_b32_e64 v8, v9, v252, s[6:7]
	v_lshl_add_u32 v252, v4, 8, v207
	ds_read_b32 v9, v252 offset:4096
	s_nop 1
	s_nop 1
	s_nop 1
	s_nop 1
	s_nop 1
	s_nop 1
	s_nop 1
	s_nop 1
	s_nop 1
	s_nop 1
	s_nop 1
	s_nop 1
	s_nop 1
	s_nop 1
	s_nop 1
	s_nop 1
	s_waitcnt lgkmcnt(0)
	v_and_b32_e32 v252, 0x7f, v9
	v_cmp_gt_i32_e64 s[6:7], 0, v9
	v_xor_b32_e32 v9, 0x7f, v252
	s_nop 0
	v_cndmask_b32_e64 v4, v9, v252, s[6:7]
	v_lshl_add_u32 v4, v8, 7, v4
	v_min_f32_e32 v8, v13, v14
	v_min_f32_e32 v9, v15, v59
	v_max_f32_e32 v13, v13, v14
	v_max_f32_e32 v59, v15, v59
	v_min_f32_e32 v10, v8, v9
	v_max_f32_e32 v8, v8, v9
	v_min_f32_e32 v11, v10, v55
	v_and_b32_e32 v173, 0xff, v11
	v_bitop3_b32 v178, v11, s10, v11 bitop3:0xc
	v_cmp_gt_i32_e64 s[8:9], 0, v11
	v_and_b32_e32 v54, 0xffffff00, v11
	v_max_f32_e32 v10, v10, v55
	v_cndmask_b32_e64 v11, v178, v173, s[8:9]
	v_lshrrev_b32_e32 v173, 4, v11
	v_lshl_add_u32 v252, v173, 8, v207
	ds_read_b32 v178, v252
	v_and_b32_e32 v11, 15, v11
	v_cmp_gt_i32_e64 s[6:7], 0, v10
	v_and_b32_e32 v55, 0xffffff00, v10
	s_nop 0
	v_min_f32_e32 v14, v13, v59
	v_min_f32_e32 v62, v60, v61
	v_max_f32_e32 v59, v13, v59
	v_max_f32_e32 v60, v60, v61
	s_nop 0
	s_nop 0
	v_min_f32_e32 v13, v59, v60
	v_and_b32_e32 v61, 0xffffff00, v13
	v_max_f32_e32 v59, v59, v60
	v_cmp_gt_i32_e32 vcc, 0, v59
	v_and_b32_e32 v60, 0xffffff00, v59
	v_sub_f32_e32 v12, v12, v60
	v_mul_f32_e32 v12, 0x3fb8aa3b, v12
	s_nop 0
	s_nop 1
	s_nop 1
	s_nop 1
	s_nop 1
	s_nop 1
	s_nop 1
	s_nop 1
	s_waitcnt lgkmcnt(0)
	v_and_b32_e32 v252, 0x7f, v178
	v_cmp_gt_i32_e64 s[8:9], 0, v178
	v_xor_b32_e32 v178, 0x7f, v252
	s_nop 0
	v_cndmask_b32_e64 v173, v178, v252, s[8:9]
	v_lshl_add_u32 v252, v11, 8, v207
	ds_read_b32 v178, v252 offset:4096
	s_nop 1
	s_nop 1
	s_nop 1
	s_nop 1
	s_nop 1
	s_nop 1
	s_nop 1
	s_nop 1
	s_nop 1
	s_nop 1
	s_nop 1
	s_nop 1
	s_nop 1
	s_nop 1
	s_nop 1
	s_nop 1
	s_waitcnt lgkmcnt(0)
	v_and_b32_e32 v252, 0x7f, v178
	v_cmp_gt_i32_e64 s[8:9], 0, v178
	v_xor_b32_e32 v178, 0x7f, v252
	s_nop 0
	v_cndmask_b32_e64 v11, v178, v252, s[8:9]
	v_lshl_add_u32 v11, v173, 7, v11
	v_and_b32_e32 v173, 0xff, v10
	v_bitop3_b32 v178, v10, s10, v10 bitop3:0xc
	v_cndmask_b32_e64 v10, v178, v173, s[6:7]
	v_lshrrev_b32_e32 v173, 4, v10
	v_lshl_add_u32 v252, v173, 8, v207
	ds_read_b32 v178, v252
	v_and_b32_e32 v10, 15, v10
	s_nop 0
	s_nop 1
	s_nop 1
	s_nop 1
	s_nop 1
	s_nop 1
	s_nop 1
	s_nop 1
	s_nop 1
	s_nop 1
	s_nop 1
	s_nop 1
	s_nop 1
	s_nop 1
	s_nop 1
	s_nop 1
	s_waitcnt lgkmcnt(0)
	v_and_b32_e32 v252, 0x7f, v178
	v_cmp_gt_i32_e64 s[6:7], 0, v178
	v_xor_b32_e32 v178, 0x7f, v252
	s_nop 0
	v_cndmask_b32_e64 v173, v178, v252, s[6:7]
	v_lshl_add_u32 v252, v10, 8, v207
	ds_read_b32 v178, v252 offset:4096
	s_nop 1
	s_nop 1
	s_nop 1
	s_nop 1
	s_nop 1
	s_nop 1
	s_nop 1
	s_nop 1
	s_nop 1
	s_nop 1
	s_nop 1
	s_nop 1
	s_nop 1
	s_nop 1
	s_nop 1
	s_nop 1
	s_waitcnt lgkmcnt(0)
	v_and_b32_e32 v252, 0x7f, v178
	v_cmp_gt_i32_e64 s[6:7], 0, v178
	v_xor_b32_e32 v178, 0x7f, v252
	s_nop 0
	v_cndmask_b32_e64 v10, v178, v252, s[6:7]
	v_lshl_add_u32 v10, v173, 7, v10
	v_min_f32_e32 v9, v8, v58
	v_and_b32_e32 v173, 0xff, v9
	v_bitop3_b32 v178, v9, s10, v9 bitop3:0xc
	v_cmp_gt_i32_e64 s[8:9], 0, v9
	v_and_b32_e32 v56, 0xffffff00, v9
	v_max_f32_e32 v8, v8, v58
	v_cndmask_b32_e64 v9, v178, v173, s[8:9]
	v_lshrrev_b32_e32 v173, 4, v9
	v_lshl_add_u32 v252, v173, 8, v207
	ds_read_b32 v178, v252
	v_and_b32_e32 v9, 15, v9
	v_cmp_gt_i32_e64 s[6:7], 0, v8
	v_and_b32_e32 v58, 0xffffff00, v8
	s_nop 0
	s_nop 1
	s_nop 1
	s_nop 1
	s_nop 1
	s_nop 1
	s_nop 1
	s_nop 1
	s_nop 1
	s_nop 1
	s_nop 1
	s_nop 1
	s_nop 1
	s_nop 1
	s_nop 1
	s_waitcnt lgkmcnt(0)
	v_and_b32_e32 v252, 0x7f, v178
	v_cmp_gt_i32_e64 s[8:9], 0, v178
	v_xor_b32_e32 v178, 0x7f, v252
	s_nop 0
	v_cndmask_b32_e64 v173, v178, v252, s[8:9]
	v_lshl_add_u32 v252, v9, 8, v207
	ds_read_b32 v178, v252 offset:4096
	s_nop 1
	s_nop 1
	s_nop 1
	s_nop 1
	s_nop 1
	s_nop 1
	s_nop 1
	s_nop 1
	s_nop 1
	s_nop 1
	s_nop 1
	s_nop 1
	s_nop 1
	s_nop 1
	s_nop 1
	s_nop 1
	s_waitcnt lgkmcnt(0)
	v_and_b32_e32 v252, 0x7f, v178
	v_cmp_gt_i32_e64 s[8:9], 0, v178
	v_xor_b32_e32 v178, 0x7f, v252
	s_nop 0
	v_cndmask_b32_e64 v9, v178, v252, s[8:9]
	v_lshl_add_u32 v9, v173, 7, v9
	v_and_b32_e32 v173, 0xff, v8
	v_bitop3_b32 v178, v8, s10, v8 bitop3:0xc
	v_cndmask_b32_e64 v8, v178, v173, s[6:7]
	v_lshrrev_b32_e32 v173, 4, v8
	v_lshl_add_u32 v252, v173, 8, v207
	ds_read_b32 v178, v252
	v_and_b32_e32 v8, 15, v8
	s_nop 0
	s_nop 1
	s_nop 1
	s_nop 1
	s_nop 1
	s_nop 1
	s_nop 1
	s_nop 1
	s_nop 1
	s_nop 1
	s_nop 1
	s_nop 1
	s_nop 1
	s_nop 1
	s_nop 1
	s_nop 1
	s_waitcnt lgkmcnt(0)
	v_and_b32_e32 v252, 0x7f, v178
	v_cmp_gt_i32_e64 s[6:7], 0, v178
	v_xor_b32_e32 v178, 0x7f, v252
	s_nop 0
	v_cndmask_b32_e64 v173, v178, v252, s[6:7]
	v_lshl_add_u32 v252, v8, 8, v207
	ds_read_b32 v178, v252 offset:4096
	s_nop 1
	s_nop 1
	s_nop 1
	s_nop 1
	s_nop 1
	s_nop 1
	s_nop 1
	s_nop 1
	s_nop 1
	s_nop 1
	s_nop 1
	s_nop 1
	s_nop 1
	s_nop 1
	s_nop 1
	s_nop 1
	s_waitcnt lgkmcnt(0)
	v_and_b32_e32 v252, 0x7f, v178
	v_cmp_gt_i32_e64 s[6:7], 0, v178
	v_xor_b32_e32 v178, 0x7f, v252
	s_nop 0
	v_cndmask_b32_e64 v8, v178, v252, s[6:7]
	v_lshl_add_u32 v8, v173, 7, v8
	v_min_f32_e32 v15, v14, v62
	v_and_b32_e32 v173, 0xff, v15
	v_bitop3_b32 v178, v15, s10, v15 bitop3:0xc
	v_cmp_gt_i32_e64 s[8:9], 0, v15
	v_and_b32_e32 v63, 0xffffff00, v15
	v_max_f32_e32 v14, v14, v62
	v_cndmask_b32_e64 v15, v178, v173, s[8:9]
	v_lshrrev_b32_e32 v173, 4, v15
	v_lshl_add_u32 v252, v173, 8, v207
	ds_read_b32 v178, v252
	v_and_b32_e32 v15, 15, v15
	v_cmp_gt_i32_e64 s[6:7], 0, v14
	v_and_b32_e32 v62, 0xffffff00, v14
	s_nop 0
	s_nop 1
	s_nop 1
	s_nop 1
	s_nop 1
	s_nop 1
	s_nop 1
	s_nop 1
	s_nop 1
	s_nop 1
	s_nop 1
	s_nop 1
	s_nop 1
	s_nop 1
	s_nop 1
	s_waitcnt lgkmcnt(0)
	v_and_b32_e32 v252, 0x7f, v178
	v_cmp_gt_i32_e64 s[8:9], 0, v178
	v_xor_b32_e32 v178, 0x7f, v252
	s_nop 0
	v_cndmask_b32_e64 v173, v178, v252, s[8:9]
	v_lshl_add_u32 v252, v15, 8, v207
	ds_read_b32 v178, v252 offset:4096
	s_nop 1
	s_nop 1
	s_nop 1
	s_nop 1
	s_nop 1
	s_nop 1
	s_nop 1
	s_nop 1
	s_nop 1
	s_nop 1
	s_nop 1
	s_nop 1
	s_nop 1
	s_nop 1
	s_nop 1
	s_nop 1
	s_waitcnt lgkmcnt(0)
	v_and_b32_e32 v252, 0x7f, v178
	v_cmp_gt_i32_e64 s[8:9], 0, v178
	v_xor_b32_e32 v178, 0x7f, v252
	s_nop 0
	v_cndmask_b32_e64 v15, v178, v252, s[8:9]
	v_lshl_add_u32 v15, v173, 7, v15
	v_and_b32_e32 v173, 0xff, v14
	v_bitop3_b32 v178, v14, s10, v14 bitop3:0xc
	v_cndmask_b32_e64 v14, v178, v173, s[6:7]
	v_lshrrev_b32_e32 v173, 4, v14
	v_lshl_add_u32 v252, v173, 8, v207
	ds_read_b32 v178, v252
	v_and_b32_e32 v14, 15, v14
	v_readlane_b32 s8, v253, 23
	v_readlane_b32 s9, v253, 24
	s_nop 0
	s_nop 1
	s_nop 1
	s_nop 1
	s_nop 1
	s_nop 1
	s_nop 1
	s_nop 1
	s_nop 1
	s_nop 1
	s_nop 1
	s_nop 1
	s_nop 1
	s_nop 1
	s_nop 1
	s_waitcnt lgkmcnt(0)
	v_and_b32_e32 v252, 0x7f, v178
	v_cmp_gt_i32_e64 s[6:7], 0, v178
	v_xor_b32_e32 v178, 0x7f, v252
	s_nop 0
	v_cndmask_b32_e64 v173, v178, v252, s[6:7]
	v_lshl_add_u32 v252, v14, 8, v207
	ds_read_b32 v178, v252 offset:4096
	s_nop 1
	s_nop 1
	s_nop 1
	s_nop 1
	s_nop 1
	s_nop 1
	s_nop 1
	s_nop 1
	s_nop 1
	s_nop 1
	s_nop 1
	s_nop 1
	s_nop 1
	s_nop 1
	s_nop 1
	s_nop 1
	s_waitcnt lgkmcnt(0)
	v_and_b32_e32 v252, 0x7f, v178
	v_cmp_gt_i32_e64 s[6:7], 0, v178
	v_xor_b32_e32 v178, 0x7f, v252
	s_nop 0
	v_cndmask_b32_e64 v14, v178, v252, s[6:7]
	v_lshl_add_u32 v14, v173, 7, v14
	v_and_b32_e32 v173, 0xff, v13
	v_bitop3_b32 v178, v13, s10, v13 bitop3:0xc
	v_cmp_gt_i32_e64 s[6:7], 0, v13
	s_nop 1
	v_cndmask_b32_e64 v13, v178, v173, s[6:7]
	v_lshrrev_b32_e32 v173, 4, v13
	v_lshl_add_u32 v252, v173, 8, v207
	ds_read_b32 v178, v252
	v_and_b32_e32 v13, 15, v13
	s_nop 0
	s_nop 1
	s_nop 1
	s_nop 1
	s_nop 1
	s_nop 1
	s_nop 1
	s_nop 1
	s_nop 1
	s_nop 1
	s_nop 1
	s_nop 1
	s_nop 1
	s_nop 1
	s_nop 1
	s_nop 1
	s_waitcnt lgkmcnt(0)
	v_and_b32_e32 v252, 0x7f, v178
	v_cmp_gt_i32_e64 s[6:7], 0, v178
	v_xor_b32_e32 v178, 0x7f, v252
	s_nop 0
	v_cndmask_b32_e64 v173, v178, v252, s[6:7]
	v_lshl_add_u32 v252, v13, 8, v207
	ds_read_b32 v178, v252 offset:4096
	s_nop 1
	s_nop 1
	s_nop 1
	s_nop 1
	s_nop 1
	s_nop 1
	s_nop 1
	s_nop 1
	s_nop 1
	s_nop 1
	s_nop 1
	s_nop 1
	s_nop 1
	s_nop 1
	s_nop 1
	s_nop 1
	s_waitcnt lgkmcnt(0)
	v_and_b32_e32 v252, 0x7f, v178
	v_cmp_gt_i32_e64 s[6:7], 0, v178
	v_xor_b32_e32 v178, 0x7f, v252
	s_nop 0
	v_cndmask_b32_e64 v13, v178, v252, s[6:7]
	v_lshl_add_u32 v13, v173, 7, v13
	v_and_b32_e32 v173, 0xff, v59
	v_bitop3_b32 v178, v59, s10, v59 bitop3:0xc
	v_cndmask_b32_e32 v59, v178, v173, vcc
	v_lshrrev_b32_e32 v173, 4, v59
	v_cmp_gt_u32_e32 vcc, 16, v59
	s_nop 1
	v_cndmask_b32_e32 v49, 0, v49, vcc
	v_cmp_eq_u32_e32 vcc, 1, v173
	s_nop 1
	v_cndmask_b32_e32 v48, v49, v48, vcc
	v_cmp_eq_u32_e32 vcc, 2, v173
	s_nop 1
	v_cndmask_b32_e32 v47, v48, v47, vcc
	v_cmp_eq_u32_e32 vcc, 3, v173
	s_nop 1
	v_cndmask_b32_e32 v46, v47, v46, vcc
	v_cmp_eq_u32_e32 vcc, 4, v173
	s_nop 1
	v_cndmask_b32_e32 v45, v46, v45, vcc
	v_cmp_eq_u32_e32 vcc, 5, v173
	s_nop 1
	v_cndmask_b32_e32 v44, v45, v44, vcc
	v_cmp_eq_u32_e32 vcc, 6, v173
	s_nop 1
	v_cndmask_b32_e32 v43, v44, v43, vcc
	v_cmp_eq_u32_e32 vcc, 7, v173
	s_nop 1
	v_cndmask_b32_e32 v42, v43, v42, vcc
	v_cmp_eq_u32_e32 vcc, 8, v173
	s_nop 1
	v_cndmask_b32_e32 v41, v42, v41, vcc
	v_cmp_eq_u32_e32 vcc, 9, v173
	s_nop 1
	v_cndmask_b32_e32 v40, v41, v40, vcc
	v_cmp_eq_u32_e32 vcc, 10, v173
	s_nop 1
	v_cndmask_b32_e32 v39, v40, v39, vcc
	v_cmp_eq_u32_e32 vcc, 11, v173
	s_nop 1
	v_cndmask_b32_e32 v38, v39, v38, vcc
	v_cmp_eq_u32_e32 vcc, 12, v173
	v_and_b32_e32 v39, 15, v59
	s_nop 0
	v_cndmask_b32_e32 v37, v38, v37, vcc
	v_cmp_eq_u32_e32 vcc, 13, v173
	s_nop 1
	v_cndmask_b32_e32 v36, v37, v36, vcc
	v_cmp_eq_u32_e32 vcc, 14, v173
	s_nop 1
	v_cndmask_b32_e32 v35, v36, v35, vcc
	v_cmp_eq_u32_e32 vcc, 15, v173
	v_exp_f32_e32 v36, v12
	v_and_b32_e32 v12, 0xffffff00, v32
	v_cndmask_b32_e32 v38, v35, v34, vcc
	v_cmp_eq_u32_e32 vcc, 0, v39
	v_sub_f32_e32 v12, v12, v60
	v_mul_f32_e32 v12, 0x3fb8aa3b, v12
	v_cndmask_b32_e32 v33, 0, v33, vcc
	v_cmp_eq_u32_e32 vcc, 1, v39
	v_exp_f32_e32 v37, v12
	s_nop 0
	v_cndmask_b32_e32 v17, v33, v17, vcc
	v_cmp_eq_u32_e32 vcc, 2, v39
	v_sub_f32_e32 v33, v51, v60
	v_mul_f32_e32 v33, 0x3fb8aa3b, v33
	v_cndmask_b32_e32 v17, v17, v18, vcc
	v_cmp_eq_u32_e32 vcc, 3, v39
	v_sub_f32_e32 v18, v60, v60
	v_mul_f32_e32 v18, 0x3fb8aa3b, v18
	v_cndmask_b32_e32 v17, v17, v19, vcc
	v_cmp_eq_u32_e32 vcc, 4, v39
	v_sub_f32_e32 v19, v61, v60
	v_exp_f32_e32 v18, v18
	v_cndmask_b32_e32 v17, v17, v20, vcc
	v_cmp_eq_u32_e32 vcc, 5, v39
	v_mul_f32_e32 v19, 0x3fb8aa3b, v19
	v_sub_f32_e32 v20, v62, v60
	v_cndmask_b32_e32 v17, v17, v21, vcc
	v_exp_f32_e32 v19, v19
	v_mul_f32_e32 v20, 0x3fb8aa3b, v20
	v_sub_f32_e32 v21, v63, v60
	v_cmp_eq_u32_e32 vcc, 6, v39
	v_exp_f32_e32 v20, v20
	v_mul_f32_e32 v21, 0x3fb8aa3b, v21
	v_cndmask_b32_e32 v17, v17, v22, vcc
	v_cmp_eq_u32_e32 vcc, 7, v39
	v_exp_f32_e32 v21, v21
	v_add_f32_e32 v22, 0, v18
	v_cndmask_b32_e32 v17, v17, v23, vcc
	v_cmp_eq_u32_e32 vcc, 8, v39
	v_add_f32_e32 v22, v19, v22
	v_add_f32_e32 v22, v20, v22
	v_cndmask_b32_e32 v17, v17, v24, vcc
	v_cmp_eq_u32_e32 vcc, 9, v39
	v_sub_f32_e32 v23, v56, v60
	v_mul_f32_e32 v23, 0x3fb8aa3b, v23
	v_cndmask_b32_e32 v17, v17, v25, vcc
	v_cmp_eq_u32_e32 vcc, 10, v39
	v_sub_f32_e32 v24, v55, v60
	v_exp_f32_e32 v23, v23
	v_cndmask_b32_e32 v17, v17, v26, vcc
	v_add_f32_e32 v26, v21, v22
	v_sub_f32_e32 v22, v58, v60
	v_mul_f32_e32 v22, 0x3fb8aa3b, v22
	v_exp_f32_e32 v22, v22
	v_mul_f32_e32 v24, 0x3fb8aa3b, v24
	v_sub_f32_e32 v25, v54, v60
	v_exp_f32_e32 v24, v24
	v_mul_f32_e32 v25, 0x3fb8aa3b, v25
	v_cmp_eq_u32_e32 vcc, 11, v39
	v_exp_f32_e32 v25, v25
	v_add_f32_e32 v26, v22, v26
	v_cndmask_b32_e32 v17, v17, v27, vcc
	v_cmp_eq_u32_e32 vcc, 12, v39
	v_add_f32_e32 v26, v23, v26
	v_add_f32_e32 v26, v24, v26
	v_cndmask_b32_e32 v17, v17, v28, vcc
	v_cmp_eq_u32_e32 vcc, 13, v39
	v_sub_f32_e32 v27, v57, v60
	v_mul_f32_e32 v27, 0x3fb8aa3b, v27
	v_cndmask_b32_e32 v17, v17, v29, vcc
	v_cmp_eq_u32_e32 vcc, 14, v39
	v_sub_f32_e32 v28, v53, v60
	v_exp_f32_e32 v27, v27
	v_cndmask_b32_e32 v17, v17, v30, vcc
	v_add_f32_e32 v30, v25, v26
	v_sub_f32_e32 v26, v209, v60
	v_mul_f32_e32 v26, 0x3fb8aa3b, v26
	v_exp_f32_e32 v26, v26
	v_mul_f32_e32 v28, 0x3fb8aa3b, v28
	v_sub_f32_e32 v29, v52, v60
	v_exp_f32_e32 v28, v28
	v_mul_f32_e32 v29, 0x3fb8aa3b, v29
	v_exp_f32_e32 v29, v29
	v_exp_f32_e32 v34, v33
	v_sub_f32_e32 v33, v50, v60
	v_add_f32_e32 v30, v26, v30
	v_mul_f32_e32 v33, 0x3fb8aa3b, v33
	v_add_f32_e32 v30, v27, v30
	v_exp_f32_e32 v35, v33
	v_add_f32_e32 v30, v28, v30
	v_add_f32_e32 v30, v29, v30
	v_add_f32_e32 v12, v34, v30
	v_add_f32_e32 v12, v35, v12
	v_add_f32_e32 v12, v36, v12
	v_add_f32_e32 v30, v37, v12
	v_div_scale_f32 v32, s[6:7], v30, v30, 1.0
	v_rcp_f32_e32 v33, v32
	v_cmp_eq_u32_e32 vcc, 15, v39
	v_readlane_b32 s6, v255, 46
	s_lshl_b32 s6, s6, 4
	v_cndmask_b32_e32 v12, v17, v31, vcc
	v_fma_f32 v17, -v32, v33, 1.0
	v_fmac_f32_e32 v33, v17, v33
	v_div_scale_f32 v17, vcc, 1.0, v30, 1.0
	v_mul_f32_e32 v31, v17, v33
	v_lshl_add_u32 v12, v38, 7, v12
	v_fma_f32 v38, -v32, v31, v17
	v_fmac_f32_e32 v31, v38, v33
	v_fma_f32 v17, -v32, v31, v17
	v_div_fmas_f32 v17, v17, v33, v31
	v_div_fixup_f32 v30, v17, v30, 1.0
	v_lshlrev_b64 v[16:17], 9, v[176:177]
	s_ashr_i32 s7, s6, 31
	v_lshl_add_u64 v[32:33], s[94:95], 0, v[16:17]
	s_lshl_b64 s[6:7], s[6:7], 2
	v_lshl_add_u64 v[32:33], v[32:33], 0, s[6:7]
	v_lshl_add_u64 v[16:17], s[8:9], 0, v[16:17]
	v_lshl_add_u64 v[16:17], v[16:17], 0, s[6:7]
	global_store_dwordx4 v[32:33], v[12:15], off
	v_readlane_b32 s8, v255, 44
	v_readlane_b32 s9, v255, 45
	v_pk_mul_f32 v[12:13], v[18:19], v[30:31] op_sel_hi:[1,0]
	v_pk_mul_f32 v[14:15], v[20:21], v[30:31] op_sel_hi:[1,0]
	global_store_dwordx4 v[16:17], v[12:15], off
	global_store_dwordx4 v[32:33], v[8:11], off offset:16
	s_nop 1
	v_pk_mul_f32 v[8:9], v[22:23], v[30:31] op_sel_hi:[1,0]
	v_pk_mul_f32 v[10:11], v[24:25], v[30:31] op_sel_hi:[1,0]
	global_store_dwordx4 v[16:17], v[8:11], off offset:16
	global_store_dwordx4 v[32:33], v[4:7], off offset:32
	s_nop 1
	v_pk_mul_f32 v[4:5], v[26:27], v[30:31] op_sel_hi:[1,0]
	v_pk_mul_f32 v[6:7], v[28:29], v[30:31] op_sel_hi:[1,0]
	global_store_dwordx4 v[16:17], v[4:7], off offset:32
	global_store_dwordx4 v[32:33], v[0:3], off offset:48
	s_nop 1
	v_pk_mul_f32 v[0:1], v[34:35], v[30:31] op_sel_hi:[1,0]
	v_pk_mul_f32 v[2:3], v[36:37], v[30:31] op_sel_hi:[1,0]
	global_store_dwordx4 v[16:17], v[0:3], off offset:48
	s_branch .LBB0_696
